# fp8 GEMM staging: redundant m0 save/restore around each LDS-DMA removed (420 sites); SwiGLU (u+1)*4 as one FMA; on top of the attention-loop interleave with early staging loads
# speedup vs baseline: 1.0084x; 1.0081x over previous
; #define PG8_WAIT_V(n) asm volatile("s_waitcnt vmcnt(" #n ")" ::: "memory")
; #define PG8_BAR __builtin_amdgcn_s_barrier()
; #define PG8_GOFF(un, d0, d1) do { PG8_GOFF1(un, 0, d0); PG8_GOFF1(un, 1, d1); } while (0)
; template <class Epi, class Sched, bool ALIGN_EPI = true, bool SP2 = true, bool FP8 = false, bool GATHER = false>
; __device__ __forceinline__ void gemm_phase(LAS unsigned char* lds, const Dims g, const Sched& S, const Epi& E, const int wv) {
;     ...
;     for (int i = 0; i < 2; ++i) { int R, C; stage_rc(tid * 16 + i * 8192, R, C); const int Rb = Epi::PERM ? ((R & ~31) + perm32(R & 31)) : R;
;         voffA[i] = (unsigned)(R * g.lda + C) * 2u; voffB[i] = (unsigned)(Rb * g.ldb + C) * 2u; }
;     const size_t kstep = (size_t)(BK * 2);
;     const size_t hstepA = (size_t)HALF * g.lda * 2, hstepB = (size_t)HALF * g.ldb * 2;
;     const unsigned ldsw = (unsigned)wid * 1024u, ldsb_ = (unsigned)(uintptr_t)lds;
;     const int aoff = lds_byte(wr * 64 + fr, fq * 8), boff = lds_byte(wc * 32 + fr, fq * 8);
;     ...
;     static_assert(!GATHER || (FP8 && SP2), "gather form: fp8 + SP2 only");
;     ...
;     unsigned vA0[2], vA1[2];
;     Unit cur, nxt; int ui = 0;
;     if (!S.next(0, cur)) return;
;     if constexpr (GATHER) PG8_GOFF(0, vA0, vA1);
;     { const unsigned dl_ = S.start_delay();
;       if (dl_) { const unsigned long long t0_ = __builtin_amdgcn_s_memrealtime(); while (__builtin_amdgcn_s_memrealtime() - t0_ < dl_) __builtin_amdgcn_s_sleep(8); } }
;     f32x4 acc[2][2][4][2];
; #pragma unroll
;     for (int a = 0; a < 2; ++a)
; #pragma unroll
;         for (int b = 0; b < 2; ++b)
; #pragma unroll
;             for (int m = 0; m < 4; ++m)
; #pragma unroll
;                 for (int n = 0; n < 2; ++n) acc[a][b][m][n] = (f32x4){0.f, 0.f, 0.f, 0.f};
;     bf16x8 At[4][2], B0[2][2], B1[2][2]; v8i_t At8[4], B08[2], B18[2];
;     const char* cA = cur.A; const char* cB = cur.B;
;     if constexpr (SP2) {
;         PG8_STAGE(PG8_SB(0, 0), cB, voffB); PG8_STAGE(PG8_SB(0, 1), cB + hstepB, voffB); PG8_STAGE_A(0, 0, cA); PG8_STAGE_A(0, 1, cA);
;         if (wr == 1) PG8_BAR;
;         PG8_WAIT_V(2); PG8_BAR;
;         PG8_STAGE(PG8_SB(1, 0), cB + kstep, voffB); PG8_STAGE_A(1, 0, cA + kstep); PG8_STAGE(PG8_SB(1, 1), cB + hstepB + kstep, voffB);
;         PG8_WAIT_V(6); PG8_BAR;
.LBB0_733:
	v_bfe_i32 v2, v164, 27, 1
	v_lshlrev_b32_e32 v0, 4, v164
	v_lshrrev_b32_e32 v2, 22, v2
	v_add_u32_e32 v2, v0, v2
	v_and_b32_e32 v2, 0xfffffc00, v2
	v_sub_u32_e32 v2, v0, v2
	v_ashrrev_i32_e32 v1, 31, v164
	v_lshrrev_b32_e32 v3, 4, v2
	v_lshrrev_b32_e32 v1, 26, v1
	v_bitop3_b32 v2, v3, v2, 32 bitop3:0x6c
	v_add_u32_e32 v1, v164, v1
	v_ashrrev_i32_e32 v4, 31, v2
	v_ashrrev_i32_e32 v1, 6, v1
	v_lshrrev_b32_e32 v4, 26, v4
	v_lshlrev_b32_e32 v3, 3, v1
	v_add_u32_e32 v4, v2, v4
	v_and_b32_e32 v3, -16, v3
	v_ashrrev_i32_e32 v5, 6, v4
	v_and_b32_e32 v4, 0xc0, v4
	v_add_u32_e32 v3, v5, v3
	v_sub_u32_e32 v2, v2, v4
	v_mov_b32_e32 v4, 1
	v_lshlrev_b32_e32 v1, 5, v1
	v_ashrrev_i16_sdwa v2, v4, sext(v2) dst_sel:DWORD dst_unused:UNUSED_PAD src0_sel:DWORD src1_sel:BYTE_0
	v_lshlrev_b32_e32 v6, 1, v3
	v_lshrrev_b32_e32 v7, 2, v3
	v_and_b32_e32 v5, 3, v5
	s_mov_b32 s8, 0x3fffe0
	v_and_b32_e32 v1, 32, v1
	v_bfe_i32 v2, v2, 0, 16
	v_and_b32_e32 v6, 24, v6
	v_and_b32_e32 v7, 4, v7
	v_and_or_b32 v5, v3, s8, v5
	v_or3_b32 v5, v5, v7, v6
	v_add_lshl_u32 v1, v1, v2, 1
	v_add_u32_e32 v0, 0x2000, v0
	v_lshl_add_u32 v165, v3, 10, v1
	v_lshl_add_u32 v166, v5, 10, v1
	v_ashrrev_i32_e32 v1, 31, v0
	v_lshrrev_b32_e32 v1, 22, v1
	v_add_u32_e32 v1, v0, v1
	v_ashrrev_i32_e32 v1, 10, v1
	v_mul_i32_i24_e32 v2, 0x400, v1
	v_sub_u32_e32 v0, v0, v2
	v_lshrrev_b32_e32 v2, 4, v0
	v_bitop3_b32 v0, v2, v0, 32 bitop3:0x6c
	v_ashrrev_i32_e32 v3, 31, v0
	v_lshrrev_b32_e32 v3, 26, v3
	v_lshlrev_b32_e32 v2, 3, v1
	v_add_u32_e32 v3, v0, v3
	v_and_b32_e32 v2, -16, v2
	v_ashrrev_i32_e32 v5, 6, v3
	v_and_b32_e32 v3, 0xc0, v3
	s_ashr_i32 s5, s14, 6
	v_add_u32_e32 v2, v5, v2
	v_sub_u32_e32 v0, v0, v3
	v_and_b32_e32 v5, 3, v5
	v_lshlrev_b32_e32 v1, 5, v1
	v_ashrrev_i16_sdwa v0, v4, sext(v0) dst_sel:DWORD dst_unused:UNUSED_PAD src0_sel:DWORD src1_sel:BYTE_0
	v_lshlrev_b32_e32 v3, 1, v2
	v_lshrrev_b32_e32 v4, 2, v2
	v_and_or_b32 v5, v2, s8, v5
	s_lshl_b32 s8, s5, 10
	v_and_b32_e32 v1, 32, v1
	v_bfe_i32 v0, v0, 0, 16
	v_and_b32_e32 v3, 24, v3
	v_and_b32_e32 v4, 4, v4
	s_add_i32 s59, s8, 0
	v_or3_b32 v3, v5, v4, v3
	v_add_lshl_u32 v0, v1, v0, 1
	s_ashr_i32 s15, s14, 8
	s_add_i32 s60, s59, 0x10000
	s_mov_b32 m0, s60
	s_nop 0
	global_load_lds_dwordx4 v166, s[46:47]
	s_add_i32 s61, s59, 0x12000
	s_add_i32 s62, s59, 0x14000
	v_lshl_add_u32 v168, v3, 10, v0
	s_mov_b32 m0, s61
	s_nop 0
	global_load_lds_dwordx4 v168, s[46:47]
	s_add_u32 s10, s46, 0x20000
	s_addc_u32 s11, s47, 0
	s_mov_b32 m0, s62
	s_nop 0
	global_load_lds_dwordx4 v166, s[10:11]
	s_add_i32 s63, s59, 0x16000
	s_mov_b32 m0, s63
	s_nop 0
	global_load_lds_dwordx4 v168, s[10:11]
	s_mov_b32 m0, s59
	s_nop 0
	global_load_lds_dwordx4 v165, s[44:45]
	s_add_i32 s64, s59, 0x2000
	s_add_i32 s65, s59, 0x4000
	v_lshl_add_u32 v167, v2, 10, v0
	s_mov_b32 m0, s64
	s_nop 0
	global_load_lds_dwordx4 v167, s[44:45]
	s_add_u32 s12, s44, 0x20000
	s_addc_u32 s13, s45, 0
	s_mov_b32 m0, s65
	s_nop 0
	global_load_lds_dwordx4 v165, s[12:13]
	s_add_i32 s66, s59, 0x6000
	s_mov_b32 m0, s66
	s_nop 0
	global_load_lds_dwordx4 v167, s[12:13]
	s_cmp_eq_u32 s15, 1
	s_mov_b32 s58, 0
	s_mov_b64 s[8:9], 0x20000
	s_cselect_b64 s[10:11], -1, 0
	s_cmp_lg_u32 s15, 1
	s_cbranch_scc1 .LBB0_735
	s_barrier
.LBB0_735:
	s_add_u32 s12, s2, 0xaf200000
	s_addc_u32 s13, s3, 0
	s_add_u32 s67, s2, 0x102000
	s_addc_u32 s68, s3, 0
	v_and_b32_e32 v0, 48, v164
	v_lshlrev_b32_e32 v1, 6, v164
	s_movk_i32 s3, 0x3c0
	v_and_or_b32 v0, v1, s3, v0
	v_lshlrev_b32_e32 v1, 2, v164
	s_lshl_b32 s2, s15, 13
	v_and_b32_e32 v1, 32, v1
	v_bitop3_b32 v2, v0, s2, v1 bitop3:0xde
	s_lshl_b32 s2, s5, 5
	s_and_b32 s70, s2, 0x60
	s_lshl_b32 s69, s15, 6
	s_lshl_b32 s2, s70, 7
	s_add_i32 s71, s59, 0x18000
	v_bitop3_b32 v0, s2, v0, v1 bitop3:0xf6
	s_add_u32 s2, s46, 0x80
	s_waitcnt vmcnt(2)
	s_barrier
	s_addc_u32 s3, s47, 0
	s_mov_b32 m0, s71
	s_nop 0
	global_load_lds_dwordx4 v166, s[2:3]
	s_add_i32 s72, s59, 0x1a000
	s_add_i32 s73, s59, 0x8000
	s_mov_b32 m0, s72
	s_nop 0
	global_load_lds_dwordx4 v168, s[2:3]
	s_add_u32 s2, s44, 0x80
	s_addc_u32 s3, s45, 0
	s_mov_b32 m0, s73
	s_nop 0
	global_load_lds_dwordx4 v165, s[2:3]
	s_add_i32 s74, s59, 0xa000
	s_add_i32 s75, s59, 0x1c000
	s_mov_b32 m0, s74
	s_nop 0
	global_load_lds_dwordx4 v167, s[2:3]
	s_add_u32 s2, s46, 0x20080
	s_addc_u32 s3, s47, 0
	s_mov_b32 m0, s75
	s_nop 0
	global_load_lds_dwordx4 v166, s[2:3]
	s_add_i32 s76, s59, 0x1e000
	s_add_i32 s77, s59, 0xc000
	s_mov_b32 m0, s76
	s_nop 0
	global_load_lds_dwordx4 v168, s[2:3]
	s_cmpk_lt_u32 s14, 0x100
	s_waitcnt vmcnt(6)
	s_cselect_b64 s[14:15], -1, 0
	s_add_i32 s78, s59, 0xe000
	s_ashr_i32 s79, s52, 31
	s_waitcnt lgkmcnt(0)
	s_cmp_lg_u64 s[6:7], 0
	v_add_u32_e32 v0, 0, v0
	s_cselect_b64 s[16:17], -1, 0
	v_mov_b64_e32 v[152:153], 0x200
	v_mov_b64_e32 v[154:155], 0x1ff
	v_add_u32_e32 v169, 0x10000, v0
	v_add_u32_e32 v170, 0x14000, v0
	v_add_u32_e32 v171, 0, v2
	v_mov_b32_e32 v172, 0x7f7f7f7f
	v_add_u32_e32 v173, 0x18000, v0
	v_add_u32_e32 v174, 0x1c000, v0
	s_mov_b32 s20, 0x3a000000
	s_mov_b64 s[22:23], 0x24000
	s_mov_b64 s[24:25], 0x28000
	s_mov_b64 s[26:27], 0x2c000
	s_mov_b64 s[40:41], s[44:45]
	s_mov_b64 s[42:43], s[46:47]
	s_barrier
	s_branch .LBB0_738

; #define PG8_WAIT_V(n) asm volatile("s_waitcnt vmcnt(" #n ")" ::: "memory")
; #define PG8_WAIT_L(n) asm volatile("s_waitcnt lgkmcnt(" #n ")" ::: "memory")
; #define PG8_BAR __builtin_amdgcn_s_barrier()
; #define PG8_SCHED __builtin_amdgcn_sched_barrier(0)
; #define PG8_STAGE_A(b, h, p) do { if constexpr (GATHER) { if ((h) == 0) PG8_STAGE(PG8_SA(b, h), p, vA0); else PG8_STAGE(PG8_SA(b, h), p, vA1); } else PG8_STAGE(PG8_SA(b, h), (p) + ((h) ? hstepA : (size_t)0), voffA); } while (0)
; #define PG8_GOFF1(un, h, d) do { int tz_ = tid; asm volatile("" : "+v"(tz_)); _Pragma("unroll") for (int i_ = 0; i_ < 2; ++i_) { int R_, C_; stage_rc(tz_ * 16 + i_ * 8192, R_, C_); \
;         d[i_] = S.gather(un, R_ + (h) * HALF) + (unsigned)C_ * 2u; } } while (0)
; template <class Epi, class Sched, bool ALIGN_EPI = true, bool SP2 = true, bool FP8 = false, bool GATHER = false>
; __device__ __forceinline__ void gemm_phase(LAS unsigned char* lds, const Dims g, const Sched& S, const Epi& E, const int wv) {
;     ...
;         for (int t = 0; t < nt; t += 2) {
;             const bool last = (t == nt - 2);
;             const char* a1 = cA + (size_t)(t + 1) * kstep;
;             const char* a2 = last ? nA : cA + (size_t)(t + 2) * kstep; const char* b2 = last ? nB : cB + (size_t)(t + 2) * kstep;
;             const char* a3 = a2 + kstep; const char* b3 = b2 + kstep;
;             if constexpr (SP2) {
;             if constexpr (GATHER) { if (last) PG8_GOFF1(un_, 0, vA0); }
;             PG8_LDB(B0, 0, 0); PG8_LDB(B1, 0, 1); PG8_SCHED; PG8_LDA(At, 0, 0); PG8_STAGE_A(1, 1, a1);
;             if constexpr (GATHER) { if (last) PG8_GOFF1(un_, 1, vA1); }
;             PG8_WAIT_V(8); PG8_WAIT_L(0); PG8_BAR; PG8_MMA(0, 0, At, B0); PG8_MMA(0, 1, At, B1); PG8_BAR; PG8_SCHED;
;             PG8_LDA(At, 0, 1); PG8_STAGE(PG8_SB(0, 0), b2, voffB); PG8_STAGE(PG8_SB(0, 1), b2 + hstepB, voffB); PG8_STAGE_A(0, 0, a2);
;             PG8_WAIT_V(8); PG8_WAIT_L(0); PG8_BAR; PG8_MMA(1, 0, At, B0); PG8_MMA(1, 1, At, B1); PG8_BAR; PG8_SCHED;
.LBB0_745:
	ds_read_b128 v[128:131], v169
	ds_read_b128 v[132:135], v169 offset:1024
	ds_read_b128 v[136:139], v169 offset:2048
	ds_read_b128 v[140:143], v169 offset:3072
	ds_read_b128 v[144:147], v170
	ds_read_b128 v[148:151], v170 offset:1024
	ds_read_b128 v[156:159], v170 offset:2048
	ds_read_b128 v[160:163], v170 offset:3072
	s_cmp_eq_u32 s82, 4
	s_cselect_b32 s50, s40, s39
	s_cselect_b32 s51, s41, s81
	s_cselect_b32 s48, s42, s5
	s_cselect_b32 s49, s43, s37
	s_add_u32 s46, s50, 0x80
	s_addc_u32 s47, s51, 0
	ds_read_b128 v[176:179], v171
	ds_read_b128 v[180:183], v171 offset:1024
	ds_read_b128 v[184:187], v171 offset:2048
	ds_read_b128 v[188:191], v171 offset:3072
	ds_read_b128 v[192:195], v171 offset:4096
	ds_read_b128 v[196:199], v171 offset:5120
	ds_read_b128 v[200:203], v171 offset:6144
	ds_read_b128 v[204:207], v171 offset:7168
	s_mov_b32 m0, s77
	s_nop 0
	global_load_lds_dwordx4 v165, s[44:45]
	s_nop 0
	s_mov_b32 m0, s78
	s_nop 0
	global_load_lds_dwordx4 v167, s[44:45]
	s_waitcnt vmcnt(8)
	s_waitcnt lgkmcnt(0)
	s_barrier
	s_setprio 1
	s_waitcnt lgkmcnt(6)
	v_mfma_scale_f32_16x16x128_f8f6f4 v[124:127], v[128:135], v[176:183], v[124:127], v172, v172 op_sel_hi:[0,0,0]
	v_mfma_scale_f32_16x16x128_f8f6f4 v[120:123], v[136:143], v[176:183], v[120:123], v172, v172 op_sel_hi:[0,0,0]
	s_waitcnt lgkmcnt(4)
	v_mfma_scale_f32_16x16x128_f8f6f4 v[108:111], v[128:135], v[184:191], v[108:111], v172, v172 op_sel_hi:[0,0,0]
	v_mfma_scale_f32_16x16x128_f8f6f4 v[104:107], v[136:143], v[184:191], v[104:107], v172, v172 op_sel_hi:[0,0,0]
	s_waitcnt lgkmcnt(2)
	v_mfma_scale_f32_16x16x128_f8f6f4 v[208:211], v[128:135], v[192:199], v[92:95], v172, v172 op_sel_hi:[0,0,0]
	v_mfma_scale_f32_16x16x128_f8f6f4 v[212:215], v[136:143], v[192:199], v[88:91], v172, v172 op_sel_hi:[0,0,0]
	s_waitcnt lgkmcnt(0)
	v_mfma_scale_f32_16x16x128_f8f6f4 v[216:219], v[128:135], v[200:207], v[76:79], v172, v172 op_sel_hi:[0,0,0]
	v_mfma_scale_f32_16x16x128_f8f6f4 v[220:223], v[136:143], v[200:207], v[72:75], v172, v172 op_sel_hi:[0,0,0]
	s_setprio 0
	s_setprio 1
	v_mfma_scale_f32_16x16x128_f8f6f4 v[116:119], v[144:151], v[176:183], v[116:119], v172, v172 op_sel_hi:[0,0,0]
	v_mfma_scale_f32_16x16x128_f8f6f4 v[112:115], v[156:163], v[176:183], v[112:115], v172, v172 op_sel_hi:[0,0,0]
	v_mfma_scale_f32_16x16x128_f8f6f4 v[100:103], v[144:151], v[184:191], v[100:103], v172, v172 op_sel_hi:[0,0,0]
	v_mfma_scale_f32_16x16x128_f8f6f4 v[96:99], v[156:163], v[184:191], v[96:99], v172, v172 op_sel_hi:[0,0,0]
	v_mfma_scale_f32_16x16x128_f8f6f4 v[176:179], v[144:151], v[192:199], v[84:87], v172, v172 op_sel_hi:[0,0,0]
	v_mfma_scale_f32_16x16x128_f8f6f4 v[180:183], v[156:163], v[192:199], v[80:83], v172, v172 op_sel_hi:[0,0,0]
	v_mfma_scale_f32_16x16x128_f8f6f4 v[184:187], v[144:151], v[200:207], v[68:71], v172, v172 op_sel_hi:[0,0,0]
	v_mfma_scale_f32_16x16x128_f8f6f4 v[188:191], v[156:163], v[200:207], v[64:67], v172, v172 op_sel_hi:[0,0,0]
	s_setprio 0
	s_barrier
	s_nop 4
	ds_read_b128 v[64:67], v171 offset:16384
	ds_read_b128 v[68:71], v171 offset:17408
	ds_read_b128 v[72:75], v171 offset:18432
	ds_read_b128 v[76:79], v171 offset:19456
	ds_read_b128 v[80:83], v171 offset:20480
	ds_read_b128 v[84:87], v171 offset:21504
	ds_read_b128 v[88:91], v171 offset:22528
	ds_read_b128 v[92:95], v171 offset:23552
	s_mov_b32 m0, s60
	s_nop 0
	global_load_lds_dwordx4 v166, s[48:49]
	s_add_u32 s84, s48, 0x20000
	s_mov_b32 m0, s61
	s_nop 0
	global_load_lds_dwordx4 v168, s[48:49]
	s_addc_u32 s85, s49, 0
	s_mov_b32 m0, s62
	s_nop 0
	global_load_lds_dwordx4 v166, s[84:85]
	s_nop 0
	s_mov_b32 m0, s63
	s_nop 0
	global_load_lds_dwordx4 v168, s[84:85]
	s_nop 0
	s_mov_b32 m0, s59
	s_nop 0
	global_load_lds_dwordx4 v165, s[50:51]
	s_nop 0
	s_mov_b32 m0, s64
	s_nop 0
	global_load_lds_dwordx4 v167, s[50:51]
	s_waitcnt vmcnt(8)
	s_waitcnt lgkmcnt(0)
	s_barrier
	s_setprio 1
	s_waitcnt lgkmcnt(6)
	v_mfma_scale_f32_16x16x128_f8f6f4 v[60:63], v[128:135], v[64:71], v[60:63], v172, v172 op_sel_hi:[0,0,0]
	v_mfma_scale_f32_16x16x128_f8f6f4 v[56:59], v[136:143], v[64:71], v[56:59], v172, v172 op_sel_hi:[0,0,0]
	s_waitcnt lgkmcnt(4)
	v_mfma_scale_f32_16x16x128_f8f6f4 v[192:195], v[128:135], v[72:79], v[44:47], v172, v172 op_sel_hi:[0,0,0]
	v_mfma_scale_f32_16x16x128_f8f6f4 v[196:199], v[136:143], v[72:79], v[40:43], v172, v172 op_sel_hi:[0,0,0]
	s_waitcnt lgkmcnt(2)
	v_mfma_scale_f32_16x16x128_f8f6f4 v[200:203], v[128:135], v[80:87], v[28:31], v172, v172 op_sel_hi:[0,0,0]
	v_mfma_scale_f32_16x16x128_f8f6f4 v[204:207], v[136:143], v[80:87], v[24:27], v172, v172 op_sel_hi:[0,0,0]
	s_waitcnt lgkmcnt(0)
	v_mfma_scale_f32_16x16x128_f8f6f4 v[224:227], v[128:135], v[88:95], v[12:15], v172, v172 op_sel_hi:[0,0,0]
	v_mfma_scale_f32_16x16x128_f8f6f4 v[228:231], v[136:143], v[88:95], v[8:11], v172, v172 op_sel_hi:[0,0,0]
	s_setprio 0
	s_setprio 1
	v_mfma_scale_f32_16x16x128_f8f6f4 v[52:55], v[144:151], v[64:71], v[52:55], v172, v172 op_sel_hi:[0,0,0]
	v_mfma_scale_f32_16x16x128_f8f6f4 v[48:51], v[156:163], v[64:71], v[48:51], v172, v172 op_sel_hi:[0,0,0]
	v_mfma_scale_f32_16x16x128_f8f6f4 v[232:235], v[144:151], v[72:79], v[36:39], v172, v172 op_sel_hi:[0,0,0]
	v_mfma_scale_f32_16x16x128_f8f6f4 v[236:239], v[156:163], v[72:79], v[32:35], v172, v172 op_sel_hi:[0,0,0]
	v_mfma_scale_f32_16x16x128_f8f6f4 v[240:243], v[144:151], v[80:87], v[20:23], v172, v172 op_sel_hi:[0,0,0]
	v_mfma_scale_f32_16x16x128_f8f6f4 v[244:247], v[156:163], v[80:87], v[16:19], v172, v172 op_sel_hi:[0,0,0]
	v_mfma_scale_f32_16x16x128_f8f6f4 v[248:251], v[144:151], v[88:95], v[4:7], v172, v172 op_sel_hi:[0,0,0]
	v_mfma_scale_f32_16x16x128_f8f6f4 v[252:255], v[156:163], v[88:95], v[0:3], v172, v172 op_sel_hi:[0,0,0]
	s_setprio 0
	s_barrier
; #define PG8_WAIT_V(n) asm volatile("s_waitcnt vmcnt(" #n ")" ::: "memory")
; #define PG8_WAIT_L(n) asm volatile("s_waitcnt lgkmcnt(" #n ")" ::: "memory")
; #define PG8_BAR __builtin_amdgcn_s_barrier()
; #define PG8_SCHED __builtin_amdgcn_sched_barrier(0)
; #define PG8_STAGE_A(b, h, p) do { if constexpr (GATHER) { if ((h) == 0) PG8_STAGE(PG8_SA(b, h), p, vA0); else PG8_STAGE(PG8_SA(b, h), p, vA1); } else PG8_STAGE(PG8_SA(b, h), (p) + ((h) ? hstepA : (size_t)0), voffA); } while (0)
; template <class Epi, class Sched, bool ALIGN_EPI = true, bool SP2 = true, bool FP8 = false, bool GATHER = false>
; __device__ __forceinline__ void gemm_phase(LAS unsigned char* lds, const Dims g, const Sched& S, const Epi& E, const int wv) {
;     ...
;         for (int t = 0; t < nt; t += 2) {
;             const bool last = (t == nt - 2);
;             const char* a1 = cA + (size_t)(t + 1) * kstep;
;             const char* a2 = last ? nA : cA + (size_t)(t + 2) * kstep; const char* b2 = last ? nB : cB + (size_t)(t + 2) * kstep;
;             const char* a3 = a2 + kstep; const char* b3 = b2 + kstep;
;             if constexpr (SP2) {
;             if constexpr (GATHER) { if (last) PG8_GOFF1(un_, 0, vA0); }
;             PG8_LDB(B0, 0, 0); PG8_LDB(B1, 0, 1); PG8_SCHED; PG8_LDA(At, 0, 0); PG8_STAGE_A(1, 1, a1);
;             if constexpr (GATHER) { if (last) PG8_GOFF1(un_, 1, vA1); }
;             PG8_WAIT_V(8); PG8_WAIT_L(0); PG8_BAR; PG8_MMA(0, 0, At, B0); PG8_MMA(0, 1, At, B1); PG8_BAR; PG8_SCHED;
;             PG8_LDA(At, 0, 1); PG8_STAGE(PG8_SB(0, 0), b2, voffB); PG8_STAGE(PG8_SB(0, 1), b2 + hstepB, voffB); PG8_STAGE_A(0, 0, a2);
;             PG8_WAIT_V(8); PG8_WAIT_L(0); PG8_BAR; PG8_MMA(1, 0, At, B0); PG8_MMA(1, 1, At, B1); PG8_BAR; PG8_SCHED;
;             PG8_LDB(B0, 1, 0); PG8_LDB(B1, 1, 1); PG8_SCHED; PG8_LDA(At, 1, 0); PG8_STAGE_A(0, 1, a2);
;             PG8_WAIT_V(8); PG8_WAIT_L(0); PG8_BAR; PG8_MMA(0, 0, At, B0); PG8_MMA(0, 1, At, B1); PG8_BAR; PG8_SCHED;
;             PG8_LDA(At, 1, 1); PG8_STAGE(PG8_SB(1, 0), b3, voffB); PG8_STAGE(PG8_SB(1, 1), b3 + hstepB, voffB); PG8_STAGE_A(1, 0, a3);
;             PG8_WAIT_V(8); PG8_WAIT_L(0); PG8_BAR; PG8_MMA(1, 0, At, B0); PG8_MMA(1, 1, At, B1); PG8_BAR; PG8_SCHED;
;     ...
;         if constexpr (ALIGN_EPI) { if (wr == 0) PG8_BAR; }
	s_nop 4
	ds_read_b128 v[0:3], v173
	ds_read_b128 v[4:7], v173 offset:1024
	ds_read_b128 v[16:19], v173 offset:2048
	ds_read_b128 v[20:23], v173 offset:3072
	ds_read_b128 v[128:131], v174
	ds_read_b128 v[132:135], v174 offset:1024
	ds_read_b128 v[136:139], v174 offset:2048
	ds_read_b128 v[140:143], v174 offset:3072
	ds_read_b128 v[8:11], v171 offset:32768
	ds_read_b128 v[12:15], v171 offset:33792
	ds_read_b128 v[24:27], v171 offset:34816
	ds_read_b128 v[28:31], v171 offset:35840
	ds_read_b128 v[32:35], v171 offset:36864
	ds_read_b128 v[36:39], v171 offset:37888
	ds_read_b128 v[40:43], v171 offset:38912
	ds_read_b128 v[44:47], v171 offset:39936
	s_add_u32 s50, s50, 0x20000
	s_addc_u32 s51, s51, 0
	s_mov_b32 m0, s65
	s_nop 0
	global_load_lds_dwordx4 v165, s[50:51]
	s_nop 0
	s_mov_b32 m0, s66
	s_nop 0
	global_load_lds_dwordx4 v167, s[50:51]
	s_waitcnt vmcnt(8)
	s_waitcnt lgkmcnt(0)
	s_barrier
	s_setprio 1
	s_waitcnt lgkmcnt(6)
	v_mfma_scale_f32_16x16x128_f8f6f4 v[124:127], v[0:7], v[8:15], v[124:127], v172, v172 op_sel_hi:[0,0,0]
	v_mfma_scale_f32_16x16x128_f8f6f4 v[120:123], v[16:23], v[8:15], v[120:123], v172, v172 op_sel_hi:[0,0,0]
	s_waitcnt lgkmcnt(4)
	v_mfma_scale_f32_16x16x128_f8f6f4 v[108:111], v[0:7], v[24:31], v[108:111], v172, v172 op_sel_hi:[0,0,0]
	v_mfma_scale_f32_16x16x128_f8f6f4 v[104:107], v[16:23], v[24:31], v[104:107], v172, v172 op_sel_hi:[0,0,0]
	s_waitcnt lgkmcnt(2)
	v_mfma_scale_f32_16x16x128_f8f6f4 v[92:95], v[0:7], v[32:39], v[208:211], v172, v172 op_sel_hi:[0,0,0]
	v_mfma_scale_f32_16x16x128_f8f6f4 v[88:91], v[16:23], v[32:39], v[212:215], v172, v172 op_sel_hi:[0,0,0]
	s_waitcnt lgkmcnt(0)
	v_mfma_scale_f32_16x16x128_f8f6f4 v[76:79], v[0:7], v[40:47], v[216:219], v172, v172 op_sel_hi:[0,0,0]
	v_mfma_scale_f32_16x16x128_f8f6f4 v[72:75], v[16:23], v[40:47], v[220:223], v172, v172 op_sel_hi:[0,0,0]
	s_setprio 0
	s_setprio 1
	v_mfma_scale_f32_16x16x128_f8f6f4 v[116:119], v[128:135], v[8:15], v[116:119], v172, v172 op_sel_hi:[0,0,0]
	v_mfma_scale_f32_16x16x128_f8f6f4 v[112:115], v[136:143], v[8:15], v[112:115], v172, v172 op_sel_hi:[0,0,0]
	v_mfma_scale_f32_16x16x128_f8f6f4 v[100:103], v[128:135], v[24:31], v[100:103], v172, v172 op_sel_hi:[0,0,0]
	v_mfma_scale_f32_16x16x128_f8f6f4 v[96:99], v[136:143], v[24:31], v[96:99], v172, v172 op_sel_hi:[0,0,0]
	v_mfma_scale_f32_16x16x128_f8f6f4 v[84:87], v[128:135], v[32:39], v[176:179], v172, v172 op_sel_hi:[0,0,0]
	v_mfma_scale_f32_16x16x128_f8f6f4 v[80:83], v[136:143], v[32:39], v[180:183], v172, v172 op_sel_hi:[0,0,0]
	v_mfma_scale_f32_16x16x128_f8f6f4 v[68:71], v[128:135], v[40:47], v[184:187], v172, v172 op_sel_hi:[0,0,0]
	v_mfma_scale_f32_16x16x128_f8f6f4 v[64:67], v[136:143], v[40:47], v[188:191], v172, v172 op_sel_hi:[0,0,0]
	s_setprio 0
	s_barrier
	ds_read_b128 v[32:35], v171 offset:49152
	ds_read_b128 v[36:39], v171 offset:50176
	ds_read_b128 v[144:147], v171 offset:51200
	ds_read_b128 v[148:151], v171 offset:52224
	ds_read_b128 v[156:159], v171 offset:53248
	ds_read_b128 v[160:163], v171 offset:54272
	ds_read_b128 v[176:179], v171 offset:55296
	ds_read_b128 v[180:183], v171 offset:56320
	s_add_u32 s50, s48, 0x80
	s_addc_u32 s51, s49, 0
	s_mov_b32 m0, s71
	s_nop 0
	global_load_lds_dwordx4 v166, s[50:51]
	s_add_u32 s48, s48, 0x20080
	s_mov_b32 m0, s72
	s_nop 0
	global_load_lds_dwordx4 v168, s[50:51]
	s_addc_u32 s49, s49, 0
	s_mov_b32 m0, s75
	s_nop 0
	global_load_lds_dwordx4 v166, s[48:49]
	s_nop 0
	s_mov_b32 m0, s76
	s_nop 0
	global_load_lds_dwordx4 v168, s[48:49]
	s_mov_b32 m0, s73
	s_nop 0
	global_load_lds_dwordx4 v165, s[46:47]
	s_nop 0
	s_mov_b32 m0, s74
	s_nop 0
	global_load_lds_dwordx4 v167, s[46:47]
	s_waitcnt vmcnt(8)
	s_waitcnt lgkmcnt(0)
	s_barrier
	s_setprio 1
	s_waitcnt lgkmcnt(6)
	v_mfma_scale_f32_16x16x128_f8f6f4 v[60:63], v[0:7], v[32:39], v[60:63], v172, v172 op_sel_hi:[0,0,0]
	v_mfma_scale_f32_16x16x128_f8f6f4 v[56:59], v[16:23], v[32:39], v[56:59], v172, v172 op_sel_hi:[0,0,0]
	s_waitcnt lgkmcnt(4)
	v_mfma_scale_f32_16x16x128_f8f6f4 v[44:47], v[0:7], v[144:151], v[192:195], v172, v172 op_sel_hi:[0,0,0]
	v_mfma_scale_f32_16x16x128_f8f6f4 v[40:43], v[16:23], v[144:151], v[196:199], v172, v172 op_sel_hi:[0,0,0]
	s_waitcnt lgkmcnt(2)
	v_mfma_scale_f32_16x16x128_f8f6f4 v[28:31], v[0:7], v[156:163], v[200:203], v172, v172 op_sel_hi:[0,0,0]
	v_mfma_scale_f32_16x16x128_f8f6f4 v[24:27], v[16:23], v[156:163], v[204:207], v172, v172 op_sel_hi:[0,0,0]
	s_waitcnt lgkmcnt(0)
	v_mfma_scale_f32_16x16x128_f8f6f4 v[12:15], v[0:7], v[176:183], v[224:227], v172, v172 op_sel_hi:[0,0,0]
	v_mfma_scale_f32_16x16x128_f8f6f4 v[8:11], v[16:23], v[176:183], v[228:231], v172, v172 op_sel_hi:[0,0,0]
	s_setprio 0
	s_setprio 1
	v_mfma_scale_f32_16x16x128_f8f6f4 v[52:55], v[128:135], v[32:39], v[52:55], v172, v172 op_sel_hi:[0,0,0]
	v_mfma_scale_f32_16x16x128_f8f6f4 v[48:51], v[136:143], v[32:39], v[48:51], v172, v172 op_sel_hi:[0,0,0]
	v_mfma_scale_f32_16x16x128_f8f6f4 v[36:39], v[128:135], v[144:151], v[232:235], v172, v172 op_sel_hi:[0,0,0]
	v_mfma_scale_f32_16x16x128_f8f6f4 v[32:35], v[136:143], v[144:151], v[236:239], v172, v172 op_sel_hi:[0,0,0]
	v_mfma_scale_f32_16x16x128_f8f6f4 v[20:23], v[128:135], v[156:163], v[240:243], v172, v172 op_sel_hi:[0,0,0]
	v_mfma_scale_f32_16x16x128_f8f6f4 v[16:19], v[136:143], v[156:163], v[244:247], v172, v172 op_sel_hi:[0,0,0]
	v_mfma_scale_f32_16x16x128_f8f6f4 v[4:7], v[128:135], v[176:183], v[248:251], v172, v172 op_sel_hi:[0,0,0]
	v_mfma_scale_f32_16x16x128_f8f6f4 v[0:3], v[136:143], v[176:183], v[252:255], v172, v172 op_sel_hi:[0,0,0]
	s_setprio 0
	s_barrier
	s_add_i32 s82, s82, 2
	s_add_u32 s5, s5, 0x100
	s_addc_u32 s37, s37, 0
	s_add_u32 s39, s39, 0x100
	s_addc_u32 s81, s81, 0
	s_add_u32 s44, s44, 0x100
	s_addc_u32 s45, s45, 0
	s_cmp_gt_u32 s82, 5
	s_cbranch_scc0 .LBB0_745
	s_and_b64 vcc, exec, s[14:15]
	s_cbranch_vccz .LBB0_748
	s_barrier

; #define PG8_WAIT_V(n) asm volatile("s_waitcnt vmcnt(" #n ")" ::: "memory")
; #define PG8_BAR __builtin_amdgcn_s_barrier()
; #define PG8_STAGE_A(b, h, p) do { if constexpr (GATHER) { if ((h) == 0) PG8_STAGE(PG8_SA(b, h), p, vA0); else PG8_STAGE(PG8_SA(b, h), p, vA1); } else PG8_STAGE(PG8_SA(b, h), (p) + ((h) ? hstepA : (size_t)0), voffA); } while (0)
; #define PG8_GOFF(un, d0, d1) do { PG8_GOFF1(un, 0, d0); PG8_GOFF1(un, 1, d1); } while (0)
; template <class Epi, class Sched, bool ALIGN_EPI = true, bool SP2 = true, bool FP8 = false, bool GATHER = false>
; __device__ __forceinline__ void gemm_phase(LAS unsigned char* lds, const Dims g, const Sched& S, const Epi& E, const int wv) {
;     ...
;     unsigned vA0[2], vA1[2];
;     Unit cur, nxt; int ui = 0;
;     if (!S.next(0, cur)) return;
;     if constexpr (GATHER) PG8_GOFF(0, vA0, vA1);
;     ...
;     if constexpr (SP2) {
;         PG8_STAGE(PG8_SB(0, 0), cB, voffB); PG8_STAGE(PG8_SB(0, 1), cB + hstepB, voffB); PG8_STAGE_A(0, 0, cA); PG8_STAGE_A(0, 1, cA);
;         if (wr == 1) PG8_BAR;
;         PG8_WAIT_V(2); PG8_BAR;
;         PG8_STAGE(PG8_SB(1, 0), cB + kstep, voffB); PG8_STAGE_A(1, 0, cA + kstep); PG8_STAGE(PG8_SB(1, 1), cB + hstepB + kstep, voffB);
;         PG8_WAIT_V(6); PG8_BAR;
.LBB0_1415:
	v_lshlrev_b32_e32 v1, 6, v3
	v_sub_u32_e32 v1, v2, v1
	v_mov_b32_e32 v193, 1
	v_and_b32_e32 v0, 32, v4
	v_ashrrev_i16_sdwa v1, v193, sext(v1) dst_sel:DWORD dst_unused:UNUSED_PAD src0_sel:DWORD src1_sel:BYTE_0
	v_add_u32_sdwa v0, v0, sext(v1) dst_sel:DWORD dst_unused:UNUSED_PAD src0_sel:DWORD src1_sel:WORD_0
	v_lshlrev_b32_e32 v1, 6, v6
	v_sub_u32_e32 v1, v5, v1
	s_waitcnt lgkmcnt(0)
	v_lshl_add_u32 v194, v0, 1, v9
	v_and_b32_e32 v0, 32, v8
	v_ashrrev_i16_sdwa v1, v193, sext(v1) dst_sel:DWORD dst_unused:UNUSED_PAD src0_sel:DWORD src1_sel:BYTE_0
	v_add_u32_sdwa v0, v0, sext(v1) dst_sel:DWORD dst_unused:UNUSED_PAD src0_sel:DWORD src1_sel:WORD_0
	v_lshlrev_b32_e32 v1, 6, v11
	v_sub_u32_e32 v1, v10, v1
	v_lshl_add_u32 v196, v0, 1, v7
	v_and_b32_e32 v0, 32, v12
	v_ashrrev_i16_sdwa v1, v193, sext(v1) dst_sel:DWORD dst_unused:UNUSED_PAD src0_sel:DWORD src1_sel:BYTE_0
	v_add_u32_sdwa v0, v0, sext(v1) dst_sel:DWORD dst_unused:UNUSED_PAD src0_sel:DWORD src1_sel:WORD_0
	v_lshlrev_b32_e32 v1, 6, v14
	v_sub_u32_e32 v1, v13, v1
	v_lshl_add_u32 v197, v0, 1, v17
	v_and_b32_e32 v0, 32, v16
	v_ashrrev_i16_sdwa v1, v193, sext(v1) dst_sel:DWORD dst_unused:UNUSED_PAD src0_sel:DWORD src1_sel:BYTE_0
	v_add_u32_sdwa v0, v0, sext(v1) dst_sel:DWORD dst_unused:UNUSED_PAD src0_sel:DWORD src1_sel:WORD_0
	v_bfe_i32 v2, v192, 27, 1
	v_lshl_add_u32 v198, v0, 1, v15
	v_lshlrev_b32_e32 v0, 4, v192
	v_lshrrev_b32_e32 v2, 22, v2
	v_add_u32_e32 v2, v0, v2
	v_and_b32_e32 v2, 0xfffffc00, v2
	v_sub_u32_e32 v2, v0, v2
	v_ashrrev_i32_e32 v1, 31, v192
	v_lshrrev_b32_e32 v3, 4, v2
	v_lshrrev_b32_e32 v1, 26, v1
	v_bitop3_b32 v2, v3, v2, 32 bitop3:0x6c
	v_add_u32_e32 v1, v192, v1
	v_ashrrev_i32_e32 v4, 31, v2
	v_ashrrev_i32_e32 v1, 6, v1
	v_lshrrev_b32_e32 v4, 26, v4
	v_lshlrev_b32_e32 v3, 3, v1
	v_add_u32_e32 v4, v2, v4
	v_and_b32_e32 v3, -16, v3
	v_ashrrev_i32_e32 v5, 6, v4
	v_and_b32_e32 v4, 0xc0, v4
	v_add_u32_e32 v3, v5, v3
	v_sub_u32_e32 v2, v2, v4
	v_lshlrev_b32_e32 v1, 5, v1
	v_ashrrev_i16_sdwa v2, v193, sext(v2) dst_sel:DWORD dst_unused:UNUSED_PAD src0_sel:DWORD src1_sel:BYTE_0
	v_lshlrev_b32_e32 v4, 1, v3
	v_lshrrev_b32_e32 v6, 2, v3
	v_and_b32_e32 v5, 3, v5
	s_mov_b32 s14, 0x3fffe0
	v_and_b32_e32 v1, 32, v1
	v_bfe_i32 v2, v2, 0, 16
	v_and_b32_e32 v4, 24, v4
	v_and_b32_e32 v6, 4, v6
	v_and_or_b32 v3, v3, s14, v5
	v_or3_b32 v3, v3, v6, v4
	v_add_lshl_u32 v1, v1, v2, 1
	v_add_u32_e32 v0, 0x2000, v0
	v_lshl_add_u32 v195, v3, 10, v1
	v_ashrrev_i32_e32 v1, 31, v0
	v_lshrrev_b32_e32 v1, 22, v1
	v_add_u32_e32 v1, v0, v1
	v_ashrrev_i32_e32 v1, 10, v1
	v_mul_i32_i24_e32 v2, 0x400, v1
	v_sub_u32_e32 v0, v0, v2
	v_lshrrev_b32_e32 v2, 4, v0
	v_bitop3_b32 v0, v2, v0, 32 bitop3:0x6c
	v_ashrrev_i32_e32 v3, 31, v0
	v_lshrrev_b32_e32 v3, 26, v3
	v_lshlrev_b32_e32 v2, 3, v1
	v_add_u32_e32 v3, v0, v3
	v_and_b32_e32 v2, -16, v2
	v_ashrrev_i32_e32 v4, 6, v3
	v_and_b32_e32 v3, 0xc0, v3
	v_add_u32_e32 v2, v4, v2
	v_sub_u32_e32 v0, v0, v3
	v_and_b32_e32 v4, 3, v4
	s_ashr_i32 s17, s23, 6
	v_lshlrev_b32_e32 v1, 5, v1
	v_ashrrev_i16_sdwa v0, v193, sext(v0) dst_sel:DWORD dst_unused:UNUSED_PAD src0_sel:DWORD src1_sel:BYTE_0
	v_lshlrev_b32_e32 v3, 1, v2
	v_lshrrev_b32_e32 v5, 2, v2
	v_and_or_b32 v2, v2, s14, v4
	s_lshl_b32 s14, s17, 10
	v_and_b32_e32 v1, 32, v1
	v_bfe_i32 v0, v0, 0, 16
	v_and_b32_e32 v3, 24, v3
	v_and_b32_e32 v5, 4, v5
	s_add_i32 s37, s14, 0
	v_or3_b32 v2, v2, v5, v3
	v_add_lshl_u32 v0, v1, v0, 1
	s_add_i32 s56, s37, 0x10000
	s_mov_b32 m0, s56
	s_nop 0
	global_load_lds_dwordx4 v195, s[42:43]
	s_ashr_i32 s16, s23, 8
	v_lshl_add_u32 v199, v2, 10, v0
	s_add_i32 s57, s37, 0x12000
	s_mov_b32 m0, s57
	s_nop 0
	global_load_lds_dwordx4 v199, s[42:43]
	s_add_i32 s58, s37, 0x14000
	s_add_u32 s14, s42, 0x20000
	s_addc_u32 s15, s43, 0
	s_mov_b32 m0, s58
	s_nop 0
	global_load_lds_dwordx4 v195, s[14:15]
	s_add_i32 s59, s37, 0x16000
	s_mov_b32 m0, s59
	s_nop 0
	global_load_lds_dwordx4 v199, s[14:15]
	s_mov_b32 m0, s37
	s_nop 0
	global_load_lds_dwordx4 v194, s[40:41]
	s_add_i32 s60, s37, 0x2000
	s_mov_b32 m0, s60
	s_nop 0
	global_load_lds_dwordx4 v196, s[40:41]
	s_add_i32 s61, s37, 0x4000
	s_mov_b32 m0, s61
	s_nop 0
	global_load_lds_dwordx4 v197, s[40:41]
	s_add_i32 s62, s37, 0x6000
	s_mov_b32 m0, s62
	s_nop 0
	global_load_lds_dwordx4 v198, s[40:41]
	s_cmp_eq_u32 s16, 1
	s_mov_b32 s81, 0
	s_cselect_b64 s[14:15], -1, 0
	s_cmp_lg_u32 s16, 1
	s_cbranch_scc1 .LBB0_1417
	s_barrier
.LBB0_1417:
	v_and_b32_e32 v0, 48, v192
	v_lshlrev_b32_e32 v1, 6, v192
	s_movk_i32 s20, 0x3c0
	s_add_u32 s12, s12, 0x8d200000
	v_and_or_b32 v0, v1, s20, v0
	v_lshlrev_b32_e32 v1, 2, v192
	s_addc_u32 s13, s13, 0
	s_lshl_b32 s63, s16, 6
	s_lshl_b32 s16, s16, 13
	v_and_b32_e32 v1, 32, v1
	v_bitop3_b32 v2, v0, s16, v1 bitop3:0xde
	s_lshl_b32 s16, s17, 5
	s_and_b32 s64, s16, 0x60
	s_lshl_b32 s16, s64, 7
	s_add_i32 s65, s37, 0x18000
	v_bitop3_b32 v0, s16, v0, v1 bitop3:0xf6
	s_add_u32 s16, s42, 0x80
	s_waitcnt vmcnt(2)
	s_barrier
	s_addc_u32 s17, s43, 0
	s_mov_b32 m0, s65
	s_nop 0
	global_load_lds_dwordx4 v195, s[16:17]
	s_add_i32 s66, s37, 0x1a000
	s_add_i32 s67, s37, 0x8000
	s_mov_b32 m0, s66
	s_nop 0
	global_load_lds_dwordx4 v199, s[16:17]
	s_add_u32 s16, s40, 0x80
	s_addc_u32 s17, s41, 0
	s_mov_b32 m0, s67
	s_nop 0
	global_load_lds_dwordx4 v194, s[16:17]
	s_add_i32 s68, s37, 0xa000
	s_add_i32 s69, s37, 0x1c000
	s_mov_b32 m0, s68
	s_nop 0
	global_load_lds_dwordx4 v196, s[16:17]
	s_add_u32 s16, s42, 0x20080
	s_addc_u32 s17, s43, 0
	s_mov_b32 m0, s69
	s_nop 0
	global_load_lds_dwordx4 v195, s[16:17]
	s_add_i32 s70, s37, 0x1e000
	s_mov_b32 m0, s70
	s_nop 0
	global_load_lds_dwordx4 v199, s[16:17]
	s_waitcnt vmcnt(6)
	s_add_i32 s71, s37, 0xc000
	s_cmpk_lt_u32 s23, 0x100
	s_cselect_b64 s[16:17], -1, 0
	s_add_i32 s72, s37, 0xe000
	v_mov_b32_e32 v200, 0x7f7f7f7f
	s_mov_b64 s[20:21], 0x1000
	s_movk_i32 s73, 0x1000
	s_mov_b32 s74, 0xc0e00000
	v_add_u32_e32 v201, 0, v0
	v_add_u32_e32 v202, 0, v2
	v_mov_b32_e32 v203, 0x40e00000
	s_barrier
	s_branch .LBB0_1420

; #define PG8_WAIT_V(n) asm volatile("s_waitcnt vmcnt(" #n ")" ::: "memory")
; #define PG8_WAIT_L(n) asm volatile("s_waitcnt lgkmcnt(" #n ")" ::: "memory")
; #define PG8_BAR __builtin_amdgcn_s_barrier()
; #define PG8_SCHED __builtin_amdgcn_sched_barrier(0)
; #define PG8_STAGE_A(b, h, p) do { if constexpr (GATHER) { if ((h) == 0) PG8_STAGE(PG8_SA(b, h), p, vA0); else PG8_STAGE(PG8_SA(b, h), p, vA1); } else PG8_STAGE(PG8_SA(b, h), (p) + ((h) ? hstepA : (size_t)0), voffA); } while (0)
; template <class Epi, class Sched, bool ALIGN_EPI = true, bool SP2 = true, bool FP8 = false, bool GATHER = false>
; __device__ __forceinline__ void gemm_phase(LAS unsigned char* lds, const Dims g, const Sched& S, const Epi& E, const int wv) {
;     ...
;             PG8_WAIT_V(8); PG8_WAIT_L(0); PG8_BAR; PG8_MMA(0, 0, At, B0); PG8_MMA(0, 1, At, B1); PG8_BAR; PG8_SCHED;
;             PG8_LDA(At, 0, 1); PG8_STAGE(PG8_SB(0, 0), b2, voffB); PG8_STAGE(PG8_SB(0, 1), b2 + hstepB, voffB); PG8_STAGE_A(0, 0, a2);
;             PG8_WAIT_V(8); PG8_WAIT_L(0); PG8_BAR; PG8_MMA(1, 0, At, B0); PG8_MMA(1, 1, At, B1); PG8_BAR; PG8_SCHED;
.LBB0_1426:
	s_add_u32 s40, s40, 0x100
	s_addc_u32 s41, s41, 0
	s_and_b64 s[42:43], s[42:43], exec
	s_cselect_b32 s48, s78, s40
	s_waitcnt vmcnt(8)
	s_cselect_b32 s49, s39, s41
	s_cselect_b32 s45, s79, s83
	s_cselect_b32 s44, s80, s82
	s_add_u32 s42, s48, 0x80
	s_waitcnt lgkmcnt(0)
	s_addc_u32 s43, s49, 0
	s_add_u32 s46, s44, 0x80
	s_addc_u32 s47, s45, 0
	s_barrier
	s_setprio 1
	s_waitcnt lgkmcnt(6)
	v_mfma_scale_f32_16x16x128_f8f6f4 v[188:191], v[16:23], v[56:63], v[188:191], v200, v200 op_sel_hi:[0,0,0]
	v_mfma_scale_f32_16x16x128_f8f6f4 v[184:187], v[24:31], v[56:63], v[184:187], v200, v200 op_sel_hi:[0,0,0]
	s_waitcnt lgkmcnt(4)
	v_mfma_scale_f32_16x16x128_f8f6f4 v[172:175], v[16:23], v[48:55], v[172:175], v200, v200 op_sel_hi:[0,0,0]
	v_mfma_scale_f32_16x16x128_f8f6f4 v[168:171], v[24:31], v[48:55], v[168:171], v200, v200 op_sel_hi:[0,0,0]
	s_waitcnt lgkmcnt(2)
	v_mfma_scale_f32_16x16x128_f8f6f4 v[156:159], v[16:23], v[40:47], v[156:159], v200, v200 op_sel_hi:[0,0,0]
	v_mfma_scale_f32_16x16x128_f8f6f4 v[152:155], v[24:31], v[40:47], v[152:155], v200, v200 op_sel_hi:[0,0,0]
	s_waitcnt lgkmcnt(0)
	v_mfma_scale_f32_16x16x128_f8f6f4 v[140:143], v[16:23], v[32:39], v[140:143], v200, v200 op_sel_hi:[0,0,0]
	v_mfma_scale_f32_16x16x128_f8f6f4 v[136:139], v[24:31], v[32:39], v[136:139], v200, v200 op_sel_hi:[0,0,0]
	s_setprio 0
	s_setprio 1
	v_mfma_scale_f32_16x16x128_f8f6f4 v[180:183], v[0:7], v[56:63], v[180:183], v200, v200 op_sel_hi:[0,0,0]
	v_mfma_scale_f32_16x16x128_f8f6f4 v[176:179], v[8:15], v[56:63], v[176:179], v200, v200 op_sel_hi:[0,0,0]
	v_mfma_scale_f32_16x16x128_f8f6f4 v[164:167], v[0:7], v[48:55], v[164:167], v200, v200 op_sel_hi:[0,0,0]
	v_mfma_scale_f32_16x16x128_f8f6f4 v[160:163], v[8:15], v[48:55], v[160:163], v200, v200 op_sel_hi:[0,0,0]
	v_mfma_scale_f32_16x16x128_f8f6f4 v[148:151], v[0:7], v[40:47], v[148:151], v200, v200 op_sel_hi:[0,0,0]
	v_mfma_scale_f32_16x16x128_f8f6f4 v[144:147], v[8:15], v[40:47], v[144:147], v200, v200 op_sel_hi:[0,0,0]
	v_mfma_scale_f32_16x16x128_f8f6f4 v[132:135], v[0:7], v[32:39], v[132:135], v200, v200 op_sel_hi:[0,0,0]
	v_mfma_scale_f32_16x16x128_f8f6f4 v[128:131], v[8:15], v[32:39], v[128:131], v200, v200 op_sel_hi:[0,0,0]
	s_setprio 0
	s_barrier
	ds_read_b128 v[32:35], v202 offset:16384
	ds_read_b128 v[36:39], v202 offset:17408
	ds_read_b128 v[40:43], v202 offset:18432
	ds_read_b128 v[44:47], v202 offset:19456
	ds_read_b128 v[48:51], v202 offset:20480
	ds_read_b128 v[52:55], v202 offset:21504
	ds_read_b128 v[56:59], v202 offset:22528
	ds_read_b128 v[60:63], v202 offset:23552
	s_mov_b32 m0, s56
	s_nop 0
	global_load_lds_dwordx4 v195, s[44:45]
	s_add_u32 s86, s44, 0x20000
	s_mov_b32 m0, s57
	s_nop 0
	global_load_lds_dwordx4 v199, s[44:45]
	s_addc_u32 s87, s45, 0
	s_mov_b32 m0, s58
	s_nop 0
	global_load_lds_dwordx4 v195, s[86:87]
	s_nop 0
	s_mov_b32 m0, s59
	s_nop 0
	global_load_lds_dwordx4 v199, s[86:87]
	s_nop 0
	s_mov_b32 m0, s37
	s_nop 0
	global_load_lds_dwordx4 v194, s[48:49]
	s_nop 0
	s_mov_b32 m0, s60
	s_nop 0
	global_load_lds_dwordx4 v196, s[48:49]
	s_waitcnt vmcnt(8)
	s_waitcnt lgkmcnt(0)
	s_barrier
	s_setprio 1
	s_waitcnt lgkmcnt(6)
	v_mfma_scale_f32_16x16x128_f8f6f4 v[124:127], v[16:23], v[32:39], v[124:127], v200, v200 op_sel_hi:[0,0,0]
	v_mfma_scale_f32_16x16x128_f8f6f4 v[120:123], v[24:31], v[32:39], v[120:123], v200, v200 op_sel_hi:[0,0,0]
	s_waitcnt lgkmcnt(4)
	v_mfma_scale_f32_16x16x128_f8f6f4 v[108:111], v[16:23], v[40:47], v[108:111], v200, v200 op_sel_hi:[0,0,0]
	v_mfma_scale_f32_16x16x128_f8f6f4 v[104:107], v[24:31], v[40:47], v[104:107], v200, v200 op_sel_hi:[0,0,0]
	s_waitcnt lgkmcnt(2)
	v_mfma_scale_f32_16x16x128_f8f6f4 v[92:95], v[16:23], v[48:55], v[92:95], v200, v200 op_sel_hi:[0,0,0]
	v_mfma_scale_f32_16x16x128_f8f6f4 v[88:91], v[24:31], v[48:55], v[88:91], v200, v200 op_sel_hi:[0,0,0]
	s_waitcnt lgkmcnt(0)
	v_mfma_scale_f32_16x16x128_f8f6f4 v[76:79], v[16:23], v[56:63], v[76:79], v200, v200 op_sel_hi:[0,0,0]
	v_mfma_scale_f32_16x16x128_f8f6f4 v[72:75], v[24:31], v[56:63], v[72:75], v200, v200 op_sel_hi:[0,0,0]
	s_setprio 0
	s_setprio 1
	v_mfma_scale_f32_16x16x128_f8f6f4 v[116:119], v[0:7], v[32:39], v[116:119], v200, v200 op_sel_hi:[0,0,0]
	v_mfma_scale_f32_16x16x128_f8f6f4 v[112:115], v[8:15], v[32:39], v[112:115], v200, v200 op_sel_hi:[0,0,0]
	v_mfma_scale_f32_16x16x128_f8f6f4 v[100:103], v[0:7], v[40:47], v[100:103], v200, v200 op_sel_hi:[0,0,0]
	v_mfma_scale_f32_16x16x128_f8f6f4 v[96:99], v[8:15], v[40:47], v[96:99], v200, v200 op_sel_hi:[0,0,0]
	v_mfma_scale_f32_16x16x128_f8f6f4 v[84:87], v[0:7], v[48:55], v[84:87], v200, v200 op_sel_hi:[0,0,0]
	v_mfma_scale_f32_16x16x128_f8f6f4 v[80:83], v[8:15], v[48:55], v[80:83], v200, v200 op_sel_hi:[0,0,0]
	v_mfma_scale_f32_16x16x128_f8f6f4 v[68:71], v[0:7], v[56:63], v[68:71], v200, v200 op_sel_hi:[0,0,0]
	v_mfma_scale_f32_16x16x128_f8f6f4 v[64:67], v[8:15], v[56:63], v[64:67], v200, v200 op_sel_hi:[0,0,0]
	s_setprio 0
	s_barrier
; #define PG8_WAIT_V(n) asm volatile("s_waitcnt vmcnt(" #n ")" ::: "memory")
; #define PG8_WAIT_L(n) asm volatile("s_waitcnt lgkmcnt(" #n ")" ::: "memory")
; #define PG8_BAR __builtin_amdgcn_s_barrier()
; #define PG8_SCHED __builtin_amdgcn_sched_barrier(0)
; #define PG8_STAGE_A(b, h, p) do { if constexpr (GATHER) { if ((h) == 0) PG8_STAGE(PG8_SA(b, h), p, vA0); else PG8_STAGE(PG8_SA(b, h), p, vA1); } else PG8_STAGE(PG8_SA(b, h), (p) + ((h) ? hstepA : (size_t)0), voffA); } while (0)
; template <class Epi, class Sched, bool ALIGN_EPI = true, bool SP2 = true, bool FP8 = false, bool GATHER = false>
; __device__ __forceinline__ void gemm_phase(LAS unsigned char* lds, const Dims g, const Sched& S, const Epi& E, const int wv) {
;     ...
;             PG8_LDB(B0, 1, 0); PG8_LDB(B1, 1, 1); PG8_SCHED; PG8_LDA(At, 1, 0); PG8_STAGE_A(0, 1, a2);
;             PG8_WAIT_V(8); PG8_WAIT_L(0); PG8_BAR; PG8_MMA(0, 0, At, B0); PG8_MMA(0, 1, At, B1); PG8_BAR; PG8_SCHED;
;             PG8_LDA(At, 1, 1); PG8_STAGE(PG8_SB(1, 0), b3, voffB); PG8_STAGE(PG8_SB(1, 1), b3 + hstepB, voffB); PG8_STAGE_A(1, 0, a3);
;             PG8_WAIT_V(8); PG8_WAIT_L(0); PG8_BAR; PG8_MMA(1, 0, At, B0); PG8_MMA(1, 1, At, B1); PG8_BAR; PG8_SCHED;
	v_add_u32_e32 v12, 0x18000, v201
	v_add_u32_e32 v28, 0x1c000, v201
	ds_read_b128 v[0:3], v12
	ds_read_b128 v[4:7], v12 offset:1024
	ds_read_b128 v[8:11], v12 offset:2048
	ds_read_b128 v[12:15], v12 offset:3072
	ds_read_b128 v[16:19], v28
	ds_read_b128 v[20:23], v28 offset:1024
	ds_read_b128 v[24:27], v28 offset:2048
	ds_read_b128 v[28:31], v28 offset:3072
	ds_read_b128 v[32:35], v202 offset:32768
	ds_read_b128 v[36:39], v202 offset:33792
	ds_read_b128 v[40:43], v202 offset:34816
	ds_read_b128 v[44:47], v202 offset:35840
	ds_read_b128 v[48:51], v202 offset:36864
	ds_read_b128 v[52:55], v202 offset:37888
	ds_read_b128 v[56:59], v202 offset:38912
	ds_read_b128 v[60:63], v202 offset:39936
	s_mov_b32 m0, s61
	s_nop 0
	global_load_lds_dwordx4 v197, s[48:49]
	s_nop 0
	s_mov_b32 m0, s62
	s_nop 0
	global_load_lds_dwordx4 v198, s[48:49]
	s_waitcnt vmcnt(8)
	s_waitcnt lgkmcnt(0)
	s_barrier
	s_setprio 1
	s_waitcnt lgkmcnt(6)
	v_mfma_scale_f32_16x16x128_f8f6f4 v[188:191], v[0:7], v[32:39], v[188:191], v200, v200 op_sel_hi:[0,0,0]
	v_mfma_scale_f32_16x16x128_f8f6f4 v[184:187], v[8:15], v[32:39], v[184:187], v200, v200 op_sel_hi:[0,0,0]
	s_waitcnt lgkmcnt(4)
	v_mfma_scale_f32_16x16x128_f8f6f4 v[172:175], v[0:7], v[40:47], v[172:175], v200, v200 op_sel_hi:[0,0,0]
	v_mfma_scale_f32_16x16x128_f8f6f4 v[168:171], v[8:15], v[40:47], v[168:171], v200, v200 op_sel_hi:[0,0,0]
	s_waitcnt lgkmcnt(2)
	v_mfma_scale_f32_16x16x128_f8f6f4 v[156:159], v[0:7], v[48:55], v[156:159], v200, v200 op_sel_hi:[0,0,0]
	v_mfma_scale_f32_16x16x128_f8f6f4 v[152:155], v[8:15], v[48:55], v[152:155], v200, v200 op_sel_hi:[0,0,0]
	s_waitcnt lgkmcnt(0)
	v_mfma_scale_f32_16x16x128_f8f6f4 v[140:143], v[0:7], v[56:63], v[140:143], v200, v200 op_sel_hi:[0,0,0]
	v_mfma_scale_f32_16x16x128_f8f6f4 v[136:139], v[8:15], v[56:63], v[136:139], v200, v200 op_sel_hi:[0,0,0]
	s_setprio 0
	s_setprio 1
	v_mfma_scale_f32_16x16x128_f8f6f4 v[180:183], v[16:23], v[32:39], v[180:183], v200, v200 op_sel_hi:[0,0,0]
	v_mfma_scale_f32_16x16x128_f8f6f4 v[176:179], v[24:31], v[32:39], v[176:179], v200, v200 op_sel_hi:[0,0,0]
	v_mfma_scale_f32_16x16x128_f8f6f4 v[164:167], v[16:23], v[40:47], v[164:167], v200, v200 op_sel_hi:[0,0,0]
	v_mfma_scale_f32_16x16x128_f8f6f4 v[160:163], v[24:31], v[40:47], v[160:163], v200, v200 op_sel_hi:[0,0,0]
	v_mfma_scale_f32_16x16x128_f8f6f4 v[148:151], v[16:23], v[48:55], v[148:151], v200, v200 op_sel_hi:[0,0,0]
	v_mfma_scale_f32_16x16x128_f8f6f4 v[144:147], v[24:31], v[48:55], v[144:147], v200, v200 op_sel_hi:[0,0,0]
	v_mfma_scale_f32_16x16x128_f8f6f4 v[132:135], v[16:23], v[56:63], v[132:135], v200, v200 op_sel_hi:[0,0,0]
	v_mfma_scale_f32_16x16x128_f8f6f4 v[128:131], v[24:31], v[56:63], v[128:131], v200, v200 op_sel_hi:[0,0,0]
	s_setprio 0
	s_barrier
	ds_read_b128 v[32:35], v202 offset:49152
	ds_read_b128 v[36:39], v202 offset:50176
	ds_read_b128 v[40:43], v202 offset:51200
	ds_read_b128 v[44:47], v202 offset:52224
	ds_read_b128 v[48:51], v202 offset:53248
	ds_read_b128 v[52:55], v202 offset:54272
	ds_read_b128 v[56:59], v202 offset:55296
	ds_read_b128 v[60:63], v202 offset:56320
	s_mov_b32 m0, s65
	s_nop 0
	global_load_lds_dwordx4 v195, s[46:47]
	s_add_u32 s44, s44, 0x20080
	s_mov_b32 m0, s66
	s_nop 0
	global_load_lds_dwordx4 v199, s[46:47]
	s_addc_u32 s45, s45, 0
	s_mov_b32 m0, s69
	s_nop 0
	global_load_lds_dwordx4 v195, s[44:45]
	s_nop 0
	s_mov_b32 m0, s70
	s_nop 0
	global_load_lds_dwordx4 v199, s[44:45]
	s_mov_b32 m0, s67
	s_nop 0
	global_load_lds_dwordx4 v194, s[42:43]
	s_nop 0
	s_mov_b32 m0, s68
	s_nop 0
	global_load_lds_dwordx4 v196, s[42:43]
	s_waitcnt vmcnt(8)
	s_waitcnt lgkmcnt(0)
	s_barrier
	s_setprio 1
	s_waitcnt lgkmcnt(6)
	v_mfma_scale_f32_16x16x128_f8f6f4 v[124:127], v[0:7], v[32:39], v[124:127], v200, v200 op_sel_hi:[0,0,0]
	v_mfma_scale_f32_16x16x128_f8f6f4 v[120:123], v[8:15], v[32:39], v[120:123], v200, v200 op_sel_hi:[0,0,0]
	s_waitcnt lgkmcnt(4)
	v_mfma_scale_f32_16x16x128_f8f6f4 v[108:111], v[0:7], v[40:47], v[108:111], v200, v200 op_sel_hi:[0,0,0]
	v_mfma_scale_f32_16x16x128_f8f6f4 v[104:107], v[8:15], v[40:47], v[104:107], v200, v200 op_sel_hi:[0,0,0]
	s_waitcnt lgkmcnt(2)
	v_mfma_scale_f32_16x16x128_f8f6f4 v[92:95], v[0:7], v[48:55], v[92:95], v200, v200 op_sel_hi:[0,0,0]
	v_mfma_scale_f32_16x16x128_f8f6f4 v[88:91], v[8:15], v[48:55], v[88:91], v200, v200 op_sel_hi:[0,0,0]
	s_waitcnt lgkmcnt(0)
	v_mfma_scale_f32_16x16x128_f8f6f4 v[76:79], v[0:7], v[56:63], v[76:79], v200, v200 op_sel_hi:[0,0,0]
	v_mfma_scale_f32_16x16x128_f8f6f4 v[72:75], v[8:15], v[56:63], v[72:75], v200, v200 op_sel_hi:[0,0,0]
	s_setprio 0
	s_setprio 1
	v_mfma_scale_f32_16x16x128_f8f6f4 v[116:119], v[16:23], v[32:39], v[116:119], v200, v200 op_sel_hi:[0,0,0]
	v_mfma_scale_f32_16x16x128_f8f6f4 v[112:115], v[24:31], v[32:39], v[112:115], v200, v200 op_sel_hi:[0,0,0]
	v_mfma_scale_f32_16x16x128_f8f6f4 v[100:103], v[16:23], v[40:47], v[100:103], v200, v200 op_sel_hi:[0,0,0]
	v_mfma_scale_f32_16x16x128_f8f6f4 v[96:99], v[24:31], v[40:47], v[96:99], v200, v200 op_sel_hi:[0,0,0]
	v_mfma_scale_f32_16x16x128_f8f6f4 v[84:87], v[16:23], v[48:55], v[84:87], v200, v200 op_sel_hi:[0,0,0]
	v_mfma_scale_f32_16x16x128_f8f6f4 v[80:83], v[24:31], v[48:55], v[80:83], v200, v200 op_sel_hi:[0,0,0]
	v_mfma_scale_f32_16x16x128_f8f6f4 v[68:71], v[16:23], v[56:63], v[68:71], v200, v200 op_sel_hi:[0,0,0]
	v_mfma_scale_f32_16x16x128_f8f6f4 v[64:67], v[24:31], v[56:63], v[64:67], v200, v200 op_sel_hi:[0,0,0]
	s_setprio 0
	s_barrier
	s_add_i32 s84, s84, 2
	s_add_u32 s82, s82, 0x100
	s_addc_u32 s83, s83, 0
	s_cmp_gt_u32 s84, 5
	s_cbranch_scc1 .LBB0_1431

; #define PG8_WAIT_V(n) asm volatile("s_waitcnt vmcnt(" #n ")" ::: "memory")
; #define PG8_WAIT_L(n) asm volatile("s_waitcnt lgkmcnt(" #n ")" ::: "memory")
; #define PG8_BAR __builtin_amdgcn_s_barrier()
; #define PG8_SCHED __builtin_amdgcn_sched_barrier(0)
; #define PG8_STAGE_A(b, h, p) do { if constexpr (GATHER) { if ((h) == 0) PG8_STAGE(PG8_SA(b, h), p, vA0); else PG8_STAGE(PG8_SA(b, h), p, vA1); } else PG8_STAGE(PG8_SA(b, h), (p) + ((h) ? hstepA : (size_t)0), voffA); } while (0)
; #define PG8_GOFF1(un, h, d) do { int tz_ = tid; asm volatile("" : "+v"(tz_)); _Pragma("unroll") for (int i_ = 0; i_ < 2; ++i_) { int R_, C_; stage_rc(tz_ * 16 + i_ * 8192, R_, C_); \
;         d[i_] = S.gather(un, R_ + (h) * HALF) + (unsigned)C_ * 2u; } } while (0)
; template <class Epi, class Sched, bool ALIGN_EPI = true, bool SP2 = true, bool FP8 = false, bool GATHER = false>
; __device__ __forceinline__ void gemm_phase(LAS unsigned char* lds, const Dims g, const Sched& S, const Epi& E, const int wv) {
;     ...
;             if constexpr (GATHER) { if (last) PG8_GOFF1(un_, 0, vA0); }
;             PG8_LDB(B0, 0, 0); PG8_LDB(B1, 0, 1); PG8_SCHED; PG8_LDA(At, 0, 0); PG8_STAGE_A(1, 1, a1);
;             if constexpr (GATHER) { if (last) PG8_GOFF1(un_, 1, vA1); }
;             PG8_WAIT_V(8); PG8_WAIT_L(0); PG8_BAR; PG8_MMA(0, 0, At, B0); PG8_MMA(0, 1, At, B1); PG8_BAR; PG8_SCHED;
.LBB0_1429:
	v_add_u32_e32 v0, 0x10000, v201
	v_add_u32_e32 v12, 0x14000, v201
	ds_read_b128 v[16:19], v0
	ds_read_b128 v[20:23], v0 offset:1024
	ds_read_b128 v[24:27], v0 offset:2048
	ds_read_b128 v[28:31], v0 offset:3072
	ds_read_b128 v[0:3], v12
	ds_read_b128 v[4:7], v12 offset:1024
	ds_read_b128 v[8:11], v12 offset:2048
	ds_read_b128 v[12:15], v12 offset:3072
	s_add_u32 s44, s40, 0x80
	s_addc_u32 s45, s41, 0
	ds_read_b128 v[56:59], v202
	ds_read_b128 v[60:63], v202 offset:1024
	ds_read_b128 v[48:51], v202 offset:2048
	ds_read_b128 v[52:55], v202 offset:3072
	ds_read_b128 v[40:43], v202 offset:4096
	ds_read_b128 v[44:47], v202 offset:5120
	ds_read_b128 v[32:35], v202 offset:6144
	ds_read_b128 v[36:39], v202 offset:7168
	s_mov_b32 m0, s71
	s_nop 0
	global_load_lds_dwordx4 v197, s[44:45]
	s_andn2_b64 vcc, exec, s[42:43]
	s_mov_b32 m0, s72
	s_nop 0
	global_load_lds_dwordx4 v198, s[44:45]
	s_cbranch_vccnz .LBB0_1426
	v_mov_b32_e32 v197, v192
	s_nop 0
	v_ashrrev_i32_e32 v204, 31, v197
	v_lshrrev_b32_e32 v204, 26, v204
	v_lshlrev_b32_e32 v198, 4, v197
	v_add_u32_e32 v204, v197, v204
	v_bfe_i32 v197, v197, 27, 1
	v_lshrrev_b32_e32 v197, 22, v197
	v_add_u32_e32 v197, v198, v197
	v_and_b32_e32 v197, 0xfffffc00, v197
	v_sub_u32_e32 v197, v198, v197
	v_lshrrev_b32_e32 v205, 4, v197
	v_bitop3_b32 v197, v205, v197, 32 bitop3:0x6c
	v_ashrrev_i32_e32 v205, 31, v197
	v_lshrrev_b32_e32 v205, 26, v205
	v_ashrrev_i32_e32 v204, 6, v204
	v_add_u32_e32 v205, v197, v205
	v_ashrrev_i32_e32 v206, 6, v205
	v_lshlrev_b32_e32 v204, 5, v204
	v_and_b32_e32 v205, 0xc0, v205
	v_and_b32_e32 v207, 32, v204
	v_sub_u32_e32 v197, v197, v205
	v_lshlrev_b32_e32 v205, 2, v206
	v_and_b32_e32 v204, 0xffffffc0, v204
	v_add_u32_e32 v198, 0x2000, v198
	v_add3_u32 v204, s81, v205, v204
	v_ashrrev_i32_e32 v205, 31, v198
	v_lshrrev_b32_e32 v205, 22, v205
	v_add_u32_e32 v205, v198, v205
	v_ashrrev_i32_e32 v205, 10, v205
	v_mul_i32_i24_e32 v206, 0x400, v205
	v_sub_u32_e32 v198, v198, v206
	v_lshrrev_b32_e32 v206, 4, v198
	v_bitop3_b32 v198, v206, v198, 32 bitop3:0x6c
	v_ashrrev_i32_e32 v206, 31, v198
	v_lshrrev_b32_e32 v206, 26, v206
	v_ashrrev_i16_sdwa v197, v193, sext(v197) dst_sel:DWORD dst_unused:UNUSED_PAD src0_sel:DWORD src1_sel:BYTE_0
	ds_read_b32 v204, v204 offset:512
	v_add_u32_e32 v206, v198, v206
	v_add_u32_sdwa v197, v207, sext(v197) dst_sel:DWORD dst_unused:UNUSED_PAD src0_sel:DWORD src1_sel:WORD_0
	v_ashrrev_i32_e32 v207, 6, v206
	v_lshlrev_b32_e32 v205, 5, v205
	v_lshlrev_b32_e32 v207, 2, v207
	v_and_b32_e32 v208, 0xffffffc0, v205
	v_add3_u32 v207, s81, v207, v208
	ds_read_b32 v207, v207 offset:512
	s_waitcnt lgkmcnt(1)
	v_lshl_add_u32 v197, v197, 1, v204
	v_and_b32_e32 v204, 32, v205
	v_and_b32_e32 v205, 0xc0, v206
	v_sub_u32_e32 v198, v198, v205
	v_ashrrev_i16_sdwa v198, v193, sext(v198) dst_sel:DWORD dst_unused:UNUSED_PAD src0_sel:DWORD src1_sel:BYTE_0
	v_add_u32_sdwa v198, v204, sext(v198) dst_sel:DWORD dst_unused:UNUSED_PAD src0_sel:DWORD src1_sel:WORD_0
	s_waitcnt lgkmcnt(0)
	v_lshl_add_u32 v198, v198, 1, v207
	s_branch .LBB0_1426

; __device__ __forceinline__ unsigned pk4_fp8(float a, float b, float c, float d) { int w = __builtin_amdgcn_cvt_pk_fp8_f32(a, b, 0, false); w = __builtin_amdgcn_cvt_pk_fp8_f32(c, d, w, true); return (unsigned)w; }
;     __device__ __forceinline__ void operator()(const f32x4 (&acc)[2][2][4][2], const Unit& u, int wr, int wc, int fr, int fq) const {
;         const int row0 = u.pm * BM + wr * 64 + fr, c0 = u.pn * HALF + wc * 32 + 8 * fq;
;         const float* bp = bgu + (size_t)u.aux * 2048 + c0;
;         const f32x4 bg0 = *(const f32x4*)(bp), bg1 = *(const f32x4*)(bp + 4), bu0 = *(const f32x4*)(bp + 1024), bu1 = *(const f32x4*)(bp + 1028);
; #pragma unroll
;         for (int ai = 0; ai < 2; ++ai)
; #pragma unroll
;             for (int mp = 0; mp < 2; ++mp) {
;                 u32x2 wq[2];
; #pragma unroll
;                 for (int mi = 0; mi < 2; ++mi) { const int m = 2 * mp + mi;
;                     const f32x4 g0 = acc[ai][0][m][0] * ascale + bg0, g1 = acc[ai][0][m][1] * ascale + bg1, u0 = acc[ai][1][m][0] * ascale + bu0, u1 = acc[ai][1][m][1] * ascale + bu1;
;                     float r[8];
; #pragma unroll
;                     for (int j = 0; j < 4; ++j) {
;                         float gg = fminf(g0[j], 7.f), uu = fminf(fmaxf(u0[j], -7.f), 7.f); r[j] = 4.f * (uu + 1.f) * gg * __builtin_amdgcn_rcpf(1.f + __expf(-1.702f * gg));
;                         gg = fminf(g1[j], 7.f); uu = fminf(fmaxf(u1[j], -7.f), 7.f); r[4 + j] = 4.f * (uu + 1.f) * gg * __builtin_amdgcn_rcpf(1.f + __expf(-1.702f * gg));
;                     }
;                     wq[mi].x = pk4_fp8(r[0], r[1], r[2], r[3]); wq[mi].y = pk4_fp8(r[4], r[5], r[6], r[7]); }
;                 *(u32x4*)(act + (size_t)(row0 + ai * HALF + (2 * mp + (fq & 1)) * 16) * EFF + (c0 - 8 * (fq & 1))) = widen16(wq[0], wq[1]);
.LBB0_1433:
	v_mov_b32_e32 v18, v192
	s_lshl_b32 s36, s36, 7
	v_lshrrev_b32_e32 v0, 1, v18
	s_ashr_i32 s39, s38, 31
	s_lshl_b32 s40, s77, 8
	v_and_or_b32 v0, v0, 24, s36
	s_lshl_b64 s[38:39], s[38:39], 13
	v_or_b32_e32 v16, s64, v0
	s_add_u32 s38, s4, s38
	s_addc_u32 s39, s5, s39
	v_ashrrev_i32_e32 v17, 31, v16
	v_lshl_add_u64 v[0:1], v[16:17], 2, s[38:39]
	global_load_dwordx4 v[12:15], v[0:1], off
	global_load_dwordx4 v[4:7], v[0:1], off offset:16
	v_add_co_u32_e32 v2, vcc, s73, v0
	v_bfe_u32 v17, v18, 4, 1
	s_nop 0
	v_addc_co_u32_e32 v3, vcc, 0, v1, vcc
	v_lshl_add_u64 v[0:1], v[0:1], 0, s[20:21]
	global_load_dwordx4 v[8:11], v[2:3], off
	v_lshlrev_b32_e32 v19, 3, v17
	global_load_dwordx4 v[0:3], v[0:1], off offset:16
	v_sub_u32_e32 v16, v16, v19
	s_add_i32 s40, s40, s63
	v_and_or_b32 v18, v18, 15, s40
	v_lshl_or_b32 v18, v17, 4, v18
	v_ashrrev_i32_e32 v17, 31, v16
	s_andn2_b64 vcc, exec, s[26:27]
	s_mov_b64 s[26:27], -1
	s_waitcnt vmcnt(3)
	v_fmamk_f32 v19, v188, 0x3a000000, v12
	s_waitcnt vmcnt(2)
	v_fmamk_f32 v20, v184, 0x3a000000, v4
	v_min_f32_e32 v19, 0x40e00000, v19
	v_min_f32_e32 v20, 0x40e00000, v20
	v_fmamk_f32 v21, v189, 0x3a000000, v13
	v_mul_f32_e32 v31, 0xbfd9db23, v19
	v_mul_f32_e32 v32, 0xbfd9db23, v20
	v_min_f32_e32 v21, 0x40e00000, v21
	v_mul_f32_e32 v31, 0x3fb8aa3b, v31
	v_mul_f32_e32 v32, 0x3fb8aa3b, v32
	s_waitcnt vmcnt(1)
	v_fmamk_f32 v25, v180, 0x3a000000, v8
	s_waitcnt vmcnt(0)
	v_fmamk_f32 v26, v176, 0x3a000000, v0
	v_mul_f32_e32 v33, 0xbfd9db23, v21
	v_exp_f32_e32 v31, v31
	v_exp_f32_e32 v32, v32
	v_med3_f32 v25, v25, s74, v203
	v_med3_f32 v26, v26, s74, v203
	v_mul_f32_e32 v33, 0x3fb8aa3b, v33
	v_fmamk_f32 v27, v181, 0x3a000000, v9
	v_exp_f32_e32 v33, v33
	v_med3_f32 v27, v27, s74, v203
	v_fmaak_f32 v25, 4.0, v25, 0x40800000
	v_fmaak_f32 v26, 4.0, v26, 0x40800000
	v_fmamk_f32 v24, v186, 0x3a000000, v6
	v_mul_f32_e32 v19, v19, v25
	v_mul_f32_e32 v20, v20, v26
	v_add_f32_e32 v25, 1.0, v31
	v_add_f32_e32 v26, 1.0, v32
	v_min_f32_e32 v24, 0x40e00000, v24
	v_fmaak_f32 v27, 4.0, v27, 0x40800000
	v_rcp_f32_e32 v25, v25
	v_rcp_f32_e32 v26, v26
	v_mul_f32_e32 v36, 0xbfd9db23, v24
	v_mul_f32_e32 v21, v21, v27
	v_add_f32_e32 v27, 1.0, v33
	v_mul_f32_e32 v36, 0x3fb8aa3b, v36
	v_rcp_f32_e32 v27, v27
	v_fmamk_f32 v30, v178, 0x3a000000, v2
	v_exp_f32_e32 v36, v36
	v_med3_f32 v30, v30, s74, v203
	v_mul_f32_e32 v19, v25, v19
	v_mul_f32_e32 v25, v26, v20
	v_fmamk_f32 v26, v191, 0x3a000000, v15
	v_min_f32_e32 v26, 0x40e00000, v26
	v_mul_f32_e32 v21, v27, v21
	v_fmaak_f32 v20, 4.0, v30, 0x40800000
	v_mul_f32_e32 v27, 0xbfd9db23, v26
	v_mul_f32_e32 v20, v24, v20
	v_add_f32_e32 v24, 1.0, v36
	v_mul_f32_e32 v27, 0x3fb8aa3b, v27
	v_rcp_f32_e32 v24, v24
	v_exp_f32_e32 v27, v27
	v_fmamk_f32 v23, v190, 0x3a000000, v14
	v_min_f32_e32 v23, 0x40e00000, v23
	v_mul_f32_e32 v24, v24, v20
	v_fmamk_f32 v20, v183, 0x3a000000, v11
	v_add_f32_e32 v27, 1.0, v27
	v_med3_f32 v20, v20, s74, v203
	v_rcp_f32_e32 v27, v27
	v_fmamk_f32 v22, v185, 0x3a000000, v5
	v_mul_f32_e32 v35, 0xbfd9db23, v23
	v_fmaak_f32 v20, 4.0, v20, 0x40800000
	v_min_f32_e32 v22, 0x40e00000, v22
	v_mul_f32_e32 v35, 0x3fb8aa3b, v35
	v_mul_f32_e32 v20, v26, v20
	v_fmamk_f32 v29, v182, 0x3a000000, v10
	v_mul_f32_e32 v34, 0xbfd9db23, v22
	v_exp_f32_e32 v35, v35
	v_mul_f32_e32 v26, v27, v20
	v_fmamk_f32 v20, v187, 0x3a000000, v7
	v_med3_f32 v29, v29, s74, v203
	v_mul_f32_e32 v34, 0x3fb8aa3b, v34
	v_min_f32_e32 v27, 0x40e00000, v20
	v_fmamk_f32 v28, v177, 0x3a000000, v1
	v_exp_f32_e32 v34, v34
	v_mul_f32_e32 v20, 0xbfd9db23, v27
	v_med3_f32 v28, v28, s74, v203
	v_fmaak_f32 v29, 4.0, v29, 0x40800000
	v_mul_f32_e32 v20, 0x3fb8aa3b, v20
	v_mul_f32_e32 v23, v23, v29
	v_add_f32_e32 v29, 1.0, v35
	v_exp_f32_e32 v20, v20
	v_fmaak_f32 v28, 4.0, v28, 0x40800000
	v_rcp_f32_e32 v29, v29
	v_mul_f32_e32 v22, v22, v28
	v_add_f32_e32 v28, 1.0, v34
	v_rcp_f32_e32 v28, v28
	v_add_f32_e32 v20, 1.0, v20
	v_mul_f32_e32 v23, v29, v23
	v_rcp_f32_e32 v29, v20
	v_mov_b32_e32 v20, 0
	v_cvt_pk_fp8_f32 v20, v19, v21
	v_mul_f32_e32 v22, v28, v22
	v_fmamk_f32 v28, v179, 0x3a000000, v3
	v_mov_b32_e32 v21, 0
	v_med3_f32 v28, v28, s74, v203
	v_cvt_pk_fp8_f32 v21, v25, v22
	v_fmamk_f32 v22, v172, 0x3a000000, v12
	v_add_f32_e32 v28, 1.0, v28
	v_min_f32_e32 v22, 0x40e00000, v22
	v_mul_f32_e32 v19, 4.0, v28
	v_cvt_pk_fp8_f32 v20, v23, v26 op_sel:[0,0,1]
	v_mul_f32_e32 v23, 0xbfd9db23, v22
	v_mul_f32_e32 v19, v27, v19
	v_mul_f32_e32 v23, 0x3fb8aa3b, v23
	v_mul_f32_e32 v19, v29, v19
	v_exp_f32_e32 v23, v23
	v_cvt_pk_fp8_f32 v21, v24, v19 op_sel:[0,0,1]
	v_fmamk_f32 v19, v164, 0x3a000000, v8
	v_med3_f32 v19, v19, s74, v203
	v_add_f32_e32 v23, 1.0, v23
	v_fmaak_f32 v19, 4.0, v19, 0x40800000
	v_rcp_f32_e32 v23, v23
	v_mul_f32_e32 v19, v22, v19
	v_fmamk_f32 v22, v168, 0x3a000000, v4
	v_min_f32_e32 v22, 0x40e00000, v22
	v_mul_f32_e32 v24, 0xbfd9db23, v22
	v_mul_f32_e32 v24, 0x3fb8aa3b, v24
	v_mul_f32_e32 v19, v23, v19
	v_fmamk_f32 v23, v160, 0x3a000000, v0
	v_exp_f32_e32 v24, v24
	v_med3_f32 v23, v23, s74, v203
	v_fmaak_f32 v23, 4.0, v23, 0x40800000
	v_mul_f32_e32 v22, v22, v23
	v_add_f32_e32 v23, 1.0, v24
	v_fmamk_f32 v24, v173, 0x3a000000, v13
	v_min_f32_e32 v24, 0x40e00000, v24
	v_mul_f32_e32 v25, 0xbfd9db23, v24
	v_mul_f32_e32 v25, 0x3fb8aa3b, v25
	v_rcp_f32_e32 v23, v23
	v_exp_f32_e32 v25, v25
	v_mul_f32_e32 v26, v23, v22
	v_fmamk_f32 v22, v165, 0x3a000000, v9
	v_add_f32_e32 v23, 1.0, v25
	v_med3_f32 v22, v22, s74, v203
	v_rcp_f32_e32 v23, v23
	v_fmaak_f32 v22, 4.0, v22, 0x40800000
	v_mul_f32_e32 v22, v24, v22
	v_mul_f32_e32 v23, v23, v22
	v_fmamk_f32 v22, v169, 0x3a000000, v5
	v_min_f32_e32 v22, 0x40e00000, v22
; __device__ __forceinline__ unsigned pk4_fp8(float a, float b, float c, float d) { int w = __builtin_amdgcn_cvt_pk_fp8_f32(a, b, 0, false); w = __builtin_amdgcn_cvt_pk_fp8_f32(c, d, w, true); return (unsigned)w; }
;     __device__ __forceinline__ void operator()(const f32x4 (&acc)[2][2][4][2], const Unit& u, int wr, int wc, int fr, int fq) const {
;     ...
;                 for (int mi = 0; mi < 2; ++mi) { const int m = 2 * mp + mi;
;                     const f32x4 g0 = acc[ai][0][m][0] * ascale + bg0, g1 = acc[ai][0][m][1] * ascale + bg1, u0 = acc[ai][1][m][0] * ascale + bu0, u1 = acc[ai][1][m][1] * ascale + bu1;
;                     float r[8];
; #pragma unroll
;                     for (int j = 0; j < 4; ++j) {
;                         float gg = fminf(g0[j], 7.f), uu = fminf(fmaxf(u0[j], -7.f), 7.f); r[j] = 4.f * (uu + 1.f) * gg * __builtin_amdgcn_rcpf(1.f + __expf(-1.702f * gg));
;                         gg = fminf(g1[j], 7.f); uu = fminf(fmaxf(u1[j], -7.f), 7.f); r[4 + j] = 4.f * (uu + 1.f) * gg * __builtin_amdgcn_rcpf(1.f + __expf(-1.702f * gg));
;                     }
;                     wq[mi].x = pk4_fp8(r[0], r[1], r[2], r[3]); wq[mi].y = pk4_fp8(r[4], r[5], r[6], r[7]); }
;                 *(u32x4*)(act + (size_t)(row0 + ai * HALF + (2 * mp + (fq & 1)) * 16) * EFF + (c0 - 8 * (fq & 1))) = widen16(wq[0], wq[1]);
	v_mul_f32_e32 v25, 0xbfd9db23, v22
	v_mul_f32_e32 v25, 0x3fb8aa3b, v25
	v_fmamk_f32 v24, v161, 0x3a000000, v1
	v_exp_f32_e32 v25, v25
	v_med3_f32 v24, v24, s74, v203
	v_fmaak_f32 v24, 4.0, v24, 0x40800000
	v_mul_f32_e32 v22, v22, v24
	v_add_f32_e32 v24, 1.0, v25
	v_fmamk_f32 v25, v174, 0x3a000000, v14
	v_min_f32_e32 v25, 0x40e00000, v25
	v_mul_f32_e32 v27, 0xbfd9db23, v25
	v_mul_f32_e32 v27, 0x3fb8aa3b, v27
	v_rcp_f32_e32 v24, v24
	v_exp_f32_e32 v27, v27
	v_mul_f32_e32 v24, v24, v22
	v_fmamk_f32 v22, v166, 0x3a000000, v10
	v_add_f32_e32 v27, 1.0, v27
	v_med3_f32 v22, v22, s74, v203
	v_rcp_f32_e32 v27, v27
	v_fmaak_f32 v22, 4.0, v22, 0x40800000
	v_mul_f32_e32 v22, v25, v22
	v_mul_f32_e32 v25, v27, v22
	v_fmamk_f32 v22, v170, 0x3a000000, v6
	v_min_f32_e32 v22, 0x40e00000, v22
	v_mul_f32_e32 v28, 0xbfd9db23, v22
	v_mul_f32_e32 v28, 0x3fb8aa3b, v28
	v_fmamk_f32 v27, v162, 0x3a000000, v2
	v_exp_f32_e32 v28, v28
	v_med3_f32 v27, v27, s74, v203
	v_fmaak_f32 v27, 4.0, v27, 0x40800000
	v_mul_f32_e32 v22, v22, v27
	v_add_f32_e32 v27, 1.0, v28
	v_fmamk_f32 v28, v175, 0x3a000000, v15
	v_min_f32_e32 v28, 0x40e00000, v28
	v_mul_f32_e32 v29, 0xbfd9db23, v28
	v_mul_f32_e32 v29, 0x3fb8aa3b, v29
	v_rcp_f32_e32 v27, v27
	v_exp_f32_e32 v29, v29
	v_mul_f32_e32 v27, v27, v22
	v_fmamk_f32 v22, v167, 0x3a000000, v11
	v_add_f32_e32 v29, 1.0, v29
	v_med3_f32 v22, v22, s74, v203
	v_rcp_f32_e32 v29, v29
	v_fmaak_f32 v22, 4.0, v22, 0x40800000
	v_mul_f32_e32 v22, v28, v22
	v_mul_f32_e32 v28, v29, v22
	v_fmamk_f32 v22, v171, 0x3a000000, v7
	v_min_f32_e32 v29, 0x40e00000, v22
	v_mul_f32_e32 v30, 0xbfd9db23, v29
	v_mul_f32_e32 v30, 0x3fb8aa3b, v30
	v_exp_f32_e32 v30, v30
	v_fmamk_f32 v22, v163, 0x3a000000, v3
	v_med3_f32 v22, v22, s74, v203
	v_add_f32_e32 v22, 1.0, v22
	v_mul_f32_e32 v31, 4.0, v22
	v_add_f32_e32 v22, 1.0, v30
	v_rcp_f32_e32 v30, v22
	v_mov_b32_e32 v22, 0
	v_cvt_pk_fp8_f32 v22, v19, v23
	v_mov_b32_e32 v23, 0
	v_cvt_pk_fp8_f32 v23, v26, v24
	v_mul_f32_e32 v19, v29, v31
	v_mul_f32_e32 v19, v30, v19
	v_cvt_pk_fp8_f32 v22, v25, v28 op_sel:[0,0,1]
	v_cvt_pk_fp8_f32 v23, v27, v19 op_sel:[0,0,1]
	v_ashrrev_i32_e32 v19, 31, v18
	v_lshlrev_b64 v[24:25], 10, v[18:19]
	v_fmamk_f32 v19, v156, 0x3a000000, v12
	v_min_f32_e32 v19, 0x40e00000, v19
	v_mul_f32_e32 v26, 0xbfd9db23, v19
	v_lshl_add_u64 v[24:25], s[12:13], 0, v[24:25]
	v_mul_f32_e32 v26, 0x3fb8aa3b, v26
	v_permlane16_swap_b32_e32 v20, v22
	v_permlane16_swap_b32_e32 v21, v23
	v_lshl_add_u64 v[24:25], v[24:25], 0, v[16:17]
	v_exp_f32_e32 v26, v26
	global_store_dwordx4 v[24:25], v[20:23], off
	v_fmamk_f32 v28, v147, 0x3a000000, v3
	v_med3_f32 v28, v28, s74, v203
	v_fmamk_f32 v20, v148, 0x3a000000, v8
	v_med3_f32 v20, v20, s74, v203
	v_add_f32_e32 v21, 1.0, v26
	v_fmaak_f32 v20, 4.0, v20, 0x40800000
	v_rcp_f32_e32 v21, v21
	v_mul_f32_e32 v19, v19, v20
	v_fmamk_f32 v20, v152, 0x3a000000, v4
	v_min_f32_e32 v20, 0x40e00000, v20
	v_mul_f32_e32 v22, 0xbfd9db23, v20
	v_mul_f32_e32 v22, 0x3fb8aa3b, v22
	v_mul_f32_e32 v19, v21, v19
	v_fmamk_f32 v21, v144, 0x3a000000, v0
	v_exp_f32_e32 v22, v22
	v_med3_f32 v21, v21, s74, v203
	v_fmaak_f32 v21, 4.0, v21, 0x40800000
	v_mul_f32_e32 v20, v20, v21
	v_add_f32_e32 v21, 1.0, v22
	v_fmamk_f32 v22, v157, 0x3a000000, v13
	v_min_f32_e32 v22, 0x40e00000, v22
	v_mul_f32_e32 v23, 0xbfd9db23, v22
	v_mul_f32_e32 v23, 0x3fb8aa3b, v23
	v_rcp_f32_e32 v21, v21
	v_exp_f32_e32 v23, v23
	v_add_f32_e32 v28, 1.0, v28
	v_mul_f32_e32 v24, v21, v20
	v_fmamk_f32 v20, v149, 0x3a000000, v9
	v_add_f32_e32 v21, 1.0, v23
	v_med3_f32 v20, v20, s74, v203
	v_rcp_f32_e32 v21, v21
	v_fmaak_f32 v20, 4.0, v20, 0x40800000
	v_mul_f32_e32 v20, v22, v20
	v_mul_f32_e32 v21, v21, v20
	v_fmamk_f32 v20, v153, 0x3a000000, v5
	v_min_f32_e32 v20, 0x40e00000, v20
	v_mul_f32_e32 v23, 0xbfd9db23, v20
	v_mul_f32_e32 v23, 0x3fb8aa3b, v23
	v_fmamk_f32 v22, v145, 0x3a000000, v1
	v_exp_f32_e32 v23, v23
	v_med3_f32 v22, v22, s74, v203
	v_fmaak_f32 v22, 4.0, v22, 0x40800000
	v_mul_f32_e32 v20, v20, v22
	v_add_f32_e32 v22, 1.0, v23
	v_fmamk_f32 v23, v158, 0x3a000000, v14
	v_min_f32_e32 v23, 0x40e00000, v23
	v_mul_f32_e32 v25, 0xbfd9db23, v23
	v_mul_f32_e32 v25, 0x3fb8aa3b, v25
	v_rcp_f32_e32 v22, v22
	v_exp_f32_e32 v25, v25
	v_mul_f32_e32 v22, v22, v20
	v_fmamk_f32 v20, v150, 0x3a000000, v10
	v_add_f32_e32 v25, 1.0, v25
	v_med3_f32 v20, v20, s74, v203
	v_rcp_f32_e32 v25, v25
	v_fmaak_f32 v20, 4.0, v20, 0x40800000
	v_mul_f32_e32 v20, v23, v20
	v_mul_f32_e32 v23, v25, v20
	v_fmamk_f32 v20, v154, 0x3a000000, v6
	v_min_f32_e32 v20, 0x40e00000, v20
	v_mul_f32_e32 v26, 0xbfd9db23, v20
	v_mul_f32_e32 v26, 0x3fb8aa3b, v26
	v_fmamk_f32 v25, v146, 0x3a000000, v2
	v_exp_f32_e32 v26, v26
	v_med3_f32 v25, v25, s74, v203
	v_fmaak_f32 v25, 4.0, v25, 0x40800000
	v_mul_f32_e32 v20, v20, v25
	v_add_f32_e32 v25, 1.0, v26
	v_fmamk_f32 v26, v159, 0x3a000000, v15
	v_min_f32_e32 v26, 0x40e00000, v26
	v_mul_f32_e32 v27, 0xbfd9db23, v26
	v_mul_f32_e32 v27, 0x3fb8aa3b, v27
	v_rcp_f32_e32 v25, v25
	v_exp_f32_e32 v27, v27
	v_mul_f32_e32 v25, v25, v20
	v_fmamk_f32 v20, v151, 0x3a000000, v11
	v_add_f32_e32 v27, 1.0, v27
	v_med3_f32 v20, v20, s74, v203
	v_rcp_f32_e32 v27, v27
	v_fmaak_f32 v20, 4.0, v20, 0x40800000
	v_mul_f32_e32 v20, v26, v20
	v_mul_f32_e32 v26, v27, v20
	v_fmamk_f32 v20, v155, 0x3a000000, v7
	v_min_f32_e32 v27, 0x40e00000, v20
	v_mul_f32_e32 v20, 0xbfd9db23, v27
	v_mul_f32_e32 v20, 0x3fb8aa3b, v20
	v_exp_f32_e32 v20, v20
	s_nop 0
	v_add_f32_e32 v20, 1.0, v20
	v_rcp_f32_e32 v29, v20
	v_mov_b32_e32 v20, 0
	v_cvt_pk_fp8_f32 v20, v19, v21
	v_mov_b32_e32 v21, 0
	v_cvt_pk_fp8_f32 v21, v24, v22
	v_fmamk_f32 v22, v140, 0x3a000000, v12
; __device__ __forceinline__ unsigned pk4_fp8(float a, float b, float c, float d) { int w = __builtin_amdgcn_cvt_pk_fp8_f32(a, b, 0, false); w = __builtin_amdgcn_cvt_pk_fp8_f32(c, d, w, true); return (unsigned)w; }
;     __device__ __forceinline__ void operator()(const f32x4 (&acc)[2][2][4][2], const Unit& u, int wr, int wc, int fr, int fq) const {
;     ...
;                 for (int mi = 0; mi < 2; ++mi) { const int m = 2 * mp + mi;
;                     const f32x4 g0 = acc[ai][0][m][0] * ascale + bg0, g1 = acc[ai][0][m][1] * ascale + bg1, u0 = acc[ai][1][m][0] * ascale + bu0, u1 = acc[ai][1][m][1] * ascale + bu1;
;                     float r[8];
; #pragma unroll
;                     for (int j = 0; j < 4; ++j) {
;                         float gg = fminf(g0[j], 7.f), uu = fminf(fmaxf(u0[j], -7.f), 7.f); r[j] = 4.f * (uu + 1.f) * gg * __builtin_amdgcn_rcpf(1.f + __expf(-1.702f * gg));
;                         gg = fminf(g1[j], 7.f); uu = fminf(fmaxf(u1[j], -7.f), 7.f); r[4 + j] = 4.f * (uu + 1.f) * gg * __builtin_amdgcn_rcpf(1.f + __expf(-1.702f * gg));
;                     }
;                     wq[mi].x = pk4_fp8(r[0], r[1], r[2], r[3]); wq[mi].y = pk4_fp8(r[4], r[5], r[6], r[7]); }
;                 *(u32x4*)(act + (size_t)(row0 + ai * HALF + (2 * mp + (fq & 1)) * 16) * EFF + (c0 - 8 * (fq & 1))) = widen16(wq[0], wq[1]);
	v_min_f32_e32 v22, 0x40e00000, v22
	v_mul_f32_e32 v19, 4.0, v28
	v_cvt_pk_fp8_f32 v20, v23, v26 op_sel:[0,0,1]
	v_mul_f32_e32 v23, 0xbfd9db23, v22
	v_mul_f32_e32 v19, v27, v19
	v_mul_f32_e32 v23, 0x3fb8aa3b, v23
	v_mul_f32_e32 v19, v29, v19
	v_exp_f32_e32 v23, v23
	v_cvt_pk_fp8_f32 v21, v25, v19 op_sel:[0,0,1]
	v_fmamk_f32 v19, v132, 0x3a000000, v8
	v_med3_f32 v19, v19, s74, v203
	v_add_f32_e32 v23, 1.0, v23
	v_fmaak_f32 v19, 4.0, v19, 0x40800000
	v_rcp_f32_e32 v23, v23
	v_mul_f32_e32 v19, v22, v19
	v_fmamk_f32 v22, v136, 0x3a000000, v4
	v_min_f32_e32 v22, 0x40e00000, v22
	v_mul_f32_e32 v24, 0xbfd9db23, v22
	v_mul_f32_e32 v24, 0x3fb8aa3b, v24
	v_mul_f32_e32 v19, v23, v19
	v_fmamk_f32 v23, v128, 0x3a000000, v0
	v_exp_f32_e32 v24, v24
	v_med3_f32 v23, v23, s74, v203
	v_fmaak_f32 v23, 4.0, v23, 0x40800000
	v_mul_f32_e32 v22, v22, v23
	v_add_f32_e32 v23, 1.0, v24
	v_fmamk_f32 v24, v141, 0x3a000000, v13
	v_min_f32_e32 v24, 0x40e00000, v24
	v_mul_f32_e32 v25, 0xbfd9db23, v24
	v_mul_f32_e32 v25, 0x3fb8aa3b, v25
	v_rcp_f32_e32 v23, v23
	v_exp_f32_e32 v25, v25
	v_mul_f32_e32 v26, v23, v22
	v_fmamk_f32 v22, v133, 0x3a000000, v9
	v_add_f32_e32 v23, 1.0, v25
	v_med3_f32 v22, v22, s74, v203
	v_rcp_f32_e32 v23, v23
	v_fmaak_f32 v22, 4.0, v22, 0x40800000
	v_mul_f32_e32 v22, v24, v22
	v_mul_f32_e32 v23, v23, v22
	v_fmamk_f32 v22, v137, 0x3a000000, v5
	v_min_f32_e32 v22, 0x40e00000, v22
	v_mul_f32_e32 v25, 0xbfd9db23, v22
	v_mul_f32_e32 v25, 0x3fb8aa3b, v25
	v_fmamk_f32 v24, v129, 0x3a000000, v1
	v_exp_f32_e32 v25, v25
	v_med3_f32 v24, v24, s74, v203
	v_fmaak_f32 v24, 4.0, v24, 0x40800000
	v_mul_f32_e32 v22, v22, v24
	v_add_f32_e32 v24, 1.0, v25
	v_fmamk_f32 v25, v142, 0x3a000000, v14
	v_min_f32_e32 v25, 0x40e00000, v25
	v_mul_f32_e32 v27, 0xbfd9db23, v25
	v_mul_f32_e32 v27, 0x3fb8aa3b, v27
	v_rcp_f32_e32 v24, v24
	v_exp_f32_e32 v27, v27
	v_mul_f32_e32 v24, v24, v22
	v_fmamk_f32 v22, v134, 0x3a000000, v10
	v_add_f32_e32 v27, 1.0, v27
	v_med3_f32 v22, v22, s74, v203
	v_rcp_f32_e32 v27, v27
	v_fmaak_f32 v22, 4.0, v22, 0x40800000
	v_mul_f32_e32 v22, v25, v22
	v_mul_f32_e32 v25, v27, v22
	v_fmamk_f32 v22, v138, 0x3a000000, v6
	v_min_f32_e32 v22, 0x40e00000, v22
	v_mul_f32_e32 v28, 0xbfd9db23, v22
	v_mul_f32_e32 v28, 0x3fb8aa3b, v28
	v_fmamk_f32 v27, v130, 0x3a000000, v2
	v_exp_f32_e32 v28, v28
	v_med3_f32 v27, v27, s74, v203
	v_fmaak_f32 v27, 4.0, v27, 0x40800000
	v_mul_f32_e32 v22, v22, v27
	v_add_f32_e32 v27, 1.0, v28
	v_fmamk_f32 v28, v143, 0x3a000000, v15
	v_min_f32_e32 v28, 0x40e00000, v28
	v_mul_f32_e32 v29, 0xbfd9db23, v28
	v_mul_f32_e32 v29, 0x3fb8aa3b, v29
	v_rcp_f32_e32 v27, v27
	v_exp_f32_e32 v29, v29
	v_mul_f32_e32 v27, v27, v22
	v_fmamk_f32 v22, v135, 0x3a000000, v11
	v_add_f32_e32 v29, 1.0, v29
	v_med3_f32 v22, v22, s74, v203
	v_rcp_f32_e32 v29, v29
	v_fmaak_f32 v22, 4.0, v22, 0x40800000
	v_mul_f32_e32 v22, v28, v22
	v_mul_f32_e32 v28, v29, v22
	v_fmamk_f32 v22, v139, 0x3a000000, v7
	v_min_f32_e32 v29, 0x40e00000, v22
	v_mul_f32_e32 v30, 0xbfd9db23, v29
	v_mul_f32_e32 v30, 0x3fb8aa3b, v30
	v_exp_f32_e32 v30, v30
	v_fmamk_f32 v22, v131, 0x3a000000, v3
	v_med3_f32 v22, v22, s74, v203
	v_add_f32_e32 v22, 1.0, v22
	v_mul_f32_e32 v31, 4.0, v22
	v_add_f32_e32 v22, 1.0, v30
	v_rcp_f32_e32 v30, v22
	v_mov_b32_e32 v22, 0
	v_cvt_pk_fp8_f32 v22, v19, v23
	v_mov_b32_e32 v23, 0
	v_cvt_pk_fp8_f32 v23, v26, v24
	v_mul_f32_e32 v19, v29, v31
	v_mul_f32_e32 v19, v30, v19
	v_cvt_pk_fp8_f32 v22, v25, v28 op_sel:[0,0,1]
	v_cvt_pk_fp8_f32 v23, v27, v19 op_sel:[0,0,1]
	v_or_b32_e32 v24, 32, v18
	v_ashrrev_i32_e32 v25, 31, v24
	v_lshlrev_b64 v[24:25], 10, v[24:25]
	v_lshl_add_u64 v[24:25], s[12:13], 0, v[24:25]
	v_fmamk_f32 v19, v124, 0x3a000000, v12
	v_permlane16_swap_b32_e32 v20, v22
	v_permlane16_swap_b32_e32 v21, v23
	v_lshl_add_u64 v[24:25], v[24:25], 0, v[16:17]
	v_min_f32_e32 v19, 0x40e00000, v19
	global_store_dwordx4 v[24:25], v[20:23], off
	v_fmamk_f32 v29, v115, 0x3a000000, v3
	v_med3_f32 v29, v29, s74, v203
	v_mul_f32_e32 v20, 0xbfd9db23, v19
	v_mul_f32_e32 v20, 0x3fb8aa3b, v20
	v_exp_f32_e32 v21, v20
	v_fmamk_f32 v22, v116, 0x3a000000, v8
	v_med3_f32 v22, v22, s74, v203
	v_add_f32_e32 v21, 1.0, v21
	v_rcp_f32_e32 v21, v21
	v_fmaak_f32 v22, 4.0, v22, 0x40800000
	v_mul_f32_e32 v19, v19, v22
	v_fmamk_f32 v22, v112, 0x3a000000, v0
	v_mul_f32_e32 v19, v21, v19
	v_fmamk_f32 v21, v120, 0x3a000000, v4
	v_min_f32_e32 v21, 0x40e00000, v21
	v_mul_f32_e32 v23, 0xbfd9db23, v21
	v_mul_f32_e32 v23, 0x3fb8aa3b, v23
	v_exp_f32_e32 v23, v23
	v_med3_f32 v22, v22, s74, v203
	v_fmaak_f32 v22, 4.0, v22, 0x40800000
	v_mul_f32_e32 v21, v21, v22
	v_add_f32_e32 v22, 1.0, v23
	v_fmamk_f32 v23, v125, 0x3a000000, v13
	v_min_f32_e32 v23, 0x40e00000, v23
	v_mul_f32_e32 v24, 0xbfd9db23, v23
	v_mul_f32_e32 v24, 0x3fb8aa3b, v24
	v_rcp_f32_e32 v22, v22
	v_exp_f32_e32 v24, v24
	v_add_f32_e32 v29, 1.0, v29
	v_add_u32_e32 v20, 0x80, v18
	v_mul_f32_e32 v21, v22, v21
	v_fmamk_f32 v22, v117, 0x3a000000, v9
	v_add_f32_e32 v24, 1.0, v24
	v_med3_f32 v22, v22, s74, v203
	v_rcp_f32_e32 v24, v24
	v_fmaak_f32 v22, 4.0, v22, 0x40800000
	v_mul_f32_e32 v22, v23, v22
	v_mul_f32_e32 v23, v24, v22
	v_fmamk_f32 v22, v121, 0x3a000000, v5
	v_min_f32_e32 v22, 0x40e00000, v22
	v_mul_f32_e32 v25, 0xbfd9db23, v22
	v_mul_f32_e32 v25, 0x3fb8aa3b, v25
	v_fmamk_f32 v24, v113, 0x3a000000, v1
	v_exp_f32_e32 v25, v25
	v_med3_f32 v24, v24, s74, v203
	v_fmaak_f32 v24, 4.0, v24, 0x40800000
	v_mul_f32_e32 v22, v22, v24
	v_add_f32_e32 v24, 1.0, v25
	v_fmamk_f32 v25, v126, 0x3a000000, v14
	v_min_f32_e32 v25, 0x40e00000, v25
	v_mul_f32_e32 v26, 0xbfd9db23, v25
	v_mul_f32_e32 v26, 0x3fb8aa3b, v26
	v_rcp_f32_e32 v24, v24
; __device__ __forceinline__ unsigned pk4_fp8(float a, float b, float c, float d) { int w = __builtin_amdgcn_cvt_pk_fp8_f32(a, b, 0, false); w = __builtin_amdgcn_cvt_pk_fp8_f32(c, d, w, true); return (unsigned)w; }
;     __device__ __forceinline__ void operator()(const f32x4 (&acc)[2][2][4][2], const Unit& u, int wr, int wc, int fr, int fq) const {
;     ...
;                 for (int mi = 0; mi < 2; ++mi) { const int m = 2 * mp + mi;
;                     const f32x4 g0 = acc[ai][0][m][0] * ascale + bg0, g1 = acc[ai][0][m][1] * ascale + bg1, u0 = acc[ai][1][m][0] * ascale + bu0, u1 = acc[ai][1][m][1] * ascale + bu1;
;                     float r[8];
; #pragma unroll
;                     for (int j = 0; j < 4; ++j) {
;                         float gg = fminf(g0[j], 7.f), uu = fminf(fmaxf(u0[j], -7.f), 7.f); r[j] = 4.f * (uu + 1.f) * gg * __builtin_amdgcn_rcpf(1.f + __expf(-1.702f * gg));
;                         gg = fminf(g1[j], 7.f); uu = fminf(fmaxf(u1[j], -7.f), 7.f); r[4 + j] = 4.f * (uu + 1.f) * gg * __builtin_amdgcn_rcpf(1.f + __expf(-1.702f * gg));
;                     }
;                     wq[mi].x = pk4_fp8(r[0], r[1], r[2], r[3]); wq[mi].y = pk4_fp8(r[4], r[5], r[6], r[7]); }
;                 *(u32x4*)(act + (size_t)(row0 + ai * HALF + (2 * mp + (fq & 1)) * 16) * EFF + (c0 - 8 * (fq & 1))) = widen16(wq[0], wq[1]);
	v_exp_f32_e32 v26, v26
	v_mul_f32_e32 v24, v24, v22
	v_fmamk_f32 v22, v118, 0x3a000000, v10
	v_add_f32_e32 v26, 1.0, v26
	v_med3_f32 v22, v22, s74, v203
	v_rcp_f32_e32 v26, v26
	v_fmaak_f32 v22, 4.0, v22, 0x40800000
	v_mul_f32_e32 v22, v25, v22
	v_mul_f32_e32 v25, v26, v22
	v_fmamk_f32 v22, v122, 0x3a000000, v6
	v_min_f32_e32 v22, 0x40e00000, v22
	v_mul_f32_e32 v27, 0xbfd9db23, v22
	v_mul_f32_e32 v27, 0x3fb8aa3b, v27
	v_fmamk_f32 v26, v114, 0x3a000000, v2
	v_exp_f32_e32 v27, v27
	v_med3_f32 v26, v26, s74, v203
	v_fmaak_f32 v26, 4.0, v26, 0x40800000
	v_mul_f32_e32 v22, v22, v26
	v_add_f32_e32 v26, 1.0, v27
	v_fmamk_f32 v27, v127, 0x3a000000, v15
	v_min_f32_e32 v27, 0x40e00000, v27
	v_mul_f32_e32 v28, 0xbfd9db23, v27
	v_mul_f32_e32 v28, 0x3fb8aa3b, v28
	v_rcp_f32_e32 v26, v26
	v_exp_f32_e32 v28, v28
	v_mul_f32_e32 v26, v26, v22
	v_fmamk_f32 v22, v119, 0x3a000000, v11
	v_add_f32_e32 v28, 1.0, v28
	v_med3_f32 v22, v22, s74, v203
	v_rcp_f32_e32 v28, v28
	v_fmaak_f32 v22, 4.0, v22, 0x40800000
	v_mul_f32_e32 v22, v27, v22
	v_mul_f32_e32 v27, v28, v22
	v_fmamk_f32 v22, v123, 0x3a000000, v7
	v_min_f32_e32 v28, 0x40e00000, v22
	v_mul_f32_e32 v22, 0xbfd9db23, v28
	v_mul_f32_e32 v22, 0x3fb8aa3b, v22
	v_exp_f32_e32 v22, v22
	s_nop 0
	v_add_f32_e32 v22, 1.0, v22
	v_rcp_f32_e32 v30, v22
	v_mov_b32_e32 v22, 0
	v_cvt_pk_fp8_f32 v22, v19, v23
	v_mov_b32_e32 v23, 0
	v_cvt_pk_fp8_f32 v23, v21, v24
	v_fmamk_f32 v21, v108, 0x3a000000, v12
	v_min_f32_e32 v21, 0x40e00000, v21
	v_mul_f32_e32 v19, 4.0, v29
	v_mul_f32_e32 v24, 0xbfd9db23, v21
	v_mul_f32_e32 v19, v28, v19
	v_mul_f32_e32 v24, 0x3fb8aa3b, v24
	v_mul_f32_e32 v19, v30, v19
	v_exp_f32_e32 v24, v24
	v_cvt_pk_fp8_f32 v23, v26, v19 op_sel:[0,0,1]
	v_fmamk_f32 v19, v100, 0x3a000000, v8
	v_med3_f32 v19, v19, s74, v203
	v_add_f32_e32 v24, 1.0, v24
	v_fmaak_f32 v19, 4.0, v19, 0x40800000
	v_rcp_f32_e32 v24, v24
	v_mul_f32_e32 v19, v21, v19
	v_fmamk_f32 v21, v104, 0x3a000000, v4
	v_min_f32_e32 v21, 0x40e00000, v21
	v_cvt_pk_fp8_f32 v22, v25, v27 op_sel:[0,0,1]
	v_mul_f32_e32 v25, 0xbfd9db23, v21
	v_mul_f32_e32 v25, 0x3fb8aa3b, v25
	v_mul_f32_e32 v19, v24, v19
	v_fmamk_f32 v24, v96, 0x3a000000, v0
	v_exp_f32_e32 v25, v25
	v_med3_f32 v24, v24, s74, v203
	v_fmaak_f32 v24, 4.0, v24, 0x40800000
	v_mul_f32_e32 v21, v21, v24
	v_add_f32_e32 v24, 1.0, v25
	v_fmamk_f32 v25, v109, 0x3a000000, v13
	v_min_f32_e32 v25, 0x40e00000, v25
	v_mul_f32_e32 v26, 0xbfd9db23, v25
	v_mul_f32_e32 v26, 0x3fb8aa3b, v26
	v_rcp_f32_e32 v24, v24
	v_exp_f32_e32 v26, v26
	v_mul_f32_e32 v21, v24, v21
	v_fmamk_f32 v24, v101, 0x3a000000, v9
	v_add_f32_e32 v26, 1.0, v26
	v_med3_f32 v24, v24, s74, v203
	v_rcp_f32_e32 v26, v26
	v_fmaak_f32 v24, 4.0, v24, 0x40800000
	v_mul_f32_e32 v24, v25, v24
	v_mul_f32_e32 v25, v26, v24
	v_fmamk_f32 v24, v105, 0x3a000000, v5
	v_min_f32_e32 v24, 0x40e00000, v24
	v_mul_f32_e32 v27, 0xbfd9db23, v24
	v_mul_f32_e32 v27, 0x3fb8aa3b, v27
	v_fmamk_f32 v26, v97, 0x3a000000, v1
	v_exp_f32_e32 v27, v27
	v_med3_f32 v26, v26, s74, v203
	v_fmaak_f32 v26, 4.0, v26, 0x40800000
	v_mul_f32_e32 v24, v24, v26
	v_add_f32_e32 v26, 1.0, v27
	v_fmamk_f32 v27, v110, 0x3a000000, v14
	v_min_f32_e32 v27, 0x40e00000, v27
	v_mul_f32_e32 v28, 0xbfd9db23, v27
	v_mul_f32_e32 v28, 0x3fb8aa3b, v28
	v_rcp_f32_e32 v26, v26
	v_exp_f32_e32 v28, v28
	v_mul_f32_e32 v26, v26, v24
	v_fmamk_f32 v24, v102, 0x3a000000, v10
	v_add_f32_e32 v28, 1.0, v28
	v_med3_f32 v24, v24, s74, v203
	v_rcp_f32_e32 v28, v28
	v_fmaak_f32 v24, 4.0, v24, 0x40800000
	v_mul_f32_e32 v24, v27, v24
	v_mul_f32_e32 v27, v28, v24
	v_fmamk_f32 v24, v106, 0x3a000000, v6
	v_min_f32_e32 v24, 0x40e00000, v24
	v_mul_f32_e32 v29, 0xbfd9db23, v24
	v_mul_f32_e32 v29, 0x3fb8aa3b, v29
	v_fmamk_f32 v28, v98, 0x3a000000, v2
	v_exp_f32_e32 v29, v29
	v_med3_f32 v28, v28, s74, v203
	v_fmaak_f32 v28, 4.0, v28, 0x40800000
	v_mul_f32_e32 v24, v24, v28
	v_add_f32_e32 v28, 1.0, v29
	v_fmamk_f32 v29, v111, 0x3a000000, v15
	v_min_f32_e32 v29, 0x40e00000, v29
	v_mul_f32_e32 v30, 0xbfd9db23, v29
	v_mul_f32_e32 v30, 0x3fb8aa3b, v30
	v_rcp_f32_e32 v28, v28
	v_exp_f32_e32 v30, v30
	v_mul_f32_e32 v28, v28, v24
	v_fmamk_f32 v24, v103, 0x3a000000, v11
	v_add_f32_e32 v30, 1.0, v30
	v_med3_f32 v24, v24, s74, v203
	v_rcp_f32_e32 v30, v30
	v_fmaak_f32 v24, 4.0, v24, 0x40800000
	v_mul_f32_e32 v24, v29, v24
	v_mul_f32_e32 v29, v30, v24
	v_fmamk_f32 v24, v107, 0x3a000000, v7
	v_min_f32_e32 v30, 0x40e00000, v24
	v_mul_f32_e32 v31, 0xbfd9db23, v30
	v_mul_f32_e32 v31, 0x3fb8aa3b, v31
	v_exp_f32_e32 v31, v31
	v_fmamk_f32 v24, v99, 0x3a000000, v3
	v_med3_f32 v24, v24, s74, v203
	v_add_f32_e32 v24, 1.0, v24
	v_mul_f32_e32 v32, 4.0, v24
	v_add_f32_e32 v24, 1.0, v31
	v_rcp_f32_e32 v31, v24
	v_mov_b32_e32 v24, 0
	v_cvt_pk_fp8_f32 v24, v19, v25
	v_mov_b32_e32 v25, 0
	v_cvt_pk_fp8_f32 v25, v21, v26
	v_mul_f32_e32 v19, v30, v32
	v_mul_f32_e32 v19, v31, v19
	v_cvt_pk_fp8_f32 v24, v27, v29 op_sel:[0,0,1]
	v_cvt_pk_fp8_f32 v25, v28, v19 op_sel:[0,0,1]
	v_fmamk_f32 v19, v92, 0x3a000000, v12
	v_ashrrev_i32_e32 v21, 31, v20
	v_min_f32_e32 v19, 0x40e00000, v19
	v_lshlrev_b64 v[20:21], 10, v[20:21]
	v_mul_f32_e32 v26, 0xbfd9db23, v19
	v_lshl_add_u64 v[20:21], s[12:13], 0, v[20:21]
	v_mul_f32_e32 v26, 0x3fb8aa3b, v26
	v_permlane16_swap_b32_e32 v22, v24
	v_permlane16_swap_b32_e32 v23, v25
	v_lshl_add_u64 v[20:21], v[20:21], 0, v[16:17]
	v_exp_f32_e32 v26, v26
	global_store_dwordx4 v[20:21], v[22:25], off
	v_fmamk_f32 v20, v84, 0x3a000000, v8
	v_med3_f32 v20, v20, s74, v203
	v_add_f32_e32 v21, 1.0, v26
	v_fmaak_f32 v20, 4.0, v20, 0x40800000
	v_rcp_f32_e32 v21, v21
	v_mul_f32_e32 v19, v19, v20
	v_fmamk_f32 v20, v88, 0x3a000000, v4
; __device__ __forceinline__ unsigned pk4_fp8(float a, float b, float c, float d) { int w = __builtin_amdgcn_cvt_pk_fp8_f32(a, b, 0, false); w = __builtin_amdgcn_cvt_pk_fp8_f32(c, d, w, true); return (unsigned)w; }
;     __device__ __forceinline__ void operator()(const f32x4 (&acc)[2][2][4][2], const Unit& u, int wr, int wc, int fr, int fq) const {
;     ...
;                 for (int mi = 0; mi < 2; ++mi) { const int m = 2 * mp + mi;
;                     const f32x4 g0 = acc[ai][0][m][0] * ascale + bg0, g1 = acc[ai][0][m][1] * ascale + bg1, u0 = acc[ai][1][m][0] * ascale + bu0, u1 = acc[ai][1][m][1] * ascale + bu1;
;                     float r[8];
; #pragma unroll
;                     for (int j = 0; j < 4; ++j) {
;                         float gg = fminf(g0[j], 7.f), uu = fminf(fmaxf(u0[j], -7.f), 7.f); r[j] = 4.f * (uu + 1.f) * gg * __builtin_amdgcn_rcpf(1.f + __expf(-1.702f * gg));
;                         gg = fminf(g1[j], 7.f); uu = fminf(fmaxf(u1[j], -7.f), 7.f); r[4 + j] = 4.f * (uu + 1.f) * gg * __builtin_amdgcn_rcpf(1.f + __expf(-1.702f * gg));
;                     }
;                     wq[mi].x = pk4_fp8(r[0], r[1], r[2], r[3]); wq[mi].y = pk4_fp8(r[4], r[5], r[6], r[7]); }
;                 *(u32x4*)(act + (size_t)(row0 + ai * HALF + (2 * mp + (fq & 1)) * 16) * EFF + (c0 - 8 * (fq & 1))) = widen16(wq[0], wq[1]);
	v_min_f32_e32 v20, 0x40e00000, v20
	v_mul_f32_e32 v22, 0xbfd9db23, v20
	v_mul_f32_e32 v22, 0x3fb8aa3b, v22
	v_mul_f32_e32 v19, v21, v19
	v_fmamk_f32 v21, v80, 0x3a000000, v0
	v_exp_f32_e32 v22, v22
	v_med3_f32 v21, v21, s74, v203
	v_fmaak_f32 v21, 4.0, v21, 0x40800000
	v_mul_f32_e32 v20, v20, v21
	v_add_f32_e32 v21, 1.0, v22
	v_fmamk_f32 v22, v93, 0x3a000000, v13
	v_min_f32_e32 v22, 0x40e00000, v22
	v_mul_f32_e32 v23, 0xbfd9db23, v22
	v_mul_f32_e32 v23, 0x3fb8aa3b, v23
	v_rcp_f32_e32 v21, v21
	v_exp_f32_e32 v23, v23
	v_fmamk_f32 v8, v68, 0x3a000000, v8
	v_med3_f32 v8, v8, s74, v203
	v_mul_f32_e32 v24, v21, v20
	v_fmamk_f32 v20, v85, 0x3a000000, v9
	v_add_f32_e32 v21, 1.0, v23
	v_med3_f32 v20, v20, s74, v203
	v_rcp_f32_e32 v21, v21
	v_fmaak_f32 v20, 4.0, v20, 0x40800000
	v_mul_f32_e32 v20, v22, v20
	v_mul_f32_e32 v21, v21, v20
	v_fmamk_f32 v20, v89, 0x3a000000, v5
	v_min_f32_e32 v20, 0x40e00000, v20
	v_mul_f32_e32 v23, 0xbfd9db23, v20
	v_mul_f32_e32 v23, 0x3fb8aa3b, v23
	v_fmamk_f32 v22, v81, 0x3a000000, v1
	v_exp_f32_e32 v23, v23
	v_med3_f32 v22, v22, s74, v203
	v_fmaak_f32 v22, 4.0, v22, 0x40800000
	v_mul_f32_e32 v20, v20, v22
	v_add_f32_e32 v22, 1.0, v23
	v_fmamk_f32 v23, v94, 0x3a000000, v14
	v_min_f32_e32 v23, 0x40e00000, v23
	v_mul_f32_e32 v25, 0xbfd9db23, v23
	v_mul_f32_e32 v25, 0x3fb8aa3b, v25
	v_rcp_f32_e32 v22, v22
	v_exp_f32_e32 v25, v25
	v_fmamk_f32 v12, v76, 0x3a000000, v12
	v_mul_f32_e32 v22, v22, v20
	v_fmamk_f32 v20, v86, 0x3a000000, v10
	v_add_f32_e32 v25, 1.0, v25
	v_med3_f32 v20, v20, s74, v203
	v_rcp_f32_e32 v25, v25
	v_fmaak_f32 v20, 4.0, v20, 0x40800000
	v_mul_f32_e32 v20, v23, v20
	v_mul_f32_e32 v23, v25, v20
	v_fmamk_f32 v20, v90, 0x3a000000, v6
	v_min_f32_e32 v20, 0x40e00000, v20
	v_mul_f32_e32 v26, 0xbfd9db23, v20
	v_mul_f32_e32 v26, 0x3fb8aa3b, v26
	v_fmamk_f32 v25, v82, 0x3a000000, v2
	v_exp_f32_e32 v26, v26
	v_med3_f32 v25, v25, s74, v203
	v_fmaak_f32 v25, 4.0, v25, 0x40800000
	v_mul_f32_e32 v20, v20, v25
	v_add_f32_e32 v25, 1.0, v26
	v_fmamk_f32 v26, v95, 0x3a000000, v15
	v_min_f32_e32 v26, 0x40e00000, v26
	v_mul_f32_e32 v27, 0xbfd9db23, v26
	v_mul_f32_e32 v27, 0x3fb8aa3b, v27
	v_rcp_f32_e32 v25, v25
	v_exp_f32_e32 v27, v27
	v_fmamk_f32 v4, v72, 0x3a000000, v4
	v_min_f32_e32 v12, 0x40e00000, v12
	v_mul_f32_e32 v25, v25, v20
	v_fmamk_f32 v20, v87, 0x3a000000, v11
	v_add_f32_e32 v27, 1.0, v27
	v_med3_f32 v20, v20, s74, v203
	v_rcp_f32_e32 v27, v27
	v_fmaak_f32 v20, 4.0, v20, 0x40800000
	v_mul_f32_e32 v20, v26, v20
	v_mul_f32_e32 v26, v27, v20
	v_fmamk_f32 v20, v91, 0x3a000000, v7
	v_min_f32_e32 v27, 0x40e00000, v20
	v_mul_f32_e32 v20, 0xbfd9db23, v27
	v_mul_f32_e32 v20, 0x3fb8aa3b, v20
	v_exp_f32_e32 v20, v20
	v_fmaak_f32 v8, 4.0, v8, 0x40800000
	v_min_f32_e32 v4, 0x40e00000, v4
	v_mul_f32_e32 v8, v12, v8
	v_add_f32_e32 v20, 1.0, v20
	v_rcp_f32_e32 v29, v20
	v_mov_b32_e32 v20, 0
	v_cvt_pk_fp8_f32 v20, v19, v21
	v_mov_b32_e32 v21, 0
	v_cvt_pk_fp8_f32 v21, v24, v22
	v_mul_f32_e32 v22, 0xbfd9db23, v12
	v_mul_f32_e32 v12, 0xbfd9db23, v4
	v_mul_f32_e32 v12, 0x3fb8aa3b, v12
	v_fmamk_f32 v0, v64, 0x3a000000, v0
	v_exp_f32_e32 v12, v12
	v_med3_f32 v0, v0, s74, v203
	v_fmaak_f32 v0, 4.0, v0, 0x40800000
	v_mul_f32_e32 v0, v4, v0
	v_add_f32_e32 v4, 1.0, v12
	v_fmamk_f32 v12, v77, 0x3a000000, v13
	v_min_f32_e32 v12, 0x40e00000, v12
	v_mul_f32_e32 v13, 0xbfd9db23, v12
	v_mul_f32_e32 v13, 0x3fb8aa3b, v13
	v_rcp_f32_e32 v4, v4
	v_exp_f32_e32 v13, v13
	v_fmamk_f32 v5, v73, 0x3a000000, v5
	v_min_f32_e32 v5, 0x40e00000, v5
	v_mul_f32_e32 v0, v4, v0
	v_fmamk_f32 v4, v69, 0x3a000000, v9
	v_add_f32_e32 v9, 1.0, v13
	v_med3_f32 v4, v4, s74, v203
	v_rcp_f32_e32 v9, v9
	v_fmaak_f32 v4, 4.0, v4, 0x40800000
	v_mul_f32_e32 v4, v12, v4
	v_mul_f32_e32 v4, v9, v4
	v_mul_f32_e32 v9, 0xbfd9db23, v5
	v_mul_f32_e32 v9, 0x3fb8aa3b, v9
	v_fmamk_f32 v1, v65, 0x3a000000, v1
	v_exp_f32_e32 v9, v9
	v_med3_f32 v1, v1, s74, v203
	v_fmaak_f32 v1, 4.0, v1, 0x40800000
	v_mul_f32_e32 v1, v5, v1
	v_add_f32_e32 v5, 1.0, v9
	v_rcp_f32_e32 v5, v5
	v_fmamk_f32 v9, v78, 0x3a000000, v14
	v_fmamk_f32 v6, v74, 0x3a000000, v6
	v_min_f32_e32 v9, 0x40e00000, v9
	v_mul_f32_e32 v1, v5, v1
	v_fmamk_f32 v5, v70, 0x3a000000, v10
	v_med3_f32 v5, v5, s74, v203
	v_fmaak_f32 v5, 4.0, v5, 0x40800000
	v_min_f32_e32 v6, 0x40e00000, v6
	v_mul_f32_e32 v12, 0xbfd9db23, v9
	v_mul_f32_e32 v5, v9, v5
	v_mul_f32_e32 v9, 0xbfd9db23, v6
	v_mul_f32_e32 v9, 0x3fb8aa3b, v9
	v_fmamk_f32 v2, v66, 0x3a000000, v2
	v_exp_f32_e32 v9, v9
	v_med3_f32 v2, v2, s74, v203
	v_mul_f32_e32 v12, 0x3fb8aa3b, v12
	v_exp_f32_e32 v12, v12
	v_fmaak_f32 v2, 4.0, v2, 0x40800000
	v_mul_f32_e32 v2, v6, v2
	v_add_f32_e32 v6, 1.0, v9
	v_rcp_f32_e32 v6, v6
	v_add_f32_e32 v10, 1.0, v12
	v_fmamk_f32 v28, v83, 0x3a000000, v3
	v_rcp_f32_e32 v10, v10
	v_fmac_f32_e32 v11, 0x3a000000, v71
	v_med3_f32 v28, v28, s74, v203
	v_mul_f32_e32 v22, 0x3fb8aa3b, v22
	v_mul_f32_e32 v2, v6, v2
	v_med3_f32 v6, v11, s74, v203
	v_add_f32_e32 v28, 1.0, v28
	v_exp_f32_e32 v22, v22
	v_fmac_f32_e32 v15, 0x3a000000, v79
	v_fmac_f32_e32 v7, 0x3a000000, v75
	v_mul_f32_e32 v19, 4.0, v28
	v_min_f32_e32 v9, 0x40e00000, v15
	v_fmaak_f32 v6, 4.0, v6, 0x40800000
	v_min_f32_e32 v7, 0x40e00000, v7
	v_mul_f32_e32 v19, v27, v19
	v_mul_f32_e32 v5, v10, v5
	v_mul_f32_e32 v10, 0xbfd9db23, v9
	v_mul_f32_e32 v6, v9, v6
	v_mul_f32_e32 v9, 0xbfd9db23, v7
	v_mul_f32_e32 v19, v29, v19
	v_mul_f32_e32 v10, 0x3fb8aa3b, v10
	v_mul_f32_e32 v9, 0x3fb8aa3b, v9
	v_cvt_pk_fp8_f32 v21, v25, v19 op_sel:[0,0,1]
	v_add_f32_e32 v19, 1.0, v22
	v_exp_f32_e32 v10, v10
	v_exp_f32_e32 v9, v9
	v_rcp_f32_e32 v19, v19
	v_fmac_f32_e32 v3, 0x3a000000, v67
	v_add_f32_e32 v10, 1.0, v10
	v_add_f32_e32 v9, 1.0, v9
	v_cvt_pk_fp8_f32 v20, v23, v26 op_sel:[0,0,1]
	v_mul_f32_e32 v8, v19, v8
	v_rcp_f32_e32 v10, v10
	v_med3_f32 v3, v3, s74, v203
	v_rcp_f32_e32 v9, v9
	v_mov_b32_e32 v22, 0
	v_mov_b32_e32 v23, 0
	v_cvt_pk_fp8_f32 v22, v8, v4
	v_cvt_pk_fp8_f32 v23, v0, v1
	v_fmaak_f32 v3, 4.0, v3, 0x40800000
	v_mul_f32_e32 v0, v7, v3
	v_mul_f32_e32 v6, v10, v6
	v_mul_f32_e32 v0, v9, v0
	v_cvt_pk_fp8_f32 v22, v5, v6 op_sel:[0,0,1]
	v_cvt_pk_fp8_f32 v23, v2, v0 op_sel:[0,0,1]
	v_add_u32_e32 v0, 0xa0, v18
	v_ashrrev_i32_e32 v1, 31, v0
	v_lshlrev_b64 v[0:1], 10, v[0:1]
	v_lshl_add_u64 v[0:1], s[12:13], 0, v[0:1]
	v_permlane16_swap_b32_e32 v20, v22
	v_permlane16_swap_b32_e32 v21, v23
	v_lshl_add_u64 v[0:1], v[0:1], 0, v[16:17]
	global_store_dwordx4 v[0:1], v[20:23], off
	s_cbranch_vccnz .LBB0_1419
	s_andn2_b64 vcc, exec, s[14:15]
	s_cbranch_vccnz .LBB0_1418
	s_barrier
	s_branch .LBB0_1418

; #define PG8_WAIT_V(n) asm volatile("s_waitcnt vmcnt(" #n ")" ::: "memory")
; #define PG8_BAR __builtin_amdgcn_s_barrier()
; #define PG8_STAGE_A(b, h, p) do { if constexpr (GATHER) { if ((h) == 0) PG8_STAGE(PG8_SA(b, h), p, vA0); else PG8_STAGE(PG8_SA(b, h), p, vA1); } else PG8_STAGE(PG8_SA(b, h), (p) + ((h) ? hstepA : (size_t)0), voffA); } while (0)
; template <class Epi, class Sched, bool ALIGN_EPI = true, bool SP2 = true, bool FP8 = false, bool GATHER = false>
; __device__ __forceinline__ void gemm_phase(LAS unsigned char* lds, const Dims g, const Sched& S, const Epi& E, const int wv) {
;     ...
;     for (int i = 0; i < 2; ++i) { int R, C; stage_rc(tid * 16 + i * 8192, R, C); const int Rb = Epi::PERM ? ((R & ~31) + perm32(R & 31)) : R;
;         voffA[i] = (unsigned)(R * g.lda + C) * 2u; voffB[i] = (unsigned)(Rb * g.ldb + C) * 2u; }
;     ...
;     if constexpr (SP2) {
;         PG8_STAGE(PG8_SB(0, 0), cB, voffB); PG8_STAGE(PG8_SB(0, 1), cB + hstepB, voffB); PG8_STAGE_A(0, 0, cA); PG8_STAGE_A(0, 1, cA);
;         if (wr == 1) PG8_BAR;
;         PG8_WAIT_V(2); PG8_BAR;
;         PG8_STAGE(PG8_SB(1, 0), cB + kstep, voffB); PG8_STAGE_A(1, 0, cA + kstep); PG8_STAGE(PG8_SB(1, 1), cB + hstepB + kstep, voffB);
;         PG8_WAIT_V(6); PG8_BAR;
.LBB0_1517:
	v_bfe_i32 v2, v152, 27, 1
	s_add_u32 s57, s16, 0x8d200000
	v_lshlrev_b32_e32 v0, 4, v152
	v_lshrrev_b32_e32 v2, 22, v2
	s_addc_u32 s58, s17, 0
	v_add_u32_e32 v2, v0, v2
	s_add_u32 s59, s16, 0x26000000
	v_and_b32_e32 v2, 0xfffffc00, v2
	s_addc_u32 s60, s17, 0
	s_ashr_i32 s39, s38, 31
	v_sub_u32_e32 v2, v0, v2
	s_lshl_b64 s[8:9], s[38:39], 18
	v_ashrrev_i32_e32 v1, 31, v152
	v_lshrrev_b32_e32 v3, 4, v2
	s_add_u32 s44, s57, s8
	v_lshrrev_b32_e32 v1, 26, v1
	v_bitop3_b32 v2, v3, v2, 32 bitop3:0x6c
	s_addc_u32 s45, s58, s9
	s_ashr_i32 s43, s42, 31
	v_add_u32_e32 v1, v152, v1
	v_ashrrev_i32_e32 v4, 31, v2
	s_lshl_b64 s[8:9], s[42:43], 20
	v_ashrrev_i32_e32 v1, 6, v1
	v_lshrrev_b32_e32 v4, 26, v4
	s_add_u32 s10, s59, s8
	v_lshlrev_b32_e32 v3, 3, v1
	v_add_u32_e32 v4, v2, v4
	s_addc_u32 s11, s60, s9
	s_ashr_i32 s41, s40, 31
	v_and_b32_e32 v3, -16, v3
	v_ashrrev_i32_e32 v5, 6, v4
	v_and_b32_e32 v4, 0xc0, v4
	s_lshl_b64 s[8:9], s[40:41], 18
	v_add_u32_e32 v3, v5, v3
	v_sub_u32_e32 v2, v2, v4
	v_mov_b32_e32 v4, 1
	s_add_u32 s46, s10, s8
	v_lshlrev_b32_e32 v1, 5, v1
	v_ashrrev_i16_sdwa v2, v4, sext(v2) dst_sel:DWORD dst_unused:UNUSED_PAD src0_sel:DWORD src1_sel:BYTE_0
	v_lshlrev_b32_e32 v6, 1, v3
	v_lshrrev_b32_e32 v7, 2, v3
	v_and_b32_e32 v5, 3, v5
	s_mov_b32 s8, 0x3fffe0
	v_and_b32_e32 v1, 32, v1
	v_bfe_i32 v2, v2, 0, 16
	v_and_b32_e32 v6, 24, v6
	v_and_b32_e32 v7, 4, v7
	v_and_or_b32 v5, v3, s8, v5
	v_or3_b32 v5, v5, v7, v6
	v_add_lshl_u32 v1, v1, v2, 1
	v_add_u32_e32 v0, 0x2000, v0
	v_lshl_add_u32 v153, v3, 10, v1
	v_lshl_add_u32 v154, v5, 10, v1
	v_ashrrev_i32_e32 v1, 31, v0
	v_lshrrev_b32_e32 v1, 22, v1
	v_add_u32_e32 v1, v0, v1
	v_ashrrev_i32_e32 v1, 10, v1
	v_mul_i32_i24_e32 v2, 0x400, v1
	v_sub_u32_e32 v0, v0, v2
	v_lshrrev_b32_e32 v2, 4, v0
	v_bitop3_b32 v0, v2, v0, 32 bitop3:0x6c
	v_ashrrev_i32_e32 v3, 31, v0
	v_lshrrev_b32_e32 v3, 26, v3
	v_lshlrev_b32_e32 v2, 3, v1
	v_add_u32_e32 v3, v0, v3
	v_and_b32_e32 v2, -16, v2
	v_ashrrev_i32_e32 v5, 6, v3
	v_and_b32_e32 v3, 0xc0, v3
	s_addc_u32 s47, s11, s9
	v_add_u32_e32 v2, v5, v2
	v_sub_u32_e32 v0, v0, v3
	v_and_b32_e32 v5, 3, v5
	s_ashr_i32 s14, s3, 6
	v_lshlrev_b32_e32 v1, 5, v1
	v_ashrrev_i16_sdwa v0, v4, sext(v0) dst_sel:DWORD dst_unused:UNUSED_PAD src0_sel:DWORD src1_sel:BYTE_0
	v_lshlrev_b32_e32 v3, 1, v2
	v_lshrrev_b32_e32 v4, 2, v2
	v_and_or_b32 v5, v2, s8, v5
	s_lshl_b32 s8, s14, 10
	v_and_b32_e32 v1, 32, v1
	v_bfe_i32 v0, v0, 0, 16
	v_and_b32_e32 v3, 24, v3
	v_and_b32_e32 v4, 4, v4
	s_add_i32 s61, s8, 0
	v_or3_b32 v3, v5, v4, v3
	v_add_lshl_u32 v0, v1, v0, 1
	s_add_i32 s62, s61, 0x10000
	s_mov_b32 m0, s62
	s_nop 0
	global_load_lds_dwordx4 v154, s[46:47]
	s_ashr_i32 s13, s3, 8
	v_lshl_add_u32 v156, v3, 10, v0
	s_add_i32 s63, s61, 0x12000
	s_mov_b32 m0, s63
	s_nop 0
	global_load_lds_dwordx4 v156, s[46:47]
	s_add_i32 s64, s61, 0x14000
	s_add_u32 s8, s46, 0x20000
	s_addc_u32 s9, s47, 0
	s_mov_b32 m0, s64
	s_nop 0
	global_load_lds_dwordx4 v154, s[8:9]
	s_add_i32 s65, s61, 0x16000
	s_mov_b32 m0, s65
	s_nop 0
	global_load_lds_dwordx4 v156, s[8:9]
	s_mov_b32 m0, s61
	s_nop 0
	global_load_lds_dwordx4 v153, s[44:45]
	s_add_i32 s66, s61, 0x2000
	s_add_i32 s67, s61, 0x4000
	v_lshl_add_u32 v155, v2, 10, v0
	s_mov_b32 m0, s66
	s_nop 0
	global_load_lds_dwordx4 v155, s[44:45]
	s_add_u32 s10, s44, 0x20000
	s_addc_u32 s11, s45, 0
	s_mov_b32 m0, s67
	s_nop 0
	global_load_lds_dwordx4 v153, s[10:11]
	s_add_i32 s68, s61, 0x6000
	s_mov_b32 m0, s68
	s_nop 0
	global_load_lds_dwordx4 v155, s[10:11]
	s_cmp_eq_u32 s13, 1
	s_mov_b32 s41, 0
	s_cselect_b64 s[8:9], -1, 0
	s_cmp_lg_u32 s13, 1
	s_cbranch_scc1 .LBB0_1519
	s_barrier
.LBB0_1519:
	v_and_b32_e32 v0, 48, v152
	v_lshlrev_b32_e32 v1, 6, v152
	s_movk_i32 s15, 0x3c0
	s_add_u32 s10, s16, 0x9e200000
	v_and_or_b32 v0, v1, s15, v0
	v_lshlrev_b32_e32 v1, 2, v152
	s_addc_u32 s11, s17, 0
	s_lshl_b32 s12, s13, 6
	s_lshl_b32 s13, s13, 13
	v_and_b32_e32 v1, 32, v1
	v_bitop3_b32 v2, v0, s13, v1 bitop3:0xde
	s_lshl_b32 s13, s14, 5
	s_and_b32 s69, s13, 0x60
	s_lshl_b32 s13, s69, 7
	s_add_i32 s70, s61, 0x18000
	s_add_u32 s14, s46, 0x80
	v_bitop3_b32 v0, s13, v0, v1 bitop3:0xf6
	s_waitcnt vmcnt(2)
	s_barrier
	s_addc_u32 s15, s47, 0
	s_mov_b32 m0, s70
	s_nop 0
	global_load_lds_dwordx4 v154, s[14:15]
	s_add_i32 s71, s61, 0x1a000
	s_add_i32 s72, s61, 0x8000
	s_mov_b32 m0, s71
	s_nop 0
	global_load_lds_dwordx4 v156, s[14:15]
	s_add_u32 s14, s44, 0x80
	s_addc_u32 s15, s45, 0
	s_mov_b32 m0, s72
	s_nop 0
	global_load_lds_dwordx4 v153, s[14:15]
	s_add_i32 s73, s61, 0xa000
	s_add_i32 s74, s61, 0x1c000
	s_mov_b32 m0, s73
	s_nop 0
	global_load_lds_dwordx4 v155, s[14:15]
	s_add_u32 s14, s46, 0x20080
	s_addc_u32 s15, s47, 0
	s_mov_b32 m0, s74
	s_nop 0
	global_load_lds_dwordx4 v154, s[14:15]
	s_add_i32 s75, s61, 0x1e000
	s_add_i32 s76, s61, 0xc000
	s_mov_b32 m0, s75
	s_nop 0
	global_load_lds_dwordx4 v156, s[14:15]
	s_cmpk_lt_u32 s3, 0x100
	s_cselect_b64 s[14:15], -1, 0
	s_ashr_i32 s13, s12, 31
	s_add_i32 s77, s61, 0xe000
	s_lshl_b64 s[22:23], s[12:13], 2
	s_add_u32 s3, s16, s22
	s_addc_u32 s16, s17, s23
	s_add_u32 s13, s3, 0x7c100000
	s_waitcnt vmcnt(6)
	s_addc_u32 s17, s16, 0
	s_lshl_b32 s16, s33, 3
	s_and_b32 s16, s16, 56
	s_bfe_u32 s20, s33, 0x30003
	v_add_u32_e32 v0, 0, v0
	s_ashr_i32 s78, s56, 31
	s_ashr_i32 s79, s33, 31
	s_ashr_i32 s3, s2, 31
	s_or_b32 s80, s20, s16
	s_ashr_i32 s81, s33, 6
	v_add_u32_e32 v157, 0x10000, v0
	v_add_u32_e32 v158, 0x14000, v0
	v_add_u32_e32 v159, 0, v2
	v_mov_b32_e32 v160, 0x7f7f7f7f
	v_add_u32_e32 v161, 0x18000, v0
	v_add_u32_e32 v162, 0x1c000, v0
	s_mov_b32 s16, 0x42000000
	s_mov_b32 s20, 0x3b000000
	s_mov_b32 s82, 0xc3e00000
	v_mov_b32_e32 v163, 0x43e00000
	s_barrier
	s_branch .LBB0_1522

; #define PG8_WAIT_V(n) asm volatile("s_waitcnt vmcnt(" #n ")" ::: "memory")
; #define PG8_WAIT_L(n) asm volatile("s_waitcnt lgkmcnt(" #n ")" ::: "memory")
; #define PG8_BAR __builtin_amdgcn_s_barrier()
; #define PG8_SCHED __builtin_amdgcn_sched_barrier(0)
; #define PG8_STAGE_A(b, h, p) do { if constexpr (GATHER) { if ((h) == 0) PG8_STAGE(PG8_SA(b, h), p, vA0); else PG8_STAGE(PG8_SA(b, h), p, vA1); } else PG8_STAGE(PG8_SA(b, h), (p) + ((h) ? hstepA : (size_t)0), voffA); } while (0)
; #define PG8_GOFF1(un, h, d) do { int tz_ = tid; asm volatile("" : "+v"(tz_)); _Pragma("unroll") for (int i_ = 0; i_ < 2; ++i_) { int R_, C_; stage_rc(tz_ * 16 + i_ * 8192, R_, C_); \
;         d[i_] = S.gather(un, R_ + (h) * HALF) + (unsigned)C_ * 2u; } } while (0)
; template <class Epi, class Sched, bool ALIGN_EPI = true, bool SP2 = true, bool FP8 = false, bool GATHER = false>
; __device__ __forceinline__ void gemm_phase(LAS unsigned char* lds, const Dims g, const Sched& S, const Epi& E, const int wv) {
;     ...
;         for (int t = 0; t < nt; t += 2) {
;             const bool last = (t == nt - 2);
;             const char* a1 = cA + (size_t)(t + 1) * kstep;
;             const char* a2 = last ? nA : cA + (size_t)(t + 2) * kstep; const char* b2 = last ? nB : cB + (size_t)(t + 2) * kstep;
;             const char* a3 = a2 + kstep; const char* b3 = b2 + kstep;
;             if constexpr (SP2) {
;             if constexpr (GATHER) { if (last) PG8_GOFF1(un_, 0, vA0); }
;             PG8_LDB(B0, 0, 0); PG8_LDB(B1, 0, 1); PG8_SCHED; PG8_LDA(At, 0, 0); PG8_STAGE_A(1, 1, a1);
;             if constexpr (GATHER) { if (last) PG8_GOFF1(un_, 1, vA1); }
;             PG8_WAIT_V(8); PG8_WAIT_L(0); PG8_BAR; PG8_MMA(0, 0, At, B0); PG8_MMA(0, 1, At, B1); PG8_BAR; PG8_SCHED;
;             PG8_LDA(At, 0, 1); PG8_STAGE(PG8_SB(0, 0), b2, voffB); PG8_STAGE(PG8_SB(0, 1), b2 + hstepB, voffB); PG8_STAGE_A(0, 0, a2);
;             PG8_WAIT_V(8); PG8_WAIT_L(0); PG8_BAR; PG8_MMA(1, 0, At, B0); PG8_MMA(1, 1, At, B1); PG8_BAR; PG8_SCHED;
.LBB0_1528:
	ds_read_b128 v[128:131], v157
	ds_read_b128 v[132:135], v157 offset:1024
	ds_read_b128 v[136:139], v157 offset:2048
	ds_read_b128 v[140:143], v157 offset:3072
	ds_read_b128 v[144:147], v158
	ds_read_b128 v[148:151], v158 offset:1024
	ds_read_b128 v[164:167], v158 offset:2048
	ds_read_b128 v[168:171], v158 offset:3072
	s_add_u32 s46, s44, 0x100
	s_addc_u32 s47, s45, 0
	s_cmp_eq_u32 s86, 4
	s_cselect_b32 s52, s43, s46
	s_cselect_b32 s53, s39, s47
	s_cselect_b32 s50, s55, s84
	s_cselect_b32 s51, s54, s85
	s_add_u32 s48, s52, 0x80
	s_addc_u32 s49, s53, 0
	ds_read_b128 v[172:175], v159
	ds_read_b128 v[176:179], v159 offset:1024
	ds_read_b128 v[180:183], v159 offset:2048
	ds_read_b128 v[184:187], v159 offset:3072
	ds_read_b128 v[188:191], v159 offset:4096
	ds_read_b128 v[192:195], v159 offset:5120
	ds_read_b128 v[196:199], v159 offset:6144
	ds_read_b128 v[200:203], v159 offset:7168
	s_add_u32 s44, s44, 0x20080
	s_addc_u32 s45, s45, 0
	s_mov_b32 m0, s76
	s_nop 0
	global_load_lds_dwordx4 v153, s[44:45]
	s_nop 0
	s_mov_b32 m0, s77
	s_nop 0
	global_load_lds_dwordx4 v155, s[44:45]
	s_waitcnt vmcnt(8)
	s_waitcnt lgkmcnt(0)
	s_barrier
	s_setprio 1
	s_waitcnt lgkmcnt(0)
	v_mfma_scale_f32_16x16x128_f8f6f4 v[124:127], v[128:135], v[172:179], v[124:127], v160, v160 op_sel_hi:[0,0,0]
	v_mfma_scale_f32_16x16x128_f8f6f4 v[120:123], v[136:143], v[172:179], v[120:123], v160, v160 op_sel_hi:[0,0,0]
	v_mfma_scale_f32_16x16x128_f8f6f4 v[116:119], v[128:135], v[180:187], v[116:119], v160, v160 op_sel_hi:[0,0,0]
	v_mfma_scale_f32_16x16x128_f8f6f4 v[112:115], v[136:143], v[180:187], v[112:115], v160, v160 op_sel_hi:[0,0,0]
	v_mfma_scale_f32_16x16x128_f8f6f4 v[204:207], v[128:135], v[188:195], v[92:95], v160, v160 op_sel_hi:[0,0,0]
	v_mfma_scale_f32_16x16x128_f8f6f4 v[208:211], v[136:143], v[188:195], v[88:91], v160, v160 op_sel_hi:[0,0,0]
	v_mfma_scale_f32_16x16x128_f8f6f4 v[212:215], v[128:135], v[196:203], v[76:79], v160, v160 op_sel_hi:[0,0,0]
	v_mfma_scale_f32_16x16x128_f8f6f4 v[216:219], v[136:143], v[196:203], v[72:75], v160, v160 op_sel_hi:[0,0,0]
	s_setprio 0
	s_setprio 1
	v_mfma_scale_f32_16x16x128_f8f6f4 v[108:111], v[144:151], v[172:179], v[108:111], v160, v160 op_sel_hi:[0,0,0]
	v_mfma_scale_f32_16x16x128_f8f6f4 v[104:107], v[164:171], v[172:179], v[104:107], v160, v160 op_sel_hi:[0,0,0]
	v_mfma_scale_f32_16x16x128_f8f6f4 v[100:103], v[144:151], v[180:187], v[100:103], v160, v160 op_sel_hi:[0,0,0]
	v_mfma_scale_f32_16x16x128_f8f6f4 v[96:99], v[164:171], v[180:187], v[96:99], v160, v160 op_sel_hi:[0,0,0]
	v_mfma_scale_f32_16x16x128_f8f6f4 v[172:175], v[144:151], v[188:195], v[84:87], v160, v160 op_sel_hi:[0,0,0]
	v_mfma_scale_f32_16x16x128_f8f6f4 v[176:179], v[164:171], v[188:195], v[80:83], v160, v160 op_sel_hi:[0,0,0]
	v_mfma_scale_f32_16x16x128_f8f6f4 v[180:183], v[144:151], v[196:203], v[68:71], v160, v160 op_sel_hi:[0,0,0]
	v_mfma_scale_f32_16x16x128_f8f6f4 v[184:187], v[164:171], v[196:203], v[64:67], v160, v160 op_sel_hi:[0,0,0]
	s_setprio 0
	s_barrier
	s_nop 4
	ds_read_b128 v[64:67], v159 offset:16384
	ds_read_b128 v[68:71], v159 offset:17408
	ds_read_b128 v[72:75], v159 offset:18432
	ds_read_b128 v[76:79], v159 offset:19456
	ds_read_b128 v[80:83], v159 offset:20480
	ds_read_b128 v[84:87], v159 offset:21504
	ds_read_b128 v[88:91], v159 offset:22528
	ds_read_b128 v[92:95], v159 offset:23552
	s_mov_b32 m0, s62
	s_nop 0
	global_load_lds_dwordx4 v154, s[50:51]
	s_nop 0
	s_mov_b32 m0, s63
	s_nop 0
	global_load_lds_dwordx4 v156, s[50:51]
	s_add_u32 s44, s50, 0x20000
	s_addc_u32 s45, s51, 0
	s_mov_b32 m0, s64
	s_nop 0
	global_load_lds_dwordx4 v154, s[44:45]
	s_nop 0
	s_mov_b32 m0, s65
	s_nop 0
	global_load_lds_dwordx4 v156, s[44:45]
	s_mov_b32 m0, s61
	s_nop 0
	global_load_lds_dwordx4 v153, s[52:53]
	s_nop 0
	s_mov_b32 m0, s66
	s_nop 0
	global_load_lds_dwordx4 v155, s[52:53]
	s_waitcnt vmcnt(8)
	s_waitcnt lgkmcnt(0)
	s_barrier
	s_setprio 1
	s_waitcnt lgkmcnt(6)
	v_mfma_scale_f32_16x16x128_f8f6f4 v[60:63], v[128:135], v[64:71], v[60:63], v160, v160 op_sel_hi:[0,0,0]
	v_mfma_scale_f32_16x16x128_f8f6f4 v[56:59], v[136:143], v[64:71], v[56:59], v160, v160 op_sel_hi:[0,0,0]
	s_waitcnt lgkmcnt(4)
	v_mfma_scale_f32_16x16x128_f8f6f4 v[188:191], v[128:135], v[72:79], v[44:47], v160, v160 op_sel_hi:[0,0,0]
	v_mfma_scale_f32_16x16x128_f8f6f4 v[192:195], v[136:143], v[72:79], v[40:43], v160, v160 op_sel_hi:[0,0,0]
	s_waitcnt lgkmcnt(2)
	v_mfma_scale_f32_16x16x128_f8f6f4 v[196:199], v[128:135], v[80:87], v[28:31], v160, v160 op_sel_hi:[0,0,0]
	v_mfma_scale_f32_16x16x128_f8f6f4 v[200:203], v[136:143], v[80:87], v[24:27], v160, v160 op_sel_hi:[0,0,0]
	s_waitcnt lgkmcnt(0)
	v_mfma_scale_f32_16x16x128_f8f6f4 v[220:223], v[128:135], v[88:95], v[12:15], v160, v160 op_sel_hi:[0,0,0]
	v_mfma_scale_f32_16x16x128_f8f6f4 v[224:227], v[136:143], v[88:95], v[8:11], v160, v160 op_sel_hi:[0,0,0]
	s_setprio 0
	s_setprio 1
	v_mfma_scale_f32_16x16x128_f8f6f4 v[52:55], v[144:151], v[64:71], v[52:55], v160, v160 op_sel_hi:[0,0,0]
	v_mfma_scale_f32_16x16x128_f8f6f4 v[48:51], v[164:171], v[64:71], v[48:51], v160, v160 op_sel_hi:[0,0,0]
	v_mfma_scale_f32_16x16x128_f8f6f4 v[228:231], v[144:151], v[72:79], v[36:39], v160, v160 op_sel_hi:[0,0,0]
	v_mfma_scale_f32_16x16x128_f8f6f4 v[232:235], v[164:171], v[72:79], v[32:35], v160, v160 op_sel_hi:[0,0,0]
	v_mfma_scale_f32_16x16x128_f8f6f4 v[236:239], v[144:151], v[80:87], v[20:23], v160, v160 op_sel_hi:[0,0,0]
	v_mfma_scale_f32_16x16x128_f8f6f4 v[240:243], v[164:171], v[80:87], v[16:19], v160, v160 op_sel_hi:[0,0,0]
	v_mfma_scale_f32_16x16x128_f8f6f4 v[244:247], v[144:151], v[88:95], v[4:7], v160, v160 op_sel_hi:[0,0,0]
	v_mfma_scale_f32_16x16x128_f8f6f4 v[248:251], v[164:171], v[88:95], v[0:3], v160, v160 op_sel_hi:[0,0,0]
	s_setprio 0
	s_barrier
; #define PG8_WAIT_V(n) asm volatile("s_waitcnt vmcnt(" #n ")" ::: "memory")
; #define PG8_WAIT_L(n) asm volatile("s_waitcnt lgkmcnt(" #n ")" ::: "memory")
; #define PG8_BAR __builtin_amdgcn_s_barrier()
; #define PG8_SCHED __builtin_amdgcn_sched_barrier(0)
; #define PG8_STAGE_A(b, h, p) do { if constexpr (GATHER) { if ((h) == 0) PG8_STAGE(PG8_SA(b, h), p, vA0); else PG8_STAGE(PG8_SA(b, h), p, vA1); } else PG8_STAGE(PG8_SA(b, h), (p) + ((h) ? hstepA : (size_t)0), voffA); } while (0)
; template <class Epi, class Sched, bool ALIGN_EPI = true, bool SP2 = true, bool FP8 = false, bool GATHER = false>
; __device__ __forceinline__ void gemm_phase(LAS unsigned char* lds, const Dims g, const Sched& S, const Epi& E, const int wv) {
;     ...
;             PG8_LDB(B0, 1, 0); PG8_LDB(B1, 1, 1); PG8_SCHED; PG8_LDA(At, 1, 0); PG8_STAGE_A(0, 1, a2);
;             PG8_WAIT_V(8); PG8_WAIT_L(0); PG8_BAR; PG8_MMA(0, 0, At, B0); PG8_MMA(0, 1, At, B1); PG8_BAR; PG8_SCHED;
;             PG8_LDA(At, 1, 1); PG8_STAGE(PG8_SB(1, 0), b3, voffB); PG8_STAGE(PG8_SB(1, 1), b3 + hstepB, voffB); PG8_STAGE_A(1, 0, a3);
;             PG8_WAIT_V(8); PG8_WAIT_L(0); PG8_BAR; PG8_MMA(1, 0, At, B0); PG8_MMA(1, 1, At, B1); PG8_BAR; PG8_SCHED;
	s_nop 4
	ds_read_b128 v[0:3], v161
	ds_read_b128 v[4:7], v161 offset:1024
	ds_read_b128 v[16:19], v161 offset:2048
	ds_read_b128 v[20:23], v161 offset:3072
	ds_read_b128 v[128:131], v162
	ds_read_b128 v[132:135], v162 offset:1024
	ds_read_b128 v[136:139], v162 offset:2048
	ds_read_b128 v[140:143], v162 offset:3072
	ds_read_b128 v[8:11], v159 offset:32768
	ds_read_b128 v[12:15], v159 offset:33792
	ds_read_b128 v[24:27], v159 offset:34816
	ds_read_b128 v[28:31], v159 offset:35840
	ds_read_b128 v[32:35], v159 offset:36864
	ds_read_b128 v[36:39], v159 offset:37888
	ds_read_b128 v[40:43], v159 offset:38912
	ds_read_b128 v[44:47], v159 offset:39936
	s_add_u32 s44, s52, 0x20000
	s_addc_u32 s45, s53, 0
	s_mov_b32 m0, s67
	s_nop 0
	global_load_lds_dwordx4 v153, s[44:45]
	s_nop 0
	s_mov_b32 m0, s68
	s_nop 0
	global_load_lds_dwordx4 v155, s[44:45]
	s_waitcnt vmcnt(8)
	s_waitcnt lgkmcnt(0)
	s_barrier
	s_setprio 1
	s_waitcnt lgkmcnt(6)
	v_mfma_scale_f32_16x16x128_f8f6f4 v[124:127], v[0:7], v[8:15], v[124:127], v160, v160 op_sel_hi:[0,0,0]
	v_mfma_scale_f32_16x16x128_f8f6f4 v[120:123], v[16:23], v[8:15], v[120:123], v160, v160 op_sel_hi:[0,0,0]
	s_waitcnt lgkmcnt(4)
	v_mfma_scale_f32_16x16x128_f8f6f4 v[116:119], v[0:7], v[24:31], v[116:119], v160, v160 op_sel_hi:[0,0,0]
	v_mfma_scale_f32_16x16x128_f8f6f4 v[112:115], v[16:23], v[24:31], v[112:115], v160, v160 op_sel_hi:[0,0,0]
	s_waitcnt lgkmcnt(2)
	v_mfma_scale_f32_16x16x128_f8f6f4 v[92:95], v[0:7], v[32:39], v[204:207], v160, v160 op_sel_hi:[0,0,0]
	v_mfma_scale_f32_16x16x128_f8f6f4 v[88:91], v[16:23], v[32:39], v[208:211], v160, v160 op_sel_hi:[0,0,0]
	s_waitcnt lgkmcnt(0)
	v_mfma_scale_f32_16x16x128_f8f6f4 v[76:79], v[0:7], v[40:47], v[212:215], v160, v160 op_sel_hi:[0,0,0]
	v_mfma_scale_f32_16x16x128_f8f6f4 v[72:75], v[16:23], v[40:47], v[216:219], v160, v160 op_sel_hi:[0,0,0]
	s_setprio 0
	s_setprio 1
	v_mfma_scale_f32_16x16x128_f8f6f4 v[108:111], v[128:135], v[8:15], v[108:111], v160, v160 op_sel_hi:[0,0,0]
	v_mfma_scale_f32_16x16x128_f8f6f4 v[104:107], v[136:143], v[8:15], v[104:107], v160, v160 op_sel_hi:[0,0,0]
	v_mfma_scale_f32_16x16x128_f8f6f4 v[100:103], v[128:135], v[24:31], v[100:103], v160, v160 op_sel_hi:[0,0,0]
	v_mfma_scale_f32_16x16x128_f8f6f4 v[96:99], v[136:143], v[24:31], v[96:99], v160, v160 op_sel_hi:[0,0,0]
	v_mfma_scale_f32_16x16x128_f8f6f4 v[84:87], v[128:135], v[32:39], v[172:175], v160, v160 op_sel_hi:[0,0,0]
	v_mfma_scale_f32_16x16x128_f8f6f4 v[80:83], v[136:143], v[32:39], v[176:179], v160, v160 op_sel_hi:[0,0,0]
	v_mfma_scale_f32_16x16x128_f8f6f4 v[68:71], v[128:135], v[40:47], v[180:183], v160, v160 op_sel_hi:[0,0,0]
	v_mfma_scale_f32_16x16x128_f8f6f4 v[64:67], v[136:143], v[40:47], v[184:187], v160, v160 op_sel_hi:[0,0,0]
	s_setprio 0
	s_barrier
	ds_read_b128 v[32:35], v159 offset:49152
	ds_read_b128 v[36:39], v159 offset:50176
	ds_read_b128 v[144:147], v159 offset:51200
	ds_read_b128 v[148:151], v159 offset:52224
	ds_read_b128 v[164:167], v159 offset:53248
	ds_read_b128 v[168:171], v159 offset:54272
	ds_read_b128 v[172:175], v159 offset:55296
	ds_read_b128 v[176:179], v159 offset:56320
	s_add_u32 s44, s50, 0x80
	s_addc_u32 s45, s51, 0
	s_mov_b32 m0, s70
	s_nop 0
	global_load_lds_dwordx4 v154, s[44:45]
	s_nop 0
	s_mov_b32 m0, s71
	s_nop 0
	global_load_lds_dwordx4 v156, s[44:45]
	s_add_u32 s44, s50, 0x20080
	s_addc_u32 s45, s51, 0
	s_mov_b32 m0, s74
	s_nop 0
	global_load_lds_dwordx4 v154, s[44:45]
	s_nop 0
	s_mov_b32 m0, s75
	s_nop 0
	global_load_lds_dwordx4 v156, s[44:45]
	s_mov_b32 m0, s72
	s_nop 0
	global_load_lds_dwordx4 v153, s[48:49]
	s_nop 0
	s_mov_b32 m0, s73
	s_nop 0
	global_load_lds_dwordx4 v155, s[48:49]
	s_waitcnt vmcnt(8)
	s_waitcnt lgkmcnt(0)
	s_barrier
	s_setprio 1
	s_waitcnt lgkmcnt(6)
	v_mfma_scale_f32_16x16x128_f8f6f4 v[60:63], v[0:7], v[32:39], v[60:63], v160, v160 op_sel_hi:[0,0,0]
	v_mfma_scale_f32_16x16x128_f8f6f4 v[56:59], v[16:23], v[32:39], v[56:59], v160, v160 op_sel_hi:[0,0,0]
	s_waitcnt lgkmcnt(4)
	v_mfma_scale_f32_16x16x128_f8f6f4 v[44:47], v[0:7], v[144:151], v[188:191], v160, v160 op_sel_hi:[0,0,0]
	v_mfma_scale_f32_16x16x128_f8f6f4 v[40:43], v[16:23], v[144:151], v[192:195], v160, v160 op_sel_hi:[0,0,0]
	s_waitcnt lgkmcnt(2)
	v_mfma_scale_f32_16x16x128_f8f6f4 v[28:31], v[0:7], v[164:171], v[196:199], v160, v160 op_sel_hi:[0,0,0]
	v_mfma_scale_f32_16x16x128_f8f6f4 v[24:27], v[16:23], v[164:171], v[200:203], v160, v160 op_sel_hi:[0,0,0]
	s_waitcnt lgkmcnt(0)
	v_mfma_scale_f32_16x16x128_f8f6f4 v[12:15], v[0:7], v[172:179], v[220:223], v160, v160 op_sel_hi:[0,0,0]
	v_mfma_scale_f32_16x16x128_f8f6f4 v[8:11], v[16:23], v[172:179], v[224:227], v160, v160 op_sel_hi:[0,0,0]
	s_setprio 0
	s_setprio 1
	v_mfma_scale_f32_16x16x128_f8f6f4 v[52:55], v[128:135], v[32:39], v[52:55], v160, v160 op_sel_hi:[0,0,0]
	v_mfma_scale_f32_16x16x128_f8f6f4 v[48:51], v[136:143], v[32:39], v[48:51], v160, v160 op_sel_hi:[0,0,0]
	v_mfma_scale_f32_16x16x128_f8f6f4 v[36:39], v[128:135], v[144:151], v[228:231], v160, v160 op_sel_hi:[0,0,0]
	v_mfma_scale_f32_16x16x128_f8f6f4 v[32:35], v[136:143], v[144:151], v[232:235], v160, v160 op_sel_hi:[0,0,0]
	v_mfma_scale_f32_16x16x128_f8f6f4 v[20:23], v[128:135], v[164:171], v[236:239], v160, v160 op_sel_hi:[0,0,0]
	v_mfma_scale_f32_16x16x128_f8f6f4 v[16:19], v[136:143], v[164:171], v[240:243], v160, v160 op_sel_hi:[0,0,0]
	v_mfma_scale_f32_16x16x128_f8f6f4 v[4:7], v[128:135], v[172:179], v[244:247], v160, v160 op_sel_hi:[0,0,0]
	v_mfma_scale_f32_16x16x128_f8f6f4 v[0:3], v[136:143], v[172:179], v[248:251], v160, v160 op_sel_hi:[0,0,0]
	s_setprio 0
	s_barrier
	s_add_i32 s86, s86, 2
	s_add_u32 s84, s84, 0x100
	s_addc_u32 s85, s85, 0
	s_cmp_gt_u32 s86, 5
	s_mov_b64 s[44:45], s[46:47]
	s_cbranch_scc0 .LBB0_1528
	s_and_b64 vcc, exec, s[14:15]
	s_cbranch_vccz .LBB0_1531
	s_barrier

; #define PG8_WAIT_V(n) asm volatile("s_waitcnt vmcnt(" #n ")" ::: "memory")
; #define PG8_BAR __builtin_amdgcn_s_barrier()
; #define PG8_STAGE_A(b, h, p) do { if constexpr (GATHER) { if ((h) == 0) PG8_STAGE(PG8_SA(b, h), p, vA0); else PG8_STAGE(PG8_SA(b, h), p, vA1); } else PG8_STAGE(PG8_SA(b, h), (p) + ((h) ? hstepA : (size_t)0), voffA); } while (0)
; template <class Epi, class Sched, bool ALIGN_EPI = true, bool SP2 = true, bool FP8 = false, bool GATHER = false>
; __device__ __forceinline__ void gemm_phase(LAS unsigned char* lds, const Dims g, const Sched& S, const Epi& E, const int wv) {
;     ...
;     for (int i = 0; i < 2; ++i) { int R, C; stage_rc(tid * 16 + i * 8192, R, C); const int Rb = Epi::PERM ? ((R & ~31) + perm32(R & 31)) : R;
;         voffA[i] = (unsigned)(R * g.lda + C) * 2u; voffB[i] = (unsigned)(Rb * g.ldb + C) * 2u; }
;     ...
;     if constexpr (SP2) {
;         PG8_STAGE(PG8_SB(0, 0), cB, voffB); PG8_STAGE(PG8_SB(0, 1), cB + hstepB, voffB); PG8_STAGE_A(0, 0, cA); PG8_STAGE_A(0, 1, cA);
;         if (wr == 1) PG8_BAR;
;         PG8_WAIT_V(2); PG8_BAR;
;         PG8_STAGE(PG8_SB(1, 0), cB + kstep, voffB); PG8_STAGE_A(1, 0, cA + kstep); PG8_STAGE(PG8_SB(1, 1), cB + hstepB + kstep, voffB);
;         PG8_WAIT_V(6); PG8_BAR;
.LBB0_1662:
	v_bfe_i32 v2, v254, 27, 1
	v_lshlrev_b32_e32 v0, 4, v254
	v_lshrrev_b32_e32 v2, 22, v2
	v_add_u32_e32 v2, v0, v2
	v_and_b32_e32 v2, 0xfffffc00, v2
	v_sub_u32_e32 v2, v0, v2
	v_ashrrev_i32_e32 v1, 31, v254
	v_lshrrev_b32_e32 v3, 4, v2
	v_lshrrev_b32_e32 v1, 26, v1
	v_bitop3_b32 v2, v3, v2, 32 bitop3:0x6c
	v_add_u32_e32 v1, v254, v1
	v_ashrrev_i32_e32 v4, 31, v2
	v_ashrrev_i32_e32 v1, 6, v1
	v_lshrrev_b32_e32 v4, 26, v4
	v_lshlrev_b32_e32 v3, 3, v1
	v_add_u32_e32 v4, v2, v4
	v_and_b32_e32 v3, -16, v3
	v_ashrrev_i32_e32 v5, 6, v4
	v_and_b32_e32 v4, 0xc0, v4
	v_add_u32_e32 v3, v5, v3
	v_sub_u32_e32 v2, v2, v4
	v_mov_b32_e32 v4, 1
	v_lshlrev_b32_e32 v1, 5, v1
	v_ashrrev_i16_sdwa v2, v4, sext(v2) dst_sel:DWORD dst_unused:UNUSED_PAD src0_sel:DWORD src1_sel:BYTE_0
	v_lshlrev_b32_e32 v6, 1, v3
	v_lshrrev_b32_e32 v7, 2, v3
	v_and_b32_e32 v5, 3, v5
	s_mov_b32 s6, 0x3fffe0
	v_and_b32_e32 v1, 32, v1
	v_bfe_i32 v2, v2, 0, 16
	v_and_b32_e32 v6, 24, v6
	v_and_b32_e32 v7, 4, v7
	v_and_or_b32 v5, v3, s6, v5
	v_or3_b32 v5, v5, v7, v6
	v_add_lshl_u32 v1, v1, v2, 1
	v_add_u32_e32 v0, 0x2000, v0
	v_lshl_add_u32 v255, v3, 10, v1
	v_lshl_add_u32 v142, v5, 10, v1
	v_ashrrev_i32_e32 v1, 31, v0
	v_lshrrev_b32_e32 v1, 22, v1
	v_add_u32_e32 v1, v0, v1
	v_ashrrev_i32_e32 v1, 10, v1
	v_mul_i32_i24_e32 v2, 0x400, v1
	v_sub_u32_e32 v0, v0, v2
	v_lshrrev_b32_e32 v2, 4, v0
	v_bitop3_b32 v0, v2, v0, 32 bitop3:0x6c
	v_ashrrev_i32_e32 v3, 31, v0
	v_lshrrev_b32_e32 v3, 26, v3
	v_lshlrev_b32_e32 v2, 3, v1
	v_add_u32_e32 v3, v0, v3
	v_and_b32_e32 v2, -16, v2
	v_ashrrev_i32_e32 v5, 6, v3
	v_add_u32_e32 v2, v5, v2
	v_and_b32_e32 v3, 0xc0, v3
	v_and_b32_e32 v5, 3, v5
	v_sub_u32_e32 v0, v0, v3
	v_and_or_b32 v5, v2, s6, v5
	s_ashr_i32 s6, s15, 6
	v_lshlrev_b32_e32 v1, 5, v1
	v_ashrrev_i16_sdwa v0, v4, sext(v0) dst_sel:DWORD dst_unused:UNUSED_PAD src0_sel:DWORD src1_sel:BYTE_0
	v_lshlrev_b32_e32 v3, 1, v2
	v_lshrrev_b32_e32 v4, 2, v2
	s_lshl_b32 s8, s6, 10
	v_and_b32_e32 v1, 32, v1
	v_bfe_i32 v0, v0, 0, 16
	v_and_b32_e32 v3, 24, v3
	v_and_b32_e32 v4, 4, v4
	s_add_i32 s56, s8, 0
	v_or3_b32 v3, v5, v4, v3
	v_add_lshl_u32 v0, v1, v0, 1
	s_add_i32 s57, s56, 0x10000
	s_mov_b32 m0, s57
	s_nop 0
	global_load_lds_dwordx4 v142, s[42:43]
	s_ashr_i32 s5, s15, 8
	v_lshl_add_u32 v144, v3, 10, v0
	s_add_i32 s58, s56, 0x12000
	s_mov_b32 m0, s58
	s_nop 0
	global_load_lds_dwordx4 v144, s[42:43]
	s_add_i32 s59, s56, 0x14000
	s_add_u32 s8, s42, 0x20000
	s_addc_u32 s9, s43, 0
	s_mov_b32 m0, s59
	s_nop 0
	global_load_lds_dwordx4 v142, s[8:9]
	s_add_i32 s60, s56, 0x16000
	s_mov_b32 m0, s60
	s_nop 0
	global_load_lds_dwordx4 v144, s[8:9]
	s_mov_b32 m0, s56
	s_nop 0
	global_load_lds_dwordx4 v255, s[40:41]
	s_add_i32 s61, s56, 0x2000
	s_add_i32 s62, s56, 0x4000
	v_lshl_add_u32 v143, v2, 10, v0
	s_mov_b32 m0, s61
	s_nop 0
	global_load_lds_dwordx4 v143, s[40:41]
	s_add_u32 s10, s40, 0x20000
	s_addc_u32 s11, s41, 0
	s_mov_b32 m0, s62
	s_nop 0
	global_load_lds_dwordx4 v255, s[10:11]
	s_add_i32 s63, s56, 0x6000
	s_mov_b32 m0, s63
	s_nop 0
	global_load_lds_dwordx4 v143, s[10:11]
	s_cmp_eq_u32 s5, 1
	s_mov_b32 s7, 0
	s_cselect_b64 s[8:9], -1, 0
	s_cmp_lg_u32 s5, 1
	s_cbranch_scc1 .LBB0_1664
	s_barrier
.LBB0_1664:
	s_add_u32 s10, s2, 0x3a000000
	s_addc_u32 s11, s3, 0
	v_and_b32_e32 v0, 48, v254
	v_lshlrev_b32_e32 v1, 6, v254
	s_movk_i32 s14, 0x3c0
	s_add_u32 s12, s2, 0x8d200000
	v_and_or_b32 v0, v1, s14, v0
	v_lshlrev_b32_e32 v1, 2, v254
	s_addc_u32 s13, s3, 0
	s_lshl_b32 s64, s5, 6
	s_lshl_b32 s5, s5, 13
	v_and_b32_e32 v1, 32, v1
	v_bitop3_b32 v2, v0, s5, v1 bitop3:0xde
	s_lshl_b32 s5, s6, 5
	s_and_b32 s14, s5, 0x60
	s_lshl_b32 s5, s14, 7
	s_add_i32 s65, s56, 0x18000
	s_add_u32 s16, s42, 0x80
	v_bitop3_b32 v0, s5, v0, v1 bitop3:0xf6
	s_waitcnt vmcnt(2)
	s_barrier
	s_addc_u32 s17, s43, 0
	s_mov_b32 m0, s65
	s_nop 0
	global_load_lds_dwordx4 v142, s[16:17]
	s_add_i32 s66, s56, 0x1a000
	s_add_i32 s67, s56, 0x8000
	s_mov_b32 m0, s66
	s_nop 0
	global_load_lds_dwordx4 v144, s[16:17]
	s_add_u32 s16, s40, 0x80
	s_addc_u32 s17, s41, 0
	s_mov_b32 m0, s67
	s_nop 0
	global_load_lds_dwordx4 v255, s[16:17]
	s_add_i32 s68, s56, 0xa000
	s_add_i32 s69, s56, 0x1c000
	s_mov_b32 m0, s68
	s_nop 0
	global_load_lds_dwordx4 v143, s[16:17]
	s_add_u32 s16, s42, 0x20080
	s_addc_u32 s17, s43, 0
	s_mov_b32 m0, s69
	s_nop 0
	global_load_lds_dwordx4 v142, s[16:17]
	s_add_i32 s70, s56, 0x1e000
	s_add_i32 s71, s56, 0xc000
	s_mov_b32 m0, s70
	s_nop 0
	global_load_lds_dwordx4 v144, s[16:17]
	s_cmpk_lt_u32 s15, 0x100
	s_cselect_b64 s[16:17], -1, 0
	s_add_i32 s72, s56, 0xe000
	s_ashr_i32 s73, s50, 31
	s_lshl_b32 s5, s14, 2
	s_add_u32 s2, s2, s5
	s_waitcnt vmcnt(6)
	s_addc_u32 s3, s3, 0
	s_add_u32 s20, s2, 0x800000
	v_add_u32_e32 v0, 0, v0
	s_mov_b32 s15, s7
	s_addc_u32 s21, s3, 0
	v_mov_b64_e32 v[152:153], 0xbff
	s_movk_i32 s74, 0x181
	v_add_u32_e32 v145, 0x10000, v0
	v_add_u32_e32 v146, 0x14000, v0
	v_add_u32_e32 v147, 0, v2
	v_mov_b32_e32 v148, 0x7f7f7f7f
	v_add_u32_e32 v149, 0x18000, v0
	v_add_u32_e32 v150, 0x1c000, v0
	v_mov_b32_e32 v133, 0
	s_brev_b32 s22, 60
	s_mov_b32 s75, 0xc3e00000
	s_movk_i32 s76, 0x3000
	v_mov_b32_e32 v151, 0x43e00000
	s_mov_b32 s77, 0
	s_mov_b64 s[38:39], s[42:43]
	s_mov_b64 s[36:37], s[40:41]
	s_barrier
	s_branch .LBB0_1667

; #define PG8_WAIT_V(n) asm volatile("s_waitcnt vmcnt(" #n ")" ::: "memory")
; #define PG8_WAIT_L(n) asm volatile("s_waitcnt lgkmcnt(" #n ")" ::: "memory")
; #define PG8_BAR __builtin_amdgcn_s_barrier()
; #define PG8_SCHED __builtin_amdgcn_sched_barrier(0)
; #define PG8_STAGE_A(b, h, p) do { if constexpr (GATHER) { if ((h) == 0) PG8_STAGE(PG8_SA(b, h), p, vA0); else PG8_STAGE(PG8_SA(b, h), p, vA1); } else PG8_STAGE(PG8_SA(b, h), (p) + ((h) ? hstepA : (size_t)0), voffA); } while (0)
; #define PG8_GOFF1(un, h, d) do { int tz_ = tid; asm volatile("" : "+v"(tz_)); _Pragma("unroll") for (int i_ = 0; i_ < 2; ++i_) { int R_, C_; stage_rc(tz_ * 16 + i_ * 8192, R_, C_); \
;         d[i_] = S.gather(un, R_ + (h) * HALF) + (unsigned)C_ * 2u; } } while (0)
; template <class Epi, class Sched, bool ALIGN_EPI = true, bool SP2 = true, bool FP8 = false, bool GATHER = false>
; __device__ __forceinline__ void gemm_phase(LAS unsigned char* lds, const Dims g, const Sched& S, const Epi& E, const int wv) {
;     ...
;         for (int t = 0; t < nt; t += 2) {
;             const bool last = (t == nt - 2);
;             const char* a1 = cA + (size_t)(t + 1) * kstep;
;             const char* a2 = last ? nA : cA + (size_t)(t + 2) * kstep; const char* b2 = last ? nB : cB + (size_t)(t + 2) * kstep;
;             const char* a3 = a2 + kstep; const char* b3 = b2 + kstep;
;             if constexpr (SP2) {
;             if constexpr (GATHER) { if (last) PG8_GOFF1(un_, 0, vA0); }
;             PG8_LDB(B0, 0, 0); PG8_LDB(B1, 0, 1); PG8_SCHED; PG8_LDA(At, 0, 0); PG8_STAGE_A(1, 1, a1);
;             if constexpr (GATHER) { if (last) PG8_GOFF1(un_, 1, vA1); }
;             PG8_WAIT_V(8); PG8_WAIT_L(0); PG8_BAR; PG8_MMA(0, 0, At, B0); PG8_MMA(0, 1, At, B1); PG8_BAR; PG8_SCHED;
;             PG8_LDA(At, 0, 1); PG8_STAGE(PG8_SB(0, 0), b2, voffB); PG8_STAGE(PG8_SB(0, 1), b2 + hstepB, voffB); PG8_STAGE_A(0, 0, a2);
;             PG8_WAIT_V(8); PG8_WAIT_L(0); PG8_BAR; PG8_MMA(1, 0, At, B0); PG8_MMA(1, 1, At, B1); PG8_BAR; PG8_SCHED;
.LBB0_1670:
	ds_read_b128 v[154:157], v145
	ds_read_b128 v[158:161], v145 offset:1024
	ds_read_b128 v[162:165], v145 offset:2048
	ds_read_b128 v[166:169], v145 offset:3072
	ds_read_b128 v[170:173], v146
	ds_read_b128 v[174:177], v146 offset:1024
	ds_read_b128 v[178:181], v146 offset:2048
	ds_read_b128 v[182:185], v146 offset:3072
	s_add_u32 s42, s40, 0x100
	s_addc_u32 s43, s41, 0
	s_cmp_eq_u32 s25, 4
	s_cselect_b32 s48, s36, s42
	s_cselect_b32 s49, s37, s43
	s_cselect_b32 s46, s38, s5
	s_cselect_b32 s47, s39, s6
	s_add_u32 s44, s48, 0x80
	s_addc_u32 s45, s49, 0
	ds_read_b128 v[186:189], v147
	ds_read_b128 v[190:193], v147 offset:1024
	ds_read_b128 v[194:197], v147 offset:2048
	ds_read_b128 v[198:201], v147 offset:3072
	ds_read_b128 v[202:205], v147 offset:4096
	ds_read_b128 v[206:209], v147 offset:5120
	ds_read_b128 v[210:213], v147 offset:6144
	ds_read_b128 v[214:217], v147 offset:7168
	s_add_u32 s40, s40, 0x20080
	s_addc_u32 s41, s41, 0
	s_mov_b32 m0, s71
	s_nop 0
	global_load_lds_dwordx4 v255, s[40:41]
	s_nop 0
	s_mov_b32 m0, s72
	s_nop 0
	global_load_lds_dwordx4 v143, s[40:41]
	s_waitcnt vmcnt(8)
	s_waitcnt lgkmcnt(0)
	s_barrier
	s_setprio 1
	s_waitcnt lgkmcnt(6)
	v_mfma_scale_f32_16x16x128_f8f6f4 v[124:127], v[154:161], v[186:193], v[124:127], v148, v148 op_sel_hi:[0,0,0]
	v_mfma_scale_f32_16x16x128_f8f6f4 v[120:123], v[162:169], v[186:193], v[120:123], v148, v148 op_sel_hi:[0,0,0]
	s_waitcnt lgkmcnt(4)
	v_mfma_scale_f32_16x16x128_f8f6f4 v[108:111], v[154:161], v[194:201], v[108:111], v148, v148 op_sel_hi:[0,0,0]
	v_mfma_scale_f32_16x16x128_f8f6f4 v[104:107], v[162:169], v[194:201], v[104:107], v148, v148 op_sel_hi:[0,0,0]
	s_waitcnt lgkmcnt(2)
	v_mfma_scale_f32_16x16x128_f8f6f4 v[134:137], v[154:161], v[202:209], v[92:95], v148, v148 op_sel_hi:[0,0,0]
	v_mfma_scale_f32_16x16x128_f8f6f4 v[218:221], v[162:169], v[202:209], v[88:91], v148, v148 op_sel_hi:[0,0,0]
	s_waitcnt lgkmcnt(0)
	v_mfma_scale_f32_16x16x128_f8f6f4 v[222:225], v[154:161], v[210:217], v[76:79], v148, v148 op_sel_hi:[0,0,0]
	v_mfma_scale_f32_16x16x128_f8f6f4 v[226:229], v[162:169], v[210:217], v[72:75], v148, v148 op_sel_hi:[0,0,0]
	s_setprio 0
	s_setprio 1
	v_mfma_scale_f32_16x16x128_f8f6f4 v[116:119], v[170:177], v[186:193], v[116:119], v148, v148 op_sel_hi:[0,0,0]
	v_mfma_scale_f32_16x16x128_f8f6f4 v[112:115], v[178:185], v[186:193], v[112:115], v148, v148 op_sel_hi:[0,0,0]
	v_mfma_scale_f32_16x16x128_f8f6f4 v[100:103], v[170:177], v[194:201], v[100:103], v148, v148 op_sel_hi:[0,0,0]
	v_mfma_scale_f32_16x16x128_f8f6f4 v[96:99], v[178:185], v[194:201], v[96:99], v148, v148 op_sel_hi:[0,0,0]
	v_mfma_scale_f32_16x16x128_f8f6f4 v[186:189], v[170:177], v[202:209], v[84:87], v148, v148 op_sel_hi:[0,0,0]
	v_mfma_scale_f32_16x16x128_f8f6f4 v[190:193], v[178:185], v[202:209], v[80:83], v148, v148 op_sel_hi:[0,0,0]
	v_mfma_scale_f32_16x16x128_f8f6f4 v[194:197], v[170:177], v[210:217], v[68:71], v148, v148 op_sel_hi:[0,0,0]
	v_mfma_scale_f32_16x16x128_f8f6f4 v[198:201], v[178:185], v[210:217], v[64:67], v148, v148 op_sel_hi:[0,0,0]
	s_setprio 0
	s_barrier
	s_nop 4
	ds_read_b128 v[64:67], v147 offset:16384
	ds_read_b128 v[68:71], v147 offset:17408
	ds_read_b128 v[72:75], v147 offset:18432
	ds_read_b128 v[76:79], v147 offset:19456
	ds_read_b128 v[80:83], v147 offset:20480
	ds_read_b128 v[84:87], v147 offset:21504
	ds_read_b128 v[88:91], v147 offset:22528
	ds_read_b128 v[92:95], v147 offset:23552
	s_mov_b32 m0, s57
	s_nop 0
	global_load_lds_dwordx4 v142, s[46:47]
	s_add_u32 s40, s46, 0x20000
	s_mov_b32 m0, s58
	s_nop 0
	global_load_lds_dwordx4 v144, s[46:47]
	s_addc_u32 s41, s47, 0
	s_mov_b32 m0, s59
	s_nop 0
	global_load_lds_dwordx4 v142, s[40:41]
	s_nop 0
	s_mov_b32 m0, s60
	s_nop 0
	global_load_lds_dwordx4 v144, s[40:41]
	s_nop 0
	s_mov_b32 m0, s56
	s_nop 0
	global_load_lds_dwordx4 v255, s[48:49]
	s_nop 0
	s_mov_b32 m0, s61
	s_nop 0
	global_load_lds_dwordx4 v143, s[48:49]
	s_waitcnt vmcnt(8)
	s_waitcnt lgkmcnt(0)
	s_barrier
	s_setprio 1
	s_waitcnt lgkmcnt(6)
	v_mfma_scale_f32_16x16x128_f8f6f4 v[60:63], v[154:161], v[64:71], v[60:63], v148, v148 op_sel_hi:[0,0,0]
	v_mfma_scale_f32_16x16x128_f8f6f4 v[56:59], v[162:169], v[64:71], v[56:59], v148, v148 op_sel_hi:[0,0,0]
	s_waitcnt lgkmcnt(4)
	v_mfma_scale_f32_16x16x128_f8f6f4 v[202:205], v[154:161], v[72:79], v[44:47], v148, v148 op_sel_hi:[0,0,0]
	v_mfma_scale_f32_16x16x128_f8f6f4 v[206:209], v[162:169], v[72:79], v[40:43], v148, v148 op_sel_hi:[0,0,0]
	s_waitcnt lgkmcnt(2)
	v_mfma_scale_f32_16x16x128_f8f6f4 v[210:213], v[154:161], v[80:87], v[28:31], v148, v148 op_sel_hi:[0,0,0]
	v_mfma_scale_f32_16x16x128_f8f6f4 v[214:217], v[162:169], v[80:87], v[24:27], v148, v148 op_sel_hi:[0,0,0]
	s_waitcnt lgkmcnt(0)
	v_mfma_scale_f32_16x16x128_f8f6f4 v[230:233], v[154:161], v[88:95], v[12:15], v148, v148 op_sel_hi:[0,0,0]
	v_mfma_scale_f32_16x16x128_f8f6f4 v[234:237], v[162:169], v[88:95], v[8:11], v148, v148 op_sel_hi:[0,0,0]
	s_setprio 0
	s_setprio 1
	v_mfma_scale_f32_16x16x128_f8f6f4 v[52:55], v[170:177], v[64:71], v[52:55], v148, v148 op_sel_hi:[0,0,0]
	v_mfma_scale_f32_16x16x128_f8f6f4 v[48:51], v[178:185], v[64:71], v[48:51], v148, v148 op_sel_hi:[0,0,0]
	v_mfma_scale_f32_16x16x128_f8f6f4 v[238:241], v[170:177], v[72:79], v[36:39], v148, v148 op_sel_hi:[0,0,0]
	v_mfma_scale_f32_16x16x128_f8f6f4 v[242:245], v[178:185], v[72:79], v[32:35], v148, v148 op_sel_hi:[0,0,0]
	v_mfma_scale_f32_16x16x128_f8f6f4 v[246:249], v[170:177], v[80:87], v[20:23], v148, v148 op_sel_hi:[0,0,0]
	v_mfma_scale_f32_16x16x128_f8f6f4 v[250:253], v[178:185], v[80:87], v[16:19], v148, v148 op_sel_hi:[0,0,0]
	v_mfma_scale_f32_16x16x128_f8f6f4 v[128:131], v[170:177], v[88:95], v[4:7], v148, v148 op_sel_hi:[0,0,0]
	v_mfma_scale_f32_16x16x128_f8f6f4 v[138:141], v[178:185], v[88:95], v[0:3], v148, v148 op_sel_hi:[0,0,0]
	s_setprio 0
	s_barrier
; #define PG8_WAIT_V(n) asm volatile("s_waitcnt vmcnt(" #n ")" ::: "memory")
; #define PG8_WAIT_L(n) asm volatile("s_waitcnt lgkmcnt(" #n ")" ::: "memory")
; #define PG8_BAR __builtin_amdgcn_s_barrier()
; #define PG8_SCHED __builtin_amdgcn_sched_barrier(0)
; #define PG8_STAGE_A(b, h, p) do { if constexpr (GATHER) { if ((h) == 0) PG8_STAGE(PG8_SA(b, h), p, vA0); else PG8_STAGE(PG8_SA(b, h), p, vA1); } else PG8_STAGE(PG8_SA(b, h), (p) + ((h) ? hstepA : (size_t)0), voffA); } while (0)
; template <class Epi, class Sched, bool ALIGN_EPI = true, bool SP2 = true, bool FP8 = false, bool GATHER = false>
; __device__ __forceinline__ void gemm_phase(LAS unsigned char* lds, const Dims g, const Sched& S, const Epi& E, const int wv) {
;     ...
;             PG8_LDB(B0, 1, 0); PG8_LDB(B1, 1, 1); PG8_SCHED; PG8_LDA(At, 1, 0); PG8_STAGE_A(0, 1, a2);
;             PG8_WAIT_V(8); PG8_WAIT_L(0); PG8_BAR; PG8_MMA(0, 0, At, B0); PG8_MMA(0, 1, At, B1); PG8_BAR; PG8_SCHED;
;             PG8_LDA(At, 1, 1); PG8_STAGE(PG8_SB(1, 0), b3, voffB); PG8_STAGE(PG8_SB(1, 1), b3 + hstepB, voffB); PG8_STAGE_A(1, 0, a3);
;             PG8_WAIT_V(8); PG8_WAIT_L(0); PG8_BAR; PG8_MMA(1, 0, At, B0); PG8_MMA(1, 1, At, B1); PG8_BAR; PG8_SCHED;
	s_nop 4
	ds_read_b128 v[0:3], v149
	ds_read_b128 v[4:7], v149 offset:1024
	ds_read_b128 v[16:19], v149 offset:2048
	ds_read_b128 v[20:23], v149 offset:3072
	ds_read_b128 v[154:157], v150
	ds_read_b128 v[158:161], v150 offset:1024
	ds_read_b128 v[162:165], v150 offset:2048
	ds_read_b128 v[166:169], v150 offset:3072
	ds_read_b128 v[8:11], v147 offset:32768
	ds_read_b128 v[12:15], v147 offset:33792
	ds_read_b128 v[24:27], v147 offset:34816
	ds_read_b128 v[28:31], v147 offset:35840
	ds_read_b128 v[32:35], v147 offset:36864
	ds_read_b128 v[36:39], v147 offset:37888
	ds_read_b128 v[40:43], v147 offset:38912
	ds_read_b128 v[44:47], v147 offset:39936
	s_add_u32 s40, s48, 0x20000
	s_addc_u32 s41, s49, 0
	s_mov_b32 m0, s62
	s_nop 0
	global_load_lds_dwordx4 v255, s[40:41]
	s_nop 0
	s_mov_b32 m0, s63
	s_nop 0
	global_load_lds_dwordx4 v143, s[40:41]
	s_waitcnt vmcnt(8)
	s_waitcnt lgkmcnt(0)
	s_barrier
	s_setprio 1
	s_waitcnt lgkmcnt(6)
	v_mfma_scale_f32_16x16x128_f8f6f4 v[124:127], v[0:7], v[8:15], v[124:127], v148, v148 op_sel_hi:[0,0,0]
	v_mfma_scale_f32_16x16x128_f8f6f4 v[120:123], v[16:23], v[8:15], v[120:123], v148, v148 op_sel_hi:[0,0,0]
	s_waitcnt lgkmcnt(4)
	v_mfma_scale_f32_16x16x128_f8f6f4 v[108:111], v[0:7], v[24:31], v[108:111], v148, v148 op_sel_hi:[0,0,0]
	v_mfma_scale_f32_16x16x128_f8f6f4 v[104:107], v[16:23], v[24:31], v[104:107], v148, v148 op_sel_hi:[0,0,0]
	s_waitcnt lgkmcnt(2)
	v_mfma_scale_f32_16x16x128_f8f6f4 v[92:95], v[0:7], v[32:39], v[134:137], v148, v148 op_sel_hi:[0,0,0]
	v_mfma_scale_f32_16x16x128_f8f6f4 v[88:91], v[16:23], v[32:39], v[218:221], v148, v148 op_sel_hi:[0,0,0]
	s_waitcnt lgkmcnt(0)
	v_mfma_scale_f32_16x16x128_f8f6f4 v[76:79], v[0:7], v[40:47], v[222:225], v148, v148 op_sel_hi:[0,0,0]
	v_mfma_scale_f32_16x16x128_f8f6f4 v[72:75], v[16:23], v[40:47], v[226:229], v148, v148 op_sel_hi:[0,0,0]
	s_setprio 0
	s_setprio 1
	v_mfma_scale_f32_16x16x128_f8f6f4 v[116:119], v[154:161], v[8:15], v[116:119], v148, v148 op_sel_hi:[0,0,0]
	v_mfma_scale_f32_16x16x128_f8f6f4 v[112:115], v[162:169], v[8:15], v[112:115], v148, v148 op_sel_hi:[0,0,0]
	v_mfma_scale_f32_16x16x128_f8f6f4 v[100:103], v[154:161], v[24:31], v[100:103], v148, v148 op_sel_hi:[0,0,0]
	v_mfma_scale_f32_16x16x128_f8f6f4 v[96:99], v[162:169], v[24:31], v[96:99], v148, v148 op_sel_hi:[0,0,0]
	v_mfma_scale_f32_16x16x128_f8f6f4 v[84:87], v[154:161], v[32:39], v[186:189], v148, v148 op_sel_hi:[0,0,0]
	v_mfma_scale_f32_16x16x128_f8f6f4 v[80:83], v[162:169], v[32:39], v[190:193], v148, v148 op_sel_hi:[0,0,0]
	v_mfma_scale_f32_16x16x128_f8f6f4 v[68:71], v[154:161], v[40:47], v[194:197], v148, v148 op_sel_hi:[0,0,0]
	v_mfma_scale_f32_16x16x128_f8f6f4 v[64:67], v[162:169], v[40:47], v[198:201], v148, v148 op_sel_hi:[0,0,0]
	s_setprio 0
	s_barrier
	ds_read_b128 v[32:35], v147 offset:49152
	ds_read_b128 v[36:39], v147 offset:50176
	ds_read_b128 v[170:173], v147 offset:51200
	ds_read_b128 v[174:177], v147 offset:52224
	ds_read_b128 v[178:181], v147 offset:53248
	ds_read_b128 v[182:185], v147 offset:54272
	ds_read_b128 v[186:189], v147 offset:55296
	ds_read_b128 v[190:193], v147 offset:56320
	s_add_u32 s40, s46, 0x80
	s_addc_u32 s41, s47, 0
	s_mov_b32 m0, s65
	s_nop 0
	global_load_lds_dwordx4 v142, s[40:41]
	s_nop 0
	s_mov_b32 m0, s66
	s_nop 0
	global_load_lds_dwordx4 v144, s[40:41]
	s_add_u32 s40, s46, 0x20080
	s_addc_u32 s41, s47, 0
	s_mov_b32 m0, s69
	s_nop 0
	global_load_lds_dwordx4 v142, s[40:41]
	s_nop 0
	s_mov_b32 m0, s70
	s_nop 0
	global_load_lds_dwordx4 v144, s[40:41]
	s_nop 0
	s_mov_b32 m0, s67
	s_nop 0
	global_load_lds_dwordx4 v255, s[44:45]
	s_nop 0
	s_mov_b32 m0, s68
	s_nop 0
	global_load_lds_dwordx4 v143, s[44:45]
	s_waitcnt vmcnt(8)
	s_waitcnt lgkmcnt(0)
	s_barrier
	s_setprio 1
	s_waitcnt lgkmcnt(6)
	v_mfma_scale_f32_16x16x128_f8f6f4 v[60:63], v[0:7], v[32:39], v[60:63], v148, v148 op_sel_hi:[0,0,0]
	v_mfma_scale_f32_16x16x128_f8f6f4 v[56:59], v[16:23], v[32:39], v[56:59], v148, v148 op_sel_hi:[0,0,0]
	s_waitcnt lgkmcnt(4)
	v_mfma_scale_f32_16x16x128_f8f6f4 v[44:47], v[0:7], v[170:177], v[202:205], v148, v148 op_sel_hi:[0,0,0]
	v_mfma_scale_f32_16x16x128_f8f6f4 v[40:43], v[16:23], v[170:177], v[206:209], v148, v148 op_sel_hi:[0,0,0]
	s_waitcnt lgkmcnt(2)
	v_mfma_scale_f32_16x16x128_f8f6f4 v[28:31], v[0:7], v[178:185], v[210:213], v148, v148 op_sel_hi:[0,0,0]
	v_mfma_scale_f32_16x16x128_f8f6f4 v[24:27], v[16:23], v[178:185], v[214:217], v148, v148 op_sel_hi:[0,0,0]
	s_waitcnt lgkmcnt(0)
	v_mfma_scale_f32_16x16x128_f8f6f4 v[12:15], v[0:7], v[186:193], v[230:233], v148, v148 op_sel_hi:[0,0,0]
	v_mfma_scale_f32_16x16x128_f8f6f4 v[8:11], v[16:23], v[186:193], v[234:237], v148, v148 op_sel_hi:[0,0,0]
	s_setprio 0
	s_setprio 1
	v_mfma_scale_f32_16x16x128_f8f6f4 v[52:55], v[154:161], v[32:39], v[52:55], v148, v148 op_sel_hi:[0,0,0]
	v_mfma_scale_f32_16x16x128_f8f6f4 v[48:51], v[162:169], v[32:39], v[48:51], v148, v148 op_sel_hi:[0,0,0]
	v_mfma_scale_f32_16x16x128_f8f6f4 v[36:39], v[154:161], v[170:177], v[238:241], v148, v148 op_sel_hi:[0,0,0]
	v_mfma_scale_f32_16x16x128_f8f6f4 v[32:35], v[162:169], v[170:177], v[242:245], v148, v148 op_sel_hi:[0,0,0]
	v_mfma_scale_f32_16x16x128_f8f6f4 v[20:23], v[154:161], v[178:185], v[246:249], v148, v148 op_sel_hi:[0,0,0]
	v_mfma_scale_f32_16x16x128_f8f6f4 v[16:19], v[162:169], v[178:185], v[250:253], v148, v148 op_sel_hi:[0,0,0]
	v_mfma_scale_f32_16x16x128_f8f6f4 v[4:7], v[154:161], v[186:193], v[128:131], v148, v148 op_sel_hi:[0,0,0]
	v_mfma_scale_f32_16x16x128_f8f6f4 v[0:3], v[162:169], v[186:193], v[138:141], v148, v148 op_sel_hi:[0,0,0]
	s_setprio 0
	s_barrier
	s_add_i32 s25, s25, 2
	s_add_u32 s5, s5, 0x100
	s_addc_u32 s6, s6, 0
	s_cmp_gt_u32 s25, 5
	s_mov_b64 s[40:41], s[42:43]
	s_cbranch_scc0 .LBB0_1670
	s_and_b64 vcc, exec, s[16:17]
	s_cbranch_vccz .LBB0_1673
	s_barrier

; #define PG8_WAIT_V(n) asm volatile("s_waitcnt vmcnt(" #n ")" ::: "memory")
; #define PG8_BAR __builtin_amdgcn_s_barrier()
; #define PG8_STAGE_A(b, h, p) do { if constexpr (GATHER) { if ((h) == 0) PG8_STAGE(PG8_SA(b, h), p, vA0); else PG8_STAGE(PG8_SA(b, h), p, vA1); } else PG8_STAGE(PG8_SA(b, h), (p) + ((h) ? hstepA : (size_t)0), voffA); } while (0)
; template <class Epi, class Sched, bool ALIGN_EPI = true, bool SP2 = true, bool FP8 = false, bool GATHER = false>
; __device__ __forceinline__ void gemm_phase(LAS unsigned char* lds, const Dims g, const Sched& S, const Epi& E, const int wv) {
;     ...
;     for (int i = 0; i < 2; ++i) { int R, C; stage_rc(tid * 16 + i * 8192, R, C); const int Rb = Epi::PERM ? ((R & ~31) + perm32(R & 31)) : R;
;         voffA[i] = (unsigned)(R * g.lda + C) * 2u; voffB[i] = (unsigned)(Rb * g.ldb + C) * 2u; }
;     ...
;     if constexpr (SP2) {
;         PG8_STAGE(PG8_SB(0, 0), cB, voffB); PG8_STAGE(PG8_SB(0, 1), cB + hstepB, voffB); PG8_STAGE_A(0, 0, cA); PG8_STAGE_A(0, 1, cA);
;         if (wr == 1) PG8_BAR;
;         PG8_WAIT_V(2); PG8_BAR;
;         PG8_STAGE(PG8_SB(1, 0), cB + kstep, voffB); PG8_STAGE_A(1, 0, cA + kstep); PG8_STAGE(PG8_SB(1, 1), cB + hstepB + kstep, voffB);
;         PG8_WAIT_V(6); PG8_BAR;
.LBB0_1901:
	v_bfe_i32 v2, v146, 27, 1
	v_lshlrev_b32_e32 v0, 4, v146
	v_lshrrev_b32_e32 v2, 22, v2
	v_add_u32_e32 v2, v0, v2
	v_and_b32_e32 v2, 0xfffffc00, v2
	v_sub_u32_e32 v2, v0, v2
	v_ashrrev_i32_e32 v1, 31, v146
	v_lshrrev_b32_e32 v3, 4, v2
	v_lshrrev_b32_e32 v1, 26, v1
	v_bitop3_b32 v2, v3, v2, 32 bitop3:0x6c
	v_add_u32_e32 v1, v146, v1
	v_ashrrev_i32_e32 v4, 31, v2
	v_ashrrev_i32_e32 v1, 6, v1
	v_lshrrev_b32_e32 v4, 26, v4
	v_lshlrev_b32_e32 v3, 3, v1
	v_add_u32_e32 v4, v2, v4
	v_and_b32_e32 v3, -16, v3
	v_ashrrev_i32_e32 v5, 6, v4
	v_and_b32_e32 v4, 0xc0, v4
	v_add_u32_e32 v3, v5, v3
	v_sub_u32_e32 v2, v2, v4
	v_mov_b32_e32 v4, 1
	v_lshlrev_b32_e32 v1, 5, v1
	v_ashrrev_i16_sdwa v2, v4, sext(v2) dst_sel:DWORD dst_unused:UNUSED_PAD src0_sel:DWORD src1_sel:BYTE_0
	v_lshlrev_b32_e32 v6, 1, v3
	v_lshrrev_b32_e32 v7, 2, v3
	v_and_b32_e32 v5, 3, v5
	s_mov_b32 s5, 0x1fffe0
	v_and_b32_e32 v1, 32, v1
	v_bfe_i32 v2, v2, 0, 16
	v_and_b32_e32 v6, 24, v6
	v_and_b32_e32 v7, 4, v7
	v_and_or_b32 v5, v3, s5, v5
	v_or3_b32 v5, v5, v7, v6
	v_add_lshl_u32 v1, v1, v2, 1
	v_add_u32_e32 v0, 0x2000, v0
	v_lshl_add_u32 v147, v3, 11, v1
	v_lshl_add_u32 v148, v5, 11, v1
	v_ashrrev_i32_e32 v1, 31, v0
	v_lshrrev_b32_e32 v1, 22, v1
	v_add_u32_e32 v1, v0, v1
	v_ashrrev_i32_e32 v1, 10, v1
	v_mul_i32_i24_e32 v2, 0x400, v1
	v_sub_u32_e32 v0, v0, v2
	v_lshrrev_b32_e32 v2, 4, v0
	v_bitop3_b32 v0, v2, v0, 32 bitop3:0x6c
	v_ashrrev_i32_e32 v3, 31, v0
	s_add_u32 s50, s2, 0x72000000
	v_lshrrev_b32_e32 v3, 26, v3
	s_addc_u32 s51, s3, 0
	v_lshlrev_b32_e32 v2, 3, v1
	v_add_u32_e32 v3, v0, v3
	s_add_u32 s52, s2, 0x5800000
	v_and_b32_e32 v2, -16, v2
	v_ashrrev_i32_e32 v5, 6, v3
	s_addc_u32 s53, s3, 0
	v_add_u32_e32 v2, v5, v2
	v_and_b32_e32 v5, 3, v5
	s_add_i32 s4, s6, s4
	v_and_or_b32 v5, v2, s5, v5
	s_ashr_i32 s5, s4, 31
	s_lshr_b32 s5, s5, 27
	s_add_i32 s5, s4, s5
	s_ashr_i32 s6, s5, 5
	s_and_b32 s5, s5, 0xffe0
	s_sub_i32 s4, s4, s5
	s_bfe_i32 s5, s4, 0x80000
	s_bfe_u32 s5, s5, 0x3000c
	s_add_i32 s5, s4, s5
	s_bfe_i32 s8, s5, 0x80000
	s_and_b32 s5, s5, 0xf8
	s_sub_i32 s4, s4, s5
	s_lshl_b32 s6, s6, 3
	s_sext_i32_i8 s4, s4
	s_add_i32 s38, s6, s4
	s_ashr_i32 s11, s10, 6
	s_sext_i32_i16 s8, s8
	s_ashr_i32 s39, s38, 31
	s_ashr_i32 s12, s10, 8
	s_lshl_b32 s7, s11, 10
	s_lshr_b32 s8, s8, 3
	s_lshl_b64 s[4:5], s[38:39], 19
	s_add_u32 s40, s50, s4
	v_and_b32_e32 v3, 0xc0, v3
	s_addc_u32 s41, s51, s5
	s_bfe_i64 s[4:5], s[8:9], 0x100000
	v_sub_u32_e32 v0, v0, v3
	s_lshl_b64 s[4:5], s[4:5], 19
	v_lshlrev_b32_e32 v1, 5, v1
	v_ashrrev_i16_sdwa v0, v4, sext(v0) dst_sel:DWORD dst_unused:UNUSED_PAD src0_sel:DWORD src1_sel:BYTE_0
	v_lshlrev_b32_e32 v3, 1, v2
	v_lshrrev_b32_e32 v4, 2, v2
	s_add_u32 s42, s52, s4
	v_and_b32_e32 v1, 32, v1
	v_bfe_i32 v0, v0, 0, 16
	v_and_b32_e32 v3, 24, v3
	v_and_b32_e32 v4, 4, v4
	s_addc_u32 s43, s53, s5
	s_add_i32 s54, s7, 0
	v_or3_b32 v3, v5, v4, v3
	v_add_lshl_u32 v0, v1, v0, 1
	s_add_i32 s55, s54, 0x10000
	s_mov_b32 m0, s55
	s_nop 0
	global_load_lds_dwordx4 v148, s[42:43]
	s_add_i32 s56, s54, 0x12000
	s_add_i32 s57, s54, 0x14000
	v_lshl_add_u32 v150, v3, 11, v0
	s_mov_b32 m0, s56
	s_nop 0
	global_load_lds_dwordx4 v150, s[42:43]
	s_add_u32 s6, s42, 0x40000
	s_addc_u32 s7, s43, 0
	s_mov_b32 m0, s57
	s_nop 0
	global_load_lds_dwordx4 v148, s[6:7]
	s_add_i32 s58, s54, 0x16000
	s_mov_b32 m0, s58
	s_nop 0
	global_load_lds_dwordx4 v150, s[6:7]
	s_mov_b32 m0, s54
	s_nop 0
	global_load_lds_dwordx4 v147, s[40:41]
	s_add_i32 s59, s54, 0x2000
	s_add_i32 s60, s54, 0x4000
	v_lshl_add_u32 v149, v2, 11, v0
	s_mov_b32 m0, s59
	s_nop 0
	global_load_lds_dwordx4 v149, s[40:41]
	s_add_u32 s14, s40, 0x40000
	s_addc_u32 s15, s41, 0
	s_mov_b32 m0, s60
	s_nop 0
	global_load_lds_dwordx4 v147, s[14:15]
	s_add_i32 s61, s54, 0x6000
	s_mov_b32 m0, s61
	s_nop 0
	global_load_lds_dwordx4 v149, s[14:15]
	s_cmp_eq_u32 s12, 1
	s_mov_b32 s39, 0
	s_mov_b64 s[4:5], 0x40000
	s_cselect_b64 s[6:7], -1, 0
	s_cmp_lg_u32 s12, 1
	s_cbranch_scc1 .LBB0_1903
	s_barrier
.LBB0_1903:
	s_sext_i32_i8 s79, s8
	s_add_u32 s8, s2, 0xaf200000
	s_addc_u32 s9, s3, 0
	s_add_u32 s62, s2, 0x132000
	s_addc_u32 s63, s3, 0
	v_and_b32_e32 v0, 48, v146
	v_lshlrev_b32_e32 v1, 6, v146
	s_movk_i32 s3, 0x3c0
	v_and_or_b32 v0, v1, s3, v0
	v_lshlrev_b32_e32 v1, 2, v146
	s_lshl_b32 s2, s12, 13
	v_and_b32_e32 v1, 32, v1
	v_bitop3_b32 v2, v0, s2, v1 bitop3:0xde
	s_lshl_b32 s2, s11, 5
	s_and_b32 s65, s2, 0x60
	s_lshl_b32 s64, s12, 6
	s_lshl_b32 s2, s65, 7
	s_add_i32 s66, s54, 0x18000
	v_bitop3_b32 v0, s2, v0, v1 bitop3:0xf6
	s_add_u32 s2, s42, 0x80
	s_waitcnt vmcnt(2)
	s_barrier
	s_addc_u32 s3, s43, 0
	s_mov_b32 m0, s66
	s_nop 0
	global_load_lds_dwordx4 v148, s[2:3]
	s_add_i32 s67, s54, 0x1a000
	s_add_i32 s68, s54, 0x8000
	s_mov_b32 m0, s67
	s_nop 0
	global_load_lds_dwordx4 v150, s[2:3]
	s_add_u32 s2, s40, 0x80
	s_addc_u32 s3, s41, 0
	s_mov_b32 m0, s68
	s_nop 0
	global_load_lds_dwordx4 v147, s[2:3]
	s_add_i32 s69, s54, 0xa000
	s_add_i32 s70, s54, 0x1c000
	s_mov_b32 m0, s69
	s_nop 0
	global_load_lds_dwordx4 v149, s[2:3]
	s_add_u32 s2, s42, 0x40080
	s_addc_u32 s3, s43, 0
	s_mov_b32 m0, s70
	s_nop 0
	global_load_lds_dwordx4 v148, s[2:3]
	s_add_i32 s71, s54, 0x1e000
	s_mov_b32 m0, s71
	s_nop 0
	global_load_lds_dwordx4 v150, s[2:3]
	s_waitcnt vmcnt(6)
	s_add_i32 s72, s54, 0xc000
	s_cmpk_lt_u32 s10, 0x100
	v_add_u32_e32 v0, 0, v0
	s_cselect_b64 s[10:11], -1, 0
	s_add_i32 s73, s54, 0xe000
	s_ashr_i32 s74, s48, 31
	v_mov_b64_e32 v[254:255], 0x200
	v_add_u32_e32 v151, 0x10000, v0
	v_add_u32_e32 v152, 0x14000, v0
	v_add_u32_e32 v153, 0, v2
	v_mov_b32_e32 v154, 0x7f7f7f7f
	v_add_u32_e32 v155, 0x18000, v0
	v_add_u32_e32 v156, 0x1c000, v0
	s_mov_b32 s12, 0x3a000000
	s_mov_b32 s75, 0x40000
	s_mov_b64 s[14:15], 0x48000
	s_mov_b32 s76, 0x48000
	s_mov_b64 s[16:17], 0x50000
	s_mov_b32 s77, 0x50000
	s_mov_b64 s[20:21], 0x58000
	s_mov_b32 s78, 0x58000
	s_mov_b64 s[26:27], s[40:41]
	s_mov_b64 s[36:37], s[42:43]
	s_barrier
	s_branch .LBB0_1906

; #define PG8_WAIT_V(n) asm volatile("s_waitcnt vmcnt(" #n ")" ::: "memory")
; #define PG8_WAIT_L(n) asm volatile("s_waitcnt lgkmcnt(" #n ")" ::: "memory")
; #define PG8_BAR __builtin_amdgcn_s_barrier()
; #define PG8_SCHED __builtin_amdgcn_sched_barrier(0)
; #define PG8_STAGE_A(b, h, p) do { if constexpr (GATHER) { if ((h) == 0) PG8_STAGE(PG8_SA(b, h), p, vA0); else PG8_STAGE(PG8_SA(b, h), p, vA1); } else PG8_STAGE(PG8_SA(b, h), (p) + ((h) ? hstepA : (size_t)0), voffA); } while (0)
; #define PG8_GOFF1(un, h, d) do { int tz_ = tid; asm volatile("" : "+v"(tz_)); _Pragma("unroll") for (int i_ = 0; i_ < 2; ++i_) { int R_, C_; stage_rc(tz_ * 16 + i_ * 8192, R_, C_); \
;         d[i_] = S.gather(un, R_ + (h) * HALF) + (unsigned)C_ * 2u; } } while (0)
; template <class Epi, class Sched, bool ALIGN_EPI = true, bool SP2 = true, bool FP8 = false, bool GATHER = false>
; __device__ __forceinline__ void gemm_phase(LAS unsigned char* lds, const Dims g, const Sched& S, const Epi& E, const int wv) {
;     ...
;         for (int t = 0; t < nt; t += 2) {
;             const bool last = (t == nt - 2);
;             const char* a1 = cA + (size_t)(t + 1) * kstep;
;             const char* a2 = last ? nA : cA + (size_t)(t + 2) * kstep; const char* b2 = last ? nB : cB + (size_t)(t + 2) * kstep;
;             const char* a3 = a2 + kstep; const char* b3 = b2 + kstep;
;             if constexpr (SP2) {
;             if constexpr (GATHER) { if (last) PG8_GOFF1(un_, 0, vA0); }
;             PG8_LDB(B0, 0, 0); PG8_LDB(B1, 0, 1); PG8_SCHED; PG8_LDA(At, 0, 0); PG8_STAGE_A(1, 1, a1);
;             if constexpr (GATHER) { if (last) PG8_GOFF1(un_, 1, vA1); }
;             PG8_WAIT_V(8); PG8_WAIT_L(0); PG8_BAR; PG8_MMA(0, 0, At, B0); PG8_MMA(0, 1, At, B1); PG8_BAR; PG8_SCHED;
;             PG8_LDA(At, 0, 1); PG8_STAGE(PG8_SB(0, 0), b2, voffB); PG8_STAGE(PG8_SB(0, 1), b2 + hstepB, voffB); PG8_STAGE_A(0, 0, a2);
;             PG8_WAIT_V(8); PG8_WAIT_L(0); PG8_BAR; PG8_MMA(1, 0, At, B0); PG8_MMA(1, 1, At, B1); PG8_BAR; PG8_SCHED;
.LBB0_1913:
	ds_read_b128 v[132:135], v151
	ds_read_b128 v[136:139], v151 offset:1024
	ds_read_b128 v[158:161], v151 offset:2048
	ds_read_b128 v[162:165], v151 offset:3072
	ds_read_b128 v[166:169], v152
	ds_read_b128 v[170:173], v152 offset:1024
	ds_read_b128 v[174:177], v152 offset:2048
	ds_read_b128 v[178:181], v152 offset:3072
	s_cmp_eq_u32 s82, 12
	s_cselect_b32 s46, s26, s80
	s_cselect_b32 s47, s27, s81
	s_cselect_b32 s44, s36, s23
	s_cselect_b32 s45, s37, s25
	s_add_u32 s42, s46, 0x80
	s_addc_u32 s43, s47, 0
	ds_read_b128 v[182:185], v153
	ds_read_b128 v[186:189], v153 offset:1024
	ds_read_b128 v[190:193], v153 offset:2048
	ds_read_b128 v[194:197], v153 offset:3072
	ds_read_b128 v[198:201], v153 offset:4096
	ds_read_b128 v[202:205], v153 offset:5120
	ds_read_b128 v[206:209], v153 offset:6144
	ds_read_b128 v[210:213], v153 offset:7168
	s_mov_b32 m0, s72
	s_nop 0
	global_load_lds_dwordx4 v147, s[40:41]
	s_nop 0
	s_mov_b32 m0, s73
	s_nop 0
	global_load_lds_dwordx4 v149, s[40:41]
	s_waitcnt vmcnt(8)
	s_waitcnt lgkmcnt(0)
	s_barrier
	s_setprio 1
	s_waitcnt lgkmcnt(6)
	v_mfma_scale_f32_16x16x128_f8f6f4 v[124:127], v[132:139], v[182:189], v[124:127], v154, v154 op_sel_hi:[0,0,0]
	v_mfma_scale_f32_16x16x128_f8f6f4 v[120:123], v[158:165], v[182:189], v[120:123], v154, v154 op_sel_hi:[0,0,0]
	s_waitcnt lgkmcnt(4)
	v_mfma_scale_f32_16x16x128_f8f6f4 v[116:119], v[132:139], v[190:197], v[116:119], v154, v154 op_sel_hi:[0,0,0]
	v_mfma_scale_f32_16x16x128_f8f6f4 v[104:107], v[158:165], v[190:197], v[104:107], v154, v154 op_sel_hi:[0,0,0]
	s_waitcnt lgkmcnt(2)
	v_mfma_scale_f32_16x16x128_f8f6f4 v[100:103], v[132:139], v[198:205], v[100:103], v154, v154 op_sel_hi:[0,0,0]
	v_mfma_scale_f32_16x16x128_f8f6f4 v[140:143], v[158:165], v[198:205], v[88:91], v154, v154 op_sel_hi:[0,0,0]
	s_waitcnt lgkmcnt(0)
	v_mfma_scale_f32_16x16x128_f8f6f4 v[214:217], v[132:139], v[206:213], v[84:87], v154, v154 op_sel_hi:[0,0,0]
	v_mfma_scale_f32_16x16x128_f8f6f4 v[218:221], v[158:165], v[206:213], v[72:75], v154, v154 op_sel_hi:[0,0,0]
	s_setprio 0
	s_setprio 1
	v_mfma_scale_f32_16x16x128_f8f6f4 v[112:115], v[166:173], v[182:189], v[112:115], v154, v154 op_sel_hi:[0,0,0]
	v_mfma_scale_f32_16x16x128_f8f6f4 v[108:111], v[174:181], v[182:189], v[108:111], v154, v154 op_sel_hi:[0,0,0]
	v_mfma_scale_f32_16x16x128_f8f6f4 v[96:99], v[166:173], v[190:197], v[96:99], v154, v154 op_sel_hi:[0,0,0]
	v_mfma_scale_f32_16x16x128_f8f6f4 v[182:185], v[174:181], v[190:197], v[92:95], v154, v154 op_sel_hi:[0,0,0]
	v_mfma_scale_f32_16x16x128_f8f6f4 v[186:189], v[166:173], v[198:205], v[80:83], v154, v154 op_sel_hi:[0,0,0]
	v_mfma_scale_f32_16x16x128_f8f6f4 v[190:193], v[174:181], v[198:205], v[76:79], v154, v154 op_sel_hi:[0,0,0]
	v_mfma_scale_f32_16x16x128_f8f6f4 v[194:197], v[166:173], v[206:213], v[68:71], v154, v154 op_sel_hi:[0,0,0]
	v_mfma_scale_f32_16x16x128_f8f6f4 v[198:201], v[174:181], v[206:213], v[64:67], v154, v154 op_sel_hi:[0,0,0]
	s_setprio 0
	s_barrier
	s_nop 4
	ds_read_b128 v[64:67], v153 offset:16384
	ds_read_b128 v[68:71], v153 offset:17408
	ds_read_b128 v[72:75], v153 offset:18432
	ds_read_b128 v[76:79], v153 offset:19456
	ds_read_b128 v[80:83], v153 offset:20480
	ds_read_b128 v[84:87], v153 offset:21504
	ds_read_b128 v[88:91], v153 offset:22528
	ds_read_b128 v[92:95], v153 offset:23552
	s_mov_b32 m0, s55
	s_nop 0
	global_load_lds_dwordx4 v148, s[44:45]
	s_add_u32 s84, s44, 0x40000
	s_mov_b32 m0, s56
	s_nop 0
	global_load_lds_dwordx4 v150, s[44:45]
	s_addc_u32 s85, s45, 0
	s_mov_b32 m0, s57
	s_nop 0
	global_load_lds_dwordx4 v148, s[84:85]
	s_nop 0
	s_mov_b32 m0, s58
	s_nop 0
	global_load_lds_dwordx4 v150, s[84:85]
	s_nop 0
	s_mov_b32 m0, s54
	s_nop 0
	global_load_lds_dwordx4 v147, s[46:47]
	s_nop 0
	s_mov_b32 m0, s59
	s_nop 0
	global_load_lds_dwordx4 v149, s[46:47]
	s_waitcnt vmcnt(8)
	s_waitcnt lgkmcnt(0)
	s_barrier
	s_setprio 1
	s_waitcnt lgkmcnt(6)
	v_mfma_scale_f32_16x16x128_f8f6f4 v[60:63], v[132:139], v[64:71], v[60:63], v154, v154 op_sel_hi:[0,0,0]
	v_mfma_scale_f32_16x16x128_f8f6f4 v[56:59], v[158:165], v[64:71], v[56:59], v154, v154 op_sel_hi:[0,0,0]
	s_waitcnt lgkmcnt(4)
	v_mfma_scale_f32_16x16x128_f8f6f4 v[48:51], v[132:139], v[72:79], v[48:51], v154, v154 op_sel_hi:[0,0,0]
	v_mfma_scale_f32_16x16x128_f8f6f4 v[202:205], v[158:165], v[72:79], v[40:43], v154, v154 op_sel_hi:[0,0,0]
	s_waitcnt lgkmcnt(2)
	v_mfma_scale_f32_16x16x128_f8f6f4 v[206:209], v[132:139], v[80:87], v[32:35], v154, v154 op_sel_hi:[0,0,0]
	v_mfma_scale_f32_16x16x128_f8f6f4 v[210:213], v[158:165], v[80:87], v[24:27], v154, v154 op_sel_hi:[0,0,0]
	s_waitcnt lgkmcnt(0)
	v_mfma_scale_f32_16x16x128_f8f6f4 v[222:225], v[132:139], v[88:95], v[16:19], v154, v154 op_sel_hi:[0,0,0]
	v_mfma_scale_f32_16x16x128_f8f6f4 v[226:229], v[158:165], v[88:95], v[8:11], v154, v154 op_sel_hi:[0,0,0]
	s_setprio 0
	s_setprio 1
	v_mfma_scale_f32_16x16x128_f8f6f4 v[52:55], v[166:173], v[64:71], v[52:55], v154, v154 op_sel_hi:[0,0,0]
	v_mfma_scale_f32_16x16x128_f8f6f4 v[230:233], v[174:181], v[64:71], v[44:47], v154, v154 op_sel_hi:[0,0,0]
	v_mfma_scale_f32_16x16x128_f8f6f4 v[234:237], v[166:173], v[72:79], v[36:39], v154, v154 op_sel_hi:[0,0,0]
	v_mfma_scale_f32_16x16x128_f8f6f4 v[238:241], v[174:181], v[72:79], v[28:31], v154, v154 op_sel_hi:[0,0,0]
	v_mfma_scale_f32_16x16x128_f8f6f4 v[242:245], v[166:173], v[80:87], v[20:23], v154, v154 op_sel_hi:[0,0,0]
	v_mfma_scale_f32_16x16x128_f8f6f4 v[246:249], v[174:181], v[80:87], v[12:15], v154, v154 op_sel_hi:[0,0,0]
	v_mfma_scale_f32_16x16x128_f8f6f4 v[250:253], v[166:173], v[88:95], v[4:7], v154, v154 op_sel_hi:[0,0,0]
	v_mfma_scale_f32_16x16x128_f8f6f4 v[128:131], v[174:181], v[88:95], v[0:3], v154, v154 op_sel_hi:[0,0,0]
	s_setprio 0
	s_barrier
; #define PG8_WAIT_V(n) asm volatile("s_waitcnt vmcnt(" #n ")" ::: "memory")
; #define PG8_WAIT_L(n) asm volatile("s_waitcnt lgkmcnt(" #n ")" ::: "memory")
; #define PG8_BAR __builtin_amdgcn_s_barrier()
; #define PG8_SCHED __builtin_amdgcn_sched_barrier(0)
; #define PG8_STAGE_A(b, h, p) do { if constexpr (GATHER) { if ((h) == 0) PG8_STAGE(PG8_SA(b, h), p, vA0); else PG8_STAGE(PG8_SA(b, h), p, vA1); } else PG8_STAGE(PG8_SA(b, h), (p) + ((h) ? hstepA : (size_t)0), voffA); } while (0)
; template <class Epi, class Sched, bool ALIGN_EPI = true, bool SP2 = true, bool FP8 = false, bool GATHER = false>
; __device__ __forceinline__ void gemm_phase(LAS unsigned char* lds, const Dims g, const Sched& S, const Epi& E, const int wv) {
;     ...
;             PG8_LDB(B0, 1, 0); PG8_LDB(B1, 1, 1); PG8_SCHED; PG8_LDA(At, 1, 0); PG8_STAGE_A(0, 1, a2);
;             PG8_WAIT_V(8); PG8_WAIT_L(0); PG8_BAR; PG8_MMA(0, 0, At, B0); PG8_MMA(0, 1, At, B1); PG8_BAR; PG8_SCHED;
;             PG8_LDA(At, 1, 1); PG8_STAGE(PG8_SB(1, 0), b3, voffB); PG8_STAGE(PG8_SB(1, 1), b3 + hstepB, voffB); PG8_STAGE_A(1, 0, a3);
;             PG8_WAIT_V(8); PG8_WAIT_L(0); PG8_BAR; PG8_MMA(1, 0, At, B0); PG8_MMA(1, 1, At, B1); PG8_BAR; PG8_SCHED;
	s_nop 4
	ds_read_b128 v[0:3], v155
	ds_read_b128 v[4:7], v155 offset:1024
	ds_read_b128 v[8:11], v155 offset:2048
	ds_read_b128 v[12:15], v155 offset:3072
	ds_read_b128 v[132:135], v156
	ds_read_b128 v[136:139], v156 offset:1024
	ds_read_b128 v[158:161], v156 offset:2048
	ds_read_b128 v[162:165], v156 offset:3072
	ds_read_b128 v[16:19], v153 offset:32768
	ds_read_b128 v[20:23], v153 offset:33792
	ds_read_b128 v[24:27], v153 offset:34816
	ds_read_b128 v[28:31], v153 offset:35840
	ds_read_b128 v[32:35], v153 offset:36864
	ds_read_b128 v[36:39], v153 offset:37888
	ds_read_b128 v[40:43], v153 offset:38912
	ds_read_b128 v[44:47], v153 offset:39936
	s_add_u32 s46, s46, 0x40000
	s_addc_u32 s47, s47, 0
	s_mov_b32 m0, s60
	s_nop 0
	global_load_lds_dwordx4 v147, s[46:47]
	s_nop 0
	s_mov_b32 m0, s61
	s_nop 0
	global_load_lds_dwordx4 v149, s[46:47]
	s_waitcnt vmcnt(8)
	s_waitcnt lgkmcnt(0)
	s_barrier
	s_setprio 1
	s_waitcnt lgkmcnt(6)
	v_mfma_scale_f32_16x16x128_f8f6f4 v[124:127], v[0:7], v[16:23], v[124:127], v154, v154 op_sel_hi:[0,0,0]
	v_mfma_scale_f32_16x16x128_f8f6f4 v[120:123], v[8:15], v[16:23], v[120:123], v154, v154 op_sel_hi:[0,0,0]
	s_waitcnt lgkmcnt(4)
	v_mfma_scale_f32_16x16x128_f8f6f4 v[116:119], v[0:7], v[24:31], v[116:119], v154, v154 op_sel_hi:[0,0,0]
	v_mfma_scale_f32_16x16x128_f8f6f4 v[104:107], v[8:15], v[24:31], v[104:107], v154, v154 op_sel_hi:[0,0,0]
	s_waitcnt lgkmcnt(2)
	v_mfma_scale_f32_16x16x128_f8f6f4 v[100:103], v[0:7], v[32:39], v[100:103], v154, v154 op_sel_hi:[0,0,0]
	v_mfma_scale_f32_16x16x128_f8f6f4 v[88:91], v[8:15], v[32:39], v[140:143], v154, v154 op_sel_hi:[0,0,0]
	s_waitcnt lgkmcnt(0)
	v_mfma_scale_f32_16x16x128_f8f6f4 v[84:87], v[0:7], v[40:47], v[214:217], v154, v154 op_sel_hi:[0,0,0]
	v_mfma_scale_f32_16x16x128_f8f6f4 v[72:75], v[8:15], v[40:47], v[218:221], v154, v154 op_sel_hi:[0,0,0]
	s_setprio 0
	s_setprio 1
	v_mfma_scale_f32_16x16x128_f8f6f4 v[112:115], v[132:139], v[16:23], v[112:115], v154, v154 op_sel_hi:[0,0,0]
	v_mfma_scale_f32_16x16x128_f8f6f4 v[108:111], v[158:165], v[16:23], v[108:111], v154, v154 op_sel_hi:[0,0,0]
	v_mfma_scale_f32_16x16x128_f8f6f4 v[96:99], v[132:139], v[24:31], v[96:99], v154, v154 op_sel_hi:[0,0,0]
	v_mfma_scale_f32_16x16x128_f8f6f4 v[92:95], v[158:165], v[24:31], v[182:185], v154, v154 op_sel_hi:[0,0,0]
	v_mfma_scale_f32_16x16x128_f8f6f4 v[80:83], v[132:139], v[32:39], v[186:189], v154, v154 op_sel_hi:[0,0,0]
	v_mfma_scale_f32_16x16x128_f8f6f4 v[76:79], v[158:165], v[32:39], v[190:193], v154, v154 op_sel_hi:[0,0,0]
	v_mfma_scale_f32_16x16x128_f8f6f4 v[68:71], v[132:139], v[40:47], v[194:197], v154, v154 op_sel_hi:[0,0,0]
	v_mfma_scale_f32_16x16x128_f8f6f4 v[64:67], v[158:165], v[40:47], v[198:201], v154, v154 op_sel_hi:[0,0,0]
	s_setprio 0
	s_barrier
	ds_read_b128 v[166:169], v153 offset:49152
	ds_read_b128 v[170:173], v153 offset:50176
	ds_read_b128 v[174:177], v153 offset:51200
	ds_read_b128 v[178:181], v153 offset:52224
	ds_read_b128 v[182:185], v153 offset:53248
	ds_read_b128 v[186:189], v153 offset:54272
	ds_read_b128 v[190:193], v153 offset:55296
	ds_read_b128 v[194:197], v153 offset:56320
	s_add_u32 s46, s44, 0x80
	s_addc_u32 s47, s45, 0
	s_mov_b32 m0, s66
	s_nop 0
	global_load_lds_dwordx4 v148, s[46:47]
	s_add_u32 s44, s44, 0x40080
	s_mov_b32 m0, s67
	s_nop 0
	global_load_lds_dwordx4 v150, s[46:47]
	s_addc_u32 s45, s45, 0
	s_mov_b32 m0, s70
	s_nop 0
	global_load_lds_dwordx4 v148, s[44:45]
	s_nop 0
	s_mov_b32 m0, s71
	s_nop 0
	global_load_lds_dwordx4 v150, s[44:45]
	s_mov_b32 m0, s68
	s_nop 0
	global_load_lds_dwordx4 v147, s[42:43]
	s_nop 0
	s_mov_b32 m0, s69
	s_nop 0
	global_load_lds_dwordx4 v149, s[42:43]
	s_waitcnt vmcnt(8)
	s_waitcnt lgkmcnt(0)
	s_barrier
	s_setprio 1
	s_waitcnt lgkmcnt(6)
	v_mfma_scale_f32_16x16x128_f8f6f4 v[60:63], v[0:7], v[166:173], v[60:63], v154, v154 op_sel_hi:[0,0,0]
	v_mfma_scale_f32_16x16x128_f8f6f4 v[56:59], v[8:15], v[166:173], v[56:59], v154, v154 op_sel_hi:[0,0,0]
	s_waitcnt lgkmcnt(4)
	v_mfma_scale_f32_16x16x128_f8f6f4 v[48:51], v[0:7], v[174:181], v[48:51], v154, v154 op_sel_hi:[0,0,0]
	v_mfma_scale_f32_16x16x128_f8f6f4 v[40:43], v[8:15], v[174:181], v[202:205], v154, v154 op_sel_hi:[0,0,0]
	s_waitcnt lgkmcnt(2)
	v_mfma_scale_f32_16x16x128_f8f6f4 v[32:35], v[0:7], v[182:189], v[206:209], v154, v154 op_sel_hi:[0,0,0]
	v_mfma_scale_f32_16x16x128_f8f6f4 v[24:27], v[8:15], v[182:189], v[210:213], v154, v154 op_sel_hi:[0,0,0]
	s_waitcnt lgkmcnt(0)
	v_mfma_scale_f32_16x16x128_f8f6f4 v[16:19], v[0:7], v[190:197], v[222:225], v154, v154 op_sel_hi:[0,0,0]
	v_mfma_scale_f32_16x16x128_f8f6f4 v[8:11], v[8:15], v[190:197], v[226:229], v154, v154 op_sel_hi:[0,0,0]
	s_setprio 0
	s_setprio 1
	v_mfma_scale_f32_16x16x128_f8f6f4 v[52:55], v[132:139], v[166:173], v[52:55], v154, v154 op_sel_hi:[0,0,0]
	v_mfma_scale_f32_16x16x128_f8f6f4 v[44:47], v[158:165], v[166:173], v[230:233], v154, v154 op_sel_hi:[0,0,0]
	v_mfma_scale_f32_16x16x128_f8f6f4 v[36:39], v[132:139], v[174:181], v[234:237], v154, v154 op_sel_hi:[0,0,0]
	v_mfma_scale_f32_16x16x128_f8f6f4 v[28:31], v[158:165], v[174:181], v[238:241], v154, v154 op_sel_hi:[0,0,0]
	v_mfma_scale_f32_16x16x128_f8f6f4 v[20:23], v[132:139], v[182:189], v[242:245], v154, v154 op_sel_hi:[0,0,0]
	v_mfma_scale_f32_16x16x128_f8f6f4 v[12:15], v[158:165], v[182:189], v[246:249], v154, v154 op_sel_hi:[0,0,0]
	v_mfma_scale_f32_16x16x128_f8f6f4 v[4:7], v[132:139], v[190:197], v[250:253], v154, v154 op_sel_hi:[0,0,0]
	v_mfma_scale_f32_16x16x128_f8f6f4 v[0:3], v[158:165], v[190:197], v[128:131], v154, v154 op_sel_hi:[0,0,0]
	s_setprio 0
	s_barrier
	s_add_i32 s82, s82, 2
	s_add_u32 s23, s23, 0x100
	s_addc_u32 s25, s25, 0
	s_add_u32 s80, s80, 0x100
	s_addc_u32 s81, s81, 0
	s_add_u32 s40, s40, 0x100
	s_addc_u32 s41, s41, 0
	s_cmp_gt_u32 s82, 13
	s_cbranch_scc0 .LBB0_1913
	s_and_b64 vcc, exec, s[10:11]
	s_cbranch_vccz .LBB0_1916
	s_barrier

; #define PG8_WAIT_V(n) asm volatile("s_waitcnt vmcnt(" #n ")" ::: "memory")
; #define PG8_BAR __builtin_amdgcn_s_barrier()
; #define PG8_STAGE_A(b, h, p) do { if constexpr (GATHER) { if ((h) == 0) PG8_STAGE(PG8_SA(b, h), p, vA0); else PG8_STAGE(PG8_SA(b, h), p, vA1); } else PG8_STAGE(PG8_SA(b, h), (p) + ((h) ? hstepA : (size_t)0), voffA); } while (0)
; #define PG8_GOFF(un, d0, d1) do { PG8_GOFF1(un, 0, d0); PG8_GOFF1(un, 1, d1); } while (0)
; template <class Epi, class Sched, bool ALIGN_EPI = true, bool SP2 = true, bool FP8 = false, bool GATHER = false>
; __device__ __forceinline__ void gemm_phase(LAS unsigned char* lds, const Dims g, const Sched& S, const Epi& E, const int wv) {
;     ...
;     unsigned vA0[2], vA1[2];
;     Unit cur, nxt; int ui = 0;
;     if (!S.next(0, cur)) return;
;     if constexpr (GATHER) PG8_GOFF(0, vA0, vA1);
;     ...
;     if constexpr (SP2) {
;         PG8_STAGE(PG8_SB(0, 0), cB, voffB); PG8_STAGE(PG8_SB(0, 1), cB + hstepB, voffB); PG8_STAGE_A(0, 0, cA); PG8_STAGE_A(0, 1, cA);
;         if (wr == 1) PG8_BAR;
;         PG8_WAIT_V(2); PG8_BAR;
;         PG8_STAGE(PG8_SB(1, 0), cB + kstep, voffB); PG8_STAGE_A(1, 0, cA + kstep); PG8_STAGE(PG8_SB(1, 1), cB + hstepB + kstep, voffB);
;         PG8_WAIT_V(6); PG8_BAR;
.LBB0_2519:
	v_lshlrev_b32_e32 v1, 6, v3
	v_sub_u32_e32 v1, v2, v1
	v_mov_b32_e32 v193, 1
	v_and_b32_e32 v0, 32, v4
	v_ashrrev_i16_sdwa v1, v193, sext(v1) dst_sel:DWORD dst_unused:UNUSED_PAD src0_sel:DWORD src1_sel:BYTE_0
	v_add_u32_sdwa v0, v0, sext(v1) dst_sel:DWORD dst_unused:UNUSED_PAD src0_sel:DWORD src1_sel:WORD_0
	v_lshlrev_b32_e32 v1, 6, v6
	v_sub_u32_e32 v1, v5, v1
	s_waitcnt lgkmcnt(0)
	v_lshl_add_u32 v194, v0, 1, v9
	v_and_b32_e32 v0, 32, v8
	v_ashrrev_i16_sdwa v1, v193, sext(v1) dst_sel:DWORD dst_unused:UNUSED_PAD src0_sel:DWORD src1_sel:BYTE_0
	v_add_u32_sdwa v0, v0, sext(v1) dst_sel:DWORD dst_unused:UNUSED_PAD src0_sel:DWORD src1_sel:WORD_0
	v_lshlrev_b32_e32 v1, 6, v11
	v_sub_u32_e32 v1, v10, v1
	v_lshl_add_u32 v196, v0, 1, v7
	v_and_b32_e32 v0, 32, v12
	v_ashrrev_i16_sdwa v1, v193, sext(v1) dst_sel:DWORD dst_unused:UNUSED_PAD src0_sel:DWORD src1_sel:BYTE_0
	v_add_u32_sdwa v0, v0, sext(v1) dst_sel:DWORD dst_unused:UNUSED_PAD src0_sel:DWORD src1_sel:WORD_0
	v_lshlrev_b32_e32 v1, 6, v14
	v_sub_u32_e32 v1, v13, v1
	v_lshl_add_u32 v197, v0, 1, v17
	v_and_b32_e32 v0, 32, v16
	v_ashrrev_i16_sdwa v1, v193, sext(v1) dst_sel:DWORD dst_unused:UNUSED_PAD src0_sel:DWORD src1_sel:BYTE_0
	v_add_u32_sdwa v0, v0, sext(v1) dst_sel:DWORD dst_unused:UNUSED_PAD src0_sel:DWORD src1_sel:WORD_0
	v_bfe_i32 v2, v192, 27, 1
	v_lshl_add_u32 v198, v0, 1, v15
	v_lshlrev_b32_e32 v0, 4, v192
	v_lshrrev_b32_e32 v2, 22, v2
	v_add_u32_e32 v2, v0, v2
	v_and_b32_e32 v2, 0xfffffc00, v2
	v_sub_u32_e32 v2, v0, v2
	v_ashrrev_i32_e32 v1, 31, v192
	v_lshrrev_b32_e32 v3, 4, v2
	v_lshrrev_b32_e32 v1, 26, v1
	v_bitop3_b32 v2, v3, v2, 32 bitop3:0x6c
	v_add_u32_e32 v1, v192, v1
	v_ashrrev_i32_e32 v4, 31, v2
	v_ashrrev_i32_e32 v1, 6, v1
	v_lshrrev_b32_e32 v4, 26, v4
	v_lshlrev_b32_e32 v3, 3, v1
	v_add_u32_e32 v4, v2, v4
	v_and_b32_e32 v3, -16, v3
	v_ashrrev_i32_e32 v5, 6, v4
	v_and_b32_e32 v4, 0xc0, v4
	v_add_u32_e32 v3, v5, v3
	v_sub_u32_e32 v2, v2, v4
	v_lshlrev_b32_e32 v1, 5, v1
	v_ashrrev_i16_sdwa v2, v193, sext(v2) dst_sel:DWORD dst_unused:UNUSED_PAD src0_sel:DWORD src1_sel:BYTE_0
	v_lshlrev_b32_e32 v4, 1, v3
	v_lshrrev_b32_e32 v6, 2, v3
	v_and_b32_e32 v5, 3, v5
	s_mov_b32 s4, 0x3fffe0
	v_and_b32_e32 v1, 32, v1
	v_bfe_i32 v2, v2, 0, 16
	v_and_b32_e32 v4, 24, v4
	v_and_b32_e32 v6, 4, v6
	v_and_or_b32 v3, v3, s4, v5
	v_or3_b32 v3, v3, v6, v4
	v_add_lshl_u32 v1, v1, v2, 1
	v_add_u32_e32 v0, 0x2000, v0
	v_lshl_add_u32 v195, v3, 10, v1
	v_ashrrev_i32_e32 v1, 31, v0
	v_lshrrev_b32_e32 v1, 22, v1
	v_add_u32_e32 v1, v0, v1
	v_ashrrev_i32_e32 v1, 10, v1
	v_mul_i32_i24_e32 v2, 0x400, v1
	v_sub_u32_e32 v0, v0, v2
	v_lshrrev_b32_e32 v2, 4, v0
	v_bitop3_b32 v0, v2, v0, 32 bitop3:0x6c
	v_ashrrev_i32_e32 v3, 31, v0
	v_lshrrev_b32_e32 v3, 26, v3
	v_lshlrev_b32_e32 v2, 3, v1
	v_add_u32_e32 v3, v0, v3
	v_and_b32_e32 v2, -16, v2
	v_ashrrev_i32_e32 v4, 6, v3
	v_and_b32_e32 v3, 0xc0, v3
	v_add_u32_e32 v2, v4, v2
	v_sub_u32_e32 v0, v0, v3
	v_and_b32_e32 v4, 3, v4
	s_ashr_i32 s17, s23, 6
	v_lshlrev_b32_e32 v1, 5, v1
	v_ashrrev_i16_sdwa v0, v193, sext(v0) dst_sel:DWORD dst_unused:UNUSED_PAD src0_sel:DWORD src1_sel:BYTE_0
	v_lshlrev_b32_e32 v3, 1, v2
	v_lshrrev_b32_e32 v5, 2, v2
	v_and_or_b32 v2, v2, s4, v4
	s_lshl_b32 s4, s17, 10
	v_and_b32_e32 v1, 32, v1
	v_bfe_i32 v0, v0, 0, 16
	v_and_b32_e32 v3, 24, v3
	v_and_b32_e32 v5, 4, v5
	s_add_i32 s27, s4, 0
	v_or3_b32 v2, v2, v5, v3
	v_add_lshl_u32 v0, v1, v0, 1
	s_add_i32 s54, s27, 0x10000
	s_mov_b32 m0, s54
	s_nop 0
	global_load_lds_dwordx4 v195, s[40:41]
	s_ashr_i32 s16, s23, 8
	v_lshl_add_u32 v199, v2, 10, v0
	s_add_i32 s55, s27, 0x12000
	s_mov_b32 m0, s55
	s_nop 0
	global_load_lds_dwordx4 v199, s[40:41]
	s_add_i32 s56, s27, 0x14000
	s_add_u32 s4, s40, 0x20000
	s_addc_u32 s5, s41, 0
	s_mov_b32 m0, s56
	s_nop 0
	global_load_lds_dwordx4 v195, s[4:5]
	s_add_i32 s57, s27, 0x16000
	s_mov_b32 m0, s57
	s_nop 0
	global_load_lds_dwordx4 v199, s[4:5]
	s_mov_b32 m0, s27
	s_nop 0
	global_load_lds_dwordx4 v194, s[38:39]
	s_add_i32 s58, s27, 0x2000
	s_mov_b32 m0, s58
	s_nop 0
	global_load_lds_dwordx4 v196, s[38:39]
	s_add_i32 s59, s27, 0x4000
	s_mov_b32 m0, s59
	s_nop 0
	global_load_lds_dwordx4 v197, s[38:39]
	s_add_i32 s60, s27, 0x6000
	s_mov_b32 m0, s60
	s_nop 0
	global_load_lds_dwordx4 v198, s[38:39]
	s_cmp_eq_u32 s16, 1
	s_mov_b32 s81, 0
	s_cselect_b64 s[4:5], -1, 0
	s_cmp_lg_u32 s16, 1
	s_cbranch_scc1 .LBB0_2521
	s_barrier
.LBB0_2521:
	s_add_u32 s12, s12, 0x8d200000
	s_addc_u32 s13, s13, 0
	s_add_u32 s61, s14, 0x40000
	s_addc_u32 s62, s15, 0
	v_and_b32_e32 v0, 48, v192
	v_lshlrev_b32_e32 v1, 6, v192
	s_movk_i32 s15, 0x3c0
	v_and_or_b32 v0, v1, s15, v0
	v_lshlrev_b32_e32 v1, 2, v192
	s_lshl_b32 s14, s16, 13
	v_and_b32_e32 v1, 32, v1
	v_bitop3_b32 v2, v0, s14, v1 bitop3:0xde
	s_lshl_b32 s14, s17, 5
	s_and_b32 s64, s14, 0x60
	s_lshl_b32 s63, s16, 6
	s_lshl_b32 s14, s64, 7
	s_add_i32 s65, s27, 0x18000
	v_bitop3_b32 v0, s14, v0, v1 bitop3:0xf6
	s_add_u32 s14, s40, 0x80
	s_waitcnt vmcnt(2)
	s_barrier
	s_addc_u32 s15, s41, 0
	s_mov_b32 m0, s65
	s_nop 0
	global_load_lds_dwordx4 v195, s[14:15]
	s_add_i32 s66, s27, 0x1a000
	s_add_i32 s67, s27, 0x8000
	s_mov_b32 m0, s66
	s_nop 0
	global_load_lds_dwordx4 v199, s[14:15]
	s_add_u32 s14, s38, 0x80
	s_addc_u32 s15, s39, 0
	s_mov_b32 m0, s67
	s_nop 0
	global_load_lds_dwordx4 v194, s[14:15]
	s_add_i32 s68, s27, 0xa000
	s_add_i32 s69, s27, 0x1c000
	s_mov_b32 m0, s68
	s_nop 0
	global_load_lds_dwordx4 v196, s[14:15]
	s_add_u32 s14, s40, 0x20080
	s_addc_u32 s15, s41, 0
	s_mov_b32 m0, s69
	s_nop 0
	global_load_lds_dwordx4 v195, s[14:15]
	s_add_i32 s70, s27, 0x1e000
	s_mov_b32 m0, s70
	s_nop 0
	global_load_lds_dwordx4 v199, s[14:15]
	s_waitcnt vmcnt(6)
	s_add_i32 s71, s27, 0xc000
	s_cmpk_lt_u32 s23, 0x100
	s_cselect_b64 s[14:15], -1, 0
	s_add_i32 s72, s27, 0xe000
	v_mov_b32_e32 v200, 0x7f7f7f7f
	s_mov_b64 s[16:17], 0x1000
	s_movk_i32 s73, 0x1000
	s_mov_b32 s74, 0xc0e00000
	v_add_u32_e32 v201, 0, v0
	v_add_u32_e32 v202, 0, v2
	v_mov_b32_e32 v203, 0x40e00000
	s_barrier
	s_branch .LBB0_2524

; #define PG8_WAIT_V(n) asm volatile("s_waitcnt vmcnt(" #n ")" ::: "memory")
; #define PG8_WAIT_L(n) asm volatile("s_waitcnt lgkmcnt(" #n ")" ::: "memory")
; #define PG8_BAR __builtin_amdgcn_s_barrier()
; #define PG8_SCHED __builtin_amdgcn_sched_barrier(0)
; #define PG8_STAGE_A(b, h, p) do { if constexpr (GATHER) { if ((h) == 0) PG8_STAGE(PG8_SA(b, h), p, vA0); else PG8_STAGE(PG8_SA(b, h), p, vA1); } else PG8_STAGE(PG8_SA(b, h), (p) + ((h) ? hstepA : (size_t)0), voffA); } while (0)
; #define PG8_GOFF1(un, h, d) do { int tz_ = tid; asm volatile("" : "+v"(tz_)); _Pragma("unroll") for (int i_ = 0; i_ < 2; ++i_) { int R_, C_; stage_rc(tz_ * 16 + i_ * 8192, R_, C_); \
;         d[i_] = S.gather(un, R_ + (h) * HALF) + (unsigned)C_ * 2u; } } while (0)
; template <class Epi, class Sched, bool ALIGN_EPI = true, bool SP2 = true, bool FP8 = false, bool GATHER = false>
; __device__ __forceinline__ void gemm_phase(LAS unsigned char* lds, const Dims g, const Sched& S, const Epi& E, const int wv) {
;     ...
;             PG8_LDB(B0, 0, 0); PG8_LDB(B1, 0, 1); PG8_SCHED; PG8_LDA(At, 0, 0); PG8_STAGE_A(1, 1, a1);
;             if constexpr (GATHER) { if (last) PG8_GOFF1(un_, 1, vA1); }
;             PG8_WAIT_V(8); PG8_WAIT_L(0); PG8_BAR; PG8_MMA(0, 0, At, B0); PG8_MMA(0, 1, At, B1); PG8_BAR; PG8_SCHED;
;             PG8_LDA(At, 0, 1); PG8_STAGE(PG8_SB(0, 0), b2, voffB); PG8_STAGE(PG8_SB(0, 1), b2 + hstepB, voffB); PG8_STAGE_A(0, 0, a2);
;             PG8_WAIT_V(8); PG8_WAIT_L(0); PG8_BAR; PG8_MMA(1, 0, At, B0); PG8_MMA(1, 1, At, B1); PG8_BAR; PG8_SCHED;
.LBB0_2530:
	s_add_u32 s38, s38, 0x100
	s_addc_u32 s39, s39, 0
	s_and_b64 s[40:41], s[40:41], exec
	s_cselect_b32 s46, s78, s38
	s_waitcnt vmcnt(8)
	s_cselect_b32 s47, s37, s39
	s_cselect_b32 s43, s79, s83
	s_cselect_b32 s42, s80, s82
	s_add_u32 s40, s46, 0x80
	s_waitcnt lgkmcnt(0)
	s_addc_u32 s41, s47, 0
	s_add_u32 s44, s42, 0x80
	s_addc_u32 s45, s43, 0
	s_barrier
	s_setprio 1
	s_waitcnt lgkmcnt(6)
	v_mfma_scale_f32_16x16x128_f8f6f4 v[188:191], v[16:23], v[56:63], v[188:191], v200, v200 op_sel_hi:[0,0,0]
	v_mfma_scale_f32_16x16x128_f8f6f4 v[184:187], v[24:31], v[56:63], v[184:187], v200, v200 op_sel_hi:[0,0,0]
	s_waitcnt lgkmcnt(4)
	v_mfma_scale_f32_16x16x128_f8f6f4 v[172:175], v[16:23], v[48:55], v[172:175], v200, v200 op_sel_hi:[0,0,0]
	v_mfma_scale_f32_16x16x128_f8f6f4 v[168:171], v[24:31], v[48:55], v[168:171], v200, v200 op_sel_hi:[0,0,0]
	s_waitcnt lgkmcnt(2)
	v_mfma_scale_f32_16x16x128_f8f6f4 v[156:159], v[16:23], v[40:47], v[156:159], v200, v200 op_sel_hi:[0,0,0]
	v_mfma_scale_f32_16x16x128_f8f6f4 v[152:155], v[24:31], v[40:47], v[152:155], v200, v200 op_sel_hi:[0,0,0]
	s_waitcnt lgkmcnt(0)
	v_mfma_scale_f32_16x16x128_f8f6f4 v[140:143], v[16:23], v[32:39], v[140:143], v200, v200 op_sel_hi:[0,0,0]
	v_mfma_scale_f32_16x16x128_f8f6f4 v[136:139], v[24:31], v[32:39], v[136:139], v200, v200 op_sel_hi:[0,0,0]
	s_setprio 0
	s_setprio 1
	v_mfma_scale_f32_16x16x128_f8f6f4 v[180:183], v[0:7], v[56:63], v[180:183], v200, v200 op_sel_hi:[0,0,0]
	v_mfma_scale_f32_16x16x128_f8f6f4 v[176:179], v[8:15], v[56:63], v[176:179], v200, v200 op_sel_hi:[0,0,0]
	v_mfma_scale_f32_16x16x128_f8f6f4 v[164:167], v[0:7], v[48:55], v[164:167], v200, v200 op_sel_hi:[0,0,0]
	v_mfma_scale_f32_16x16x128_f8f6f4 v[160:163], v[8:15], v[48:55], v[160:163], v200, v200 op_sel_hi:[0,0,0]
	v_mfma_scale_f32_16x16x128_f8f6f4 v[148:151], v[0:7], v[40:47], v[148:151], v200, v200 op_sel_hi:[0,0,0]
	v_mfma_scale_f32_16x16x128_f8f6f4 v[144:147], v[8:15], v[40:47], v[144:147], v200, v200 op_sel_hi:[0,0,0]
	v_mfma_scale_f32_16x16x128_f8f6f4 v[132:135], v[0:7], v[32:39], v[132:135], v200, v200 op_sel_hi:[0,0,0]
	v_mfma_scale_f32_16x16x128_f8f6f4 v[128:131], v[8:15], v[32:39], v[128:131], v200, v200 op_sel_hi:[0,0,0]
	s_setprio 0
	s_barrier
	ds_read_b128 v[32:35], v202 offset:16384
	ds_read_b128 v[36:39], v202 offset:17408
	ds_read_b128 v[40:43], v202 offset:18432
	ds_read_b128 v[44:47], v202 offset:19456
	ds_read_b128 v[48:51], v202 offset:20480
	ds_read_b128 v[52:55], v202 offset:21504
	ds_read_b128 v[56:59], v202 offset:22528
	ds_read_b128 v[60:63], v202 offset:23552
	s_mov_b32 m0, s54
	s_nop 0
	global_load_lds_dwordx4 v195, s[42:43]
	s_add_u32 s86, s42, 0x20000
	s_mov_b32 m0, s55
	s_nop 0
	global_load_lds_dwordx4 v199, s[42:43]
	s_addc_u32 s87, s43, 0
	s_mov_b32 m0, s56
	s_nop 0
	global_load_lds_dwordx4 v195, s[86:87]
	s_nop 0
	s_mov_b32 m0, s57
	s_nop 0
	global_load_lds_dwordx4 v199, s[86:87]
	s_nop 0
	s_mov_b32 m0, s27
	s_nop 0
	global_load_lds_dwordx4 v194, s[46:47]
	s_nop 0
	s_mov_b32 m0, s58
	s_nop 0
	global_load_lds_dwordx4 v196, s[46:47]
	s_waitcnt vmcnt(8)
	s_waitcnt lgkmcnt(0)
	s_barrier
	s_setprio 1
	s_waitcnt lgkmcnt(6)
	v_mfma_scale_f32_16x16x128_f8f6f4 v[124:127], v[16:23], v[32:39], v[124:127], v200, v200 op_sel_hi:[0,0,0]
	v_mfma_scale_f32_16x16x128_f8f6f4 v[120:123], v[24:31], v[32:39], v[120:123], v200, v200 op_sel_hi:[0,0,0]
	s_waitcnt lgkmcnt(4)
	v_mfma_scale_f32_16x16x128_f8f6f4 v[108:111], v[16:23], v[40:47], v[108:111], v200, v200 op_sel_hi:[0,0,0]
	v_mfma_scale_f32_16x16x128_f8f6f4 v[104:107], v[24:31], v[40:47], v[104:107], v200, v200 op_sel_hi:[0,0,0]
	s_waitcnt lgkmcnt(2)
	v_mfma_scale_f32_16x16x128_f8f6f4 v[92:95], v[16:23], v[48:55], v[92:95], v200, v200 op_sel_hi:[0,0,0]
	v_mfma_scale_f32_16x16x128_f8f6f4 v[88:91], v[24:31], v[48:55], v[88:91], v200, v200 op_sel_hi:[0,0,0]
	s_waitcnt lgkmcnt(0)
	v_mfma_scale_f32_16x16x128_f8f6f4 v[76:79], v[16:23], v[56:63], v[76:79], v200, v200 op_sel_hi:[0,0,0]
	v_mfma_scale_f32_16x16x128_f8f6f4 v[72:75], v[24:31], v[56:63], v[72:75], v200, v200 op_sel_hi:[0,0,0]
	s_setprio 0
	s_setprio 1
	v_mfma_scale_f32_16x16x128_f8f6f4 v[116:119], v[0:7], v[32:39], v[116:119], v200, v200 op_sel_hi:[0,0,0]
	v_mfma_scale_f32_16x16x128_f8f6f4 v[112:115], v[8:15], v[32:39], v[112:115], v200, v200 op_sel_hi:[0,0,0]
	v_mfma_scale_f32_16x16x128_f8f6f4 v[100:103], v[0:7], v[40:47], v[100:103], v200, v200 op_sel_hi:[0,0,0]
	v_mfma_scale_f32_16x16x128_f8f6f4 v[96:99], v[8:15], v[40:47], v[96:99], v200, v200 op_sel_hi:[0,0,0]
	v_mfma_scale_f32_16x16x128_f8f6f4 v[84:87], v[0:7], v[48:55], v[84:87], v200, v200 op_sel_hi:[0,0,0]
	v_mfma_scale_f32_16x16x128_f8f6f4 v[80:83], v[8:15], v[48:55], v[80:83], v200, v200 op_sel_hi:[0,0,0]
	v_mfma_scale_f32_16x16x128_f8f6f4 v[68:71], v[0:7], v[56:63], v[68:71], v200, v200 op_sel_hi:[0,0,0]
	v_mfma_scale_f32_16x16x128_f8f6f4 v[64:67], v[8:15], v[56:63], v[64:67], v200, v200 op_sel_hi:[0,0,0]
	s_setprio 0
	s_barrier
; #define PG8_WAIT_V(n) asm volatile("s_waitcnt vmcnt(" #n ")" ::: "memory")
; #define PG8_WAIT_L(n) asm volatile("s_waitcnt lgkmcnt(" #n ")" ::: "memory")
; #define PG8_BAR __builtin_amdgcn_s_barrier()
; #define PG8_SCHED __builtin_amdgcn_sched_barrier(0)
; #define PG8_STAGE_A(b, h, p) do { if constexpr (GATHER) { if ((h) == 0) PG8_STAGE(PG8_SA(b, h), p, vA0); else PG8_STAGE(PG8_SA(b, h), p, vA1); } else PG8_STAGE(PG8_SA(b, h), (p) + ((h) ? hstepA : (size_t)0), voffA); } while (0)
; template <class Epi, class Sched, bool ALIGN_EPI = true, bool SP2 = true, bool FP8 = false, bool GATHER = false>
; __device__ __forceinline__ void gemm_phase(LAS unsigned char* lds, const Dims g, const Sched& S, const Epi& E, const int wv) {
;     ...
;             PG8_LDB(B0, 1, 0); PG8_LDB(B1, 1, 1); PG8_SCHED; PG8_LDA(At, 1, 0); PG8_STAGE_A(0, 1, a2);
;             PG8_WAIT_V(8); PG8_WAIT_L(0); PG8_BAR; PG8_MMA(0, 0, At, B0); PG8_MMA(0, 1, At, B1); PG8_BAR; PG8_SCHED;
;             PG8_LDA(At, 1, 1); PG8_STAGE(PG8_SB(1, 0), b3, voffB); PG8_STAGE(PG8_SB(1, 1), b3 + hstepB, voffB); PG8_STAGE_A(1, 0, a3);
;             PG8_WAIT_V(8); PG8_WAIT_L(0); PG8_BAR; PG8_MMA(1, 0, At, B0); PG8_MMA(1, 1, At, B1); PG8_BAR; PG8_SCHED;
	v_add_u32_e32 v12, 0x18000, v201
	v_add_u32_e32 v28, 0x1c000, v201
	ds_read_b128 v[0:3], v12
	ds_read_b128 v[4:7], v12 offset:1024
	ds_read_b128 v[8:11], v12 offset:2048
	ds_read_b128 v[12:15], v12 offset:3072
	ds_read_b128 v[16:19], v28
	ds_read_b128 v[20:23], v28 offset:1024
	ds_read_b128 v[24:27], v28 offset:2048
	ds_read_b128 v[28:31], v28 offset:3072
	ds_read_b128 v[32:35], v202 offset:32768
	ds_read_b128 v[36:39], v202 offset:33792
	ds_read_b128 v[40:43], v202 offset:34816
	ds_read_b128 v[44:47], v202 offset:35840
	ds_read_b128 v[48:51], v202 offset:36864
	ds_read_b128 v[52:55], v202 offset:37888
	ds_read_b128 v[56:59], v202 offset:38912
	ds_read_b128 v[60:63], v202 offset:39936
	s_mov_b32 m0, s59
	s_nop 0
	global_load_lds_dwordx4 v197, s[46:47]
	s_nop 0
	s_mov_b32 m0, s60
	s_nop 0
	global_load_lds_dwordx4 v198, s[46:47]
	s_waitcnt vmcnt(8)
	s_waitcnt lgkmcnt(0)
	s_barrier
	s_setprio 1
	s_waitcnt lgkmcnt(6)
	v_mfma_scale_f32_16x16x128_f8f6f4 v[188:191], v[0:7], v[32:39], v[188:191], v200, v200 op_sel_hi:[0,0,0]
	v_mfma_scale_f32_16x16x128_f8f6f4 v[184:187], v[8:15], v[32:39], v[184:187], v200, v200 op_sel_hi:[0,0,0]
	s_waitcnt lgkmcnt(4)
	v_mfma_scale_f32_16x16x128_f8f6f4 v[172:175], v[0:7], v[40:47], v[172:175], v200, v200 op_sel_hi:[0,0,0]
	v_mfma_scale_f32_16x16x128_f8f6f4 v[168:171], v[8:15], v[40:47], v[168:171], v200, v200 op_sel_hi:[0,0,0]
	s_waitcnt lgkmcnt(2)
	v_mfma_scale_f32_16x16x128_f8f6f4 v[156:159], v[0:7], v[48:55], v[156:159], v200, v200 op_sel_hi:[0,0,0]
	v_mfma_scale_f32_16x16x128_f8f6f4 v[152:155], v[8:15], v[48:55], v[152:155], v200, v200 op_sel_hi:[0,0,0]
	s_waitcnt lgkmcnt(0)
	v_mfma_scale_f32_16x16x128_f8f6f4 v[140:143], v[0:7], v[56:63], v[140:143], v200, v200 op_sel_hi:[0,0,0]
	v_mfma_scale_f32_16x16x128_f8f6f4 v[136:139], v[8:15], v[56:63], v[136:139], v200, v200 op_sel_hi:[0,0,0]
	s_setprio 0
	s_setprio 1
	v_mfma_scale_f32_16x16x128_f8f6f4 v[180:183], v[16:23], v[32:39], v[180:183], v200, v200 op_sel_hi:[0,0,0]
	v_mfma_scale_f32_16x16x128_f8f6f4 v[176:179], v[24:31], v[32:39], v[176:179], v200, v200 op_sel_hi:[0,0,0]
	v_mfma_scale_f32_16x16x128_f8f6f4 v[164:167], v[16:23], v[40:47], v[164:167], v200, v200 op_sel_hi:[0,0,0]
	v_mfma_scale_f32_16x16x128_f8f6f4 v[160:163], v[24:31], v[40:47], v[160:163], v200, v200 op_sel_hi:[0,0,0]
	v_mfma_scale_f32_16x16x128_f8f6f4 v[148:151], v[16:23], v[48:55], v[148:151], v200, v200 op_sel_hi:[0,0,0]
	v_mfma_scale_f32_16x16x128_f8f6f4 v[144:147], v[24:31], v[48:55], v[144:147], v200, v200 op_sel_hi:[0,0,0]
	v_mfma_scale_f32_16x16x128_f8f6f4 v[132:135], v[16:23], v[56:63], v[132:135], v200, v200 op_sel_hi:[0,0,0]
	v_mfma_scale_f32_16x16x128_f8f6f4 v[128:131], v[24:31], v[56:63], v[128:131], v200, v200 op_sel_hi:[0,0,0]
	s_setprio 0
	s_barrier
	ds_read_b128 v[32:35], v202 offset:49152
	ds_read_b128 v[36:39], v202 offset:50176
	ds_read_b128 v[40:43], v202 offset:51200
	ds_read_b128 v[44:47], v202 offset:52224
	ds_read_b128 v[48:51], v202 offset:53248
	ds_read_b128 v[52:55], v202 offset:54272
	ds_read_b128 v[56:59], v202 offset:55296
	ds_read_b128 v[60:63], v202 offset:56320
	s_mov_b32 m0, s65
	s_nop 0
	global_load_lds_dwordx4 v195, s[44:45]
	s_add_u32 s42, s42, 0x20080
	s_mov_b32 m0, s66
	s_nop 0
	global_load_lds_dwordx4 v199, s[44:45]
	s_addc_u32 s43, s43, 0
	s_mov_b32 m0, s69
	s_nop 0
	global_load_lds_dwordx4 v195, s[42:43]
	s_nop 0
	s_mov_b32 m0, s70
	s_nop 0
	global_load_lds_dwordx4 v199, s[42:43]
	s_mov_b32 m0, s67
	s_nop 0
	global_load_lds_dwordx4 v194, s[40:41]
	s_nop 0
	s_mov_b32 m0, s68
	s_nop 0
	global_load_lds_dwordx4 v196, s[40:41]
	s_waitcnt vmcnt(8)
	s_waitcnt lgkmcnt(0)
	s_barrier
	s_setprio 1
	s_waitcnt lgkmcnt(6)
	v_mfma_scale_f32_16x16x128_f8f6f4 v[124:127], v[0:7], v[32:39], v[124:127], v200, v200 op_sel_hi:[0,0,0]
	v_mfma_scale_f32_16x16x128_f8f6f4 v[120:123], v[8:15], v[32:39], v[120:123], v200, v200 op_sel_hi:[0,0,0]
	s_waitcnt lgkmcnt(4)
	v_mfma_scale_f32_16x16x128_f8f6f4 v[108:111], v[0:7], v[40:47], v[108:111], v200, v200 op_sel_hi:[0,0,0]
	v_mfma_scale_f32_16x16x128_f8f6f4 v[104:107], v[8:15], v[40:47], v[104:107], v200, v200 op_sel_hi:[0,0,0]
	s_waitcnt lgkmcnt(2)
	v_mfma_scale_f32_16x16x128_f8f6f4 v[92:95], v[0:7], v[48:55], v[92:95], v200, v200 op_sel_hi:[0,0,0]
	v_mfma_scale_f32_16x16x128_f8f6f4 v[88:91], v[8:15], v[48:55], v[88:91], v200, v200 op_sel_hi:[0,0,0]
	s_waitcnt lgkmcnt(0)
	v_mfma_scale_f32_16x16x128_f8f6f4 v[76:79], v[0:7], v[56:63], v[76:79], v200, v200 op_sel_hi:[0,0,0]
	v_mfma_scale_f32_16x16x128_f8f6f4 v[72:75], v[8:15], v[56:63], v[72:75], v200, v200 op_sel_hi:[0,0,0]
	s_setprio 0
	s_setprio 1
	v_mfma_scale_f32_16x16x128_f8f6f4 v[116:119], v[16:23], v[32:39], v[116:119], v200, v200 op_sel_hi:[0,0,0]
	v_mfma_scale_f32_16x16x128_f8f6f4 v[112:115], v[24:31], v[32:39], v[112:115], v200, v200 op_sel_hi:[0,0,0]
	v_mfma_scale_f32_16x16x128_f8f6f4 v[100:103], v[16:23], v[40:47], v[100:103], v200, v200 op_sel_hi:[0,0,0]
	v_mfma_scale_f32_16x16x128_f8f6f4 v[96:99], v[24:31], v[40:47], v[96:99], v200, v200 op_sel_hi:[0,0,0]
	v_mfma_scale_f32_16x16x128_f8f6f4 v[84:87], v[16:23], v[48:55], v[84:87], v200, v200 op_sel_hi:[0,0,0]
	v_mfma_scale_f32_16x16x128_f8f6f4 v[80:83], v[24:31], v[48:55], v[80:83], v200, v200 op_sel_hi:[0,0,0]
	v_mfma_scale_f32_16x16x128_f8f6f4 v[68:71], v[16:23], v[56:63], v[68:71], v200, v200 op_sel_hi:[0,0,0]
	v_mfma_scale_f32_16x16x128_f8f6f4 v[64:67], v[24:31], v[56:63], v[64:67], v200, v200 op_sel_hi:[0,0,0]
	s_setprio 0
	s_barrier
	s_add_i32 s84, s84, 2
	s_add_u32 s82, s82, 0x100
	s_addc_u32 s83, s83, 0
	s_cmp_gt_u32 s84, 5
	s_cbranch_scc1 .LBB0_2535

; #define PG8_SCHED __builtin_amdgcn_sched_barrier(0)
; #define PG8_STAGE_A(b, h, p) do { if constexpr (GATHER) { if ((h) == 0) PG8_STAGE(PG8_SA(b, h), p, vA0); else PG8_STAGE(PG8_SA(b, h), p, vA1); } else PG8_STAGE(PG8_SA(b, h), (p) + ((h) ? hstepA : (size_t)0), voffA); } while (0)
; #define PG8_GOFF1(un, h, d) do { int tz_ = tid; asm volatile("" : "+v"(tz_)); _Pragma("unroll") for (int i_ = 0; i_ < 2; ++i_) { int R_, C_; stage_rc(tz_ * 16 + i_ * 8192, R_, C_); \
;         d[i_] = S.gather(un, R_ + (h) * HALF) + (unsigned)C_ * 2u; } } while (0)
; template <class Epi, class Sched, bool ALIGN_EPI = true, bool SP2 = true, bool FP8 = false, bool GATHER = false>
; __device__ __forceinline__ void gemm_phase(LAS unsigned char* lds, const Dims g, const Sched& S, const Epi& E, const int wv) {
;     ...
;             if constexpr (GATHER) { if (last) PG8_GOFF1(un_, 0, vA0); }
;             PG8_LDB(B0, 0, 0); PG8_LDB(B1, 0, 1); PG8_SCHED; PG8_LDA(At, 0, 0); PG8_STAGE_A(1, 1, a1);
;             if constexpr (GATHER) { if (last) PG8_GOFF1(un_, 1, vA1); }
.LBB0_2533:
	v_add_u32_e32 v0, 0x10000, v201
	v_add_u32_e32 v12, 0x14000, v201
	ds_read_b128 v[16:19], v0
	ds_read_b128 v[20:23], v0 offset:1024
	ds_read_b128 v[24:27], v0 offset:2048
	ds_read_b128 v[28:31], v0 offset:3072
	ds_read_b128 v[0:3], v12
	ds_read_b128 v[4:7], v12 offset:1024
	ds_read_b128 v[8:11], v12 offset:2048
	ds_read_b128 v[12:15], v12 offset:3072
	s_add_u32 s42, s38, 0x80
	s_addc_u32 s43, s39, 0
	ds_read_b128 v[56:59], v202
	ds_read_b128 v[60:63], v202 offset:1024
	ds_read_b128 v[48:51], v202 offset:2048
	ds_read_b128 v[52:55], v202 offset:3072
	ds_read_b128 v[40:43], v202 offset:4096
	ds_read_b128 v[44:47], v202 offset:5120
	ds_read_b128 v[32:35], v202 offset:6144
	ds_read_b128 v[36:39], v202 offset:7168
	s_mov_b32 m0, s71
	s_nop 0
	global_load_lds_dwordx4 v197, s[42:43]
	s_andn2_b64 vcc, exec, s[40:41]
	s_mov_b32 m0, s72
	s_nop 0
	global_load_lds_dwordx4 v198, s[42:43]
	s_cbranch_vccnz .LBB0_2530
	v_mov_b32_e32 v197, v192
	s_nop 0
	v_ashrrev_i32_e32 v204, 31, v197
	v_lshrrev_b32_e32 v204, 26, v204
	v_lshlrev_b32_e32 v198, 4, v197
	v_add_u32_e32 v204, v197, v204
	v_bfe_i32 v197, v197, 27, 1
	v_lshrrev_b32_e32 v197, 22, v197
	v_add_u32_e32 v197, v198, v197
	v_and_b32_e32 v197, 0xfffffc00, v197
	v_sub_u32_e32 v197, v198, v197
	v_lshrrev_b32_e32 v205, 4, v197
	v_bitop3_b32 v197, v205, v197, 32 bitop3:0x6c
	v_ashrrev_i32_e32 v205, 31, v197
	v_lshrrev_b32_e32 v205, 26, v205
	v_ashrrev_i32_e32 v204, 6, v204
	v_add_u32_e32 v205, v197, v205
	v_ashrrev_i32_e32 v206, 6, v205
	v_lshlrev_b32_e32 v204, 5, v204
	v_and_b32_e32 v205, 0xc0, v205
	v_and_b32_e32 v207, 32, v204
	v_sub_u32_e32 v197, v197, v205
	v_lshlrev_b32_e32 v205, 2, v206
	v_and_b32_e32 v204, 0xffffffc0, v204
	v_add_u32_e32 v198, 0x2000, v198
	v_add3_u32 v204, s81, v205, v204
	v_ashrrev_i32_e32 v205, 31, v198
	v_lshrrev_b32_e32 v205, 22, v205
	v_add_u32_e32 v205, v198, v205
	v_ashrrev_i32_e32 v205, 10, v205
	v_mul_i32_i24_e32 v206, 0x400, v205
	v_sub_u32_e32 v198, v198, v206
	v_lshrrev_b32_e32 v206, 4, v198
	v_bitop3_b32 v198, v206, v198, 32 bitop3:0x6c
	v_ashrrev_i32_e32 v206, 31, v198
	v_lshrrev_b32_e32 v206, 26, v206
	v_ashrrev_i16_sdwa v197, v193, sext(v197) dst_sel:DWORD dst_unused:UNUSED_PAD src0_sel:DWORD src1_sel:BYTE_0
	ds_read_b32 v204, v204 offset:512
	v_add_u32_e32 v206, v198, v206
	v_add_u32_sdwa v197, v207, sext(v197) dst_sel:DWORD dst_unused:UNUSED_PAD src0_sel:DWORD src1_sel:WORD_0
	v_ashrrev_i32_e32 v207, 6, v206
	v_lshlrev_b32_e32 v205, 5, v205
	v_lshlrev_b32_e32 v207, 2, v207
	v_and_b32_e32 v208, 0xffffffc0, v205
	v_add3_u32 v207, s81, v207, v208
	ds_read_b32 v207, v207 offset:512
	s_waitcnt lgkmcnt(1)
	v_lshl_add_u32 v197, v197, 1, v204
	v_and_b32_e32 v204, 32, v205
	v_and_b32_e32 v205, 0xc0, v206
	v_sub_u32_e32 v198, v198, v205
	v_ashrrev_i16_sdwa v198, v193, sext(v198) dst_sel:DWORD dst_unused:UNUSED_PAD src0_sel:DWORD src1_sel:BYTE_0
	v_add_u32_sdwa v198, v204, sext(v198) dst_sel:DWORD dst_unused:UNUSED_PAD src0_sel:DWORD src1_sel:WORD_0
	s_waitcnt lgkmcnt(0)
	v_lshl_add_u32 v198, v198, 1, v207
	s_branch .LBB0_2530

; __device__ __forceinline__ unsigned pk4_fp8(float a, float b, float c, float d) { int w = __builtin_amdgcn_cvt_pk_fp8_f32(a, b, 0, false); w = __builtin_amdgcn_cvt_pk_fp8_f32(c, d, w, true); return (unsigned)w; }
;     __device__ __forceinline__ void operator()(const f32x4 (&acc)[2][2][4][2], const Unit& u, int wr, int wc, int fr, int fq) const {
;         const int row0 = u.pm * BM + wr * 64 + fr, c0 = u.pn * HALF + wc * 32 + 8 * fq;
;         const float* bp = bgu + (size_t)u.aux * 2048 + c0;
;         const f32x4 bg0 = *(const f32x4*)(bp), bg1 = *(const f32x4*)(bp + 4), bu0 = *(const f32x4*)(bp + 1024), bu1 = *(const f32x4*)(bp + 1028);
; #pragma unroll
;         for (int ai = 0; ai < 2; ++ai)
; #pragma unroll
;             for (int mp = 0; mp < 2; ++mp) {
;                 u32x2 wq[2];
; #pragma unroll
;                 for (int mi = 0; mi < 2; ++mi) { const int m = 2 * mp + mi;
;                     const f32x4 g0 = acc[ai][0][m][0] * ascale + bg0, g1 = acc[ai][0][m][1] * ascale + bg1, u0 = acc[ai][1][m][0] * ascale + bu0, u1 = acc[ai][1][m][1] * ascale + bu1;
;                     float r[8];
; #pragma unroll
;                     for (int j = 0; j < 4; ++j) {
;                         float gg = fminf(g0[j], 7.f), uu = fminf(fmaxf(u0[j], -7.f), 7.f); r[j] = 4.f * (uu + 1.f) * gg * __builtin_amdgcn_rcpf(1.f + __expf(-1.702f * gg));
;                         gg = fminf(g1[j], 7.f); uu = fminf(fmaxf(u1[j], -7.f), 7.f); r[4 + j] = 4.f * (uu + 1.f) * gg * __builtin_amdgcn_rcpf(1.f + __expf(-1.702f * gg));
;                     }
;                     wq[mi].x = pk4_fp8(r[0], r[1], r[2], r[3]); wq[mi].y = pk4_fp8(r[4], r[5], r[6], r[7]); }
;                 *(u32x4*)(act + (size_t)(row0 + ai * HALF + (2 * mp + (fq & 1)) * 16) * EFF + (c0 - 8 * (fq & 1))) = widen16(wq[0], wq[1]);
.LBB0_2537:
	v_mov_b32_e32 v18, v192
	s_lshl_b32 s26, s26, 7
	v_lshrrev_b32_e32 v0, 1, v18
	s_ashr_i32 s37, s36, 31
	s_lshl_b32 s38, s77, 8
	v_and_or_b32 v0, v0, 24, s26
	s_lshl_b64 s[36:37], s[36:37], 13
	v_or_b32_e32 v16, s64, v0
	s_add_u32 s36, s61, s36
	s_addc_u32 s37, s62, s37
	v_ashrrev_i32_e32 v17, 31, v16
	v_lshl_add_u64 v[0:1], v[16:17], 2, s[36:37]
	global_load_dwordx4 v[12:15], v[0:1], off
	global_load_dwordx4 v[4:7], v[0:1], off offset:16
	v_add_co_u32_e32 v2, vcc, s73, v0
	v_bfe_u32 v17, v18, 4, 1
	s_nop 0
	v_addc_co_u32_e32 v3, vcc, 0, v1, vcc
	v_lshl_add_u64 v[0:1], v[0:1], 0, s[16:17]
	global_load_dwordx4 v[8:11], v[2:3], off
	v_lshlrev_b32_e32 v19, 3, v17
	global_load_dwordx4 v[0:3], v[0:1], off offset:16
	v_sub_u32_e32 v16, v16, v19
	s_add_i32 s38, s38, s63
	v_and_or_b32 v18, v18, 15, s38
	v_lshl_or_b32 v18, v17, 4, v18
	v_ashrrev_i32_e32 v17, 31, v16
	s_andn2_b64 vcc, exec, s[24:25]
	s_mov_b64 s[24:25], -1
	s_waitcnt vmcnt(3)
	v_fmamk_f32 v19, v188, 0x3a000000, v12
	s_waitcnt vmcnt(2)
	v_fmamk_f32 v20, v184, 0x3a000000, v4
	v_min_f32_e32 v19, 0x40e00000, v19
	v_min_f32_e32 v20, 0x40e00000, v20
	v_fmamk_f32 v21, v189, 0x3a000000, v13
	v_mul_f32_e32 v31, 0xbfd9db23, v19
	v_mul_f32_e32 v32, 0xbfd9db23, v20
	v_min_f32_e32 v21, 0x40e00000, v21
	v_mul_f32_e32 v31, 0x3fb8aa3b, v31
	v_mul_f32_e32 v32, 0x3fb8aa3b, v32
	s_waitcnt vmcnt(1)
	v_fmamk_f32 v25, v180, 0x3a000000, v8
	s_waitcnt vmcnt(0)
	v_fmamk_f32 v26, v176, 0x3a000000, v0
	v_mul_f32_e32 v33, 0xbfd9db23, v21
	v_exp_f32_e32 v31, v31
	v_exp_f32_e32 v32, v32
	v_med3_f32 v25, v25, s74, v203
	v_med3_f32 v26, v26, s74, v203
	v_mul_f32_e32 v33, 0x3fb8aa3b, v33
	v_fmamk_f32 v27, v181, 0x3a000000, v9
	v_exp_f32_e32 v33, v33
	v_med3_f32 v27, v27, s74, v203
	v_fmaak_f32 v25, 4.0, v25, 0x40800000
	v_fmaak_f32 v26, 4.0, v26, 0x40800000
	v_fmamk_f32 v24, v186, 0x3a000000, v6
	v_mul_f32_e32 v19, v19, v25
	v_mul_f32_e32 v20, v20, v26
	v_add_f32_e32 v25, 1.0, v31
	v_add_f32_e32 v26, 1.0, v32
	v_min_f32_e32 v24, 0x40e00000, v24
	v_fmaak_f32 v27, 4.0, v27, 0x40800000
	v_rcp_f32_e32 v25, v25
	v_rcp_f32_e32 v26, v26
	v_mul_f32_e32 v36, 0xbfd9db23, v24
	v_mul_f32_e32 v21, v21, v27
	v_add_f32_e32 v27, 1.0, v33
	v_mul_f32_e32 v36, 0x3fb8aa3b, v36
	v_rcp_f32_e32 v27, v27
	v_fmamk_f32 v30, v178, 0x3a000000, v2
	v_exp_f32_e32 v36, v36
	v_med3_f32 v30, v30, s74, v203
	v_mul_f32_e32 v19, v25, v19
	v_mul_f32_e32 v25, v26, v20
	v_fmamk_f32 v26, v191, 0x3a000000, v15
	v_min_f32_e32 v26, 0x40e00000, v26
	v_mul_f32_e32 v21, v27, v21
	v_fmaak_f32 v20, 4.0, v30, 0x40800000
	v_mul_f32_e32 v27, 0xbfd9db23, v26
	v_mul_f32_e32 v20, v24, v20
	v_add_f32_e32 v24, 1.0, v36
	v_mul_f32_e32 v27, 0x3fb8aa3b, v27
	v_rcp_f32_e32 v24, v24
	v_exp_f32_e32 v27, v27
	v_fmamk_f32 v23, v190, 0x3a000000, v14
	v_min_f32_e32 v23, 0x40e00000, v23
	v_mul_f32_e32 v24, v24, v20
	v_fmamk_f32 v20, v183, 0x3a000000, v11
	v_add_f32_e32 v27, 1.0, v27
	v_med3_f32 v20, v20, s74, v203
	v_rcp_f32_e32 v27, v27
	v_fmamk_f32 v22, v185, 0x3a000000, v5
	v_mul_f32_e32 v35, 0xbfd9db23, v23
	v_fmaak_f32 v20, 4.0, v20, 0x40800000
	v_min_f32_e32 v22, 0x40e00000, v22
	v_mul_f32_e32 v35, 0x3fb8aa3b, v35
	v_mul_f32_e32 v20, v26, v20
	v_fmamk_f32 v29, v182, 0x3a000000, v10
	v_mul_f32_e32 v34, 0xbfd9db23, v22
	v_exp_f32_e32 v35, v35
	v_mul_f32_e32 v26, v27, v20
	v_fmamk_f32 v20, v187, 0x3a000000, v7
	v_med3_f32 v29, v29, s74, v203
	v_mul_f32_e32 v34, 0x3fb8aa3b, v34
	v_min_f32_e32 v27, 0x40e00000, v20
	v_fmamk_f32 v28, v177, 0x3a000000, v1
	v_exp_f32_e32 v34, v34
	v_mul_f32_e32 v20, 0xbfd9db23, v27
	v_med3_f32 v28, v28, s74, v203
	v_fmaak_f32 v29, 4.0, v29, 0x40800000
	v_mul_f32_e32 v20, 0x3fb8aa3b, v20
	v_mul_f32_e32 v23, v23, v29
	v_add_f32_e32 v29, 1.0, v35
	v_exp_f32_e32 v20, v20
	v_fmaak_f32 v28, 4.0, v28, 0x40800000
	v_rcp_f32_e32 v29, v29
	v_mul_f32_e32 v22, v22, v28
	v_add_f32_e32 v28, 1.0, v34
	v_rcp_f32_e32 v28, v28
	v_add_f32_e32 v20, 1.0, v20
	v_mul_f32_e32 v23, v29, v23
	v_rcp_f32_e32 v29, v20
	v_mov_b32_e32 v20, 0
	v_cvt_pk_fp8_f32 v20, v19, v21
	v_mul_f32_e32 v22, v28, v22
	v_fmamk_f32 v28, v179, 0x3a000000, v3
	v_mov_b32_e32 v21, 0
	v_med3_f32 v28, v28, s74, v203
	v_cvt_pk_fp8_f32 v21, v25, v22
	v_fmamk_f32 v22, v172, 0x3a000000, v12
	v_add_f32_e32 v28, 1.0, v28
	v_min_f32_e32 v22, 0x40e00000, v22
	v_mul_f32_e32 v19, 4.0, v28
	v_cvt_pk_fp8_f32 v20, v23, v26 op_sel:[0,0,1]
	v_mul_f32_e32 v23, 0xbfd9db23, v22
	v_mul_f32_e32 v19, v27, v19
	v_mul_f32_e32 v23, 0x3fb8aa3b, v23
	v_mul_f32_e32 v19, v29, v19
	v_exp_f32_e32 v23, v23
	v_cvt_pk_fp8_f32 v21, v24, v19 op_sel:[0,0,1]
	v_fmamk_f32 v19, v164, 0x3a000000, v8
	v_med3_f32 v19, v19, s74, v203
	v_add_f32_e32 v23, 1.0, v23
	v_fmaak_f32 v19, 4.0, v19, 0x40800000
	v_rcp_f32_e32 v23, v23
	v_mul_f32_e32 v19, v22, v19
	v_fmamk_f32 v22, v168, 0x3a000000, v4
	v_min_f32_e32 v22, 0x40e00000, v22
	v_mul_f32_e32 v24, 0xbfd9db23, v22
	v_mul_f32_e32 v24, 0x3fb8aa3b, v24
	v_mul_f32_e32 v19, v23, v19
	v_fmamk_f32 v23, v160, 0x3a000000, v0
	v_exp_f32_e32 v24, v24
	v_med3_f32 v23, v23, s74, v203
	v_fmaak_f32 v23, 4.0, v23, 0x40800000
	v_mul_f32_e32 v22, v22, v23
	v_add_f32_e32 v23, 1.0, v24
	v_fmamk_f32 v24, v173, 0x3a000000, v13
	v_min_f32_e32 v24, 0x40e00000, v24
	v_mul_f32_e32 v25, 0xbfd9db23, v24
	v_mul_f32_e32 v25, 0x3fb8aa3b, v25
	v_rcp_f32_e32 v23, v23
	v_exp_f32_e32 v25, v25
	v_mul_f32_e32 v26, v23, v22
	v_fmamk_f32 v22, v165, 0x3a000000, v9
	v_add_f32_e32 v23, 1.0, v25
	v_med3_f32 v22, v22, s74, v203
	v_rcp_f32_e32 v23, v23
	v_fmaak_f32 v22, 4.0, v22, 0x40800000
	v_mul_f32_e32 v22, v24, v22
	v_mul_f32_e32 v23, v23, v22
	v_fmamk_f32 v22, v169, 0x3a000000, v5
	v_min_f32_e32 v22, 0x40e00000, v22
; __device__ __forceinline__ unsigned pk4_fp8(float a, float b, float c, float d) { int w = __builtin_amdgcn_cvt_pk_fp8_f32(a, b, 0, false); w = __builtin_amdgcn_cvt_pk_fp8_f32(c, d, w, true); return (unsigned)w; }
;     __device__ __forceinline__ void operator()(const f32x4 (&acc)[2][2][4][2], const Unit& u, int wr, int wc, int fr, int fq) const {
;     ...
;                 for (int mi = 0; mi < 2; ++mi) { const int m = 2 * mp + mi;
;                     const f32x4 g0 = acc[ai][0][m][0] * ascale + bg0, g1 = acc[ai][0][m][1] * ascale + bg1, u0 = acc[ai][1][m][0] * ascale + bu0, u1 = acc[ai][1][m][1] * ascale + bu1;
;                     float r[8];
; #pragma unroll
;                     for (int j = 0; j < 4; ++j) {
;                         float gg = fminf(g0[j], 7.f), uu = fminf(fmaxf(u0[j], -7.f), 7.f); r[j] = 4.f * (uu + 1.f) * gg * __builtin_amdgcn_rcpf(1.f + __expf(-1.702f * gg));
;                         gg = fminf(g1[j], 7.f); uu = fminf(fmaxf(u1[j], -7.f), 7.f); r[4 + j] = 4.f * (uu + 1.f) * gg * __builtin_amdgcn_rcpf(1.f + __expf(-1.702f * gg));
;                     }
;                     wq[mi].x = pk4_fp8(r[0], r[1], r[2], r[3]); wq[mi].y = pk4_fp8(r[4], r[5], r[6], r[7]); }
;                 *(u32x4*)(act + (size_t)(row0 + ai * HALF + (2 * mp + (fq & 1)) * 16) * EFF + (c0 - 8 * (fq & 1))) = widen16(wq[0], wq[1]);
	v_mul_f32_e32 v25, 0xbfd9db23, v22
	v_mul_f32_e32 v25, 0x3fb8aa3b, v25
	v_fmamk_f32 v24, v161, 0x3a000000, v1
	v_exp_f32_e32 v25, v25
	v_med3_f32 v24, v24, s74, v203
	v_fmaak_f32 v24, 4.0, v24, 0x40800000
	v_mul_f32_e32 v22, v22, v24
	v_add_f32_e32 v24, 1.0, v25
	v_fmamk_f32 v25, v174, 0x3a000000, v14
	v_min_f32_e32 v25, 0x40e00000, v25
	v_mul_f32_e32 v27, 0xbfd9db23, v25
	v_mul_f32_e32 v27, 0x3fb8aa3b, v27
	v_rcp_f32_e32 v24, v24
	v_exp_f32_e32 v27, v27
	v_mul_f32_e32 v24, v24, v22
	v_fmamk_f32 v22, v166, 0x3a000000, v10
	v_add_f32_e32 v27, 1.0, v27
	v_med3_f32 v22, v22, s74, v203
	v_rcp_f32_e32 v27, v27
	v_fmaak_f32 v22, 4.0, v22, 0x40800000
	v_mul_f32_e32 v22, v25, v22
	v_mul_f32_e32 v25, v27, v22
	v_fmamk_f32 v22, v170, 0x3a000000, v6
	v_min_f32_e32 v22, 0x40e00000, v22
	v_mul_f32_e32 v28, 0xbfd9db23, v22
	v_mul_f32_e32 v28, 0x3fb8aa3b, v28
	v_fmamk_f32 v27, v162, 0x3a000000, v2
	v_exp_f32_e32 v28, v28
	v_med3_f32 v27, v27, s74, v203
	v_fmaak_f32 v27, 4.0, v27, 0x40800000
	v_mul_f32_e32 v22, v22, v27
	v_add_f32_e32 v27, 1.0, v28
	v_fmamk_f32 v28, v175, 0x3a000000, v15
	v_min_f32_e32 v28, 0x40e00000, v28
	v_mul_f32_e32 v29, 0xbfd9db23, v28
	v_mul_f32_e32 v29, 0x3fb8aa3b, v29
	v_rcp_f32_e32 v27, v27
	v_exp_f32_e32 v29, v29
	v_mul_f32_e32 v27, v27, v22
	v_fmamk_f32 v22, v167, 0x3a000000, v11
	v_add_f32_e32 v29, 1.0, v29
	v_med3_f32 v22, v22, s74, v203
	v_rcp_f32_e32 v29, v29
	v_fmaak_f32 v22, 4.0, v22, 0x40800000
	v_mul_f32_e32 v22, v28, v22
	v_mul_f32_e32 v28, v29, v22
	v_fmamk_f32 v22, v171, 0x3a000000, v7
	v_min_f32_e32 v29, 0x40e00000, v22
	v_mul_f32_e32 v30, 0xbfd9db23, v29
	v_mul_f32_e32 v30, 0x3fb8aa3b, v30
	v_exp_f32_e32 v30, v30
	v_fmamk_f32 v22, v163, 0x3a000000, v3
	v_med3_f32 v22, v22, s74, v203
	v_add_f32_e32 v22, 1.0, v22
	v_mul_f32_e32 v31, 4.0, v22
	v_add_f32_e32 v22, 1.0, v30
	v_rcp_f32_e32 v30, v22
	v_mov_b32_e32 v22, 0
	v_cvt_pk_fp8_f32 v22, v19, v23
	v_mov_b32_e32 v23, 0
	v_cvt_pk_fp8_f32 v23, v26, v24
	v_mul_f32_e32 v19, v29, v31
	v_mul_f32_e32 v19, v30, v19
	v_cvt_pk_fp8_f32 v22, v25, v28 op_sel:[0,0,1]
	v_cvt_pk_fp8_f32 v23, v27, v19 op_sel:[0,0,1]
	v_ashrrev_i32_e32 v19, 31, v18
	v_lshlrev_b64 v[24:25], 10, v[18:19]
	v_fmamk_f32 v19, v156, 0x3a000000, v12
	v_min_f32_e32 v19, 0x40e00000, v19
	v_mul_f32_e32 v26, 0xbfd9db23, v19
	v_lshl_add_u64 v[24:25], s[12:13], 0, v[24:25]
	v_mul_f32_e32 v26, 0x3fb8aa3b, v26
	v_permlane16_swap_b32_e32 v20, v22
	v_permlane16_swap_b32_e32 v21, v23
	v_lshl_add_u64 v[24:25], v[24:25], 0, v[16:17]
	v_exp_f32_e32 v26, v26
	global_store_dwordx4 v[24:25], v[20:23], off
	v_fmamk_f32 v28, v147, 0x3a000000, v3
	v_med3_f32 v28, v28, s74, v203
	v_fmamk_f32 v20, v148, 0x3a000000, v8
	v_med3_f32 v20, v20, s74, v203
	v_add_f32_e32 v21, 1.0, v26
	v_fmaak_f32 v20, 4.0, v20, 0x40800000
	v_rcp_f32_e32 v21, v21
	v_mul_f32_e32 v19, v19, v20
	v_fmamk_f32 v20, v152, 0x3a000000, v4
	v_min_f32_e32 v20, 0x40e00000, v20
	v_mul_f32_e32 v22, 0xbfd9db23, v20
	v_mul_f32_e32 v22, 0x3fb8aa3b, v22
	v_mul_f32_e32 v19, v21, v19
	v_fmamk_f32 v21, v144, 0x3a000000, v0
	v_exp_f32_e32 v22, v22
	v_med3_f32 v21, v21, s74, v203
	v_fmaak_f32 v21, 4.0, v21, 0x40800000
	v_mul_f32_e32 v20, v20, v21
	v_add_f32_e32 v21, 1.0, v22
	v_fmamk_f32 v22, v157, 0x3a000000, v13
	v_min_f32_e32 v22, 0x40e00000, v22
	v_mul_f32_e32 v23, 0xbfd9db23, v22
	v_mul_f32_e32 v23, 0x3fb8aa3b, v23
	v_rcp_f32_e32 v21, v21
	v_exp_f32_e32 v23, v23
	v_add_f32_e32 v28, 1.0, v28
	v_mul_f32_e32 v24, v21, v20
	v_fmamk_f32 v20, v149, 0x3a000000, v9
	v_add_f32_e32 v21, 1.0, v23
	v_med3_f32 v20, v20, s74, v203
	v_rcp_f32_e32 v21, v21
	v_fmaak_f32 v20, 4.0, v20, 0x40800000
	v_mul_f32_e32 v20, v22, v20
	v_mul_f32_e32 v21, v21, v20
	v_fmamk_f32 v20, v153, 0x3a000000, v5
	v_min_f32_e32 v20, 0x40e00000, v20
	v_mul_f32_e32 v23, 0xbfd9db23, v20
	v_mul_f32_e32 v23, 0x3fb8aa3b, v23
	v_fmamk_f32 v22, v145, 0x3a000000, v1
	v_exp_f32_e32 v23, v23
	v_med3_f32 v22, v22, s74, v203
	v_fmaak_f32 v22, 4.0, v22, 0x40800000
	v_mul_f32_e32 v20, v20, v22
	v_add_f32_e32 v22, 1.0, v23
	v_fmamk_f32 v23, v158, 0x3a000000, v14
	v_min_f32_e32 v23, 0x40e00000, v23
	v_mul_f32_e32 v25, 0xbfd9db23, v23
	v_mul_f32_e32 v25, 0x3fb8aa3b, v25
	v_rcp_f32_e32 v22, v22
	v_exp_f32_e32 v25, v25
	v_mul_f32_e32 v22, v22, v20
	v_fmamk_f32 v20, v150, 0x3a000000, v10
	v_add_f32_e32 v25, 1.0, v25
	v_med3_f32 v20, v20, s74, v203
	v_rcp_f32_e32 v25, v25
	v_fmaak_f32 v20, 4.0, v20, 0x40800000
	v_mul_f32_e32 v20, v23, v20
	v_mul_f32_e32 v23, v25, v20
	v_fmamk_f32 v20, v154, 0x3a000000, v6
	v_min_f32_e32 v20, 0x40e00000, v20
	v_mul_f32_e32 v26, 0xbfd9db23, v20
	v_mul_f32_e32 v26, 0x3fb8aa3b, v26
	v_fmamk_f32 v25, v146, 0x3a000000, v2
	v_exp_f32_e32 v26, v26
	v_med3_f32 v25, v25, s74, v203
	v_fmaak_f32 v25, 4.0, v25, 0x40800000
	v_mul_f32_e32 v20, v20, v25
	v_add_f32_e32 v25, 1.0, v26
	v_fmamk_f32 v26, v159, 0x3a000000, v15
	v_min_f32_e32 v26, 0x40e00000, v26
	v_mul_f32_e32 v27, 0xbfd9db23, v26
	v_mul_f32_e32 v27, 0x3fb8aa3b, v27
	v_rcp_f32_e32 v25, v25
	v_exp_f32_e32 v27, v27
	v_mul_f32_e32 v25, v25, v20
	v_fmamk_f32 v20, v151, 0x3a000000, v11
	v_add_f32_e32 v27, 1.0, v27
	v_med3_f32 v20, v20, s74, v203
	v_rcp_f32_e32 v27, v27
	v_fmaak_f32 v20, 4.0, v20, 0x40800000
	v_mul_f32_e32 v20, v26, v20
	v_mul_f32_e32 v26, v27, v20
	v_fmamk_f32 v20, v155, 0x3a000000, v7
	v_min_f32_e32 v27, 0x40e00000, v20
	v_mul_f32_e32 v20, 0xbfd9db23, v27
	v_mul_f32_e32 v20, 0x3fb8aa3b, v20
	v_exp_f32_e32 v20, v20
	s_nop 0
	v_add_f32_e32 v20, 1.0, v20
	v_rcp_f32_e32 v29, v20
	v_mov_b32_e32 v20, 0
	v_cvt_pk_fp8_f32 v20, v19, v21
	v_mov_b32_e32 v21, 0
	v_cvt_pk_fp8_f32 v21, v24, v22
	v_fmamk_f32 v22, v140, 0x3a000000, v12
; __device__ __forceinline__ unsigned pk4_fp8(float a, float b, float c, float d) { int w = __builtin_amdgcn_cvt_pk_fp8_f32(a, b, 0, false); w = __builtin_amdgcn_cvt_pk_fp8_f32(c, d, w, true); return (unsigned)w; }
;     __device__ __forceinline__ void operator()(const f32x4 (&acc)[2][2][4][2], const Unit& u, int wr, int wc, int fr, int fq) const {
;     ...
;                 for (int mi = 0; mi < 2; ++mi) { const int m = 2 * mp + mi;
;                     const f32x4 g0 = acc[ai][0][m][0] * ascale + bg0, g1 = acc[ai][0][m][1] * ascale + bg1, u0 = acc[ai][1][m][0] * ascale + bu0, u1 = acc[ai][1][m][1] * ascale + bu1;
;                     float r[8];
; #pragma unroll
;                     for (int j = 0; j < 4; ++j) {
;                         float gg = fminf(g0[j], 7.f), uu = fminf(fmaxf(u0[j], -7.f), 7.f); r[j] = 4.f * (uu + 1.f) * gg * __builtin_amdgcn_rcpf(1.f + __expf(-1.702f * gg));
;                         gg = fminf(g1[j], 7.f); uu = fminf(fmaxf(u1[j], -7.f), 7.f); r[4 + j] = 4.f * (uu + 1.f) * gg * __builtin_amdgcn_rcpf(1.f + __expf(-1.702f * gg));
;                     }
;                     wq[mi].x = pk4_fp8(r[0], r[1], r[2], r[3]); wq[mi].y = pk4_fp8(r[4], r[5], r[6], r[7]); }
;                 *(u32x4*)(act + (size_t)(row0 + ai * HALF + (2 * mp + (fq & 1)) * 16) * EFF + (c0 - 8 * (fq & 1))) = widen16(wq[0], wq[1]);
	v_min_f32_e32 v22, 0x40e00000, v22
	v_mul_f32_e32 v19, 4.0, v28
	v_cvt_pk_fp8_f32 v20, v23, v26 op_sel:[0,0,1]
	v_mul_f32_e32 v23, 0xbfd9db23, v22
	v_mul_f32_e32 v19, v27, v19
	v_mul_f32_e32 v23, 0x3fb8aa3b, v23
	v_mul_f32_e32 v19, v29, v19
	v_exp_f32_e32 v23, v23
	v_cvt_pk_fp8_f32 v21, v25, v19 op_sel:[0,0,1]
	v_fmamk_f32 v19, v132, 0x3a000000, v8
	v_med3_f32 v19, v19, s74, v203
	v_add_f32_e32 v23, 1.0, v23
	v_fmaak_f32 v19, 4.0, v19, 0x40800000
	v_rcp_f32_e32 v23, v23
	v_mul_f32_e32 v19, v22, v19
	v_fmamk_f32 v22, v136, 0x3a000000, v4
	v_min_f32_e32 v22, 0x40e00000, v22
	v_mul_f32_e32 v24, 0xbfd9db23, v22
	v_mul_f32_e32 v24, 0x3fb8aa3b, v24
	v_mul_f32_e32 v19, v23, v19
	v_fmamk_f32 v23, v128, 0x3a000000, v0
	v_exp_f32_e32 v24, v24
	v_med3_f32 v23, v23, s74, v203
	v_fmaak_f32 v23, 4.0, v23, 0x40800000
	v_mul_f32_e32 v22, v22, v23
	v_add_f32_e32 v23, 1.0, v24
	v_fmamk_f32 v24, v141, 0x3a000000, v13
	v_min_f32_e32 v24, 0x40e00000, v24
	v_mul_f32_e32 v25, 0xbfd9db23, v24
	v_mul_f32_e32 v25, 0x3fb8aa3b, v25
	v_rcp_f32_e32 v23, v23
	v_exp_f32_e32 v25, v25
	v_mul_f32_e32 v26, v23, v22
	v_fmamk_f32 v22, v133, 0x3a000000, v9
	v_add_f32_e32 v23, 1.0, v25
	v_med3_f32 v22, v22, s74, v203
	v_rcp_f32_e32 v23, v23
	v_fmaak_f32 v22, 4.0, v22, 0x40800000
	v_mul_f32_e32 v22, v24, v22
	v_mul_f32_e32 v23, v23, v22
	v_fmamk_f32 v22, v137, 0x3a000000, v5
	v_min_f32_e32 v22, 0x40e00000, v22
	v_mul_f32_e32 v25, 0xbfd9db23, v22
	v_mul_f32_e32 v25, 0x3fb8aa3b, v25
	v_fmamk_f32 v24, v129, 0x3a000000, v1
	v_exp_f32_e32 v25, v25
	v_med3_f32 v24, v24, s74, v203
	v_fmaak_f32 v24, 4.0, v24, 0x40800000
	v_mul_f32_e32 v22, v22, v24
	v_add_f32_e32 v24, 1.0, v25
	v_fmamk_f32 v25, v142, 0x3a000000, v14
	v_min_f32_e32 v25, 0x40e00000, v25
	v_mul_f32_e32 v27, 0xbfd9db23, v25
	v_mul_f32_e32 v27, 0x3fb8aa3b, v27
	v_rcp_f32_e32 v24, v24
	v_exp_f32_e32 v27, v27
	v_mul_f32_e32 v24, v24, v22
	v_fmamk_f32 v22, v134, 0x3a000000, v10
	v_add_f32_e32 v27, 1.0, v27
	v_med3_f32 v22, v22, s74, v203
	v_rcp_f32_e32 v27, v27
	v_fmaak_f32 v22, 4.0, v22, 0x40800000
	v_mul_f32_e32 v22, v25, v22
	v_mul_f32_e32 v25, v27, v22
	v_fmamk_f32 v22, v138, 0x3a000000, v6
	v_min_f32_e32 v22, 0x40e00000, v22
	v_mul_f32_e32 v28, 0xbfd9db23, v22
	v_mul_f32_e32 v28, 0x3fb8aa3b, v28
	v_fmamk_f32 v27, v130, 0x3a000000, v2
	v_exp_f32_e32 v28, v28
	v_med3_f32 v27, v27, s74, v203
	v_fmaak_f32 v27, 4.0, v27, 0x40800000
	v_mul_f32_e32 v22, v22, v27
	v_add_f32_e32 v27, 1.0, v28
	v_fmamk_f32 v28, v143, 0x3a000000, v15
	v_min_f32_e32 v28, 0x40e00000, v28
	v_mul_f32_e32 v29, 0xbfd9db23, v28
	v_mul_f32_e32 v29, 0x3fb8aa3b, v29
	v_rcp_f32_e32 v27, v27
	v_exp_f32_e32 v29, v29
	v_mul_f32_e32 v27, v27, v22
	v_fmamk_f32 v22, v135, 0x3a000000, v11
	v_add_f32_e32 v29, 1.0, v29
	v_med3_f32 v22, v22, s74, v203
	v_rcp_f32_e32 v29, v29
	v_fmaak_f32 v22, 4.0, v22, 0x40800000
	v_mul_f32_e32 v22, v28, v22
	v_mul_f32_e32 v28, v29, v22
	v_fmamk_f32 v22, v139, 0x3a000000, v7
	v_min_f32_e32 v29, 0x40e00000, v22
	v_mul_f32_e32 v30, 0xbfd9db23, v29
	v_mul_f32_e32 v30, 0x3fb8aa3b, v30
	v_exp_f32_e32 v30, v30
	v_fmamk_f32 v22, v131, 0x3a000000, v3
	v_med3_f32 v22, v22, s74, v203
	v_add_f32_e32 v22, 1.0, v22
	v_mul_f32_e32 v31, 4.0, v22
	v_add_f32_e32 v22, 1.0, v30
	v_rcp_f32_e32 v30, v22
	v_mov_b32_e32 v22, 0
	v_cvt_pk_fp8_f32 v22, v19, v23
	v_mov_b32_e32 v23, 0
	v_cvt_pk_fp8_f32 v23, v26, v24
	v_mul_f32_e32 v19, v29, v31
	v_mul_f32_e32 v19, v30, v19
	v_cvt_pk_fp8_f32 v22, v25, v28 op_sel:[0,0,1]
	v_cvt_pk_fp8_f32 v23, v27, v19 op_sel:[0,0,1]
	v_or_b32_e32 v24, 32, v18
	v_ashrrev_i32_e32 v25, 31, v24
	v_lshlrev_b64 v[24:25], 10, v[24:25]
	v_lshl_add_u64 v[24:25], s[12:13], 0, v[24:25]
	v_fmamk_f32 v19, v124, 0x3a000000, v12
	v_permlane16_swap_b32_e32 v20, v22
	v_permlane16_swap_b32_e32 v21, v23
	v_lshl_add_u64 v[24:25], v[24:25], 0, v[16:17]
	v_min_f32_e32 v19, 0x40e00000, v19
	global_store_dwordx4 v[24:25], v[20:23], off
	v_fmamk_f32 v29, v115, 0x3a000000, v3
	v_med3_f32 v29, v29, s74, v203
	v_mul_f32_e32 v20, 0xbfd9db23, v19
	v_mul_f32_e32 v20, 0x3fb8aa3b, v20
	v_exp_f32_e32 v21, v20
	v_fmamk_f32 v22, v116, 0x3a000000, v8
	v_med3_f32 v22, v22, s74, v203
	v_add_f32_e32 v21, 1.0, v21
	v_rcp_f32_e32 v21, v21
	v_fmaak_f32 v22, 4.0, v22, 0x40800000
	v_mul_f32_e32 v19, v19, v22
	v_fmamk_f32 v22, v112, 0x3a000000, v0
	v_mul_f32_e32 v19, v21, v19
	v_fmamk_f32 v21, v120, 0x3a000000, v4
	v_min_f32_e32 v21, 0x40e00000, v21
	v_mul_f32_e32 v23, 0xbfd9db23, v21
	v_mul_f32_e32 v23, 0x3fb8aa3b, v23
	v_exp_f32_e32 v23, v23
	v_med3_f32 v22, v22, s74, v203
	v_fmaak_f32 v22, 4.0, v22, 0x40800000
	v_mul_f32_e32 v21, v21, v22
	v_add_f32_e32 v22, 1.0, v23
	v_fmamk_f32 v23, v125, 0x3a000000, v13
	v_min_f32_e32 v23, 0x40e00000, v23
	v_mul_f32_e32 v24, 0xbfd9db23, v23
	v_mul_f32_e32 v24, 0x3fb8aa3b, v24
	v_rcp_f32_e32 v22, v22
	v_exp_f32_e32 v24, v24
	v_add_f32_e32 v29, 1.0, v29
	v_add_u32_e32 v20, 0x80, v18
	v_mul_f32_e32 v21, v22, v21
	v_fmamk_f32 v22, v117, 0x3a000000, v9
	v_add_f32_e32 v24, 1.0, v24
	v_med3_f32 v22, v22, s74, v203
	v_rcp_f32_e32 v24, v24
	v_fmaak_f32 v22, 4.0, v22, 0x40800000
	v_mul_f32_e32 v22, v23, v22
	v_mul_f32_e32 v23, v24, v22
	v_fmamk_f32 v22, v121, 0x3a000000, v5
	v_min_f32_e32 v22, 0x40e00000, v22
	v_mul_f32_e32 v25, 0xbfd9db23, v22
	v_mul_f32_e32 v25, 0x3fb8aa3b, v25
	v_fmamk_f32 v24, v113, 0x3a000000, v1
	v_exp_f32_e32 v25, v25
	v_med3_f32 v24, v24, s74, v203
	v_fmaak_f32 v24, 4.0, v24, 0x40800000
	v_mul_f32_e32 v22, v22, v24
	v_add_f32_e32 v24, 1.0, v25
	v_fmamk_f32 v25, v126, 0x3a000000, v14
	v_min_f32_e32 v25, 0x40e00000, v25
	v_mul_f32_e32 v26, 0xbfd9db23, v25
	v_mul_f32_e32 v26, 0x3fb8aa3b, v26
	v_rcp_f32_e32 v24, v24
; __device__ __forceinline__ unsigned pk4_fp8(float a, float b, float c, float d) { int w = __builtin_amdgcn_cvt_pk_fp8_f32(a, b, 0, false); w = __builtin_amdgcn_cvt_pk_fp8_f32(c, d, w, true); return (unsigned)w; }
;     __device__ __forceinline__ void operator()(const f32x4 (&acc)[2][2][4][2], const Unit& u, int wr, int wc, int fr, int fq) const {
;     ...
;                 for (int mi = 0; mi < 2; ++mi) { const int m = 2 * mp + mi;
;                     const f32x4 g0 = acc[ai][0][m][0] * ascale + bg0, g1 = acc[ai][0][m][1] * ascale + bg1, u0 = acc[ai][1][m][0] * ascale + bu0, u1 = acc[ai][1][m][1] * ascale + bu1;
;                     float r[8];
; #pragma unroll
;                     for (int j = 0; j < 4; ++j) {
;                         float gg = fminf(g0[j], 7.f), uu = fminf(fmaxf(u0[j], -7.f), 7.f); r[j] = 4.f * (uu + 1.f) * gg * __builtin_amdgcn_rcpf(1.f + __expf(-1.702f * gg));
;                         gg = fminf(g1[j], 7.f); uu = fminf(fmaxf(u1[j], -7.f), 7.f); r[4 + j] = 4.f * (uu + 1.f) * gg * __builtin_amdgcn_rcpf(1.f + __expf(-1.702f * gg));
;                     }
;                     wq[mi].x = pk4_fp8(r[0], r[1], r[2], r[3]); wq[mi].y = pk4_fp8(r[4], r[5], r[6], r[7]); }
;                 *(u32x4*)(act + (size_t)(row0 + ai * HALF + (2 * mp + (fq & 1)) * 16) * EFF + (c0 - 8 * (fq & 1))) = widen16(wq[0], wq[1]);
	v_exp_f32_e32 v26, v26
	v_mul_f32_e32 v24, v24, v22
	v_fmamk_f32 v22, v118, 0x3a000000, v10
	v_add_f32_e32 v26, 1.0, v26
	v_med3_f32 v22, v22, s74, v203
	v_rcp_f32_e32 v26, v26
	v_fmaak_f32 v22, 4.0, v22, 0x40800000
	v_mul_f32_e32 v22, v25, v22
	v_mul_f32_e32 v25, v26, v22
	v_fmamk_f32 v22, v122, 0x3a000000, v6
	v_min_f32_e32 v22, 0x40e00000, v22
	v_mul_f32_e32 v27, 0xbfd9db23, v22
	v_mul_f32_e32 v27, 0x3fb8aa3b, v27
	v_fmamk_f32 v26, v114, 0x3a000000, v2
	v_exp_f32_e32 v27, v27
	v_med3_f32 v26, v26, s74, v203
	v_fmaak_f32 v26, 4.0, v26, 0x40800000
	v_mul_f32_e32 v22, v22, v26
	v_add_f32_e32 v26, 1.0, v27
	v_fmamk_f32 v27, v127, 0x3a000000, v15
	v_min_f32_e32 v27, 0x40e00000, v27
	v_mul_f32_e32 v28, 0xbfd9db23, v27
	v_mul_f32_e32 v28, 0x3fb8aa3b, v28
	v_rcp_f32_e32 v26, v26
	v_exp_f32_e32 v28, v28
	v_mul_f32_e32 v26, v26, v22
	v_fmamk_f32 v22, v119, 0x3a000000, v11
	v_add_f32_e32 v28, 1.0, v28
	v_med3_f32 v22, v22, s74, v203
	v_rcp_f32_e32 v28, v28
	v_fmaak_f32 v22, 4.0, v22, 0x40800000
	v_mul_f32_e32 v22, v27, v22
	v_mul_f32_e32 v27, v28, v22
	v_fmamk_f32 v22, v123, 0x3a000000, v7
	v_min_f32_e32 v28, 0x40e00000, v22
	v_mul_f32_e32 v22, 0xbfd9db23, v28
	v_mul_f32_e32 v22, 0x3fb8aa3b, v22
	v_exp_f32_e32 v22, v22
	s_nop 0
	v_add_f32_e32 v22, 1.0, v22
	v_rcp_f32_e32 v30, v22
	v_mov_b32_e32 v22, 0
	v_cvt_pk_fp8_f32 v22, v19, v23
	v_mov_b32_e32 v23, 0
	v_cvt_pk_fp8_f32 v23, v21, v24
	v_fmamk_f32 v21, v108, 0x3a000000, v12
	v_min_f32_e32 v21, 0x40e00000, v21
	v_mul_f32_e32 v19, 4.0, v29
	v_mul_f32_e32 v24, 0xbfd9db23, v21
	v_mul_f32_e32 v19, v28, v19
	v_mul_f32_e32 v24, 0x3fb8aa3b, v24
	v_mul_f32_e32 v19, v30, v19
	v_exp_f32_e32 v24, v24
	v_cvt_pk_fp8_f32 v23, v26, v19 op_sel:[0,0,1]
	v_fmamk_f32 v19, v100, 0x3a000000, v8
	v_med3_f32 v19, v19, s74, v203
	v_add_f32_e32 v24, 1.0, v24
	v_fmaak_f32 v19, 4.0, v19, 0x40800000
	v_rcp_f32_e32 v24, v24
	v_mul_f32_e32 v19, v21, v19
	v_fmamk_f32 v21, v104, 0x3a000000, v4
	v_min_f32_e32 v21, 0x40e00000, v21
	v_cvt_pk_fp8_f32 v22, v25, v27 op_sel:[0,0,1]
	v_mul_f32_e32 v25, 0xbfd9db23, v21
	v_mul_f32_e32 v25, 0x3fb8aa3b, v25
	v_mul_f32_e32 v19, v24, v19
	v_fmamk_f32 v24, v96, 0x3a000000, v0
	v_exp_f32_e32 v25, v25
	v_med3_f32 v24, v24, s74, v203
	v_fmaak_f32 v24, 4.0, v24, 0x40800000
	v_mul_f32_e32 v21, v21, v24
	v_add_f32_e32 v24, 1.0, v25
	v_fmamk_f32 v25, v109, 0x3a000000, v13
	v_min_f32_e32 v25, 0x40e00000, v25
	v_mul_f32_e32 v26, 0xbfd9db23, v25
	v_mul_f32_e32 v26, 0x3fb8aa3b, v26
	v_rcp_f32_e32 v24, v24
	v_exp_f32_e32 v26, v26
	v_mul_f32_e32 v21, v24, v21
	v_fmamk_f32 v24, v101, 0x3a000000, v9
	v_add_f32_e32 v26, 1.0, v26
	v_med3_f32 v24, v24, s74, v203
	v_rcp_f32_e32 v26, v26
	v_fmaak_f32 v24, 4.0, v24, 0x40800000
	v_mul_f32_e32 v24, v25, v24
	v_mul_f32_e32 v25, v26, v24
	v_fmamk_f32 v24, v105, 0x3a000000, v5
	v_min_f32_e32 v24, 0x40e00000, v24
	v_mul_f32_e32 v27, 0xbfd9db23, v24
	v_mul_f32_e32 v27, 0x3fb8aa3b, v27
	v_fmamk_f32 v26, v97, 0x3a000000, v1
	v_exp_f32_e32 v27, v27
	v_med3_f32 v26, v26, s74, v203
	v_fmaak_f32 v26, 4.0, v26, 0x40800000
	v_mul_f32_e32 v24, v24, v26
	v_add_f32_e32 v26, 1.0, v27
	v_fmamk_f32 v27, v110, 0x3a000000, v14
	v_min_f32_e32 v27, 0x40e00000, v27
	v_mul_f32_e32 v28, 0xbfd9db23, v27
	v_mul_f32_e32 v28, 0x3fb8aa3b, v28
	v_rcp_f32_e32 v26, v26
	v_exp_f32_e32 v28, v28
	v_mul_f32_e32 v26, v26, v24
	v_fmamk_f32 v24, v102, 0x3a000000, v10
	v_add_f32_e32 v28, 1.0, v28
	v_med3_f32 v24, v24, s74, v203
	v_rcp_f32_e32 v28, v28
	v_fmaak_f32 v24, 4.0, v24, 0x40800000
	v_mul_f32_e32 v24, v27, v24
	v_mul_f32_e32 v27, v28, v24
	v_fmamk_f32 v24, v106, 0x3a000000, v6
	v_min_f32_e32 v24, 0x40e00000, v24
	v_mul_f32_e32 v29, 0xbfd9db23, v24
	v_mul_f32_e32 v29, 0x3fb8aa3b, v29
	v_fmamk_f32 v28, v98, 0x3a000000, v2
	v_exp_f32_e32 v29, v29
	v_med3_f32 v28, v28, s74, v203
	v_fmaak_f32 v28, 4.0, v28, 0x40800000
	v_mul_f32_e32 v24, v24, v28
	v_add_f32_e32 v28, 1.0, v29
	v_fmamk_f32 v29, v111, 0x3a000000, v15
	v_min_f32_e32 v29, 0x40e00000, v29
	v_mul_f32_e32 v30, 0xbfd9db23, v29
	v_mul_f32_e32 v30, 0x3fb8aa3b, v30
	v_rcp_f32_e32 v28, v28
	v_exp_f32_e32 v30, v30
	v_mul_f32_e32 v28, v28, v24
	v_fmamk_f32 v24, v103, 0x3a000000, v11
	v_add_f32_e32 v30, 1.0, v30
	v_med3_f32 v24, v24, s74, v203
	v_rcp_f32_e32 v30, v30
	v_fmaak_f32 v24, 4.0, v24, 0x40800000
	v_mul_f32_e32 v24, v29, v24
	v_mul_f32_e32 v29, v30, v24
	v_fmamk_f32 v24, v107, 0x3a000000, v7
	v_min_f32_e32 v30, 0x40e00000, v24
	v_mul_f32_e32 v31, 0xbfd9db23, v30
	v_mul_f32_e32 v31, 0x3fb8aa3b, v31
	v_exp_f32_e32 v31, v31
	v_fmamk_f32 v24, v99, 0x3a000000, v3
	v_med3_f32 v24, v24, s74, v203
	v_add_f32_e32 v24, 1.0, v24
	v_mul_f32_e32 v32, 4.0, v24
	v_add_f32_e32 v24, 1.0, v31
	v_rcp_f32_e32 v31, v24
	v_mov_b32_e32 v24, 0
	v_cvt_pk_fp8_f32 v24, v19, v25
	v_mov_b32_e32 v25, 0
	v_cvt_pk_fp8_f32 v25, v21, v26
	v_mul_f32_e32 v19, v30, v32
	v_mul_f32_e32 v19, v31, v19
	v_cvt_pk_fp8_f32 v24, v27, v29 op_sel:[0,0,1]
	v_cvt_pk_fp8_f32 v25, v28, v19 op_sel:[0,0,1]
	v_fmamk_f32 v19, v92, 0x3a000000, v12
	v_ashrrev_i32_e32 v21, 31, v20
	v_min_f32_e32 v19, 0x40e00000, v19
	v_lshlrev_b64 v[20:21], 10, v[20:21]
	v_mul_f32_e32 v26, 0xbfd9db23, v19
	v_lshl_add_u64 v[20:21], s[12:13], 0, v[20:21]
	v_mul_f32_e32 v26, 0x3fb8aa3b, v26
	v_permlane16_swap_b32_e32 v22, v24
	v_permlane16_swap_b32_e32 v23, v25
	v_lshl_add_u64 v[20:21], v[20:21], 0, v[16:17]
	v_exp_f32_e32 v26, v26
	global_store_dwordx4 v[20:21], v[22:25], off
	v_fmamk_f32 v20, v84, 0x3a000000, v8
	v_med3_f32 v20, v20, s74, v203
	v_add_f32_e32 v21, 1.0, v26
	v_fmaak_f32 v20, 4.0, v20, 0x40800000
	v_rcp_f32_e32 v21, v21
	v_mul_f32_e32 v19, v19, v20
	v_fmamk_f32 v20, v88, 0x3a000000, v4
; __device__ __forceinline__ unsigned pk4_fp8(float a, float b, float c, float d) { int w = __builtin_amdgcn_cvt_pk_fp8_f32(a, b, 0, false); w = __builtin_amdgcn_cvt_pk_fp8_f32(c, d, w, true); return (unsigned)w; }
;     __device__ __forceinline__ void operator()(const f32x4 (&acc)[2][2][4][2], const Unit& u, int wr, int wc, int fr, int fq) const {
;     ...
;                 for (int mi = 0; mi < 2; ++mi) { const int m = 2 * mp + mi;
;                     const f32x4 g0 = acc[ai][0][m][0] * ascale + bg0, g1 = acc[ai][0][m][1] * ascale + bg1, u0 = acc[ai][1][m][0] * ascale + bu0, u1 = acc[ai][1][m][1] * ascale + bu1;
;                     float r[8];
; #pragma unroll
;                     for (int j = 0; j < 4; ++j) {
;                         float gg = fminf(g0[j], 7.f), uu = fminf(fmaxf(u0[j], -7.f), 7.f); r[j] = 4.f * (uu + 1.f) * gg * __builtin_amdgcn_rcpf(1.f + __expf(-1.702f * gg));
;                         gg = fminf(g1[j], 7.f); uu = fminf(fmaxf(u1[j], -7.f), 7.f); r[4 + j] = 4.f * (uu + 1.f) * gg * __builtin_amdgcn_rcpf(1.f + __expf(-1.702f * gg));
;                     }
;                     wq[mi].x = pk4_fp8(r[0], r[1], r[2], r[3]); wq[mi].y = pk4_fp8(r[4], r[5], r[6], r[7]); }
;                 *(u32x4*)(act + (size_t)(row0 + ai * HALF + (2 * mp + (fq & 1)) * 16) * EFF + (c0 - 8 * (fq & 1))) = widen16(wq[0], wq[1]);
	v_min_f32_e32 v20, 0x40e00000, v20
	v_mul_f32_e32 v22, 0xbfd9db23, v20
	v_mul_f32_e32 v22, 0x3fb8aa3b, v22
	v_mul_f32_e32 v19, v21, v19
	v_fmamk_f32 v21, v80, 0x3a000000, v0
	v_exp_f32_e32 v22, v22
	v_med3_f32 v21, v21, s74, v203
	v_fmaak_f32 v21, 4.0, v21, 0x40800000
	v_mul_f32_e32 v20, v20, v21
	v_add_f32_e32 v21, 1.0, v22
	v_fmamk_f32 v22, v93, 0x3a000000, v13
	v_min_f32_e32 v22, 0x40e00000, v22
	v_mul_f32_e32 v23, 0xbfd9db23, v22
	v_mul_f32_e32 v23, 0x3fb8aa3b, v23
	v_rcp_f32_e32 v21, v21
	v_exp_f32_e32 v23, v23
	v_fmamk_f32 v8, v68, 0x3a000000, v8
	v_med3_f32 v8, v8, s74, v203
	v_mul_f32_e32 v24, v21, v20
	v_fmamk_f32 v20, v85, 0x3a000000, v9
	v_add_f32_e32 v21, 1.0, v23
	v_med3_f32 v20, v20, s74, v203
	v_rcp_f32_e32 v21, v21
	v_fmaak_f32 v20, 4.0, v20, 0x40800000
	v_mul_f32_e32 v20, v22, v20
	v_mul_f32_e32 v21, v21, v20
	v_fmamk_f32 v20, v89, 0x3a000000, v5
	v_min_f32_e32 v20, 0x40e00000, v20
	v_mul_f32_e32 v23, 0xbfd9db23, v20
	v_mul_f32_e32 v23, 0x3fb8aa3b, v23
	v_fmamk_f32 v22, v81, 0x3a000000, v1
	v_exp_f32_e32 v23, v23
	v_med3_f32 v22, v22, s74, v203
	v_fmaak_f32 v22, 4.0, v22, 0x40800000
	v_mul_f32_e32 v20, v20, v22
	v_add_f32_e32 v22, 1.0, v23
	v_fmamk_f32 v23, v94, 0x3a000000, v14
	v_min_f32_e32 v23, 0x40e00000, v23
	v_mul_f32_e32 v25, 0xbfd9db23, v23
	v_mul_f32_e32 v25, 0x3fb8aa3b, v25
	v_rcp_f32_e32 v22, v22
	v_exp_f32_e32 v25, v25
	v_fmamk_f32 v12, v76, 0x3a000000, v12
	v_mul_f32_e32 v22, v22, v20
	v_fmamk_f32 v20, v86, 0x3a000000, v10
	v_add_f32_e32 v25, 1.0, v25
	v_med3_f32 v20, v20, s74, v203
	v_rcp_f32_e32 v25, v25
	v_fmaak_f32 v20, 4.0, v20, 0x40800000
	v_mul_f32_e32 v20, v23, v20
	v_mul_f32_e32 v23, v25, v20
	v_fmamk_f32 v20, v90, 0x3a000000, v6
	v_min_f32_e32 v20, 0x40e00000, v20
	v_mul_f32_e32 v26, 0xbfd9db23, v20
	v_mul_f32_e32 v26, 0x3fb8aa3b, v26
	v_fmamk_f32 v25, v82, 0x3a000000, v2
	v_exp_f32_e32 v26, v26
	v_med3_f32 v25, v25, s74, v203
	v_fmaak_f32 v25, 4.0, v25, 0x40800000
	v_mul_f32_e32 v20, v20, v25
	v_add_f32_e32 v25, 1.0, v26
	v_fmamk_f32 v26, v95, 0x3a000000, v15
	v_min_f32_e32 v26, 0x40e00000, v26
	v_mul_f32_e32 v27, 0xbfd9db23, v26
	v_mul_f32_e32 v27, 0x3fb8aa3b, v27
	v_rcp_f32_e32 v25, v25
	v_exp_f32_e32 v27, v27
	v_fmamk_f32 v4, v72, 0x3a000000, v4
	v_min_f32_e32 v12, 0x40e00000, v12
	v_mul_f32_e32 v25, v25, v20
	v_fmamk_f32 v20, v87, 0x3a000000, v11
	v_add_f32_e32 v27, 1.0, v27
	v_med3_f32 v20, v20, s74, v203
	v_rcp_f32_e32 v27, v27
	v_fmaak_f32 v20, 4.0, v20, 0x40800000
	v_mul_f32_e32 v20, v26, v20
	v_mul_f32_e32 v26, v27, v20
	v_fmamk_f32 v20, v91, 0x3a000000, v7
	v_min_f32_e32 v27, 0x40e00000, v20
	v_mul_f32_e32 v20, 0xbfd9db23, v27
	v_mul_f32_e32 v20, 0x3fb8aa3b, v20
	v_exp_f32_e32 v20, v20
	v_fmaak_f32 v8, 4.0, v8, 0x40800000
	v_min_f32_e32 v4, 0x40e00000, v4
	v_mul_f32_e32 v8, v12, v8
	v_add_f32_e32 v20, 1.0, v20
	v_rcp_f32_e32 v29, v20
	v_mov_b32_e32 v20, 0
	v_cvt_pk_fp8_f32 v20, v19, v21
	v_mov_b32_e32 v21, 0
	v_cvt_pk_fp8_f32 v21, v24, v22
	v_mul_f32_e32 v22, 0xbfd9db23, v12
	v_mul_f32_e32 v12, 0xbfd9db23, v4
	v_mul_f32_e32 v12, 0x3fb8aa3b, v12
	v_fmamk_f32 v0, v64, 0x3a000000, v0
	v_exp_f32_e32 v12, v12
	v_med3_f32 v0, v0, s74, v203
	v_fmaak_f32 v0, 4.0, v0, 0x40800000
	v_mul_f32_e32 v0, v4, v0
	v_add_f32_e32 v4, 1.0, v12
	v_fmamk_f32 v12, v77, 0x3a000000, v13
	v_min_f32_e32 v12, 0x40e00000, v12
	v_mul_f32_e32 v13, 0xbfd9db23, v12
	v_mul_f32_e32 v13, 0x3fb8aa3b, v13
	v_rcp_f32_e32 v4, v4
	v_exp_f32_e32 v13, v13
	v_fmamk_f32 v5, v73, 0x3a000000, v5
	v_min_f32_e32 v5, 0x40e00000, v5
	v_mul_f32_e32 v0, v4, v0
	v_fmamk_f32 v4, v69, 0x3a000000, v9
	v_add_f32_e32 v9, 1.0, v13
	v_med3_f32 v4, v4, s74, v203
	v_rcp_f32_e32 v9, v9
	v_fmaak_f32 v4, 4.0, v4, 0x40800000
	v_mul_f32_e32 v4, v12, v4
	v_mul_f32_e32 v4, v9, v4
	v_mul_f32_e32 v9, 0xbfd9db23, v5
	v_mul_f32_e32 v9, 0x3fb8aa3b, v9
	v_fmamk_f32 v1, v65, 0x3a000000, v1
	v_exp_f32_e32 v9, v9
	v_med3_f32 v1, v1, s74, v203
	v_fmaak_f32 v1, 4.0, v1, 0x40800000
	v_mul_f32_e32 v1, v5, v1
	v_add_f32_e32 v5, 1.0, v9
	v_rcp_f32_e32 v5, v5
	v_fmamk_f32 v9, v78, 0x3a000000, v14
	v_fmamk_f32 v6, v74, 0x3a000000, v6
	v_min_f32_e32 v9, 0x40e00000, v9
	v_mul_f32_e32 v1, v5, v1
	v_fmamk_f32 v5, v70, 0x3a000000, v10
	v_med3_f32 v5, v5, s74, v203
	v_fmaak_f32 v5, 4.0, v5, 0x40800000
	v_min_f32_e32 v6, 0x40e00000, v6
	v_mul_f32_e32 v12, 0xbfd9db23, v9
	v_mul_f32_e32 v5, v9, v5
	v_mul_f32_e32 v9, 0xbfd9db23, v6
	v_mul_f32_e32 v9, 0x3fb8aa3b, v9
	v_fmamk_f32 v2, v66, 0x3a000000, v2
	v_exp_f32_e32 v9, v9
	v_med3_f32 v2, v2, s74, v203
	v_mul_f32_e32 v12, 0x3fb8aa3b, v12
	v_exp_f32_e32 v12, v12
	v_fmaak_f32 v2, 4.0, v2, 0x40800000
	v_mul_f32_e32 v2, v6, v2
	v_add_f32_e32 v6, 1.0, v9
	v_rcp_f32_e32 v6, v6
	v_add_f32_e32 v10, 1.0, v12
	v_fmamk_f32 v28, v83, 0x3a000000, v3
	v_rcp_f32_e32 v10, v10
	v_fmac_f32_e32 v11, 0x3a000000, v71
	v_med3_f32 v28, v28, s74, v203
	v_mul_f32_e32 v22, 0x3fb8aa3b, v22
	v_mul_f32_e32 v2, v6, v2
	v_med3_f32 v6, v11, s74, v203
	v_add_f32_e32 v28, 1.0, v28
	v_exp_f32_e32 v22, v22
	v_fmac_f32_e32 v15, 0x3a000000, v79
	v_fmac_f32_e32 v7, 0x3a000000, v75
	v_mul_f32_e32 v19, 4.0, v28
	v_min_f32_e32 v9, 0x40e00000, v15
	v_fmaak_f32 v6, 4.0, v6, 0x40800000
	v_min_f32_e32 v7, 0x40e00000, v7
	v_mul_f32_e32 v19, v27, v19
	v_mul_f32_e32 v5, v10, v5
	v_mul_f32_e32 v10, 0xbfd9db23, v9
	v_mul_f32_e32 v6, v9, v6
	v_mul_f32_e32 v9, 0xbfd9db23, v7
	v_mul_f32_e32 v19, v29, v19
	v_mul_f32_e32 v10, 0x3fb8aa3b, v10
	v_mul_f32_e32 v9, 0x3fb8aa3b, v9
	v_cvt_pk_fp8_f32 v21, v25, v19 op_sel:[0,0,1]
	v_add_f32_e32 v19, 1.0, v22
	v_exp_f32_e32 v10, v10
	v_exp_f32_e32 v9, v9
	v_rcp_f32_e32 v19, v19
	v_fmac_f32_e32 v3, 0x3a000000, v67
	v_add_f32_e32 v10, 1.0, v10
	v_add_f32_e32 v9, 1.0, v9
	v_cvt_pk_fp8_f32 v20, v23, v26 op_sel:[0,0,1]
	v_mul_f32_e32 v8, v19, v8
	v_rcp_f32_e32 v10, v10
	v_med3_f32 v3, v3, s74, v203
	v_rcp_f32_e32 v9, v9
	v_mov_b32_e32 v22, 0
	v_mov_b32_e32 v23, 0
	v_cvt_pk_fp8_f32 v22, v8, v4
	v_cvt_pk_fp8_f32 v23, v0, v1
	v_fmaak_f32 v3, 4.0, v3, 0x40800000
	v_mul_f32_e32 v0, v7, v3
	v_mul_f32_e32 v6, v10, v6
	v_mul_f32_e32 v0, v9, v0
	v_cvt_pk_fp8_f32 v22, v5, v6 op_sel:[0,0,1]
	v_cvt_pk_fp8_f32 v23, v2, v0 op_sel:[0,0,1]
	v_add_u32_e32 v0, 0xa0, v18
	v_ashrrev_i32_e32 v1, 31, v0
	v_lshlrev_b64 v[0:1], 10, v[0:1]
	v_lshl_add_u64 v[0:1], s[12:13], 0, v[0:1]
	v_permlane16_swap_b32_e32 v20, v22
	v_permlane16_swap_b32_e32 v21, v23
	v_lshl_add_u64 v[0:1], v[0:1], 0, v[16:17]
	global_store_dwordx4 v[0:1], v[20:23], off
	s_cbranch_vccnz .LBB0_2523
	s_andn2_b64 vcc, exec, s[4:5]
	s_cbranch_vccnz .LBB0_2522
	s_barrier
	s_branch .LBB0_2522

; #define PG8_WAIT_V(n) asm volatile("s_waitcnt vmcnt(" #n ")" ::: "memory")
; #define PG8_BAR __builtin_amdgcn_s_barrier()
; #define PG8_STAGE_A(b, h, p) do { if constexpr (GATHER) { if ((h) == 0) PG8_STAGE(PG8_SA(b, h), p, vA0); else PG8_STAGE(PG8_SA(b, h), p, vA1); } else PG8_STAGE(PG8_SA(b, h), (p) + ((h) ? hstepA : (size_t)0), voffA); } while (0)
; template <class Epi, class Sched, bool ALIGN_EPI = true, bool SP2 = true, bool FP8 = false, bool GATHER = false>
; __device__ __forceinline__ void gemm_phase(LAS unsigned char* lds, const Dims g, const Sched& S, const Epi& E, const int wv) {
;     ...
;     for (int i = 0; i < 2; ++i) { int R, C; stage_rc(tid * 16 + i * 8192, R, C); const int Rb = Epi::PERM ? ((R & ~31) + perm32(R & 31)) : R;
;         voffA[i] = (unsigned)(R * g.lda + C) * 2u; voffB[i] = (unsigned)(Rb * g.ldb + C) * 2u; }
;     const size_t kstep = (size_t)(BK * 2);
;     const size_t hstepA = (size_t)HALF * g.lda * 2, hstepB = (size_t)HALF * g.ldb * 2;
;     const unsigned ldsw = (unsigned)wid * 1024u, ldsb_ = (unsigned)(uintptr_t)lds;
;     const int aoff = lds_byte(wr * 64 + fr, fq * 8), boff = lds_byte(wc * 32 + fr, fq * 8);
;     ...
;     if constexpr (SP2) {
;         PG8_STAGE(PG8_SB(0, 0), cB, voffB); PG8_STAGE(PG8_SB(0, 1), cB + hstepB, voffB); PG8_STAGE_A(0, 0, cA); PG8_STAGE_A(0, 1, cA);
;         if (wr == 1) PG8_BAR;
;         PG8_WAIT_V(2); PG8_BAR;
;         PG8_STAGE(PG8_SB(1, 0), cB + kstep, voffB); PG8_STAGE_A(1, 0, cA + kstep); PG8_STAGE(PG8_SB(1, 1), cB + hstepB + kstep, voffB);
;         PG8_WAIT_V(6); PG8_BAR;
.LBB0_2621:
	v_bfe_i32 v2, v152, 27, 1
	s_add_u32 s55, s14, 0x8d200000
	v_lshlrev_b32_e32 v0, 4, v152
	v_lshrrev_b32_e32 v2, 22, v2
	s_addc_u32 s56, s15, 0
	v_add_u32_e32 v2, v0, v2
	s_add_u32 s57, s14, 0x28000000
	v_and_b32_e32 v2, 0xfffffc00, v2
	s_addc_u32 s58, s15, 0
	s_ashr_i32 s37, s36, 31
	v_sub_u32_e32 v2, v0, v2
	s_lshl_b64 s[6:7], s[36:37], 18
	v_ashrrev_i32_e32 v1, 31, v152
	v_lshrrev_b32_e32 v3, 4, v2
	s_add_u32 s42, s55, s6
	v_lshrrev_b32_e32 v1, 26, v1
	v_bitop3_b32 v2, v3, v2, 32 bitop3:0x6c
	s_addc_u32 s43, s56, s7
	s_ashr_i32 s41, s40, 31
	v_add_u32_e32 v1, v152, v1
	v_ashrrev_i32_e32 v4, 31, v2
	s_lshl_b64 s[6:7], s[40:41], 20
	v_ashrrev_i32_e32 v1, 6, v1
	v_lshrrev_b32_e32 v4, 26, v4
	s_add_u32 s8, s57, s6
	v_lshlrev_b32_e32 v3, 3, v1
	v_add_u32_e32 v4, v2, v4
	s_addc_u32 s9, s58, s7
	s_ashr_i32 s39, s38, 31
	v_and_b32_e32 v3, -16, v3
	v_ashrrev_i32_e32 v5, 6, v4
	v_and_b32_e32 v4, 0xc0, v4
	s_lshl_b64 s[6:7], s[38:39], 18
	v_add_u32_e32 v3, v5, v3
	v_sub_u32_e32 v2, v2, v4
	v_mov_b32_e32 v4, 1
	s_add_u32 s44, s8, s6
	v_lshlrev_b32_e32 v1, 5, v1
	v_ashrrev_i16_sdwa v2, v4, sext(v2) dst_sel:DWORD dst_unused:UNUSED_PAD src0_sel:DWORD src1_sel:BYTE_0
	v_lshlrev_b32_e32 v6, 1, v3
	v_lshrrev_b32_e32 v7, 2, v3
	v_and_b32_e32 v5, 3, v5
	s_mov_b32 s6, 0x3fffe0
	v_and_b32_e32 v1, 32, v1
	v_bfe_i32 v2, v2, 0, 16
	v_and_b32_e32 v6, 24, v6
	v_and_b32_e32 v7, 4, v7
	v_and_or_b32 v5, v3, s6, v5
	v_or3_b32 v5, v5, v7, v6
	v_add_lshl_u32 v1, v1, v2, 1
	v_add_u32_e32 v0, 0x2000, v0
	v_lshl_add_u32 v153, v3, 10, v1
	v_lshl_add_u32 v154, v5, 10, v1
	v_ashrrev_i32_e32 v1, 31, v0
	v_lshrrev_b32_e32 v1, 22, v1
	v_add_u32_e32 v1, v0, v1
	v_ashrrev_i32_e32 v1, 10, v1
	v_mul_i32_i24_e32 v2, 0x400, v1
	v_sub_u32_e32 v0, v0, v2
	v_lshrrev_b32_e32 v2, 4, v0
	v_bitop3_b32 v0, v2, v0, 32 bitop3:0x6c
	v_ashrrev_i32_e32 v3, 31, v0
	v_lshrrev_b32_e32 v3, 26, v3
	v_lshlrev_b32_e32 v2, 3, v1
	v_add_u32_e32 v3, v0, v3
	v_and_b32_e32 v2, -16, v2
	v_ashrrev_i32_e32 v5, 6, v3
	v_and_b32_e32 v3, 0xc0, v3
	s_addc_u32 s45, s9, s7
	v_add_u32_e32 v2, v5, v2
	v_sub_u32_e32 v0, v0, v3
	v_and_b32_e32 v5, 3, v5
	s_ashr_i32 s13, s3, 6
	v_lshlrev_b32_e32 v1, 5, v1
	v_ashrrev_i16_sdwa v0, v4, sext(v0) dst_sel:DWORD dst_unused:UNUSED_PAD src0_sel:DWORD src1_sel:BYTE_0
	v_lshlrev_b32_e32 v3, 1, v2
	v_lshrrev_b32_e32 v4, 2, v2
	v_and_or_b32 v5, v2, s6, v5
	s_lshl_b32 s6, s13, 10
	v_and_b32_e32 v1, 32, v1
	v_bfe_i32 v0, v0, 0, 16
	v_and_b32_e32 v3, 24, v3
	v_and_b32_e32 v4, 4, v4
	s_add_i32 s59, s6, 0
	v_or3_b32 v3, v5, v4, v3
	v_add_lshl_u32 v0, v1, v0, 1
	s_add_i32 s60, s59, 0x10000
	s_mov_b32 m0, s60
	s_nop 0
	global_load_lds_dwordx4 v154, s[44:45]
	s_ashr_i32 s12, s3, 8
	v_lshl_add_u32 v156, v3, 10, v0
	s_add_i32 s61, s59, 0x12000
	s_mov_b32 m0, s61
	s_nop 0
	global_load_lds_dwordx4 v156, s[44:45]
	s_add_i32 s62, s59, 0x14000
	s_add_u32 s6, s44, 0x20000
	s_addc_u32 s7, s45, 0
	s_mov_b32 m0, s62
	s_nop 0
	global_load_lds_dwordx4 v154, s[6:7]
	s_add_i32 s63, s59, 0x16000
	s_mov_b32 m0, s63
	s_nop 0
	global_load_lds_dwordx4 v156, s[6:7]
	s_mov_b32 m0, s59
	s_nop 0
	global_load_lds_dwordx4 v153, s[42:43]
	s_add_i32 s64, s59, 0x2000
	s_add_i32 s65, s59, 0x4000
	v_lshl_add_u32 v155, v2, 10, v0
	s_mov_b32 m0, s64
	s_nop 0
	global_load_lds_dwordx4 v155, s[42:43]
	s_add_u32 s8, s42, 0x20000
	s_addc_u32 s9, s43, 0
	s_mov_b32 m0, s65
	s_nop 0
	global_load_lds_dwordx4 v153, s[8:9]
	s_add_i32 s66, s59, 0x6000
	s_mov_b32 m0, s66
	s_nop 0
	global_load_lds_dwordx4 v155, s[8:9]
	s_cmp_eq_u32 s12, 1
	s_mov_b32 s39, 0
	s_cselect_b64 s[6:7], -1, 0
	s_cmp_lg_u32 s12, 1
	s_cbranch_scc1 .LBB0_2623
	s_barrier
.LBB0_2623:
	s_add_u32 s8, s14, 0x9e200000
	s_addc_u32 s9, s15, 0
	s_waitcnt lgkmcnt(0)
	s_add_u32 s67, s10, 0x20000
	s_addc_u32 s68, s11, 0
	s_lshl_b32 s10, s12, 6
	v_and_b32_e32 v0, 48, v152
	s_lshl_b32 s11, s12, 13
	v_lshlrev_b32_e32 v1, 6, v152
	s_movk_i32 s12, 0x3c0
	v_and_or_b32 v0, v1, s12, v0
	v_lshlrev_b32_e32 v1, 2, v152
	v_and_b32_e32 v1, 32, v1
	v_bitop3_b32 v2, v0, s11, v1 bitop3:0xde
	s_lshl_b32 s11, s13, 5
	s_and_b32 s69, s11, 0x60
	s_lshl_b32 s11, s69, 7
	s_add_i32 s70, s59, 0x18000
	s_add_u32 s12, s44, 0x80
	v_bitop3_b32 v0, s11, v0, v1 bitop3:0xf6
	s_waitcnt vmcnt(2)
	s_barrier
	s_addc_u32 s13, s45, 0
	s_mov_b32 m0, s70
	s_nop 0
	global_load_lds_dwordx4 v154, s[12:13]
	s_add_i32 s71, s59, 0x1a000
	s_add_i32 s72, s59, 0x8000
	s_mov_b32 m0, s71
	s_nop 0
	global_load_lds_dwordx4 v156, s[12:13]
	s_add_u32 s12, s42, 0x80
	s_addc_u32 s13, s43, 0
	s_mov_b32 m0, s72
	s_nop 0
	global_load_lds_dwordx4 v153, s[12:13]
	s_add_i32 s73, s59, 0xa000
	s_add_i32 s74, s59, 0x1c000
	s_mov_b32 m0, s73
	s_nop 0
	global_load_lds_dwordx4 v155, s[12:13]
	s_add_u32 s12, s44, 0x20080
	s_addc_u32 s13, s45, 0
	s_mov_b32 m0, s74
	s_nop 0
	global_load_lds_dwordx4 v154, s[12:13]
	s_add_i32 s75, s59, 0x1e000
	s_add_i32 s76, s59, 0xc000
	s_mov_b32 m0, s75
	s_nop 0
	global_load_lds_dwordx4 v156, s[12:13]
	s_cmpk_lt_u32 s3, 0x100
	s_cselect_b64 s[12:13], -1, 0
	s_ashr_i32 s11, s10, 31
	s_add_i32 s77, s59, 0xe000
	s_lshl_b64 s[20:21], s[10:11], 2
	s_add_u32 s3, s14, s20
	s_addc_u32 s14, s15, s21
	s_add_u32 s11, s3, 0x7c100000
	s_waitcnt vmcnt(6)
	s_addc_u32 s15, s14, 0
	s_lshl_b32 s14, s33, 3
	s_and_b32 s14, s14, 56
	s_bfe_u32 s16, s33, 0x30003
	v_add_u32_e32 v0, 0, v0
	s_ashr_i32 s78, s54, 31
	s_ashr_i32 s79, s33, 31
	s_ashr_i32 s3, s2, 31
	s_or_b32 s80, s16, s14
	s_ashr_i32 s81, s33, 6
	v_add_u32_e32 v157, 0x10000, v0
	v_add_u32_e32 v158, 0x14000, v0
	v_add_u32_e32 v159, 0, v2
	v_mov_b32_e32 v160, 0x7f7f7f7f
	v_add_u32_e32 v161, 0x18000, v0
	v_add_u32_e32 v162, 0x1c000, v0
	s_mov_b32 s14, 0x42000000
	s_mov_b32 s16, 0x3b000000
	s_mov_b32 s82, 0xc3e00000
	v_mov_b32_e32 v163, 0x43e00000
	s_barrier
	s_branch .LBB0_2626

; #define PG8_WAIT_V(n) asm volatile("s_waitcnt vmcnt(" #n ")" ::: "memory")
; #define PG8_WAIT_L(n) asm volatile("s_waitcnt lgkmcnt(" #n ")" ::: "memory")
; #define PG8_BAR __builtin_amdgcn_s_barrier()
; #define PG8_SCHED __builtin_amdgcn_sched_barrier(0)
; #define PG8_STAGE_A(b, h, p) do { if constexpr (GATHER) { if ((h) == 0) PG8_STAGE(PG8_SA(b, h), p, vA0); else PG8_STAGE(PG8_SA(b, h), p, vA1); } else PG8_STAGE(PG8_SA(b, h), (p) + ((h) ? hstepA : (size_t)0), voffA); } while (0)
; #define PG8_GOFF1(un, h, d) do { int tz_ = tid; asm volatile("" : "+v"(tz_)); _Pragma("unroll") for (int i_ = 0; i_ < 2; ++i_) { int R_, C_; stage_rc(tz_ * 16 + i_ * 8192, R_, C_); \
;         d[i_] = S.gather(un, R_ + (h) * HALF) + (unsigned)C_ * 2u; } } while (0)
; template <class Epi, class Sched, bool ALIGN_EPI = true, bool SP2 = true, bool FP8 = false, bool GATHER = false>
; __device__ __forceinline__ void gemm_phase(LAS unsigned char* lds, const Dims g, const Sched& S, const Epi& E, const int wv) {
;     ...
;             PG8_LDB(B0, 0, 0); PG8_LDB(B1, 0, 1); PG8_SCHED; PG8_LDA(At, 0, 0); PG8_STAGE_A(1, 1, a1);
;             if constexpr (GATHER) { if (last) PG8_GOFF1(un_, 1, vA1); }
;             PG8_WAIT_V(8); PG8_WAIT_L(0); PG8_BAR; PG8_MMA(0, 0, At, B0); PG8_MMA(0, 1, At, B1); PG8_BAR; PG8_SCHED;
;             PG8_LDA(At, 0, 1); PG8_STAGE(PG8_SB(0, 0), b2, voffB); PG8_STAGE(PG8_SB(0, 1), b2 + hstepB, voffB); PG8_STAGE_A(0, 0, a2);
;             PG8_WAIT_V(8); PG8_WAIT_L(0); PG8_BAR; PG8_MMA(1, 0, At, B0); PG8_MMA(1, 1, At, B1); PG8_BAR; PG8_SCHED;
;             PG8_LDB(B0, 1, 0); PG8_LDB(B1, 1, 1); PG8_SCHED; PG8_LDA(At, 1, 0); PG8_STAGE_A(0, 1, a2);
;             PG8_WAIT_V(8); PG8_WAIT_L(0); PG8_BAR; PG8_MMA(0, 0, At, B0); PG8_MMA(0, 1, At, B1); PG8_BAR; PG8_SCHED;
;             PG8_LDA(At, 1, 1); PG8_STAGE(PG8_SB(1, 0), b3, voffB); PG8_STAGE(PG8_SB(1, 1), b3 + hstepB, voffB); PG8_STAGE_A(1, 0, a3);
;             PG8_WAIT_V(8); PG8_WAIT_L(0); PG8_BAR; PG8_MMA(1, 0, At, B0); PG8_MMA(1, 1, At, B1); PG8_BAR; PG8_SCHED;
.LBB0_2632:
	ds_read_b128 v[128:131], v157
	ds_read_b128 v[132:135], v157 offset:1024
	ds_read_b128 v[136:139], v157 offset:2048
	ds_read_b128 v[140:143], v157 offset:3072
	ds_read_b128 v[144:147], v158
	ds_read_b128 v[148:151], v158 offset:1024
	ds_read_b128 v[164:167], v158 offset:2048
	ds_read_b128 v[168:171], v158 offset:3072
	s_add_u32 s44, s42, 0x100
	s_addc_u32 s45, s43, 0
	s_cmp_eq_u32 s86, 4
	s_cselect_b32 s50, s41, s44
	s_cselect_b32 s51, s37, s45
	s_cselect_b32 s48, s53, s84
	s_cselect_b32 s49, s52, s85
	s_add_u32 s46, s50, 0x80
	s_addc_u32 s47, s51, 0
	ds_read_b128 v[172:175], v159
	ds_read_b128 v[176:179], v159 offset:1024
	ds_read_b128 v[180:183], v159 offset:2048
	ds_read_b128 v[184:187], v159 offset:3072
	ds_read_b128 v[188:191], v159 offset:4096
	ds_read_b128 v[192:195], v159 offset:5120
	ds_read_b128 v[196:199], v159 offset:6144
	ds_read_b128 v[200:203], v159 offset:7168
	s_add_u32 s42, s42, 0x20080
	s_addc_u32 s43, s43, 0
	s_mov_b32 m0, s76
	s_nop 0
	global_load_lds_dwordx4 v153, s[42:43]
	s_nop 0
	s_mov_b32 m0, s77
	s_nop 0
	global_load_lds_dwordx4 v155, s[42:43]
	s_waitcnt vmcnt(8)
	s_waitcnt lgkmcnt(0)
	s_barrier
	s_setprio 1
	s_waitcnt lgkmcnt(6)
	v_mfma_scale_f32_16x16x128_f8f6f4 v[124:127], v[128:135], v[172:179], v[124:127], v160, v160 op_sel_hi:[0,0,0]
	v_mfma_scale_f32_16x16x128_f8f6f4 v[120:123], v[136:143], v[172:179], v[120:123], v160, v160 op_sel_hi:[0,0,0]
	s_waitcnt lgkmcnt(4)
	v_mfma_scale_f32_16x16x128_f8f6f4 v[116:119], v[128:135], v[180:187], v[116:119], v160, v160 op_sel_hi:[0,0,0]
	v_mfma_scale_f32_16x16x128_f8f6f4 v[112:115], v[136:143], v[180:187], v[112:115], v160, v160 op_sel_hi:[0,0,0]
	s_waitcnt lgkmcnt(2)
	v_mfma_scale_f32_16x16x128_f8f6f4 v[204:207], v[128:135], v[188:195], v[92:95], v160, v160 op_sel_hi:[0,0,0]
	v_mfma_scale_f32_16x16x128_f8f6f4 v[208:211], v[136:143], v[188:195], v[88:91], v160, v160 op_sel_hi:[0,0,0]
	s_waitcnt lgkmcnt(0)
	v_mfma_scale_f32_16x16x128_f8f6f4 v[212:215], v[128:135], v[196:203], v[76:79], v160, v160 op_sel_hi:[0,0,0]
	v_mfma_scale_f32_16x16x128_f8f6f4 v[216:219], v[136:143], v[196:203], v[72:75], v160, v160 op_sel_hi:[0,0,0]
	s_setprio 0
	s_setprio 1
	v_mfma_scale_f32_16x16x128_f8f6f4 v[108:111], v[144:151], v[172:179], v[108:111], v160, v160 op_sel_hi:[0,0,0]
	v_mfma_scale_f32_16x16x128_f8f6f4 v[104:107], v[164:171], v[172:179], v[104:107], v160, v160 op_sel_hi:[0,0,0]
	v_mfma_scale_f32_16x16x128_f8f6f4 v[100:103], v[144:151], v[180:187], v[100:103], v160, v160 op_sel_hi:[0,0,0]
	v_mfma_scale_f32_16x16x128_f8f6f4 v[96:99], v[164:171], v[180:187], v[96:99], v160, v160 op_sel_hi:[0,0,0]
	v_mfma_scale_f32_16x16x128_f8f6f4 v[172:175], v[144:151], v[188:195], v[84:87], v160, v160 op_sel_hi:[0,0,0]
	v_mfma_scale_f32_16x16x128_f8f6f4 v[176:179], v[164:171], v[188:195], v[80:83], v160, v160 op_sel_hi:[0,0,0]
	v_mfma_scale_f32_16x16x128_f8f6f4 v[180:183], v[144:151], v[196:203], v[68:71], v160, v160 op_sel_hi:[0,0,0]
	v_mfma_scale_f32_16x16x128_f8f6f4 v[184:187], v[164:171], v[196:203], v[64:67], v160, v160 op_sel_hi:[0,0,0]
	s_setprio 0
	s_barrier
	s_nop 4
	ds_read_b128 v[64:67], v159 offset:16384
	ds_read_b128 v[68:71], v159 offset:17408
	ds_read_b128 v[72:75], v159 offset:18432
	ds_read_b128 v[76:79], v159 offset:19456
	ds_read_b128 v[80:83], v159 offset:20480
	ds_read_b128 v[84:87], v159 offset:21504
	ds_read_b128 v[88:91], v159 offset:22528
	ds_read_b128 v[92:95], v159 offset:23552
	s_mov_b32 m0, s60
	s_nop 0
	global_load_lds_dwordx4 v154, s[48:49]
	s_nop 0
	s_mov_b32 m0, s61
	s_nop 0
	global_load_lds_dwordx4 v156, s[48:49]
	s_add_u32 s42, s48, 0x20000
	s_addc_u32 s43, s49, 0
	s_mov_b32 m0, s62
	s_nop 0
	global_load_lds_dwordx4 v154, s[42:43]
	s_nop 0
	s_mov_b32 m0, s63
	s_nop 0
	global_load_lds_dwordx4 v156, s[42:43]
	s_mov_b32 m0, s59
	s_nop 0
	global_load_lds_dwordx4 v153, s[50:51]
	s_nop 0
	s_mov_b32 m0, s64
	s_nop 0
	global_load_lds_dwordx4 v155, s[50:51]
	s_waitcnt vmcnt(8)
	s_waitcnt lgkmcnt(0)
	s_barrier
	s_setprio 1
	s_waitcnt lgkmcnt(6)
	v_mfma_scale_f32_16x16x128_f8f6f4 v[60:63], v[128:135], v[64:71], v[60:63], v160, v160 op_sel_hi:[0,0,0]
	v_mfma_scale_f32_16x16x128_f8f6f4 v[56:59], v[136:143], v[64:71], v[56:59], v160, v160 op_sel_hi:[0,0,0]
	s_waitcnt lgkmcnt(4)
	v_mfma_scale_f32_16x16x128_f8f6f4 v[188:191], v[128:135], v[72:79], v[44:47], v160, v160 op_sel_hi:[0,0,0]
	v_mfma_scale_f32_16x16x128_f8f6f4 v[192:195], v[136:143], v[72:79], v[40:43], v160, v160 op_sel_hi:[0,0,0]
	s_waitcnt lgkmcnt(2)
	v_mfma_scale_f32_16x16x128_f8f6f4 v[196:199], v[128:135], v[80:87], v[28:31], v160, v160 op_sel_hi:[0,0,0]
	v_mfma_scale_f32_16x16x128_f8f6f4 v[200:203], v[136:143], v[80:87], v[24:27], v160, v160 op_sel_hi:[0,0,0]
	s_waitcnt lgkmcnt(0)
	v_mfma_scale_f32_16x16x128_f8f6f4 v[220:223], v[128:135], v[88:95], v[12:15], v160, v160 op_sel_hi:[0,0,0]
	v_mfma_scale_f32_16x16x128_f8f6f4 v[224:227], v[136:143], v[88:95], v[8:11], v160, v160 op_sel_hi:[0,0,0]
	s_setprio 0
	s_setprio 1
	v_mfma_scale_f32_16x16x128_f8f6f4 v[52:55], v[144:151], v[64:71], v[52:55], v160, v160 op_sel_hi:[0,0,0]
	v_mfma_scale_f32_16x16x128_f8f6f4 v[48:51], v[164:171], v[64:71], v[48:51], v160, v160 op_sel_hi:[0,0,0]
	v_mfma_scale_f32_16x16x128_f8f6f4 v[228:231], v[144:151], v[72:79], v[36:39], v160, v160 op_sel_hi:[0,0,0]
	v_mfma_scale_f32_16x16x128_f8f6f4 v[232:235], v[164:171], v[72:79], v[32:35], v160, v160 op_sel_hi:[0,0,0]
	v_mfma_scale_f32_16x16x128_f8f6f4 v[236:239], v[144:151], v[80:87], v[20:23], v160, v160 op_sel_hi:[0,0,0]
	v_mfma_scale_f32_16x16x128_f8f6f4 v[240:243], v[164:171], v[80:87], v[16:19], v160, v160 op_sel_hi:[0,0,0]
	v_mfma_scale_f32_16x16x128_f8f6f4 v[244:247], v[144:151], v[88:95], v[4:7], v160, v160 op_sel_hi:[0,0,0]
	v_mfma_scale_f32_16x16x128_f8f6f4 v[248:251], v[164:171], v[88:95], v[0:3], v160, v160 op_sel_hi:[0,0,0]
	s_setprio 0
	s_barrier
; #define PG8_WAIT_V(n) asm volatile("s_waitcnt vmcnt(" #n ")" ::: "memory")
; #define PG8_WAIT_L(n) asm volatile("s_waitcnt lgkmcnt(" #n ")" ::: "memory")
; #define PG8_BAR __builtin_amdgcn_s_barrier()
; #define PG8_SCHED __builtin_amdgcn_sched_barrier(0)
; #define PG8_STAGE_A(b, h, p) do { if constexpr (GATHER) { if ((h) == 0) PG8_STAGE(PG8_SA(b, h), p, vA0); else PG8_STAGE(PG8_SA(b, h), p, vA1); } else PG8_STAGE(PG8_SA(b, h), (p) + ((h) ? hstepA : (size_t)0), voffA); } while (0)
; #define PG8_GOFF1(un, h, d) do { int tz_ = tid; asm volatile("" : "+v"(tz_)); _Pragma("unroll") for (int i_ = 0; i_ < 2; ++i_) { int R_, C_; stage_rc(tz_ * 16 + i_ * 8192, R_, C_); \
;         d[i_] = S.gather(un, R_ + (h) * HALF) + (unsigned)C_ * 2u; } } while (0)
; template <class Epi, class Sched, bool ALIGN_EPI = true, bool SP2 = true, bool FP8 = false, bool GATHER = false>
; __device__ __forceinline__ void gemm_phase(LAS unsigned char* lds, const Dims g, const Sched& S, const Epi& E, const int wv) {
;     ...
;             PG8_LDB(B0, 0, 0); PG8_LDB(B1, 0, 1); PG8_SCHED; PG8_LDA(At, 0, 0); PG8_STAGE_A(1, 1, a1);
;             if constexpr (GATHER) { if (last) PG8_GOFF1(un_, 1, vA1); }
;             PG8_WAIT_V(8); PG8_WAIT_L(0); PG8_BAR; PG8_MMA(0, 0, At, B0); PG8_MMA(0, 1, At, B1); PG8_BAR; PG8_SCHED;
;             PG8_LDA(At, 0, 1); PG8_STAGE(PG8_SB(0, 0), b2, voffB); PG8_STAGE(PG8_SB(0, 1), b2 + hstepB, voffB); PG8_STAGE_A(0, 0, a2);
;             PG8_WAIT_V(8); PG8_WAIT_L(0); PG8_BAR; PG8_MMA(1, 0, At, B0); PG8_MMA(1, 1, At, B1); PG8_BAR; PG8_SCHED;
;             PG8_LDB(B0, 1, 0); PG8_LDB(B1, 1, 1); PG8_SCHED; PG8_LDA(At, 1, 0); PG8_STAGE_A(0, 1, a2);
;             PG8_WAIT_V(8); PG8_WAIT_L(0); PG8_BAR; PG8_MMA(0, 0, At, B0); PG8_MMA(0, 1, At, B1); PG8_BAR; PG8_SCHED;
;             PG8_LDA(At, 1, 1); PG8_STAGE(PG8_SB(1, 0), b3, voffB); PG8_STAGE(PG8_SB(1, 1), b3 + hstepB, voffB); PG8_STAGE_A(1, 0, a3);
;             PG8_WAIT_V(8); PG8_WAIT_L(0); PG8_BAR; PG8_MMA(1, 0, At, B0); PG8_MMA(1, 1, At, B1); PG8_BAR; PG8_SCHED;
	s_nop 4
	ds_read_b128 v[0:3], v161
	ds_read_b128 v[4:7], v161 offset:1024
	ds_read_b128 v[16:19], v161 offset:2048
	ds_read_b128 v[20:23], v161 offset:3072
	ds_read_b128 v[128:131], v162
	ds_read_b128 v[132:135], v162 offset:1024
	ds_read_b128 v[136:139], v162 offset:2048
	ds_read_b128 v[140:143], v162 offset:3072
	ds_read_b128 v[8:11], v159 offset:32768
	ds_read_b128 v[12:15], v159 offset:33792
	ds_read_b128 v[24:27], v159 offset:34816
	ds_read_b128 v[28:31], v159 offset:35840
	ds_read_b128 v[32:35], v159 offset:36864
	ds_read_b128 v[36:39], v159 offset:37888
	ds_read_b128 v[40:43], v159 offset:38912
	ds_read_b128 v[44:47], v159 offset:39936
	s_add_u32 s42, s50, 0x20000
	s_addc_u32 s43, s51, 0
	s_mov_b32 m0, s65
	s_nop 0
	global_load_lds_dwordx4 v153, s[42:43]
	s_nop 0
	s_mov_b32 m0, s66
	s_nop 0
	global_load_lds_dwordx4 v155, s[42:43]
	s_waitcnt vmcnt(8)
	s_waitcnt lgkmcnt(0)
	s_barrier
	s_setprio 1
	s_waitcnt lgkmcnt(6)
	v_mfma_scale_f32_16x16x128_f8f6f4 v[124:127], v[0:7], v[8:15], v[124:127], v160, v160 op_sel_hi:[0,0,0]
	v_mfma_scale_f32_16x16x128_f8f6f4 v[120:123], v[16:23], v[8:15], v[120:123], v160, v160 op_sel_hi:[0,0,0]
	s_waitcnt lgkmcnt(4)
	v_mfma_scale_f32_16x16x128_f8f6f4 v[116:119], v[0:7], v[24:31], v[116:119], v160, v160 op_sel_hi:[0,0,0]
	v_mfma_scale_f32_16x16x128_f8f6f4 v[112:115], v[16:23], v[24:31], v[112:115], v160, v160 op_sel_hi:[0,0,0]
	s_waitcnt lgkmcnt(2)
	v_mfma_scale_f32_16x16x128_f8f6f4 v[92:95], v[0:7], v[32:39], v[204:207], v160, v160 op_sel_hi:[0,0,0]
	v_mfma_scale_f32_16x16x128_f8f6f4 v[88:91], v[16:23], v[32:39], v[208:211], v160, v160 op_sel_hi:[0,0,0]
	s_waitcnt lgkmcnt(0)
	v_mfma_scale_f32_16x16x128_f8f6f4 v[76:79], v[0:7], v[40:47], v[212:215], v160, v160 op_sel_hi:[0,0,0]
	v_mfma_scale_f32_16x16x128_f8f6f4 v[72:75], v[16:23], v[40:47], v[216:219], v160, v160 op_sel_hi:[0,0,0]
	s_setprio 0
	s_setprio 1
	v_mfma_scale_f32_16x16x128_f8f6f4 v[108:111], v[128:135], v[8:15], v[108:111], v160, v160 op_sel_hi:[0,0,0]
	v_mfma_scale_f32_16x16x128_f8f6f4 v[104:107], v[136:143], v[8:15], v[104:107], v160, v160 op_sel_hi:[0,0,0]
	v_mfma_scale_f32_16x16x128_f8f6f4 v[100:103], v[128:135], v[24:31], v[100:103], v160, v160 op_sel_hi:[0,0,0]
	v_mfma_scale_f32_16x16x128_f8f6f4 v[96:99], v[136:143], v[24:31], v[96:99], v160, v160 op_sel_hi:[0,0,0]
	v_mfma_scale_f32_16x16x128_f8f6f4 v[84:87], v[128:135], v[32:39], v[172:175], v160, v160 op_sel_hi:[0,0,0]
	v_mfma_scale_f32_16x16x128_f8f6f4 v[80:83], v[136:143], v[32:39], v[176:179], v160, v160 op_sel_hi:[0,0,0]
	v_mfma_scale_f32_16x16x128_f8f6f4 v[68:71], v[128:135], v[40:47], v[180:183], v160, v160 op_sel_hi:[0,0,0]
	v_mfma_scale_f32_16x16x128_f8f6f4 v[64:67], v[136:143], v[40:47], v[184:187], v160, v160 op_sel_hi:[0,0,0]
	s_setprio 0
	s_barrier
	ds_read_b128 v[32:35], v159 offset:49152
	ds_read_b128 v[36:39], v159 offset:50176
	ds_read_b128 v[144:147], v159 offset:51200
	ds_read_b128 v[148:151], v159 offset:52224
	ds_read_b128 v[164:167], v159 offset:53248
	ds_read_b128 v[168:171], v159 offset:54272
	ds_read_b128 v[172:175], v159 offset:55296
	ds_read_b128 v[176:179], v159 offset:56320
	s_add_u32 s42, s48, 0x80
	s_addc_u32 s43, s49, 0
	s_mov_b32 m0, s70
	s_nop 0
	global_load_lds_dwordx4 v154, s[42:43]
	s_nop 0
	s_mov_b32 m0, s71
	s_nop 0
	global_load_lds_dwordx4 v156, s[42:43]
	s_add_u32 s42, s48, 0x20080
	s_addc_u32 s43, s49, 0
	s_mov_b32 m0, s74
	s_nop 0
	global_load_lds_dwordx4 v154, s[42:43]
	s_nop 0
	s_mov_b32 m0, s75
	s_nop 0
	global_load_lds_dwordx4 v156, s[42:43]
	s_mov_b32 m0, s72
	s_nop 0
	global_load_lds_dwordx4 v153, s[46:47]
	s_nop 0
	s_mov_b32 m0, s73
	s_nop 0
	global_load_lds_dwordx4 v155, s[46:47]
	s_waitcnt vmcnt(8)
	s_waitcnt lgkmcnt(0)
	s_barrier
	s_setprio 1
	s_waitcnt lgkmcnt(6)
	v_mfma_scale_f32_16x16x128_f8f6f4 v[60:63], v[0:7], v[32:39], v[60:63], v160, v160 op_sel_hi:[0,0,0]
	v_mfma_scale_f32_16x16x128_f8f6f4 v[56:59], v[16:23], v[32:39], v[56:59], v160, v160 op_sel_hi:[0,0,0]
	s_waitcnt lgkmcnt(4)
	v_mfma_scale_f32_16x16x128_f8f6f4 v[44:47], v[0:7], v[144:151], v[188:191], v160, v160 op_sel_hi:[0,0,0]
	v_mfma_scale_f32_16x16x128_f8f6f4 v[40:43], v[16:23], v[144:151], v[192:195], v160, v160 op_sel_hi:[0,0,0]
	s_waitcnt lgkmcnt(2)
	v_mfma_scale_f32_16x16x128_f8f6f4 v[28:31], v[0:7], v[164:171], v[196:199], v160, v160 op_sel_hi:[0,0,0]
	v_mfma_scale_f32_16x16x128_f8f6f4 v[24:27], v[16:23], v[164:171], v[200:203], v160, v160 op_sel_hi:[0,0,0]
	s_waitcnt lgkmcnt(0)
	v_mfma_scale_f32_16x16x128_f8f6f4 v[12:15], v[0:7], v[172:179], v[220:223], v160, v160 op_sel_hi:[0,0,0]
	v_mfma_scale_f32_16x16x128_f8f6f4 v[8:11], v[16:23], v[172:179], v[224:227], v160, v160 op_sel_hi:[0,0,0]
	s_setprio 0
	s_setprio 1
	v_mfma_scale_f32_16x16x128_f8f6f4 v[52:55], v[128:135], v[32:39], v[52:55], v160, v160 op_sel_hi:[0,0,0]
	v_mfma_scale_f32_16x16x128_f8f6f4 v[48:51], v[136:143], v[32:39], v[48:51], v160, v160 op_sel_hi:[0,0,0]
	v_mfma_scale_f32_16x16x128_f8f6f4 v[36:39], v[128:135], v[144:151], v[228:231], v160, v160 op_sel_hi:[0,0,0]
	v_mfma_scale_f32_16x16x128_f8f6f4 v[32:35], v[136:143], v[144:151], v[232:235], v160, v160 op_sel_hi:[0,0,0]
	v_mfma_scale_f32_16x16x128_f8f6f4 v[20:23], v[128:135], v[164:171], v[236:239], v160, v160 op_sel_hi:[0,0,0]
	v_mfma_scale_f32_16x16x128_f8f6f4 v[16:19], v[136:143], v[164:171], v[240:243], v160, v160 op_sel_hi:[0,0,0]
	v_mfma_scale_f32_16x16x128_f8f6f4 v[4:7], v[128:135], v[172:179], v[244:247], v160, v160 op_sel_hi:[0,0,0]
	v_mfma_scale_f32_16x16x128_f8f6f4 v[0:3], v[136:143], v[172:179], v[248:251], v160, v160 op_sel_hi:[0,0,0]
	s_setprio 0
	s_barrier
	s_add_i32 s86, s86, 2
	s_add_u32 s84, s84, 0x100
	s_addc_u32 s85, s85, 0
	s_cmp_gt_u32 s86, 5
	s_mov_b64 s[42:43], s[44:45]
	s_cbranch_scc0 .LBB0_2632
	s_and_b64 vcc, exec, s[12:13]
	s_cbranch_vccz .LBB0_2635
	s_barrier

; #define PG8_WAIT_V(n) asm volatile("s_waitcnt vmcnt(" #n ")" ::: "memory")
; #define PG8_BAR __builtin_amdgcn_s_barrier()
; #define PG8_STAGE_A(b, h, p) do { if constexpr (GATHER) { if ((h) == 0) PG8_STAGE(PG8_SA(b, h), p, vA0); else PG8_STAGE(PG8_SA(b, h), p, vA1); } else PG8_STAGE(PG8_SA(b, h), (p) + ((h) ? hstepA : (size_t)0), voffA); } while (0)
; template <class Epi, class Sched, bool ALIGN_EPI = true, bool SP2 = true, bool FP8 = false, bool GATHER = false>
; __device__ __forceinline__ void gemm_phase(LAS unsigned char* lds, const Dims g, const Sched& S, const Epi& E, const int wv) {
;     ...
;     for (int i = 0; i < 2; ++i) { int R, C; stage_rc(tid * 16 + i * 8192, R, C); const int Rb = Epi::PERM ? ((R & ~31) + perm32(R & 31)) : R;
;         voffA[i] = (unsigned)(R * g.lda + C) * 2u; voffB[i] = (unsigned)(Rb * g.ldb + C) * 2u; }
;     const size_t kstep = (size_t)(BK * 2);
;     const size_t hstepA = (size_t)HALF * g.lda * 2, hstepB = (size_t)HALF * g.ldb * 2;
;     const unsigned ldsw = (unsigned)wid * 1024u, ldsb_ = (unsigned)(uintptr_t)lds;
;     const int aoff = lds_byte(wr * 64 + fr, fq * 8), boff = lds_byte(wc * 32 + fr, fq * 8);
;     ...
;     if constexpr (SP2) {
;         PG8_STAGE(PG8_SB(0, 0), cB, voffB); PG8_STAGE(PG8_SB(0, 1), cB + hstepB, voffB); PG8_STAGE_A(0, 0, cA); PG8_STAGE_A(0, 1, cA);
;         if (wr == 1) PG8_BAR;
;         PG8_WAIT_V(2); PG8_BAR;
;         PG8_STAGE(PG8_SB(1, 0), cB + kstep, voffB); PG8_STAGE_A(1, 0, cA + kstep); PG8_STAGE(PG8_SB(1, 1), cB + hstepB + kstep, voffB);
;         PG8_WAIT_V(6); PG8_BAR;
.LBB0_3272:
	v_bfe_i32 v2, v146, 27, 1
	v_lshlrev_b32_e32 v0, 4, v146
	v_lshrrev_b32_e32 v2, 22, v2
	v_add_u32_e32 v2, v0, v2
	v_and_b32_e32 v2, 0xfffffc00, v2
	v_sub_u32_e32 v2, v0, v2
	v_ashrrev_i32_e32 v1, 31, v146
	v_lshrrev_b32_e32 v3, 4, v2
	v_lshrrev_b32_e32 v1, 26, v1
	v_bitop3_b32 v2, v3, v2, 32 bitop3:0x6c
	v_add_u32_e32 v1, v146, v1
	v_ashrrev_i32_e32 v4, 31, v2
	v_ashrrev_i32_e32 v1, 6, v1
	v_lshrrev_b32_e32 v4, 26, v4
	v_lshlrev_b32_e32 v3, 3, v1
	v_add_u32_e32 v4, v2, v4
	v_and_b32_e32 v3, -16, v3
	v_ashrrev_i32_e32 v5, 6, v4
	v_and_b32_e32 v4, 0xc0, v4
	v_add_u32_e32 v3, v5, v3
	v_sub_u32_e32 v2, v2, v4
	v_mov_b32_e32 v4, 1
	v_lshlrev_b32_e32 v1, 5, v1
	v_ashrrev_i16_sdwa v2, v4, sext(v2) dst_sel:DWORD dst_unused:UNUSED_PAD src0_sel:DWORD src1_sel:BYTE_0
	v_lshlrev_b32_e32 v6, 1, v3
	v_lshrrev_b32_e32 v7, 2, v3
	v_and_b32_e32 v5, 3, v5
	s_mov_b32 s5, 0x3fffe0
	v_and_b32_e32 v1, 32, v1
	v_bfe_i32 v2, v2, 0, 16
	v_and_b32_e32 v6, 24, v6
	v_and_b32_e32 v7, 4, v7
	v_and_or_b32 v5, v3, s5, v5
	v_or3_b32 v5, v5, v7, v6
	v_add_lshl_u32 v1, v1, v2, 1
	v_add_u32_e32 v0, 0x2000, v0
	v_lshl_add_u32 v147, v3, 10, v1
	v_lshl_add_u32 v148, v5, 10, v1
	v_ashrrev_i32_e32 v1, 31, v0
	v_lshrrev_b32_e32 v1, 22, v1
	v_add_u32_e32 v1, v0, v1
	v_ashrrev_i32_e32 v1, 10, v1
	v_mul_i32_i24_e32 v2, 0x400, v1
	v_sub_u32_e32 v0, v0, v2
	v_lshrrev_b32_e32 v2, 4, v0
	v_bitop3_b32 v0, v2, v0, 32 bitop3:0x6c
	v_ashrrev_i32_e32 v3, 31, v0
	s_add_u32 s50, s2, 0x72000000
	v_lshrrev_b32_e32 v3, 26, v3
	s_addc_u32 s51, s3, 0
	v_lshlrev_b32_e32 v2, 3, v1
	v_add_u32_e32 v3, v0, v3
	s_add_u32 s52, s2, 0x3d00000
	v_and_b32_e32 v2, -16, v2
	v_ashrrev_i32_e32 v5, 6, v3
	s_addc_u32 s53, s3, 0
	v_add_u32_e32 v2, v5, v2
	v_and_b32_e32 v5, 3, v5
	s_add_i32 s4, s6, s4
	v_and_or_b32 v5, v2, s5, v5
	s_ashr_i32 s5, s4, 31
	s_lshr_b32 s5, s5, 27
	s_add_i32 s5, s4, s5
	s_ashr_i32 s6, s5, 5
	s_and_b32 s5, s5, 0xffe0
	s_sub_i32 s4, s4, s5
	s_bfe_i32 s5, s4, 0x80000
	s_bfe_u32 s5, s5, 0x3000c
	s_add_i32 s5, s4, s5
	s_lshl_b32 s12, s6, 3
	s_bfe_i32 s6, s5, 0x80000
	s_and_b32 s5, s5, 0xf8
	s_sub_i32 s4, s4, s5
	s_sext_i32_i8 s4, s4
	s_add_i32 s38, s12, s4
	s_ashr_i32 s9, s8, 6
	s_sext_i32_i16 s6, s6
	s_ashr_i32 s39, s38, 31
	s_ashr_i32 s10, s8, 8
	s_lshl_b32 s7, s9, 10
	s_lshr_b32 s6, s6, 3
	s_lshl_b64 s[4:5], s[38:39], 18
	s_add_u32 s40, s50, s4
	v_and_b32_e32 v3, 0xc0, v3
	s_addc_u32 s41, s51, s5
	s_bfe_i64 s[4:5], s[6:7], 0x100000
	v_sub_u32_e32 v0, v0, v3
	s_lshl_b64 s[4:5], s[4:5], 18
	v_lshlrev_b32_e32 v1, 5, v1
	v_ashrrev_i16_sdwa v0, v4, sext(v0) dst_sel:DWORD dst_unused:UNUSED_PAD src0_sel:DWORD src1_sel:BYTE_0
	v_lshlrev_b32_e32 v3, 1, v2
	v_lshrrev_b32_e32 v4, 2, v2
	s_add_u32 s42, s52, s4
	v_and_b32_e32 v1, 32, v1
	v_bfe_i32 v0, v0, 0, 16
	v_and_b32_e32 v3, 24, v3
	v_and_b32_e32 v4, 4, v4
	s_addc_u32 s43, s53, s5
	s_add_i32 s54, s7, 0
	v_or3_b32 v3, v5, v4, v3
	v_add_lshl_u32 v0, v1, v0, 1
	s_add_i32 s55, s54, 0x10000
	s_mov_b32 m0, s55
	s_nop 0
	global_load_lds_dwordx4 v148, s[42:43]
	v_lshl_add_u32 v150, v3, 10, v0
	s_add_i32 s56, s54, 0x12000
	s_mov_b32 m0, s56
	s_nop 0
	global_load_lds_dwordx4 v150, s[42:43]
	s_add_i32 s57, s54, 0x14000
	s_add_u32 s4, s42, 0x20000
	s_addc_u32 s5, s43, 0
	s_mov_b32 m0, s57
	s_nop 0
	global_load_lds_dwordx4 v148, s[4:5]
	s_add_i32 s58, s54, 0x16000
	s_mov_b32 m0, s58
	s_nop 0
	global_load_lds_dwordx4 v150, s[4:5]
	s_mov_b32 m0, s54
	s_nop 0
	global_load_lds_dwordx4 v147, s[40:41]
	s_add_i32 s59, s54, 0x2000
	s_add_i32 s60, s54, 0x4000
	v_lshl_add_u32 v149, v2, 10, v0
	s_mov_b32 m0, s59
	s_nop 0
	global_load_lds_dwordx4 v149, s[40:41]
	s_add_u32 s12, s40, 0x20000
	s_addc_u32 s13, s41, 0
	s_mov_b32 m0, s60
	s_nop 0
	global_load_lds_dwordx4 v147, s[12:13]
	s_add_i32 s61, s54, 0x6000
	s_mov_b32 m0, s61
	s_nop 0
	global_load_lds_dwordx4 v149, s[12:13]
	s_cmp_eq_u32 s10, 1
	s_mov_b32 s39, 0
	s_cselect_b64 s[4:5], -1, 0
	s_cmp_lg_u32 s10, 1
	s_cbranch_scc1 .LBB0_3274
	s_barrier
.LBB0_3274:
	s_sext_i32_i8 s79, s6
	s_add_u32 s6, s2, 0xaf200000
	s_addc_u32 s7, s3, 0
	s_add_u32 s62, s2, 0x162000
	s_addc_u32 s63, s3, 0
	v_and_b32_e32 v0, 48, v146
	v_lshlrev_b32_e32 v1, 6, v146
	s_movk_i32 s3, 0x3c0
	v_and_or_b32 v0, v1, s3, v0
	v_lshlrev_b32_e32 v1, 2, v146
	s_lshl_b32 s2, s10, 13
	v_and_b32_e32 v1, 32, v1
	v_bitop3_b32 v2, v0, s2, v1 bitop3:0xde
	s_lshl_b32 s2, s9, 5
	s_and_b32 s65, s2, 0x60
	s_lshl_b32 s64, s10, 6
	s_lshl_b32 s2, s65, 7
	s_add_i32 s66, s54, 0x18000
	v_bitop3_b32 v0, s2, v0, v1 bitop3:0xf6
	s_add_u32 s2, s42, 0x80
	s_waitcnt vmcnt(2)
	s_barrier
	s_addc_u32 s3, s43, 0
	s_mov_b32 m0, s66
	s_nop 0
	global_load_lds_dwordx4 v148, s[2:3]
	s_add_i32 s67, s54, 0x1a000
	s_add_i32 s68, s54, 0x8000
	s_mov_b32 m0, s67
	s_nop 0
	global_load_lds_dwordx4 v150, s[2:3]
	s_add_u32 s2, s40, 0x80
	s_addc_u32 s3, s41, 0
	s_mov_b32 m0, s68
	s_nop 0
	global_load_lds_dwordx4 v147, s[2:3]
	s_add_i32 s69, s54, 0xa000
	s_add_i32 s70, s54, 0x1c000
	s_mov_b32 m0, s69
	s_nop 0
	global_load_lds_dwordx4 v149, s[2:3]
	s_add_u32 s2, s42, 0x20080
	s_addc_u32 s3, s43, 0
	s_mov_b32 m0, s70
	s_nop 0
	global_load_lds_dwordx4 v148, s[2:3]
	s_add_i32 s71, s54, 0x1e000
	s_mov_b32 m0, s71
	s_nop 0
	global_load_lds_dwordx4 v150, s[2:3]
	s_waitcnt vmcnt(6)
	s_add_i32 s72, s54, 0xc000
	s_cmpk_lt_u32 s8, 0x100
	v_add_u32_e32 v0, 0, v0
	s_cselect_b64 s[8:9], -1, 0
	s_add_i32 s73, s54, 0xe000
	s_ashr_i32 s74, s48, 31
	v_mov_b64_e32 v[254:255], 0x200
	v_add_u32_e32 v151, 0x10000, v0
	v_add_u32_e32 v152, 0x14000, v0
	v_add_u32_e32 v153, 0, v2
	v_mov_b32_e32 v154, 0x7f7f7f7f
	v_add_u32_e32 v155, 0x18000, v0
	v_add_u32_e32 v156, 0x1c000, v0
	s_mov_b32 s10, 0x3a000000
	s_mov_b64 s[12:13], 0x40000
	s_mov_b32 s75, 0x40000
	s_mov_b64 s[14:15], 0x48000
	s_mov_b32 s76, 0x48000
	s_mov_b64 s[16:17], 0x50000
	s_mov_b32 s77, 0x50000
	s_mov_b64 s[20:21], 0x58000
	s_mov_b32 s78, 0x58000
	s_mov_b64 s[26:27], s[40:41]
	s_mov_b64 s[36:37], s[42:43]
	s_barrier
	s_branch .LBB0_3277

; #define PG8_WAIT_V(n) asm volatile("s_waitcnt vmcnt(" #n ")" ::: "memory")
; #define PG8_WAIT_L(n) asm volatile("s_waitcnt lgkmcnt(" #n ")" ::: "memory")
; #define PG8_BAR __builtin_amdgcn_s_barrier()
; #define PG8_SCHED __builtin_amdgcn_sched_barrier(0)
; #define PG8_STAGE_A(b, h, p) do { if constexpr (GATHER) { if ((h) == 0) PG8_STAGE(PG8_SA(b, h), p, vA0); else PG8_STAGE(PG8_SA(b, h), p, vA1); } else PG8_STAGE(PG8_SA(b, h), (p) + ((h) ? hstepA : (size_t)0), voffA); } while (0)
; #define PG8_GOFF1(un, h, d) do { int tz_ = tid; asm volatile("" : "+v"(tz_)); _Pragma("unroll") for (int i_ = 0; i_ < 2; ++i_) { int R_, C_; stage_rc(tz_ * 16 + i_ * 8192, R_, C_); \
;         d[i_] = S.gather(un, R_ + (h) * HALF) + (unsigned)C_ * 2u; } } while (0)
; template <class Epi, class Sched, bool ALIGN_EPI = true, bool SP2 = true, bool FP8 = false, bool GATHER = false>
; __device__ __forceinline__ void gemm_phase(LAS unsigned char* lds, const Dims g, const Sched& S, const Epi& E, const int wv) {
;     ...
;             PG8_LDB(B0, 0, 0); PG8_LDB(B1, 0, 1); PG8_SCHED; PG8_LDA(At, 0, 0); PG8_STAGE_A(1, 1, a1);
;             if constexpr (GATHER) { if (last) PG8_GOFF1(un_, 1, vA1); }
;             PG8_WAIT_V(8); PG8_WAIT_L(0); PG8_BAR; PG8_MMA(0, 0, At, B0); PG8_MMA(0, 1, At, B1); PG8_BAR; PG8_SCHED;
;             PG8_LDA(At, 0, 1); PG8_STAGE(PG8_SB(0, 0), b2, voffB); PG8_STAGE(PG8_SB(0, 1), b2 + hstepB, voffB); PG8_STAGE_A(0, 0, a2);
;             PG8_WAIT_V(8); PG8_WAIT_L(0); PG8_BAR; PG8_MMA(1, 0, At, B0); PG8_MMA(1, 1, At, B1); PG8_BAR; PG8_SCHED;
;             PG8_LDB(B0, 1, 0); PG8_LDB(B1, 1, 1); PG8_SCHED; PG8_LDA(At, 1, 0); PG8_STAGE_A(0, 1, a2);
;             PG8_WAIT_V(8); PG8_WAIT_L(0); PG8_BAR; PG8_MMA(0, 0, At, B0); PG8_MMA(0, 1, At, B1); PG8_BAR; PG8_SCHED;
;             PG8_LDA(At, 1, 1); PG8_STAGE(PG8_SB(1, 0), b3, voffB); PG8_STAGE(PG8_SB(1, 1), b3 + hstepB, voffB); PG8_STAGE_A(1, 0, a3);
;             PG8_WAIT_V(8); PG8_WAIT_L(0); PG8_BAR; PG8_MMA(1, 0, At, B0); PG8_MMA(1, 1, At, B1); PG8_BAR; PG8_SCHED;
.LBB0_3284:
	ds_read_b128 v[132:135], v151
	ds_read_b128 v[136:139], v151 offset:1024
	ds_read_b128 v[158:161], v151 offset:2048
	ds_read_b128 v[162:165], v151 offset:3072
	ds_read_b128 v[166:169], v152
	ds_read_b128 v[170:173], v152 offset:1024
	ds_read_b128 v[174:177], v152 offset:2048
	ds_read_b128 v[178:181], v152 offset:3072
	s_cmp_eq_u32 s82, 4
	s_cselect_b32 s46, s26, s80
	s_cselect_b32 s47, s27, s81
	s_cselect_b32 s44, s36, s23
	s_cselect_b32 s45, s37, s25
	s_add_u32 s42, s46, 0x80
	s_addc_u32 s43, s47, 0
	ds_read_b128 v[182:185], v153
	ds_read_b128 v[186:189], v153 offset:1024
	ds_read_b128 v[190:193], v153 offset:2048
	ds_read_b128 v[194:197], v153 offset:3072
	ds_read_b128 v[198:201], v153 offset:4096
	ds_read_b128 v[202:205], v153 offset:5120
	ds_read_b128 v[206:209], v153 offset:6144
	ds_read_b128 v[210:213], v153 offset:7168
	s_mov_b32 m0, s72
	s_nop 0
	global_load_lds_dwordx4 v147, s[40:41]
	s_nop 0
	s_mov_b32 m0, s73
	s_nop 0
	global_load_lds_dwordx4 v149, s[40:41]
	s_waitcnt vmcnt(8)
	s_waitcnt lgkmcnt(0)
	s_barrier
	s_setprio 1
	s_waitcnt lgkmcnt(6)
	v_mfma_scale_f32_16x16x128_f8f6f4 v[124:127], v[132:139], v[182:189], v[124:127], v154, v154 op_sel_hi:[0,0,0]
	v_mfma_scale_f32_16x16x128_f8f6f4 v[120:123], v[158:165], v[182:189], v[120:123], v154, v154 op_sel_hi:[0,0,0]
	s_waitcnt lgkmcnt(4)
	v_mfma_scale_f32_16x16x128_f8f6f4 v[116:119], v[132:139], v[190:197], v[116:119], v154, v154 op_sel_hi:[0,0,0]
	v_mfma_scale_f32_16x16x128_f8f6f4 v[104:107], v[158:165], v[190:197], v[104:107], v154, v154 op_sel_hi:[0,0,0]
	s_waitcnt lgkmcnt(2)
	v_mfma_scale_f32_16x16x128_f8f6f4 v[100:103], v[132:139], v[198:205], v[100:103], v154, v154 op_sel_hi:[0,0,0]
	v_mfma_scale_f32_16x16x128_f8f6f4 v[140:143], v[158:165], v[198:205], v[88:91], v154, v154 op_sel_hi:[0,0,0]
	s_waitcnt lgkmcnt(0)
	v_mfma_scale_f32_16x16x128_f8f6f4 v[214:217], v[132:139], v[206:213], v[84:87], v154, v154 op_sel_hi:[0,0,0]
	v_mfma_scale_f32_16x16x128_f8f6f4 v[218:221], v[158:165], v[206:213], v[72:75], v154, v154 op_sel_hi:[0,0,0]
	s_setprio 0
	s_setprio 1
	v_mfma_scale_f32_16x16x128_f8f6f4 v[112:115], v[166:173], v[182:189], v[112:115], v154, v154 op_sel_hi:[0,0,0]
	v_mfma_scale_f32_16x16x128_f8f6f4 v[108:111], v[174:181], v[182:189], v[108:111], v154, v154 op_sel_hi:[0,0,0]
	v_mfma_scale_f32_16x16x128_f8f6f4 v[96:99], v[166:173], v[190:197], v[96:99], v154, v154 op_sel_hi:[0,0,0]
	v_mfma_scale_f32_16x16x128_f8f6f4 v[182:185], v[174:181], v[190:197], v[92:95], v154, v154 op_sel_hi:[0,0,0]
	v_mfma_scale_f32_16x16x128_f8f6f4 v[186:189], v[166:173], v[198:205], v[80:83], v154, v154 op_sel_hi:[0,0,0]
	v_mfma_scale_f32_16x16x128_f8f6f4 v[190:193], v[174:181], v[198:205], v[76:79], v154, v154 op_sel_hi:[0,0,0]
	v_mfma_scale_f32_16x16x128_f8f6f4 v[194:197], v[166:173], v[206:213], v[68:71], v154, v154 op_sel_hi:[0,0,0]
	v_mfma_scale_f32_16x16x128_f8f6f4 v[198:201], v[174:181], v[206:213], v[64:67], v154, v154 op_sel_hi:[0,0,0]
	s_setprio 0
	s_barrier
	s_nop 4
	ds_read_b128 v[64:67], v153 offset:16384
	ds_read_b128 v[68:71], v153 offset:17408
	ds_read_b128 v[72:75], v153 offset:18432
	ds_read_b128 v[76:79], v153 offset:19456
	ds_read_b128 v[80:83], v153 offset:20480
	ds_read_b128 v[84:87], v153 offset:21504
	ds_read_b128 v[88:91], v153 offset:22528
	ds_read_b128 v[92:95], v153 offset:23552
	s_mov_b32 m0, s55
	s_nop 0
	global_load_lds_dwordx4 v148, s[44:45]
	s_add_u32 s84, s44, 0x20000
	s_mov_b32 m0, s56
	s_nop 0
	global_load_lds_dwordx4 v150, s[44:45]
	s_addc_u32 s85, s45, 0
	s_mov_b32 m0, s57
	s_nop 0
	global_load_lds_dwordx4 v148, s[84:85]
	s_nop 0
	s_mov_b32 m0, s58
	s_nop 0
	global_load_lds_dwordx4 v150, s[84:85]
	s_nop 0
	s_mov_b32 m0, s54
	s_nop 0
	global_load_lds_dwordx4 v147, s[46:47]
	s_nop 0
	s_mov_b32 m0, s59
	s_nop 0
	global_load_lds_dwordx4 v149, s[46:47]
	s_waitcnt vmcnt(8)
	s_waitcnt lgkmcnt(0)
	s_barrier
	s_setprio 1
	s_waitcnt lgkmcnt(6)
	v_mfma_scale_f32_16x16x128_f8f6f4 v[60:63], v[132:139], v[64:71], v[60:63], v154, v154 op_sel_hi:[0,0,0]
	v_mfma_scale_f32_16x16x128_f8f6f4 v[56:59], v[158:165], v[64:71], v[56:59], v154, v154 op_sel_hi:[0,0,0]
	s_waitcnt lgkmcnt(4)
	v_mfma_scale_f32_16x16x128_f8f6f4 v[48:51], v[132:139], v[72:79], v[48:51], v154, v154 op_sel_hi:[0,0,0]
	v_mfma_scale_f32_16x16x128_f8f6f4 v[202:205], v[158:165], v[72:79], v[40:43], v154, v154 op_sel_hi:[0,0,0]
	s_waitcnt lgkmcnt(2)
	v_mfma_scale_f32_16x16x128_f8f6f4 v[206:209], v[132:139], v[80:87], v[32:35], v154, v154 op_sel_hi:[0,0,0]
	v_mfma_scale_f32_16x16x128_f8f6f4 v[210:213], v[158:165], v[80:87], v[24:27], v154, v154 op_sel_hi:[0,0,0]
	s_waitcnt lgkmcnt(0)
	v_mfma_scale_f32_16x16x128_f8f6f4 v[222:225], v[132:139], v[88:95], v[16:19], v154, v154 op_sel_hi:[0,0,0]
	v_mfma_scale_f32_16x16x128_f8f6f4 v[226:229], v[158:165], v[88:95], v[8:11], v154, v154 op_sel_hi:[0,0,0]
	s_setprio 0
	s_setprio 1
	v_mfma_scale_f32_16x16x128_f8f6f4 v[52:55], v[166:173], v[64:71], v[52:55], v154, v154 op_sel_hi:[0,0,0]
	v_mfma_scale_f32_16x16x128_f8f6f4 v[230:233], v[174:181], v[64:71], v[44:47], v154, v154 op_sel_hi:[0,0,0]
	v_mfma_scale_f32_16x16x128_f8f6f4 v[234:237], v[166:173], v[72:79], v[36:39], v154, v154 op_sel_hi:[0,0,0]
	v_mfma_scale_f32_16x16x128_f8f6f4 v[238:241], v[174:181], v[72:79], v[28:31], v154, v154 op_sel_hi:[0,0,0]
	v_mfma_scale_f32_16x16x128_f8f6f4 v[242:245], v[166:173], v[80:87], v[20:23], v154, v154 op_sel_hi:[0,0,0]
	v_mfma_scale_f32_16x16x128_f8f6f4 v[246:249], v[174:181], v[80:87], v[12:15], v154, v154 op_sel_hi:[0,0,0]
	v_mfma_scale_f32_16x16x128_f8f6f4 v[250:253], v[166:173], v[88:95], v[4:7], v154, v154 op_sel_hi:[0,0,0]
	v_mfma_scale_f32_16x16x128_f8f6f4 v[128:131], v[174:181], v[88:95], v[0:3], v154, v154 op_sel_hi:[0,0,0]
	s_setprio 0
	s_barrier
; #define PG8_WAIT_V(n) asm volatile("s_waitcnt vmcnt(" #n ")" ::: "memory")
; #define PG8_WAIT_L(n) asm volatile("s_waitcnt lgkmcnt(" #n ")" ::: "memory")
; #define PG8_BAR __builtin_amdgcn_s_barrier()
; #define PG8_SCHED __builtin_amdgcn_sched_barrier(0)
; #define PG8_STAGE_A(b, h, p) do { if constexpr (GATHER) { if ((h) == 0) PG8_STAGE(PG8_SA(b, h), p, vA0); else PG8_STAGE(PG8_SA(b, h), p, vA1); } else PG8_STAGE(PG8_SA(b, h), (p) + ((h) ? hstepA : (size_t)0), voffA); } while (0)
; #define PG8_GOFF1(un, h, d) do { int tz_ = tid; asm volatile("" : "+v"(tz_)); _Pragma("unroll") for (int i_ = 0; i_ < 2; ++i_) { int R_, C_; stage_rc(tz_ * 16 + i_ * 8192, R_, C_); \
;         d[i_] = S.gather(un, R_ + (h) * HALF) + (unsigned)C_ * 2u; } } while (0)
; template <class Epi, class Sched, bool ALIGN_EPI = true, bool SP2 = true, bool FP8 = false, bool GATHER = false>
; __device__ __forceinline__ void gemm_phase(LAS unsigned char* lds, const Dims g, const Sched& S, const Epi& E, const int wv) {
;     ...
;             PG8_LDB(B0, 0, 0); PG8_LDB(B1, 0, 1); PG8_SCHED; PG8_LDA(At, 0, 0); PG8_STAGE_A(1, 1, a1);
;             if constexpr (GATHER) { if (last) PG8_GOFF1(un_, 1, vA1); }
;             PG8_WAIT_V(8); PG8_WAIT_L(0); PG8_BAR; PG8_MMA(0, 0, At, B0); PG8_MMA(0, 1, At, B1); PG8_BAR; PG8_SCHED;
;             PG8_LDA(At, 0, 1); PG8_STAGE(PG8_SB(0, 0), b2, voffB); PG8_STAGE(PG8_SB(0, 1), b2 + hstepB, voffB); PG8_STAGE_A(0, 0, a2);
;             PG8_WAIT_V(8); PG8_WAIT_L(0); PG8_BAR; PG8_MMA(1, 0, At, B0); PG8_MMA(1, 1, At, B1); PG8_BAR; PG8_SCHED;
;             PG8_LDB(B0, 1, 0); PG8_LDB(B1, 1, 1); PG8_SCHED; PG8_LDA(At, 1, 0); PG8_STAGE_A(0, 1, a2);
;             PG8_WAIT_V(8); PG8_WAIT_L(0); PG8_BAR; PG8_MMA(0, 0, At, B0); PG8_MMA(0, 1, At, B1); PG8_BAR; PG8_SCHED;
;             PG8_LDA(At, 1, 1); PG8_STAGE(PG8_SB(1, 0), b3, voffB); PG8_STAGE(PG8_SB(1, 1), b3 + hstepB, voffB); PG8_STAGE_A(1, 0, a3);
;             PG8_WAIT_V(8); PG8_WAIT_L(0); PG8_BAR; PG8_MMA(1, 0, At, B0); PG8_MMA(1, 1, At, B1); PG8_BAR; PG8_SCHED;
	s_nop 4
	ds_read_b128 v[0:3], v155
	ds_read_b128 v[4:7], v155 offset:1024
	ds_read_b128 v[8:11], v155 offset:2048
	ds_read_b128 v[12:15], v155 offset:3072
	ds_read_b128 v[132:135], v156
	ds_read_b128 v[136:139], v156 offset:1024
	ds_read_b128 v[158:161], v156 offset:2048
	ds_read_b128 v[162:165], v156 offset:3072
	ds_read_b128 v[16:19], v153 offset:32768
	ds_read_b128 v[20:23], v153 offset:33792
	ds_read_b128 v[24:27], v153 offset:34816
	ds_read_b128 v[28:31], v153 offset:35840
	ds_read_b128 v[32:35], v153 offset:36864
	ds_read_b128 v[36:39], v153 offset:37888
	ds_read_b128 v[40:43], v153 offset:38912
	ds_read_b128 v[44:47], v153 offset:39936
	s_add_u32 s46, s46, 0x20000
	s_addc_u32 s47, s47, 0
	s_mov_b32 m0, s60
	s_nop 0
	global_load_lds_dwordx4 v147, s[46:47]
	s_nop 0
	s_mov_b32 m0, s61
	s_nop 0
	global_load_lds_dwordx4 v149, s[46:47]
	s_waitcnt vmcnt(8)
	s_waitcnt lgkmcnt(0)
	s_barrier
	s_setprio 1
	s_waitcnt lgkmcnt(6)
	v_mfma_scale_f32_16x16x128_f8f6f4 v[124:127], v[0:7], v[16:23], v[124:127], v154, v154 op_sel_hi:[0,0,0]
	v_mfma_scale_f32_16x16x128_f8f6f4 v[120:123], v[8:15], v[16:23], v[120:123], v154, v154 op_sel_hi:[0,0,0]
	s_waitcnt lgkmcnt(4)
	v_mfma_scale_f32_16x16x128_f8f6f4 v[116:119], v[0:7], v[24:31], v[116:119], v154, v154 op_sel_hi:[0,0,0]
	v_mfma_scale_f32_16x16x128_f8f6f4 v[104:107], v[8:15], v[24:31], v[104:107], v154, v154 op_sel_hi:[0,0,0]
	s_waitcnt lgkmcnt(2)
	v_mfma_scale_f32_16x16x128_f8f6f4 v[100:103], v[0:7], v[32:39], v[100:103], v154, v154 op_sel_hi:[0,0,0]
	v_mfma_scale_f32_16x16x128_f8f6f4 v[88:91], v[8:15], v[32:39], v[140:143], v154, v154 op_sel_hi:[0,0,0]
	s_waitcnt lgkmcnt(0)
	v_mfma_scale_f32_16x16x128_f8f6f4 v[84:87], v[0:7], v[40:47], v[214:217], v154, v154 op_sel_hi:[0,0,0]
	v_mfma_scale_f32_16x16x128_f8f6f4 v[72:75], v[8:15], v[40:47], v[218:221], v154, v154 op_sel_hi:[0,0,0]
	s_setprio 0
	s_setprio 1
	v_mfma_scale_f32_16x16x128_f8f6f4 v[112:115], v[132:139], v[16:23], v[112:115], v154, v154 op_sel_hi:[0,0,0]
	v_mfma_scale_f32_16x16x128_f8f6f4 v[108:111], v[158:165], v[16:23], v[108:111], v154, v154 op_sel_hi:[0,0,0]
	v_mfma_scale_f32_16x16x128_f8f6f4 v[96:99], v[132:139], v[24:31], v[96:99], v154, v154 op_sel_hi:[0,0,0]
	v_mfma_scale_f32_16x16x128_f8f6f4 v[92:95], v[158:165], v[24:31], v[182:185], v154, v154 op_sel_hi:[0,0,0]
	v_mfma_scale_f32_16x16x128_f8f6f4 v[80:83], v[132:139], v[32:39], v[186:189], v154, v154 op_sel_hi:[0,0,0]
	v_mfma_scale_f32_16x16x128_f8f6f4 v[76:79], v[158:165], v[32:39], v[190:193], v154, v154 op_sel_hi:[0,0,0]
	v_mfma_scale_f32_16x16x128_f8f6f4 v[68:71], v[132:139], v[40:47], v[194:197], v154, v154 op_sel_hi:[0,0,0]
	v_mfma_scale_f32_16x16x128_f8f6f4 v[64:67], v[158:165], v[40:47], v[198:201], v154, v154 op_sel_hi:[0,0,0]
	s_setprio 0
	s_barrier
	ds_read_b128 v[166:169], v153 offset:49152
	ds_read_b128 v[170:173], v153 offset:50176
	ds_read_b128 v[174:177], v153 offset:51200
	ds_read_b128 v[178:181], v153 offset:52224
	ds_read_b128 v[182:185], v153 offset:53248
	ds_read_b128 v[186:189], v153 offset:54272
	ds_read_b128 v[190:193], v153 offset:55296
	ds_read_b128 v[194:197], v153 offset:56320
	s_add_u32 s46, s44, 0x80
	s_addc_u32 s47, s45, 0
	s_mov_b32 m0, s66
	s_nop 0
	global_load_lds_dwordx4 v148, s[46:47]
	s_add_u32 s44, s44, 0x20080
	s_mov_b32 m0, s67
	s_nop 0
	global_load_lds_dwordx4 v150, s[46:47]
	s_addc_u32 s45, s45, 0
	s_mov_b32 m0, s70
	s_nop 0
	global_load_lds_dwordx4 v148, s[44:45]
	s_nop 0
	s_mov_b32 m0, s71
	s_nop 0
	global_load_lds_dwordx4 v150, s[44:45]
	s_mov_b32 m0, s68
	s_nop 0
	global_load_lds_dwordx4 v147, s[42:43]
	s_nop 0
	s_mov_b32 m0, s69
	s_nop 0
	global_load_lds_dwordx4 v149, s[42:43]
	s_waitcnt vmcnt(8)
	s_waitcnt lgkmcnt(0)
	s_barrier
	s_setprio 1
	s_waitcnt lgkmcnt(6)
	v_mfma_scale_f32_16x16x128_f8f6f4 v[60:63], v[0:7], v[166:173], v[60:63], v154, v154 op_sel_hi:[0,0,0]
	v_mfma_scale_f32_16x16x128_f8f6f4 v[56:59], v[8:15], v[166:173], v[56:59], v154, v154 op_sel_hi:[0,0,0]
	s_waitcnt lgkmcnt(4)
	v_mfma_scale_f32_16x16x128_f8f6f4 v[48:51], v[0:7], v[174:181], v[48:51], v154, v154 op_sel_hi:[0,0,0]
	v_mfma_scale_f32_16x16x128_f8f6f4 v[40:43], v[8:15], v[174:181], v[202:205], v154, v154 op_sel_hi:[0,0,0]
	s_waitcnt lgkmcnt(2)
	v_mfma_scale_f32_16x16x128_f8f6f4 v[32:35], v[0:7], v[182:189], v[206:209], v154, v154 op_sel_hi:[0,0,0]
	v_mfma_scale_f32_16x16x128_f8f6f4 v[24:27], v[8:15], v[182:189], v[210:213], v154, v154 op_sel_hi:[0,0,0]
	s_waitcnt lgkmcnt(0)
	v_mfma_scale_f32_16x16x128_f8f6f4 v[16:19], v[0:7], v[190:197], v[222:225], v154, v154 op_sel_hi:[0,0,0]
	v_mfma_scale_f32_16x16x128_f8f6f4 v[8:11], v[8:15], v[190:197], v[226:229], v154, v154 op_sel_hi:[0,0,0]
	s_setprio 0
	s_setprio 1
	v_mfma_scale_f32_16x16x128_f8f6f4 v[52:55], v[132:139], v[166:173], v[52:55], v154, v154 op_sel_hi:[0,0,0]
	v_mfma_scale_f32_16x16x128_f8f6f4 v[44:47], v[158:165], v[166:173], v[230:233], v154, v154 op_sel_hi:[0,0,0]
	v_mfma_scale_f32_16x16x128_f8f6f4 v[36:39], v[132:139], v[174:181], v[234:237], v154, v154 op_sel_hi:[0,0,0]
	v_mfma_scale_f32_16x16x128_f8f6f4 v[28:31], v[158:165], v[174:181], v[238:241], v154, v154 op_sel_hi:[0,0,0]
	v_mfma_scale_f32_16x16x128_f8f6f4 v[20:23], v[132:139], v[182:189], v[242:245], v154, v154 op_sel_hi:[0,0,0]
	v_mfma_scale_f32_16x16x128_f8f6f4 v[12:15], v[158:165], v[182:189], v[246:249], v154, v154 op_sel_hi:[0,0,0]
	v_mfma_scale_f32_16x16x128_f8f6f4 v[4:7], v[132:139], v[190:197], v[250:253], v154, v154 op_sel_hi:[0,0,0]
	v_mfma_scale_f32_16x16x128_f8f6f4 v[0:3], v[158:165], v[190:197], v[128:131], v154, v154 op_sel_hi:[0,0,0]
	s_setprio 0
	s_barrier
	s_add_i32 s82, s82, 2
	s_add_u32 s23, s23, 0x100
	s_addc_u32 s25, s25, 0
	s_add_u32 s80, s80, 0x100
	s_addc_u32 s81, s81, 0
	s_add_u32 s40, s40, 0x100
	s_addc_u32 s41, s41, 0
	s_cmp_gt_u32 s82, 5
	s_cbranch_scc0 .LBB0_3284
	s_and_b64 vcc, exec, s[8:9]
	s_cbranch_vccz .LBB0_3287
	s_barrier

; #define PG8_WAIT_V(n) asm volatile("s_waitcnt vmcnt(" #n ")" ::: "memory")
; #define PG8_BAR __builtin_amdgcn_s_barrier()
; #define PG8_STAGE_A(b, h, p) do { if constexpr (GATHER) { if ((h) == 0) PG8_STAGE(PG8_SA(b, h), p, vA0); else PG8_STAGE(PG8_SA(b, h), p, vA1); } else PG8_STAGE(PG8_SA(b, h), (p) + ((h) ? hstepA : (size_t)0), voffA); } while (0)
; template <class Epi, class Sched, bool ALIGN_EPI = true, bool SP2 = true, bool FP8 = false, bool GATHER = false>
; __device__ __forceinline__ void gemm_phase(LAS unsigned char* lds, const Dims g, const Sched& S, const Epi& E, const int wv) {
;     ...
;     if constexpr (SP2) {
;         PG8_STAGE(PG8_SB(0, 0), cB, voffB); PG8_STAGE(PG8_SB(0, 1), cB + hstepB, voffB); PG8_STAGE_A(0, 0, cA); PG8_STAGE_A(0, 1, cA);
;         if (wr == 1) PG8_BAR;
;         PG8_WAIT_V(2); PG8_BAR;
;         PG8_STAGE(PG8_SB(1, 0), cB + kstep, voffB); PG8_STAGE_A(1, 0, cA + kstep); PG8_STAGE(PG8_SB(1, 1), cB + hstepB + kstep, voffB);
;         PG8_WAIT_V(6); PG8_BAR;
.LBB0_3892:
	s_add_u32 s12, s12, 0x8d200000
	s_addc_u32 s13, s13, 0
	s_add_u32 s61, s14, 0x80000
	s_addc_u32 s62, s15, 0
	v_and_b32_e32 v0, 48, v192
	v_lshlrev_b32_e32 v1, 6, v192
	s_movk_i32 s15, 0x3c0
	v_and_or_b32 v0, v1, s15, v0
	v_lshlrev_b32_e32 v1, 2, v192
	s_lshl_b32 s14, s16, 13
	v_and_b32_e32 v1, 32, v1
	v_bitop3_b32 v2, v0, s14, v1 bitop3:0xde
	s_lshl_b32 s14, s17, 5
	s_and_b32 s64, s14, 0x60
	s_lshl_b32 s63, s16, 6
	s_lshl_b32 s14, s64, 7
	s_add_i32 s65, s27, 0x18000
	v_bitop3_b32 v0, s14, v0, v1 bitop3:0xf6
	s_add_u32 s14, s40, 0x80
	s_waitcnt vmcnt(2)
	s_barrier
	s_addc_u32 s15, s41, 0
	s_mov_b32 m0, s65
	s_nop 0
	global_load_lds_dwordx4 v195, s[14:15]
	s_add_i32 s66, s27, 0x1a000
	s_add_i32 s67, s27, 0x8000
	s_mov_b32 m0, s66
	s_nop 0
	global_load_lds_dwordx4 v199, s[14:15]
	s_add_u32 s14, s38, 0x80
	s_addc_u32 s15, s39, 0
	s_mov_b32 m0, s67
	s_nop 0
	global_load_lds_dwordx4 v194, s[14:15]
	s_add_i32 s68, s27, 0xa000
	s_add_i32 s69, s27, 0x1c000
	s_mov_b32 m0, s68
	s_nop 0
	global_load_lds_dwordx4 v196, s[14:15]
	s_add_u32 s14, s40, 0x20080
	s_addc_u32 s15, s41, 0
	s_mov_b32 m0, s69
	s_nop 0
	global_load_lds_dwordx4 v195, s[14:15]
	s_add_i32 s70, s27, 0x1e000
	s_mov_b32 m0, s70
	s_nop 0
	global_load_lds_dwordx4 v199, s[14:15]
	s_waitcnt vmcnt(6)
	s_add_i32 s71, s27, 0xc000
	s_cmpk_lt_u32 s23, 0x100
	s_cselect_b64 s[14:15], -1, 0
	s_add_i32 s72, s27, 0xe000
	v_mov_b32_e32 v200, 0x7f7f7f7f
	s_mov_b64 s[16:17], 0x1000
	s_movk_i32 s73, 0x1000
	s_mov_b32 s74, 0xc0e00000
	v_add_u32_e32 v201, 0, v0
	v_add_u32_e32 v202, 0, v2
	v_mov_b32_e32 v203, 0x40e00000
	s_barrier
	s_branch .LBB0_3895

; #define PG8_WAIT_V(n) asm volatile("s_waitcnt vmcnt(" #n ")" ::: "memory")
; #define PG8_BAR __builtin_amdgcn_s_barrier()
; #define PG8_STAGE_A(b, h, p) do { if constexpr (GATHER) { if ((h) == 0) PG8_STAGE(PG8_SA(b, h), p, vA0); else PG8_STAGE(PG8_SA(b, h), p, vA1); } else PG8_STAGE(PG8_SA(b, h), (p) + ((h) ? hstepA : (size_t)0), voffA); } while (0)
; template <class Epi, class Sched, bool ALIGN_EPI = true, bool SP2 = true, bool FP8 = false, bool GATHER = false>
; __device__ __forceinline__ void gemm_phase(LAS unsigned char* lds, const Dims g, const Sched& S, const Epi& E, const int wv) {
;     ...
;     for (int i = 0; i < 2; ++i) { int R, C; stage_rc(tid * 16 + i * 8192, R, C); const int Rb = Epi::PERM ? ((R & ~31) + perm32(R & 31)) : R;
;         voffA[i] = (unsigned)(R * g.lda + C) * 2u; voffB[i] = (unsigned)(Rb * g.ldb + C) * 2u; }
;     const size_t kstep = (size_t)(BK * 2);
;     const size_t hstepA = (size_t)HALF * g.lda * 2, hstepB = (size_t)HALF * g.ldb * 2;
;     const unsigned ldsw = (unsigned)wid * 1024u, ldsb_ = (unsigned)(uintptr_t)lds;
;     const int aoff = lds_byte(wr * 64 + fr, fq * 8), boff = lds_byte(wc * 32 + fr, fq * 8);
;     ...
;     if constexpr (SP2) {
;         PG8_STAGE(PG8_SB(0, 0), cB, voffB); PG8_STAGE(PG8_SB(0, 1), cB + hstepB, voffB); PG8_STAGE_A(0, 0, cA); PG8_STAGE_A(0, 1, cA);
;         if (wr == 1) PG8_BAR;
;         PG8_WAIT_V(2); PG8_BAR;
;         PG8_STAGE(PG8_SB(1, 0), cB + kstep, voffB); PG8_STAGE_A(1, 0, cA + kstep); PG8_STAGE(PG8_SB(1, 1), cB + hstepB + kstep, voffB);
;         PG8_WAIT_V(6); PG8_BAR;
.LBB0_3992:
	v_bfe_i32 v2, v152, 27, 1
	s_add_u32 s55, s14, 0x8d200000
	v_lshlrev_b32_e32 v0, 4, v152
	v_lshrrev_b32_e32 v2, 22, v2
	s_addc_u32 s56, s15, 0
	v_add_u32_e32 v2, v0, v2
	s_add_u32 s57, s14, 0x2a000000
	v_and_b32_e32 v2, 0xfffffc00, v2
	s_addc_u32 s58, s15, 0
	s_ashr_i32 s37, s36, 31
	v_sub_u32_e32 v2, v0, v2
	s_lshl_b64 s[6:7], s[36:37], 18
	v_ashrrev_i32_e32 v1, 31, v152
	v_lshrrev_b32_e32 v3, 4, v2
	s_add_u32 s42, s55, s6
	v_lshrrev_b32_e32 v1, 26, v1
	v_bitop3_b32 v2, v3, v2, 32 bitop3:0x6c
	s_addc_u32 s43, s56, s7
	s_ashr_i32 s41, s40, 31
	v_add_u32_e32 v1, v152, v1
	v_ashrrev_i32_e32 v4, 31, v2
	s_lshl_b64 s[6:7], s[40:41], 20
	v_ashrrev_i32_e32 v1, 6, v1
	v_lshrrev_b32_e32 v4, 26, v4
	s_add_u32 s8, s57, s6
	v_lshlrev_b32_e32 v3, 3, v1
	v_add_u32_e32 v4, v2, v4
	s_addc_u32 s9, s58, s7
	s_ashr_i32 s39, s38, 31
	v_and_b32_e32 v3, -16, v3
	v_ashrrev_i32_e32 v5, 6, v4
	v_and_b32_e32 v4, 0xc0, v4
	s_lshl_b64 s[6:7], s[38:39], 18
	v_add_u32_e32 v3, v5, v3
	v_sub_u32_e32 v2, v2, v4
	v_mov_b32_e32 v4, 1
	s_add_u32 s44, s8, s6
	v_lshlrev_b32_e32 v1, 5, v1
	v_ashrrev_i16_sdwa v2, v4, sext(v2) dst_sel:DWORD dst_unused:UNUSED_PAD src0_sel:DWORD src1_sel:BYTE_0
	v_lshlrev_b32_e32 v6, 1, v3
	v_lshrrev_b32_e32 v7, 2, v3
	v_and_b32_e32 v5, 3, v5
	s_mov_b32 s6, 0x3fffe0
	v_and_b32_e32 v1, 32, v1
	v_bfe_i32 v2, v2, 0, 16
	v_and_b32_e32 v6, 24, v6
	v_and_b32_e32 v7, 4, v7
	v_and_or_b32 v5, v3, s6, v5
	v_or3_b32 v5, v5, v7, v6
	v_add_lshl_u32 v1, v1, v2, 1
	v_add_u32_e32 v0, 0x2000, v0
	v_lshl_add_u32 v153, v3, 10, v1
	v_lshl_add_u32 v154, v5, 10, v1
	v_ashrrev_i32_e32 v1, 31, v0
	v_lshrrev_b32_e32 v1, 22, v1
	v_add_u32_e32 v1, v0, v1
	v_ashrrev_i32_e32 v1, 10, v1
	v_mul_i32_i24_e32 v2, 0x400, v1
	v_sub_u32_e32 v0, v0, v2
	v_lshrrev_b32_e32 v2, 4, v0
	v_bitop3_b32 v0, v2, v0, 32 bitop3:0x6c
	v_ashrrev_i32_e32 v3, 31, v0
	v_lshrrev_b32_e32 v3, 26, v3
	v_lshlrev_b32_e32 v2, 3, v1
	v_add_u32_e32 v3, v0, v3
	v_and_b32_e32 v2, -16, v2
	v_ashrrev_i32_e32 v5, 6, v3
	v_and_b32_e32 v3, 0xc0, v3
	s_addc_u32 s45, s9, s7
	v_add_u32_e32 v2, v5, v2
	v_sub_u32_e32 v0, v0, v3
	v_and_b32_e32 v5, 3, v5
	s_ashr_i32 s13, s3, 6
	v_lshlrev_b32_e32 v1, 5, v1
	v_ashrrev_i16_sdwa v0, v4, sext(v0) dst_sel:DWORD dst_unused:UNUSED_PAD src0_sel:DWORD src1_sel:BYTE_0
	v_lshlrev_b32_e32 v3, 1, v2
	v_lshrrev_b32_e32 v4, 2, v2
	v_and_or_b32 v5, v2, s6, v5
	s_lshl_b32 s6, s13, 10
	v_and_b32_e32 v1, 32, v1
	v_bfe_i32 v0, v0, 0, 16
	v_and_b32_e32 v3, 24, v3
	v_and_b32_e32 v4, 4, v4
	s_add_i32 s59, s6, 0
	v_or3_b32 v3, v5, v4, v3
	v_add_lshl_u32 v0, v1, v0, 1
	s_add_i32 s60, s59, 0x10000
	s_mov_b32 m0, s60
	s_nop 0
	global_load_lds_dwordx4 v154, s[44:45]
	s_ashr_i32 s12, s3, 8
	v_lshl_add_u32 v156, v3, 10, v0
	s_add_i32 s61, s59, 0x12000
	s_mov_b32 m0, s61
	s_nop 0
	global_load_lds_dwordx4 v156, s[44:45]
	s_add_i32 s62, s59, 0x14000
	s_add_u32 s6, s44, 0x20000
	s_addc_u32 s7, s45, 0
	s_mov_b32 m0, s62
	s_nop 0
	global_load_lds_dwordx4 v154, s[6:7]
	s_add_i32 s63, s59, 0x16000
	s_mov_b32 m0, s63
	s_nop 0
	global_load_lds_dwordx4 v156, s[6:7]
	s_mov_b32 m0, s59
	s_nop 0
	global_load_lds_dwordx4 v153, s[42:43]
	s_add_i32 s64, s59, 0x2000
	s_add_i32 s65, s59, 0x4000
	v_lshl_add_u32 v155, v2, 10, v0
	s_mov_b32 m0, s64
	s_nop 0
	global_load_lds_dwordx4 v155, s[42:43]
	s_add_u32 s8, s42, 0x20000
	s_addc_u32 s9, s43, 0
	s_mov_b32 m0, s65
	s_nop 0
	global_load_lds_dwordx4 v153, s[8:9]
	s_add_i32 s66, s59, 0x6000
	s_mov_b32 m0, s66
	s_nop 0
	global_load_lds_dwordx4 v155, s[8:9]
	s_cmp_eq_u32 s12, 1
	s_mov_b32 s39, 0
	s_cselect_b64 s[6:7], -1, 0
	s_cmp_lg_u32 s12, 1
	s_cbranch_scc1 .LBB0_3994
	s_barrier
.LBB0_3994:
	s_add_u32 s8, s14, 0x9e200000
	s_addc_u32 s9, s15, 0
	s_waitcnt lgkmcnt(0)
	s_add_u32 s67, s10, 0x40000
	s_addc_u32 s68, s11, 0
	s_lshl_b32 s10, s12, 6
	v_and_b32_e32 v0, 48, v152
	s_lshl_b32 s11, s12, 13
	v_lshlrev_b32_e32 v1, 6, v152
	s_movk_i32 s12, 0x3c0
	v_and_or_b32 v0, v1, s12, v0
	v_lshlrev_b32_e32 v1, 2, v152
	v_and_b32_e32 v1, 32, v1
	v_bitop3_b32 v2, v0, s11, v1 bitop3:0xde
	s_lshl_b32 s11, s13, 5
	s_and_b32 s69, s11, 0x60
	s_lshl_b32 s11, s69, 7
	s_add_i32 s70, s59, 0x18000
	s_add_u32 s12, s44, 0x80
	v_bitop3_b32 v0, s11, v0, v1 bitop3:0xf6
	s_waitcnt vmcnt(2)
	s_barrier
	s_addc_u32 s13, s45, 0
	s_mov_b32 m0, s70
	s_nop 0
	global_load_lds_dwordx4 v154, s[12:13]
	s_add_i32 s71, s59, 0x1a000
	s_add_i32 s72, s59, 0x8000
	s_mov_b32 m0, s71
	s_nop 0
	global_load_lds_dwordx4 v156, s[12:13]
	s_add_u32 s12, s42, 0x80
	s_addc_u32 s13, s43, 0
	s_mov_b32 m0, s72
	s_nop 0
	global_load_lds_dwordx4 v153, s[12:13]
	s_add_i32 s73, s59, 0xa000
	s_add_i32 s74, s59, 0x1c000
	s_mov_b32 m0, s73
	s_nop 0
	global_load_lds_dwordx4 v155, s[12:13]
	s_add_u32 s12, s44, 0x20080
	s_addc_u32 s13, s45, 0
	s_mov_b32 m0, s74
	s_nop 0
	global_load_lds_dwordx4 v154, s[12:13]
	s_add_i32 s75, s59, 0x1e000
	s_add_i32 s76, s59, 0xc000
	s_mov_b32 m0, s75
	s_nop 0
	global_load_lds_dwordx4 v156, s[12:13]
	s_cmpk_lt_u32 s3, 0x100
	s_cselect_b64 s[12:13], -1, 0
	s_ashr_i32 s11, s10, 31
	s_add_i32 s77, s59, 0xe000
	s_lshl_b64 s[20:21], s[10:11], 2
	s_add_u32 s3, s14, s20
	s_addc_u32 s14, s15, s21
	s_add_u32 s11, s3, 0x7c100000
	s_waitcnt vmcnt(6)
	s_addc_u32 s15, s14, 0
	s_lshl_b32 s14, s33, 3
	s_and_b32 s14, s14, 56
	s_bfe_u32 s16, s33, 0x30003
	v_add_u32_e32 v0, 0, v0
	s_ashr_i32 s78, s54, 31
	s_ashr_i32 s79, s33, 31
	s_ashr_i32 s3, s2, 31
	s_or_b32 s80, s16, s14
	s_ashr_i32 s81, s33, 6
	v_add_u32_e32 v157, 0x10000, v0
	v_add_u32_e32 v158, 0x14000, v0
	v_add_u32_e32 v159, 0, v2
	v_mov_b32_e32 v160, 0x7f7f7f7f
	v_add_u32_e32 v161, 0x18000, v0
	v_add_u32_e32 v162, 0x1c000, v0
	s_mov_b32 s14, 0x42000000
	s_mov_b32 s16, 0x3b000000
	s_mov_b32 s82, 0xc3e00000
	v_mov_b32_e32 v163, 0x43e00000
	s_barrier
	s_branch .LBB0_3997

; #define PG8_WAIT_V(n) asm volatile("s_waitcnt vmcnt(" #n ")" ::: "memory")
; #define PG8_BAR __builtin_amdgcn_s_barrier()
; #define PG8_STAGE_A(b, h, p) do { if constexpr (GATHER) { if ((h) == 0) PG8_STAGE(PG8_SA(b, h), p, vA0); else PG8_STAGE(PG8_SA(b, h), p, vA1); } else PG8_STAGE(PG8_SA(b, h), (p) + ((h) ? hstepA : (size_t)0), voffA); } while (0)
; template <class Epi, class Sched, bool ALIGN_EPI = true, bool SP2 = true, bool FP8 = false, bool GATHER = false>
; __device__ __forceinline__ void gemm_phase(LAS unsigned char* lds, const Dims g, const Sched& S, const Epi& E, const int wv) {
;     ...
;     for (int i = 0; i < 2; ++i) { int R, C; stage_rc(tid * 16 + i * 8192, R, C); const int Rb = Epi::PERM ? ((R & ~31) + perm32(R & 31)) : R;
;         voffA[i] = (unsigned)(R * g.lda + C) * 2u; voffB[i] = (unsigned)(Rb * g.ldb + C) * 2u; }
;     const size_t kstep = (size_t)(BK * 2);
;     const size_t hstepA = (size_t)HALF * g.lda * 2, hstepB = (size_t)HALF * g.ldb * 2;
;     const unsigned ldsw = (unsigned)wid * 1024u, ldsb_ = (unsigned)(uintptr_t)lds;
;     const int aoff = lds_byte(wr * 64 + fr, fq * 8), boff = lds_byte(wc * 32 + fr, fq * 8);
;     ...
;     if constexpr (SP2) {
;         PG8_STAGE(PG8_SB(0, 0), cB, voffB); PG8_STAGE(PG8_SB(0, 1), cB + hstepB, voffB); PG8_STAGE_A(0, 0, cA); PG8_STAGE_A(0, 1, cA);
;         if (wr == 1) PG8_BAR;
;         PG8_WAIT_V(2); PG8_BAR;
;         PG8_STAGE(PG8_SB(1, 0), cB + kstep, voffB); PG8_STAGE_A(1, 0, cA + kstep); PG8_STAGE(PG8_SB(1, 1), cB + hstepB + kstep, voffB);
;         PG8_WAIT_V(6); PG8_BAR;
.LBB0_4376:
	v_bfe_i32 v2, v146, 27, 1
	v_lshlrev_b32_e32 v0, 4, v146
	v_lshrrev_b32_e32 v2, 22, v2
	v_add_u32_e32 v2, v0, v2
	v_and_b32_e32 v2, 0xfffffc00, v2
	v_sub_u32_e32 v2, v0, v2
	v_ashrrev_i32_e32 v1, 31, v146
	v_lshrrev_b32_e32 v3, 4, v2
	v_lshrrev_b32_e32 v1, 26, v1
	v_bitop3_b32 v2, v3, v2, 32 bitop3:0x6c
	v_add_u32_e32 v1, v146, v1
	v_ashrrev_i32_e32 v4, 31, v2
	v_ashrrev_i32_e32 v1, 6, v1
	v_lshrrev_b32_e32 v4, 26, v4
	v_lshlrev_b32_e32 v3, 3, v1
	v_add_u32_e32 v4, v2, v4
	v_and_b32_e32 v3, -16, v3
	v_ashrrev_i32_e32 v5, 6, v4
	v_and_b32_e32 v4, 0xc0, v4
	v_add_u32_e32 v3, v5, v3
	v_sub_u32_e32 v2, v2, v4
	v_mov_b32_e32 v4, 1
	v_lshlrev_b32_e32 v1, 5, v1
	v_ashrrev_i16_sdwa v2, v4, sext(v2) dst_sel:DWORD dst_unused:UNUSED_PAD src0_sel:DWORD src1_sel:BYTE_0
	v_lshlrev_b32_e32 v6, 1, v3
	v_lshrrev_b32_e32 v7, 2, v3
	v_and_b32_e32 v5, 3, v5
	s_mov_b32 s5, 0x1fffe0
	v_and_b32_e32 v1, 32, v1
	v_bfe_i32 v2, v2, 0, 16
	v_and_b32_e32 v6, 24, v6
	v_and_b32_e32 v7, 4, v7
	v_and_or_b32 v5, v3, s5, v5
	v_or3_b32 v5, v5, v7, v6
	v_add_lshl_u32 v1, v1, v2, 1
	v_add_u32_e32 v0, 0x2000, v0
	v_lshl_add_u32 v147, v3, 11, v1
	v_lshl_add_u32 v148, v5, 11, v1
	v_ashrrev_i32_e32 v1, 31, v0
	v_lshrrev_b32_e32 v1, 22, v1
	v_add_u32_e32 v1, v0, v1
	v_ashrrev_i32_e32 v1, 10, v1
	v_mul_i32_i24_e32 v2, 0x400, v1
	v_sub_u32_e32 v0, v0, v2
	v_lshrrev_b32_e32 v2, 4, v0
	v_bitop3_b32 v0, v2, v0, 32 bitop3:0x6c
	v_ashrrev_i32_e32 v3, 31, v0
	s_add_u32 s50, s2, 0x72000000
	v_lshrrev_b32_e32 v3, 26, v3
	s_addc_u32 s51, s3, 0
	v_lshlrev_b32_e32 v2, 3, v1
	v_add_u32_e32 v3, v0, v3
	s_add_u32 s52, s2, 0x5a00000
	v_and_b32_e32 v2, -16, v2
	v_ashrrev_i32_e32 v5, 6, v3
	s_addc_u32 s53, s3, 0
	v_add_u32_e32 v2, v5, v2
	v_and_b32_e32 v5, 3, v5
	s_add_i32 s4, s6, s4
	v_and_or_b32 v5, v2, s5, v5
	s_ashr_i32 s5, s4, 31
	s_lshr_b32 s5, s5, 27
	s_add_i32 s5, s4, s5
	s_ashr_i32 s6, s5, 5
	s_and_b32 s5, s5, 0xffe0
	s_sub_i32 s4, s4, s5
	s_bfe_i32 s5, s4, 0x80000
	s_bfe_u32 s5, s5, 0x3000c
	s_add_i32 s5, s4, s5
	s_bfe_i32 s8, s5, 0x80000
	s_and_b32 s5, s5, 0xf8
	s_sub_i32 s4, s4, s5
	s_lshl_b32 s6, s6, 3
	s_sext_i32_i8 s4, s4
	s_add_i32 s38, s6, s4
	s_ashr_i32 s11, s10, 6
	s_sext_i32_i16 s8, s8
	s_ashr_i32 s39, s38, 31
	s_ashr_i32 s12, s10, 8
	s_lshl_b32 s7, s11, 10
	s_lshr_b32 s8, s8, 3
	s_lshl_b64 s[4:5], s[38:39], 19
	s_add_u32 s40, s50, s4
	v_and_b32_e32 v3, 0xc0, v3
	s_addc_u32 s41, s51, s5
	s_bfe_i64 s[4:5], s[8:9], 0x100000
	v_sub_u32_e32 v0, v0, v3
	s_lshl_b64 s[4:5], s[4:5], 19
	v_lshlrev_b32_e32 v1, 5, v1
	v_ashrrev_i16_sdwa v0, v4, sext(v0) dst_sel:DWORD dst_unused:UNUSED_PAD src0_sel:DWORD src1_sel:BYTE_0
	v_lshlrev_b32_e32 v3, 1, v2
	v_lshrrev_b32_e32 v4, 2, v2
	s_add_u32 s42, s52, s4
	v_and_b32_e32 v1, 32, v1
	v_bfe_i32 v0, v0, 0, 16
	v_and_b32_e32 v3, 24, v3
	v_and_b32_e32 v4, 4, v4
	s_addc_u32 s43, s53, s5
	s_add_i32 s54, s7, 0
	v_or3_b32 v3, v5, v4, v3
	v_add_lshl_u32 v0, v1, v0, 1
	s_add_i32 s55, s54, 0x10000
	s_mov_b32 m0, s55
	s_nop 0
	global_load_lds_dwordx4 v148, s[42:43]
	s_add_i32 s56, s54, 0x12000
	s_add_i32 s57, s54, 0x14000
	v_lshl_add_u32 v150, v3, 11, v0
	s_mov_b32 m0, s56
	s_nop 0
	global_load_lds_dwordx4 v150, s[42:43]
	s_add_u32 s6, s42, 0x40000
	s_addc_u32 s7, s43, 0
	s_mov_b32 m0, s57
	s_nop 0
	global_load_lds_dwordx4 v148, s[6:7]
	s_add_i32 s58, s54, 0x16000
	s_mov_b32 m0, s58
	s_nop 0
	global_load_lds_dwordx4 v150, s[6:7]
	s_mov_b32 m0, s54
	s_nop 0
	global_load_lds_dwordx4 v147, s[40:41]
	s_add_i32 s59, s54, 0x2000
	s_add_i32 s60, s54, 0x4000
	v_lshl_add_u32 v149, v2, 11, v0
	s_mov_b32 m0, s59
	s_nop 0
	global_load_lds_dwordx4 v149, s[40:41]
	s_add_u32 s14, s40, 0x40000
	s_addc_u32 s15, s41, 0
	s_mov_b32 m0, s60
	s_nop 0
	global_load_lds_dwordx4 v147, s[14:15]
	s_add_i32 s61, s54, 0x6000
	s_mov_b32 m0, s61
	s_nop 0
	global_load_lds_dwordx4 v149, s[14:15]
	s_cmp_eq_u32 s12, 1
	s_mov_b32 s39, 0
	s_mov_b64 s[4:5], 0x40000
	s_cselect_b64 s[6:7], -1, 0
	s_cmp_lg_u32 s12, 1
	s_cbranch_scc1 .LBB0_4378
	s_barrier
.LBB0_4378:
	s_sext_i32_i8 s79, s8
	s_add_u32 s8, s2, 0xaf200000
	s_addc_u32 s9, s3, 0
	s_add_u32 s62, s2, 0x192000
	s_addc_u32 s63, s3, 0
	v_and_b32_e32 v0, 48, v146
	v_lshlrev_b32_e32 v1, 6, v146
	s_movk_i32 s3, 0x3c0
	v_and_or_b32 v0, v1, s3, v0
	v_lshlrev_b32_e32 v1, 2, v146
	s_lshl_b32 s2, s12, 13
	v_and_b32_e32 v1, 32, v1
	v_bitop3_b32 v2, v0, s2, v1 bitop3:0xde
	s_lshl_b32 s2, s11, 5
	s_and_b32 s65, s2, 0x60
	s_lshl_b32 s64, s12, 6
	s_lshl_b32 s2, s65, 7
	s_add_i32 s66, s54, 0x18000
	v_bitop3_b32 v0, s2, v0, v1 bitop3:0xf6
	s_add_u32 s2, s42, 0x80
	s_waitcnt vmcnt(2)
	s_barrier
	s_addc_u32 s3, s43, 0
	s_mov_b32 m0, s66
	s_nop 0
	global_load_lds_dwordx4 v148, s[2:3]
	s_add_i32 s67, s54, 0x1a000
	s_add_i32 s68, s54, 0x8000
	s_mov_b32 m0, s67
	s_nop 0
	global_load_lds_dwordx4 v150, s[2:3]
	s_add_u32 s2, s40, 0x80
	s_addc_u32 s3, s41, 0
	s_mov_b32 m0, s68
	s_nop 0
	global_load_lds_dwordx4 v147, s[2:3]
	s_add_i32 s69, s54, 0xa000
	s_add_i32 s70, s54, 0x1c000
	s_mov_b32 m0, s69
	s_nop 0
	global_load_lds_dwordx4 v149, s[2:3]
	s_add_u32 s2, s42, 0x40080
	s_addc_u32 s3, s43, 0
	s_mov_b32 m0, s70
	s_nop 0
	global_load_lds_dwordx4 v148, s[2:3]
	s_add_i32 s71, s54, 0x1e000
	s_mov_b32 m0, s71
	s_nop 0
	global_load_lds_dwordx4 v150, s[2:3]
	s_waitcnt vmcnt(6)
	s_add_i32 s72, s54, 0xc000
	s_cmpk_lt_u32 s10, 0x100
	v_add_u32_e32 v0, 0, v0
	s_cselect_b64 s[10:11], -1, 0
	s_add_i32 s73, s54, 0xe000
	s_ashr_i32 s74, s48, 31
	v_mov_b64_e32 v[254:255], 0x200
	v_add_u32_e32 v151, 0x10000, v0
	v_add_u32_e32 v152, 0x14000, v0
	v_add_u32_e32 v153, 0, v2
	v_mov_b32_e32 v154, 0x7f7f7f7f
	v_add_u32_e32 v155, 0x18000, v0
	v_add_u32_e32 v156, 0x1c000, v0
	s_mov_b32 s12, 0x3a000000
	s_mov_b32 s75, 0x40000
	s_mov_b64 s[14:15], 0x48000
	s_mov_b32 s76, 0x48000
	s_mov_b64 s[16:17], 0x50000
	s_mov_b32 s77, 0x50000
	s_mov_b64 s[20:21], 0x58000
	s_mov_b32 s78, 0x58000
	s_mov_b64 s[26:27], s[40:41]
	s_mov_b64 s[36:37], s[42:43]
	s_barrier
	s_branch .LBB0_4381

; #define PG8_WAIT_V(n) asm volatile("s_waitcnt vmcnt(" #n ")" ::: "memory")
; #define PG8_BAR __builtin_amdgcn_s_barrier()
; #define PG8_STAGE_A(b, h, p) do { if constexpr (GATHER) { if ((h) == 0) PG8_STAGE(PG8_SA(b, h), p, vA0); else PG8_STAGE(PG8_SA(b, h), p, vA1); } else PG8_STAGE(PG8_SA(b, h), (p) + ((h) ? hstepA : (size_t)0), voffA); } while (0)
; template <class Epi, class Sched, bool ALIGN_EPI = true, bool SP2 = true, bool FP8 = false, bool GATHER = false>
; __device__ __forceinline__ void gemm_phase(LAS unsigned char* lds, const Dims g, const Sched& S, const Epi& E, const int wv) {
;     ...
;     if constexpr (SP2) {
;         PG8_STAGE(PG8_SB(0, 0), cB, voffB); PG8_STAGE(PG8_SB(0, 1), cB + hstepB, voffB); PG8_STAGE_A(0, 0, cA); PG8_STAGE_A(0, 1, cA);
;         if (wr == 1) PG8_BAR;
;         PG8_WAIT_V(2); PG8_BAR;
;         PG8_STAGE(PG8_SB(1, 0), cB + kstep, voffB); PG8_STAGE_A(1, 0, cA + kstep); PG8_STAGE(PG8_SB(1, 1), cB + hstepB + kstep, voffB);
;         PG8_WAIT_V(6); PG8_BAR;
.LBB0_4996:
	s_add_u32 s12, s12, 0x8d200000
	s_addc_u32 s13, s13, 0
	s_add_u32 s61, s14, 0xc0000
	s_addc_u32 s62, s15, 0
	v_and_b32_e32 v0, 48, v192
	v_lshlrev_b32_e32 v1, 6, v192
	s_movk_i32 s15, 0x3c0
	v_and_or_b32 v0, v1, s15, v0
	v_lshlrev_b32_e32 v1, 2, v192
	s_lshl_b32 s14, s16, 13
	v_and_b32_e32 v1, 32, v1
	v_bitop3_b32 v2, v0, s14, v1 bitop3:0xde
	s_lshl_b32 s14, s17, 5
	s_and_b32 s64, s14, 0x60
	s_lshl_b32 s63, s16, 6
	s_lshl_b32 s14, s64, 7
	s_add_i32 s65, s27, 0x18000
	v_bitop3_b32 v0, s14, v0, v1 bitop3:0xf6
	s_add_u32 s14, s40, 0x80
	s_waitcnt vmcnt(2)
	s_barrier
	s_addc_u32 s15, s41, 0
	s_mov_b32 m0, s65
	s_nop 0
	global_load_lds_dwordx4 v195, s[14:15]
	s_add_i32 s66, s27, 0x1a000
	s_add_i32 s67, s27, 0x8000
	s_mov_b32 m0, s66
	s_nop 0
	global_load_lds_dwordx4 v199, s[14:15]
	s_add_u32 s14, s38, 0x80
	s_addc_u32 s15, s39, 0
	s_mov_b32 m0, s67
	s_nop 0
	global_load_lds_dwordx4 v194, s[14:15]
	s_add_i32 s68, s27, 0xa000
	s_add_i32 s69, s27, 0x1c000
	s_mov_b32 m0, s68
	s_nop 0
	global_load_lds_dwordx4 v196, s[14:15]
	s_add_u32 s14, s40, 0x20080
	s_addc_u32 s15, s41, 0
	s_mov_b32 m0, s69
	s_nop 0
	global_load_lds_dwordx4 v195, s[14:15]
	s_add_i32 s70, s27, 0x1e000
	s_mov_b32 m0, s70
	s_nop 0
	global_load_lds_dwordx4 v199, s[14:15]
	s_waitcnt vmcnt(6)
	s_add_i32 s71, s27, 0xc000
	s_cmpk_lt_u32 s23, 0x100
	s_cselect_b64 s[14:15], -1, 0
	s_add_i32 s72, s27, 0xe000
	v_mov_b32_e32 v200, 0x7f7f7f7f
	s_mov_b64 s[16:17], 0x1000
	s_movk_i32 s73, 0x1000
	s_mov_b32 s74, 0xc0e00000
	v_add_u32_e32 v201, 0, v0
	v_add_u32_e32 v202, 0, v2
	v_mov_b32_e32 v203, 0x40e00000
	s_barrier
	s_branch .LBB0_4999

; #define PG8_WAIT_V(n) asm volatile("s_waitcnt vmcnt(" #n ")" ::: "memory")
; #define PG8_BAR __builtin_amdgcn_s_barrier()
; #define PG8_STAGE_A(b, h, p) do { if constexpr (GATHER) { if ((h) == 0) PG8_STAGE(PG8_SA(b, h), p, vA0); else PG8_STAGE(PG8_SA(b, h), p, vA1); } else PG8_STAGE(PG8_SA(b, h), (p) + ((h) ? hstepA : (size_t)0), voffA); } while (0)
; template <class Epi, class Sched, bool ALIGN_EPI = true, bool SP2 = true, bool FP8 = false, bool GATHER = false>
; __device__ __forceinline__ void gemm_phase(LAS unsigned char* lds, const Dims g, const Sched& S, const Epi& E, const int wv) {
;     ...
;     for (int i = 0; i < 2; ++i) { int R, C; stage_rc(tid * 16 + i * 8192, R, C); const int Rb = Epi::PERM ? ((R & ~31) + perm32(R & 31)) : R;
;         voffA[i] = (unsigned)(R * g.lda + C) * 2u; voffB[i] = (unsigned)(Rb * g.ldb + C) * 2u; }
;     const size_t kstep = (size_t)(BK * 2);
;     const size_t hstepA = (size_t)HALF * g.lda * 2, hstepB = (size_t)HALF * g.ldb * 2;
;     const unsigned ldsw = (unsigned)wid * 1024u, ldsb_ = (unsigned)(uintptr_t)lds;
;     const int aoff = lds_byte(wr * 64 + fr, fq * 8), boff = lds_byte(wc * 32 + fr, fq * 8);
;     ...
;     if constexpr (SP2) {
;         PG8_STAGE(PG8_SB(0, 0), cB, voffB); PG8_STAGE(PG8_SB(0, 1), cB + hstepB, voffB); PG8_STAGE_A(0, 0, cA); PG8_STAGE_A(0, 1, cA);
;         if (wr == 1) PG8_BAR;
;         PG8_WAIT_V(2); PG8_BAR;
;         PG8_STAGE(PG8_SB(1, 0), cB + kstep, voffB); PG8_STAGE_A(1, 0, cA + kstep); PG8_STAGE(PG8_SB(1, 1), cB + hstepB + kstep, voffB);
;         PG8_WAIT_V(6); PG8_BAR;
.LBB0_5096:
	v_bfe_i32 v2, v152, 27, 1
	s_add_u32 s55, s14, 0x8d200000
	v_lshlrev_b32_e32 v0, 4, v152
	v_lshrrev_b32_e32 v2, 22, v2
	s_addc_u32 s56, s15, 0
	v_add_u32_e32 v2, v0, v2
	s_add_u32 s57, s14, 0x2c000000
	v_and_b32_e32 v2, 0xfffffc00, v2
	s_addc_u32 s58, s15, 0
	s_ashr_i32 s37, s36, 31
	v_sub_u32_e32 v2, v0, v2
	s_lshl_b64 s[6:7], s[36:37], 18
	v_ashrrev_i32_e32 v1, 31, v152
	v_lshrrev_b32_e32 v3, 4, v2
	s_add_u32 s42, s55, s6
	v_lshrrev_b32_e32 v1, 26, v1
	v_bitop3_b32 v2, v3, v2, 32 bitop3:0x6c
	s_addc_u32 s43, s56, s7
	s_ashr_i32 s41, s40, 31
	v_add_u32_e32 v1, v152, v1
	v_ashrrev_i32_e32 v4, 31, v2
	s_lshl_b64 s[6:7], s[40:41], 20
	v_ashrrev_i32_e32 v1, 6, v1
	v_lshrrev_b32_e32 v4, 26, v4
	s_add_u32 s8, s57, s6
	v_lshlrev_b32_e32 v3, 3, v1
	v_add_u32_e32 v4, v2, v4
	s_addc_u32 s9, s58, s7
	s_ashr_i32 s39, s38, 31
	v_and_b32_e32 v3, -16, v3
	v_ashrrev_i32_e32 v5, 6, v4
	v_and_b32_e32 v4, 0xc0, v4
	s_lshl_b64 s[6:7], s[38:39], 18
	v_add_u32_e32 v3, v5, v3
	v_sub_u32_e32 v2, v2, v4
	v_mov_b32_e32 v4, 1
	s_add_u32 s44, s8, s6
	v_lshlrev_b32_e32 v1, 5, v1
	v_ashrrev_i16_sdwa v2, v4, sext(v2) dst_sel:DWORD dst_unused:UNUSED_PAD src0_sel:DWORD src1_sel:BYTE_0
	v_lshlrev_b32_e32 v6, 1, v3
	v_lshrrev_b32_e32 v7, 2, v3
	v_and_b32_e32 v5, 3, v5
	s_mov_b32 s6, 0x3fffe0
	v_and_b32_e32 v1, 32, v1
	v_bfe_i32 v2, v2, 0, 16
	v_and_b32_e32 v6, 24, v6
	v_and_b32_e32 v7, 4, v7
	v_and_or_b32 v5, v3, s6, v5
	v_or3_b32 v5, v5, v7, v6
	v_add_lshl_u32 v1, v1, v2, 1
	v_add_u32_e32 v0, 0x2000, v0
	v_lshl_add_u32 v153, v3, 10, v1
	v_lshl_add_u32 v154, v5, 10, v1
	v_ashrrev_i32_e32 v1, 31, v0
	v_lshrrev_b32_e32 v1, 22, v1
	v_add_u32_e32 v1, v0, v1
	v_ashrrev_i32_e32 v1, 10, v1
	v_mul_i32_i24_e32 v2, 0x400, v1
	v_sub_u32_e32 v0, v0, v2
	v_lshrrev_b32_e32 v2, 4, v0
	v_bitop3_b32 v0, v2, v0, 32 bitop3:0x6c
	v_ashrrev_i32_e32 v3, 31, v0
	v_lshrrev_b32_e32 v3, 26, v3
	v_lshlrev_b32_e32 v2, 3, v1
	v_add_u32_e32 v3, v0, v3
	v_and_b32_e32 v2, -16, v2
	v_ashrrev_i32_e32 v5, 6, v3
	v_and_b32_e32 v3, 0xc0, v3
	s_addc_u32 s45, s9, s7
	v_add_u32_e32 v2, v5, v2
	v_sub_u32_e32 v0, v0, v3
	v_and_b32_e32 v5, 3, v5
	s_ashr_i32 s13, s3, 6
	v_lshlrev_b32_e32 v1, 5, v1
	v_ashrrev_i16_sdwa v0, v4, sext(v0) dst_sel:DWORD dst_unused:UNUSED_PAD src0_sel:DWORD src1_sel:BYTE_0
	v_lshlrev_b32_e32 v3, 1, v2
	v_lshrrev_b32_e32 v4, 2, v2
	v_and_or_b32 v5, v2, s6, v5
	s_lshl_b32 s6, s13, 10
	v_and_b32_e32 v1, 32, v1
	v_bfe_i32 v0, v0, 0, 16
	v_and_b32_e32 v3, 24, v3
	v_and_b32_e32 v4, 4, v4
	s_add_i32 s59, s6, 0
	v_or3_b32 v3, v5, v4, v3
	v_add_lshl_u32 v0, v1, v0, 1
	s_add_i32 s60, s59, 0x10000
	s_mov_b32 m0, s60
	s_nop 0
	global_load_lds_dwordx4 v154, s[44:45]
	s_ashr_i32 s12, s3, 8
	v_lshl_add_u32 v156, v3, 10, v0
	s_add_i32 s61, s59, 0x12000
	s_mov_b32 m0, s61
	s_nop 0
	global_load_lds_dwordx4 v156, s[44:45]
	s_add_i32 s62, s59, 0x14000
	s_add_u32 s6, s44, 0x20000
	s_addc_u32 s7, s45, 0
	s_mov_b32 m0, s62
	s_nop 0
	global_load_lds_dwordx4 v154, s[6:7]
	s_add_i32 s63, s59, 0x16000
	s_mov_b32 m0, s63
	s_nop 0
	global_load_lds_dwordx4 v156, s[6:7]
	s_mov_b32 m0, s59
	s_nop 0
	global_load_lds_dwordx4 v153, s[42:43]
	s_add_i32 s64, s59, 0x2000
	s_add_i32 s65, s59, 0x4000
	v_lshl_add_u32 v155, v2, 10, v0
	s_mov_b32 m0, s64
	s_nop 0
	global_load_lds_dwordx4 v155, s[42:43]
	s_add_u32 s8, s42, 0x20000
	s_addc_u32 s9, s43, 0
	s_mov_b32 m0, s65
	s_nop 0
	global_load_lds_dwordx4 v153, s[8:9]
	s_add_i32 s66, s59, 0x6000
	s_mov_b32 m0, s66
	s_nop 0
	global_load_lds_dwordx4 v155, s[8:9]
	s_cmp_eq_u32 s12, 1
	s_mov_b32 s39, 0
	s_cselect_b64 s[6:7], -1, 0
	s_cmp_lg_u32 s12, 1
	s_cbranch_scc1 .LBB0_5098
	s_barrier
.LBB0_5098:
	s_add_u32 s8, s14, 0x9e200000
	s_addc_u32 s9, s15, 0
	s_waitcnt lgkmcnt(0)
	s_add_u32 s67, s10, 0x60000
	s_addc_u32 s68, s11, 0
	s_lshl_b32 s10, s12, 6
	v_and_b32_e32 v0, 48, v152
	s_lshl_b32 s11, s12, 13
	v_lshlrev_b32_e32 v1, 6, v152
	s_movk_i32 s12, 0x3c0
	v_and_or_b32 v0, v1, s12, v0
	v_lshlrev_b32_e32 v1, 2, v152
	v_and_b32_e32 v1, 32, v1
	v_bitop3_b32 v2, v0, s11, v1 bitop3:0xde
	s_lshl_b32 s11, s13, 5
	s_and_b32 s69, s11, 0x60
	s_lshl_b32 s11, s69, 7
	s_add_i32 s70, s59, 0x18000
	s_add_u32 s12, s44, 0x80
	v_bitop3_b32 v0, s11, v0, v1 bitop3:0xf6
	s_waitcnt vmcnt(2)
	s_barrier
	s_addc_u32 s13, s45, 0
	s_mov_b32 m0, s70
	s_nop 0
	global_load_lds_dwordx4 v154, s[12:13]
	s_add_i32 s71, s59, 0x1a000
	s_add_i32 s72, s59, 0x8000
	s_mov_b32 m0, s71
	s_nop 0
	global_load_lds_dwordx4 v156, s[12:13]
	s_add_u32 s12, s42, 0x80
	s_addc_u32 s13, s43, 0
	s_mov_b32 m0, s72
	s_nop 0
	global_load_lds_dwordx4 v153, s[12:13]
	s_add_i32 s73, s59, 0xa000
	s_add_i32 s74, s59, 0x1c000
	s_mov_b32 m0, s73
	s_nop 0
	global_load_lds_dwordx4 v155, s[12:13]
	s_add_u32 s12, s44, 0x20080
	s_addc_u32 s13, s45, 0
	s_mov_b32 m0, s74
	s_nop 0
	global_load_lds_dwordx4 v154, s[12:13]
	s_add_i32 s75, s59, 0x1e000
	s_add_i32 s76, s59, 0xc000
	s_mov_b32 m0, s75
	s_nop 0
	global_load_lds_dwordx4 v156, s[12:13]
	s_cmpk_lt_u32 s3, 0x100
	s_cselect_b64 s[12:13], -1, 0
	s_ashr_i32 s11, s10, 31
	s_add_i32 s77, s59, 0xe000
	s_lshl_b64 s[20:21], s[10:11], 2
	s_add_u32 s3, s14, s20
	s_addc_u32 s14, s15, s21
	s_add_u32 s11, s3, 0x7c100000
	s_waitcnt vmcnt(6)
	s_addc_u32 s15, s14, 0
	s_lshl_b32 s14, s33, 3
	s_and_b32 s14, s14, 56
	s_bfe_u32 s16, s33, 0x30003
	v_add_u32_e32 v0, 0, v0
	s_ashr_i32 s78, s54, 31
	s_ashr_i32 s79, s33, 31
	s_ashr_i32 s3, s2, 31
	s_or_b32 s80, s16, s14
	s_ashr_i32 s81, s33, 6
	v_add_u32_e32 v157, 0x10000, v0
	v_add_u32_e32 v158, 0x14000, v0
	v_add_u32_e32 v159, 0, v2
	v_mov_b32_e32 v160, 0x7f7f7f7f
	v_add_u32_e32 v161, 0x18000, v0
	v_add_u32_e32 v162, 0x1c000, v0
	s_mov_b32 s14, 0x42000000
	s_mov_b32 s16, 0x3b000000
	s_mov_b32 s82, 0xc3e00000
	v_mov_b32_e32 v163, 0x43e00000
	s_barrier
	s_branch .LBB0_5101
